# GEMM epilogue output stores of P7/P9/P11/P17 written through (sc1) so the seam's L2 write-back has less to flush
# baseline (speedup 1.0000x reference)
;     __device__ __forceinline__ void operator()(const f32x4 (&acc)[2][2][4][2], const Unit& u, int wr, int wc, int fr, int fq) const {
;     ...
;         if (QI8) {
; #pragma unroll
;             for (int ai = 0; ai < 2; ++ai)
; #pragma unroll
;                 for (int m = 0; m < 4; ++m) ra[ai][m] = sa[row0 + ai * HALF + m * 16];
; #pragma unroll
;             for (int bj = 0; bj < 2; ++bj) { cb[bj][0] = *(const f32x4*)(sb + col0 + bj * HALF) * tsc; cb[bj][1] = *(const f32x4*)(sb + col0 + bj * HALF + 4) * tsc; } }
;         else if (MODE == 1) {
; #pragma unroll
;             for (int bj = 0; bj < 2; ++bj) { cb[bj][0] = *(const f32x4*)(colscale + col0 + bj * HALF); cb[bj][1] = *(const f32x4*)(colscale + col0 + bj * HALF + 4); } }
;         const bool dual = (MODE == 0) && aux != nullptr && u.pn >= ZC_KV / 256 && u.pn < ZC_KV / 256 + 4;
;         u32x4 gq[2][2], aq[2][2]; f32x4 rs[2][2][2];
;     ...
;         EPB_LOAD(0);
; #pragma unroll
;         for (int kb = 0; kb < 8; ++kb) { const int ai = kb >> 2, m = kb & 3;
;             if (kb < 7) EPB_LOAD(kb + 1);
;             { const int row = row0 + ai * HALF + m * 16; float rmx = 0.f;
; #pragma unroll
;                 for (int bj = 0; bj < 2; ++bj) { const int col = col0 + bj * HALF; f32x4 v0 = acc[ai][bj][m][0], v1 = acc[ai][bj][m][1];
;                     if (QI8) { const f32x4 c0 = cb[bj][0] * ra[ai][m], c1 = cb[bj][1] * ra[ai][m]; const i32x4 i0 = __builtin_bit_cast(i32x4, v0), i1 = __builtin_bit_cast(i32x4, v1);
;                         v0 = (f32x4){(float)i0[0], (float)i0[1], (float)i0[2], (float)i0[3]} * c0; v1 = (f32x4){(float)i1[0], (float)i1[1], (float)i1[2], (float)i1[3]} * c1; }
;                     else if (MODE == 0) { v0 = v0 * tsc; v1 = v1 * tsc; }
;                     if (!QI8 && MODE == 1) { v0 = v0 * cb[bj][0]; v1 = v1 * cb[bj][1]; }
;                     if (MODE == 2 || MODE == 3) { const u32x4 g = gq[kb & 1][bj];
;                         f32x4 g0 = {sigmoidf_(bflo(g.x)), sigmoidf_(bfhi(g.x)), sigmoidf_(bflo(g.y)), sigmoidf_(bfhi(g.y))};
;                         f32x4 g1 = {sigmoidf_(bflo(g.z)), sigmoidf_(bfhi(g.z)), sigmoidf_(bflo(g.w)), sigmoidf_(bfhi(g.w))};
;                         v0 = v0 * g0; v1 = v1 * g1;
;                         if (MODE == 3) { const u32x4 q = aq[kb & 1][bj];
.LBB0_1003:
	v_lshl_or_b32 v70, s66, 8, v231
	v_lshl_add_u32 v152, s30, 8, v229
	v_ashrrev_i32_e32 v71, 31, v70
	v_mov_b64_e32 v[154:155], s[14:15]
	v_ashrrev_i32_e32 v153, 31, v152
	v_mad_i64_i32 v[144:145], s[34:35], v152, s64, v[154:155]
	v_lshlrev_b64 v[146:147], 1, v[70:71]
	v_lshl_add_u64 v[142:143], v[152:153], 2, s[10:11]
	v_lshl_add_u64 v[72:73], v[70:71], 2, s[12:13]
	v_lshl_add_u64 v[144:145], v[144:145], 0, v[146:147]
	global_load_dword v178, v[142:143], off
	global_load_dwordx4 v[78:81], v[72:73], off
	global_load_dwordx4 v[74:77], v[72:73], off offset:16
	global_load_dwordx4 v[170:173], v[144:145], off nt
	v_cvt_f32_i32_e32 v181, v69
	v_cvt_f32_i32_e32 v180, v68
	v_cvt_f32_i32_e32 v183, v67
	v_cvt_f32_i32_e32 v182, v66
	global_load_dwordx4 v[66:69], v[72:73], off offset:528
	s_nop 0
	global_load_dwordx4 v[70:73], v[72:73], off offset:512
	s_nop 0
	global_load_dwordx4 v[174:177], v[144:145], off offset:256 nt
	global_load_dword v166, v[142:143], off offset:64
	global_load_dword v164, v[142:143], off offset:128
	global_load_dword v162, v[142:143], off offset:192
	global_load_dword v158, v[142:143], off offset:512
	global_load_dword v156, v[142:143], off offset:576
	global_load_dword v150, v[142:143], off offset:640
	global_load_dword v148, v[142:143], off offset:704
	v_or_b32_e32 v168, 16, v152
	v_cvt_f32_i32_e32 v187, v139
	v_cvt_f32_i32_e32 v186, v138
	v_mad_i64_i32 v[138:139], s[34:35], v168, s64, v[154:155]
	v_lshl_add_u64 v[138:139], v[138:139], 0, v[146:147]
	v_cvt_f32_i32_e32 v185, v141
	v_cvt_f32_i32_e32 v184, v140
	global_load_dwordx4 v[142:145], v[138:139], off nt
	s_nop 0
	global_load_dwordx4 v[138:141], v[138:139], off offset:256 nt
	v_cvt_f32_i32_e32 v137, v137
	v_cvt_f32_i32_e32 v136, v136
	v_cvt_f32_i32_e32 v135, v135
	v_cvt_f32_i32_e32 v134, v134
	v_cvt_f32_i32_e32 v133, v133
	v_cvt_f32_i32_e32 v132, v132
	v_cvt_f32_i32_e32 v131, v131
	v_cvt_f32_i32_e32 v130, v130
	v_cvt_f32_i32_e32 v129, v129
	v_cvt_f32_i32_e32 v128, v128
	v_cvt_f32_i32_e32 v127, v127
	v_cvt_f32_i32_e32 v126, v126
	v_cvt_f32_i32_e32 v125, v125
	v_cvt_f32_i32_e32 v124, v124
	v_cvt_f32_i32_e32 v123, v123
	v_cvt_f32_i32_e32 v122, v122
	v_ashrrev_i32_e32 v169, 31, v168
	v_cvt_f32_i32_e32 v119, v119
	v_cvt_f32_i32_e32 v118, v118
	v_cvt_f32_i32_e32 v121, v121
	v_cvt_f32_i32_e32 v120, v120
	v_cvt_f32_i32_e32 v117, v117
	v_cvt_f32_i32_e32 v116, v116
	v_cvt_f32_i32_e32 v115, v115
	v_cvt_f32_i32_e32 v114, v114
	v_cvt_f32_i32_e32 v111, v111
	v_cvt_f32_i32_e32 v110, v110
	v_cvt_f32_i32_e32 v113, v113
	v_cvt_f32_i32_e32 v112, v112
	v_cvt_f32_i32_e32 v109, v109
	v_cvt_f32_i32_e32 v108, v108
	v_cvt_f32_i32_e32 v107, v107
	v_cvt_f32_i32_e32 v106, v106
	v_cvt_f32_i32_e32 v103, v103
	v_cvt_f32_i32_e32 v102, v102
	v_cvt_f32_i32_e32 v105, v105
	v_cvt_f32_i32_e32 v104, v104
	v_cvt_f32_i32_e32 v101, v101
	v_cvt_f32_i32_e32 v100, v100
	v_cvt_f32_i32_e32 v99, v99
	v_cvt_f32_i32_e32 v98, v98
	v_add_u32_e32 v160, 0x80, v152
	v_cvt_f32_i32_e32 v95, v95
	v_cvt_f32_i32_e32 v94, v94
	v_cvt_f32_i32_e32 v97, v97
	v_cvt_f32_i32_e32 v96, v96
	v_cvt_f32_i32_e32 v93, v93
	v_cvt_f32_i32_e32 v92, v92
	v_cvt_f32_i32_e32 v91, v91
	v_cvt_f32_i32_e32 v90, v90
	v_cvt_f32_i32_e32 v87, v87
	v_cvt_f32_i32_e32 v86, v86
	v_cvt_f32_i32_e32 v89, v89
	v_cvt_f32_i32_e32 v88, v88
	v_cvt_f32_i32_e32 v85, v85
	v_cvt_f32_i32_e32 v84, v84
	v_cvt_f32_i32_e32 v83, v83
	v_cvt_f32_i32_e32 v82, v82
	v_cvt_f32_i32_e32 v63, v63
	v_cvt_f32_i32_e32 v62, v62
	v_cvt_f32_i32_e32 v65, v65
	v_cvt_f32_i32_e32 v64, v64
	s_waitcnt vmcnt(0)
	v_pk_mul_f32 v[188:189], v[178:179], v[80:81] op_sel_hi:[0,1]
	v_pk_mul_f32 v[190:191], v[178:179], v[78:79] op_sel_hi:[0,1]
	v_lshlrev_b32_e32 v149, 16, v170
	v_and_b32_e32 v151, 0xffff0000, v170
	v_lshlrev_b32_e32 v157, 16, v171
	v_and_b32_e32 v159, 0xffff0000, v171
	v_lshlrev_b32_e32 v167, 16, v173
	v_and_b32_e32 v170, 0xffff0000, v173
	v_lshlrev_b32_e32 v163, 16, v172
	v_and_b32_e32 v165, 0xffff0000, v172
	v_mul_f32_e32 v149, 0xbfb8aa3b, v149
	v_mul_f32_e32 v151, 0xbfb8aa3b, v151
	v_mul_f32_e32 v157, 0xbfb8aa3b, v157
	v_mul_f32_e32 v159, 0xbfb8aa3b, v159
	v_mul_f32_e32 v167, 0xbfb8aa3b, v167
	v_mul_f32_e32 v170, 0xbfb8aa3b, v170
	v_mul_f32_e32 v163, 0xbfb8aa3b, v163
	v_mul_f32_e32 v165, 0xbfb8aa3b, v165
	v_exp_f32_e32 v149, v149
	v_exp_f32_e32 v151, v151
	v_exp_f32_e32 v157, v157
	v_exp_f32_e32 v159, v159
	v_exp_f32_e32 v167, v167
	v_exp_f32_e32 v170, v170
	v_exp_f32_e32 v163, v163
	v_exp_f32_e32 v165, v165
	v_pk_mul_f32 v[192:193], v[178:179], v[76:77] op_sel_hi:[0,1]
	v_pk_mul_f32 v[212:213], v[178:179], v[74:75] op_sel_hi:[0,1]
	v_add_f32_e32 v149, 1.0, v149
	v_add_f32_e32 v151, 1.0, v151
	v_add_f32_e32 v157, 1.0, v157
	v_add_f32_e32 v159, 1.0, v159
	v_add_f32_e32 v167, 1.0, v167
	v_add_f32_e32 v179, 1.0, v170
	v_pk_mul_f32 v[182:183], v[190:191], v[182:183]
	v_add_f32_e32 v163, 1.0, v163
	v_add_f32_e32 v165, 1.0, v165
	v_rcp_f32_e32 v170, v149
	v_rcp_f32_e32 v171, v151
	v_rcp_f32_e32 v172, v157
	v_rcp_f32_e32 v173, v159
	v_rcp_f32_e32 v190, v167
	v_rcp_f32_e32 v191, v179
	v_pk_mul_f32 v[180:181], v[188:189], v[180:181]
	v_rcp_f32_e32 v188, v163
	v_rcp_f32_e32 v189, v165
	v_pk_mul_f32 v[184:185], v[192:193], v[184:185]
	v_lshlrev_b32_e32 v149, 16, v174
	v_pk_mul_f32 v[186:187], v[212:213], v[186:187]
	v_pk_mul_f32 v[172:173], v[180:181], v[172:173]
	v_pk_mul_f32 v[170:171], v[182:183], v[170:171]
	v_pk_mul_f32 v[180:181], v[184:185], v[190:191]
	v_mul_f32_e32 v149, 0xbfb8aa3b, v149
	v_and_b32_e32 v151, 0xffff0000, v174
	v_pk_mul_f32 v[182:183], v[186:187], v[188:189]
	v_cvt_pk_bf16_f32 v170, v170, v171
	v_cvt_pk_bf16_f32 v171, v172, v173
	v_exp_f32_e32 v149, v149
;     __device__ __forceinline__ void operator()(const f32x4 (&acc)[2][2][4][2], const Unit& u, int wr, int wc, int fr, int fq) const {
;     ...
;         EPB_LOAD(0);
; #pragma unroll
;         for (int kb = 0; kb < 8; ++kb) { const int ai = kb >> 2, m = kb & 3;
;             if (kb < 7) EPB_LOAD(kb + 1);
;             { const int row = row0 + ai * HALF + m * 16; float rmx = 0.f;
; #pragma unroll
;                 for (int bj = 0; bj < 2; ++bj) { const int col = col0 + bj * HALF; f32x4 v0 = acc[ai][bj][m][0], v1 = acc[ai][bj][m][1];
;                     if (QI8) { const f32x4 c0 = cb[bj][0] * ra[ai][m], c1 = cb[bj][1] * ra[ai][m]; const i32x4 i0 = __builtin_bit_cast(i32x4, v0), i1 = __builtin_bit_cast(i32x4, v1);
;                         v0 = (f32x4){(float)i0[0], (float)i0[1], (float)i0[2], (float)i0[3]} * c0; v1 = (f32x4){(float)i1[0], (float)i1[1], (float)i1[2], (float)i1[3]} * c1; }
;                     else if (MODE == 0) { v0 = v0 * tsc; v1 = v1 * tsc; }
;                     if (!QI8 && MODE == 1) { v0 = v0 * cb[bj][0]; v1 = v1 * cb[bj][1]; }
;                     if (MODE == 2 || MODE == 3) { const u32x4 g = gq[kb & 1][bj];
;                         f32x4 g0 = {sigmoidf_(bflo(g.x)), sigmoidf_(bfhi(g.x)), sigmoidf_(bflo(g.y)), sigmoidf_(bfhi(g.y))};
;                         f32x4 g1 = {sigmoidf_(bflo(g.z)), sigmoidf_(bfhi(g.z)), sigmoidf_(bflo(g.w)), sigmoidf_(bfhi(g.w))};
;                         v0 = v0 * g0; v1 = v1 * g1;
;                         if (MODE == 3) { const u32x4 q = aq[kb & 1][bj];
;                             v0 = v0 + (f32x4){bflo(q.x), bfhi(q.x), bflo(q.y), bfhi(q.y)}; v1 = v1 + (f32x4){bflo(q.z), bfhi(q.z), bflo(q.w), bfhi(q.w)}; } }
;                     if (MODE == 4) { v0 = v0 + rs[kb & 1][bj][0]; v1 = v1 + rs[kb & 1][bj][1]; }
;                     if (MODE == 5) { const u32x4 c = gq[kb & 1][bj], q = aq[kb & 1][bj];
;                         v0 = (f32x4){bflo(c.x) + sigmoidf_(v0[0]) * bflo(q.x), bfhi(c.x) + sigmoidf_(v0[1]) * bfhi(q.x), bflo(c.y) + sigmoidf_(v0[2]) * bflo(q.y), bfhi(c.y) + sigmoidf_(v0[3]) * bfhi(q.y)};
;                         v1 = (f32x4){bflo(c.z) + sigmoidf_(v1[0]) * bflo(q.z), bfhi(c.z) + sigmoidf_(v1[1]) * bfhi(q.z), bflo(c.w) + sigmoidf_(v1[2]) * bflo(q.w), bfhi(c.w) + sigmoidf_(v1[3]) * bfhi(q.w)}; }
	v_cvt_pk_bf16_f32 v172, v182, v183
	v_cvt_pk_bf16_f32 v173, v180, v181
	v_lshlrev_b64 v[180:181], 13, v[152:153]
	v_mul_f32_e32 v151, 0xbfb8aa3b, v151
	v_lshlrev_b32_e32 v153, 16, v175
	v_exp_f32_e32 v151, v151
	v_mul_f32_e32 v153, 0xbfb8aa3b, v153
	v_lshl_add_u64 v[180:181], s[0:1], 0, v[180:181]
	v_exp_f32_e32 v153, v153
	v_lshl_add_u64 v[180:181], v[180:181], 0, v[146:147]
	global_store_dwordx4 v[180:181], v[170:173], off sc1
	v_add_f32_e32 v149, 1.0, v149
	v_pk_mul_f32 v[182:183], v[178:179], v[68:69] op_sel_hi:[0,1]
	v_pk_mul_f32 v[170:171], v[178:179], v[72:73] op_sel_hi:[0,1]
	v_pk_mul_f32 v[136:137], v[170:171], v[136:137]
	v_rcp_f32_e32 v170, v149
	v_add_f32_e32 v149, 1.0, v151
	v_and_b32_e32 v151, 0xffff0000, v175
	v_rcp_f32_e32 v171, v149
	v_add_f32_e32 v149, 1.0, v153
	v_mul_f32_e32 v151, 0xbfb8aa3b, v151
	v_lshlrev_b32_e32 v153, 16, v176
	v_exp_f32_e32 v151, v151
	v_mul_f32_e32 v153, 0xbfb8aa3b, v153
	v_exp_f32_e32 v153, v153
	v_pk_mul_f32 v[172:173], v[178:179], v[70:71] op_sel_hi:[0,1]
	v_pk_mul_f32 v[134:135], v[172:173], v[134:135]
	v_rcp_f32_e32 v172, v149
	v_add_f32_e32 v149, 1.0, v151
	v_rcp_f32_e32 v173, v149
	v_add_f32_e32 v149, 1.0, v153
	v_lshlrev_b32_e32 v151, 16, v177
	v_rcp_f32_e32 v174, v149
	v_and_b32_e32 v149, 0xffff0000, v176
	v_mul_f32_e32 v151, 0xbfb8aa3b, v151
	v_and_b32_e32 v153, 0xffff0000, v177
	v_mul_f32_e32 v149, 0xbfb8aa3b, v149
	v_exp_f32_e32 v151, v151
	v_mul_f32_e32 v153, 0xbfb8aa3b, v153
	v_exp_f32_e32 v149, v149
	v_exp_f32_e32 v153, v153
	v_add_f32_e32 v151, 1.0, v151
	v_rcp_f32_e32 v176, v151
	v_add_f32_e32 v149, 1.0, v149
	v_add_f32_e32 v151, 1.0, v153
	v_rcp_f32_e32 v177, v151
	v_rcp_f32_e32 v175, v149
	v_lshlrev_b32_e32 v149, 16, v142
	v_mul_f32_e32 v149, 0xbfb8aa3b, v149
	v_pk_mul_f32 v[178:179], v[178:179], v[66:67] op_sel_hi:[0,1]
	v_exp_f32_e32 v149, v149
	v_pk_mul_f32 v[130:131], v[178:179], v[130:131]
	v_pk_mul_f32 v[132:133], v[182:183], v[132:133]
	v_pk_mul_f32 v[134:135], v[134:135], v[170:171]
	v_pk_mul_f32 v[170:171], v[132:133], v[176:177]
	v_pk_mul_f32 v[132:133], v[130:131], v[174:175]
	v_pk_mul_f32 v[136:137], v[136:137], v[172:173]
	v_cvt_pk_bf16_f32 v130, v134, v135
	v_pk_mul_f32 v[172:173], v[166:167], v[80:81] op_sel_hi:[0,1]
	v_cvt_pk_bf16_f32 v131, v136, v137
	v_cvt_pk_bf16_f32 v132, v132, v133
	v_cvt_pk_bf16_f32 v133, v170, v171
	v_or_b32_e32 v170, 32, v152
	global_store_dwordx4 v[180:181], v[130:133], off offset:256 sc1
	v_add_f32_e32 v149, 1.0, v149
	v_pk_mul_f32 v[128:129], v[172:173], v[128:129]
	v_mad_i64_i32 v[130:131], s[34:35], v170, s64, v[154:155]
	v_lshl_add_u64 v[130:131], v[130:131], 0, v[146:147]
	v_rcp_f32_e32 v172, v149
	v_lshlrev_b32_e32 v149, 16, v144
	global_load_dwordx4 v[134:137], v[130:131], off nt
	s_nop 0
	global_load_dwordx4 v[130:133], v[130:131], off offset:256 nt
	v_mul_f32_e32 v149, 0xbfb8aa3b, v149
	v_exp_f32_e32 v149, v149
	v_pk_mul_f32 v[174:175], v[166:167], v[78:79] op_sel_hi:[0,1]
	v_and_b32_e32 v142, 0xffff0000, v142
	v_pk_mul_f32 v[126:127], v[174:175], v[126:127]
	v_add_f32_e32 v149, 1.0, v149
	v_mul_f32_e32 v142, 0xbfb8aa3b, v142
	v_lshlrev_b32_e32 v151, 16, v143
	v_and_b32_e32 v143, 0xffff0000, v143
	v_rcp_f32_e32 v174, v149
	v_and_b32_e32 v144, 0xffff0000, v144
	v_lshlrev_b32_e32 v149, 16, v145
	v_and_b32_e32 v145, 0xffff0000, v145
	v_exp_f32_e32 v142, v142
	v_mul_f32_e32 v151, 0xbfb8aa3b, v151
	v_mul_f32_e32 v143, 0xbfb8aa3b, v143
	v_mul_f32_e32 v144, 0xbfb8aa3b, v144
	v_mul_f32_e32 v149, 0xbfb8aa3b, v149
	v_mul_f32_e32 v145, 0xbfb8aa3b, v145
	v_exp_f32_e32 v151, v151
	v_exp_f32_e32 v143, v143
	v_exp_f32_e32 v144, v144
	v_exp_f32_e32 v149, v149
	v_exp_f32_e32 v145, v145
	v_add_f32_e32 v142, 1.0, v142
	v_rcp_f32_e32 v173, v142
	v_add_f32_e32 v142, 1.0, v151
	v_add_f32_e32 v143, 1.0, v143
	v_add_f32_e32 v151, 1.0, v144
	v_add_f32_e32 v144, 1.0, v149
	v_add_f32_e32 v145, 1.0, v145
	v_rcp_f32_e32 v142, v142
	v_rcp_f32_e32 v143, v143
	v_rcp_f32_e32 v144, v144
	v_rcp_f32_e32 v145, v145
	v_rcp_f32_e32 v175, v151
	v_pk_mul_f32 v[176:177], v[166:167], v[76:77] op_sel_hi:[0,1]
	v_pk_mul_f32 v[178:179], v[166:167], v[74:75] op_sel_hi:[0,1]
	v_pk_mul_f32 v[122:123], v[178:179], v[122:123]
	v_pk_mul_f32 v[124:125], v[176:177], v[124:125]
	v_pk_mul_f32 v[126:127], v[126:127], v[172:173]
	v_pk_mul_f32 v[128:129], v[128:129], v[142:143]
	v_pk_mul_f32 v[142:143], v[124:125], v[144:145]
	v_pk_mul_f32 v[124:125], v[122:123], v[174:175]
	v_cvt_pk_bf16_f32 v122, v126, v127
	v_lshlrev_b64 v[126:127], 13, v[168:169]
	v_lshl_add_u64 v[126:127], s[0:1], 0, v[126:127]
	v_cvt_pk_bf16_f32 v123, v128, v129
	v_cvt_pk_bf16_f32 v124, v124, v125
	v_cvt_pk_bf16_f32 v125, v142, v143
	v_lshl_add_u64 v[126:127], v[126:127], 0, v[146:147]
	global_store_dwordx4 v[126:127], v[122:125], off sc1
	v_pk_mul_f32 v[128:129], v[166:167], v[68:69] op_sel_hi:[0,1]
	v_pk_mul_f32 v[116:117], v[128:129], v[116:117]
	v_pk_mul_f32 v[124:125], v[166:167], v[70:71] op_sel_hi:[0,1]
	v_pk_mul_f32 v[118:119], v[124:125], v[118:119]
	v_lshlrev_b32_e32 v124, 16, v138
	v_mul_f32_e32 v124, 0xbfb8aa3b, v124
	v_exp_f32_e32 v124, v124
	v_pk_mul_f32 v[122:123], v[166:167], v[72:73] op_sel_hi:[0,1]
	v_pk_mul_f32 v[120:121], v[122:123], v[120:121]
	v_and_b32_e32 v123, 0xffff0000, v138
	v_add_f32_e32 v122, 1.0, v124
	v_lshlrev_b32_e32 v124, 16, v139
	v_and_b32_e32 v125, 0xffff0000, v139
	v_lshlrev_b32_e32 v128, 16, v140
	v_and_b32_e32 v129, 0xffff0000, v140
	v_lshlrev_b32_e32 v138, 16, v141
	v_and_b32_e32 v139, 0xffff0000, v141
	v_mul_f32_e32 v123, 0xbfb8aa3b, v123
	v_mul_f32_e32 v128, 0xbfb8aa3b, v128
	v_mul_f32_e32 v129, 0xbfb8aa3b, v129
	v_mul_f32_e32 v138, 0xbfb8aa3b, v138
;     __device__ __forceinline__ void operator()(const f32x4 (&acc)[2][2][4][2], const Unit& u, int wr, int wc, int fr, int fq) const {
;     ...
;         EPB_LOAD(0);
; #pragma unroll
;         for (int kb = 0; kb < 8; ++kb) { const int ai = kb >> 2, m = kb & 3;
;             if (kb < 7) EPB_LOAD(kb + 1);
;             { const int row = row0 + ai * HALF + m * 16; float rmx = 0.f;
; #pragma unroll
;                 for (int bj = 0; bj < 2; ++bj) { const int col = col0 + bj * HALF; f32x4 v0 = acc[ai][bj][m][0], v1 = acc[ai][bj][m][1];
;                     if (QI8) { const f32x4 c0 = cb[bj][0] * ra[ai][m], c1 = cb[bj][1] * ra[ai][m]; const i32x4 i0 = __builtin_bit_cast(i32x4, v0), i1 = __builtin_bit_cast(i32x4, v1);
;                         v0 = (f32x4){(float)i0[0], (float)i0[1], (float)i0[2], (float)i0[3]} * c0; v1 = (f32x4){(float)i1[0], (float)i1[1], (float)i1[2], (float)i1[3]} * c1; }
;                     else if (MODE == 0) { v0 = v0 * tsc; v1 = v1 * tsc; }
;                     if (!QI8 && MODE == 1) { v0 = v0 * cb[bj][0]; v1 = v1 * cb[bj][1]; }
;                     if (MODE == 2 || MODE == 3) { const u32x4 g = gq[kb & 1][bj];
;                         f32x4 g0 = {sigmoidf_(bflo(g.x)), sigmoidf_(bfhi(g.x)), sigmoidf_(bflo(g.y)), sigmoidf_(bfhi(g.y))};
;                         f32x4 g1 = {sigmoidf_(bflo(g.z)), sigmoidf_(bfhi(g.z)), sigmoidf_(bflo(g.w)), sigmoidf_(bfhi(g.w))};
;                         v0 = v0 * g0; v1 = v1 * g1;
;                         if (MODE == 3) { const u32x4 q = aq[kb & 1][bj];
;                             v0 = v0 + (f32x4){bflo(q.x), bfhi(q.x), bflo(q.y), bfhi(q.y)}; v1 = v1 + (f32x4){bflo(q.z), bfhi(q.z), bflo(q.w), bfhi(q.w)}; } }
;                     if (MODE == 4) { v0 = v0 + rs[kb & 1][bj][0]; v1 = v1 + rs[kb & 1][bj][1]; }
;                     if (MODE == 5) { const u32x4 c = gq[kb & 1][bj], q = aq[kb & 1][bj];
;                         v0 = (f32x4){bflo(c.x) + sigmoidf_(v0[0]) * bflo(q.x), bfhi(c.x) + sigmoidf_(v0[1]) * bfhi(q.x), bflo(c.y) + sigmoidf_(v0[2]) * bflo(q.y), bfhi(c.y) + sigmoidf_(v0[3]) * bfhi(q.y)};
;                         v1 = (f32x4){bflo(c.z) + sigmoidf_(v1[0]) * bflo(q.z), bfhi(c.z) + sigmoidf_(v1[1]) * bfhi(q.z), bflo(c.w) + sigmoidf_(v1[2]) * bflo(q.w), bfhi(c.w) + sigmoidf_(v1[3]) * bfhi(q.w)}; }
	v_mul_f32_e32 v139, 0xbfb8aa3b, v139
	v_exp_f32_e32 v123, v123
	v_mul_f32_e32 v124, 0xbfb8aa3b, v124
	v_mul_f32_e32 v125, 0xbfb8aa3b, v125
	v_exp_f32_e32 v128, v128
	v_exp_f32_e32 v129, v129
	v_exp_f32_e32 v138, v138
	v_exp_f32_e32 v139, v139
	v_exp_f32_e32 v124, v124
	v_exp_f32_e32 v125, v125
	v_add_f32_e32 v123, 1.0, v123
	v_add_f32_e32 v128, 1.0, v128
	v_add_f32_e32 v129, 1.0, v129
	v_add_f32_e32 v138, 1.0, v138
	v_add_f32_e32 v139, 1.0, v139
	v_rcp_f32_e32 v122, v122
	v_rcp_f32_e32 v123, v123
	v_add_f32_e32 v124, 1.0, v124
	v_add_f32_e32 v125, 1.0, v125
	v_rcp_f32_e32 v128, v128
	v_rcp_f32_e32 v138, v138
	v_rcp_f32_e32 v139, v139
	v_rcp_f32_e32 v129, v129
	v_rcp_f32_e32 v124, v124
	v_rcp_f32_e32 v125, v125
	v_pk_mul_f32 v[142:143], v[166:167], v[66:67] op_sel_hi:[0,1]
	v_pk_mul_f32 v[114:115], v[142:143], v[114:115]
	v_pk_mul_f32 v[118:119], v[118:119], v[122:123]
	v_pk_mul_f32 v[122:123], v[116:117], v[138:139]
	v_pk_mul_f32 v[116:117], v[114:115], v[128:129]
	v_pk_mul_f32 v[120:121], v[120:121], v[124:125]
	v_cvt_pk_bf16_f32 v114, v118, v119
	v_pk_mul_f32 v[124:125], v[164:165], v[80:81] op_sel_hi:[0,1]
	v_cvt_pk_bf16_f32 v115, v120, v121
	v_cvt_pk_bf16_f32 v116, v116, v117
	v_cvt_pk_bf16_f32 v117, v122, v123
	v_or_b32_e32 v122, 48, v152
	global_store_dwordx4 v[126:127], v[114:117], off offset:256 sc1
	v_pk_mul_f32 v[126:127], v[164:165], v[78:79] op_sel_hi:[0,1]
	v_pk_mul_f32 v[110:111], v[126:127], v[110:111]
	v_mad_i64_i32 v[114:115], s[34:35], v122, s64, v[154:155]
	v_lshl_add_u64 v[114:115], v[114:115], 0, v[146:147]
	global_load_dwordx4 v[118:121], v[114:115], off nt
	s_nop 0
	global_load_dwordx4 v[114:117], v[114:115], off offset:256 nt
	s_waitcnt vmcnt(5)
	v_lshlrev_b32_e32 v126, 16, v134
	v_mul_f32_e32 v126, 0xbfb8aa3b, v126
	v_exp_f32_e32 v126, v126
	v_pk_mul_f32 v[128:129], v[164:165], v[76:77] op_sel_hi:[0,1]
	v_pk_mul_f32 v[112:113], v[124:125], v[112:113]
	v_and_b32_e32 v125, 0xffff0000, v134
	v_pk_mul_f32 v[108:109], v[128:129], v[108:109]
	v_add_f32_e32 v124, 1.0, v126
	v_mul_f32_e32 v125, 0xbfb8aa3b, v125
	v_lshlrev_b32_e32 v126, 16, v135
	v_and_b32_e32 v127, 0xffff0000, v135
	v_lshlrev_b32_e32 v128, 16, v136
	v_and_b32_e32 v129, 0xffff0000, v136
	v_lshlrev_b32_e32 v134, 16, v137
	v_and_b32_e32 v135, 0xffff0000, v137
	v_exp_f32_e32 v125, v125
	v_mul_f32_e32 v128, 0xbfb8aa3b, v128
	v_mul_f32_e32 v129, 0xbfb8aa3b, v129
	v_mul_f32_e32 v134, 0xbfb8aa3b, v134
	v_mul_f32_e32 v135, 0xbfb8aa3b, v135
	v_exp_f32_e32 v128, v128
	v_exp_f32_e32 v129, v129
	v_exp_f32_e32 v134, v134
	v_exp_f32_e32 v135, v135
	v_mul_f32_e32 v126, 0xbfb8aa3b, v126
	v_mul_f32_e32 v127, 0xbfb8aa3b, v127
	v_exp_f32_e32 v126, v126
	v_exp_f32_e32 v127, v127
	v_add_f32_e32 v125, 1.0, v125
	v_rcp_f32_e32 v124, v124
	v_rcp_f32_e32 v125, v125
	v_add_f32_e32 v128, 1.0, v128
	v_add_f32_e32 v129, 1.0, v129
	v_add_f32_e32 v134, 1.0, v134
	v_add_f32_e32 v135, 1.0, v135
	v_rcp_f32_e32 v128, v128
	v_rcp_f32_e32 v134, v134
	v_rcp_f32_e32 v135, v135
	v_rcp_f32_e32 v129, v129
	v_add_f32_e32 v126, 1.0, v126
	v_add_f32_e32 v127, 1.0, v127
	v_pk_mul_f32 v[138:139], v[164:165], v[74:75] op_sel_hi:[0,1]
	v_rcp_f32_e32 v126, v126
	v_rcp_f32_e32 v127, v127
	v_ashrrev_i32_e32 v171, 31, v170
	v_pk_mul_f32 v[106:107], v[138:139], v[106:107]
	v_pk_mul_f32 v[110:111], v[110:111], v[124:125]
	v_pk_mul_f32 v[124:125], v[108:109], v[134:135]
	v_pk_mul_f32 v[108:109], v[106:107], v[128:129]
	v_cvt_pk_bf16_f32 v106, v110, v111
	v_lshlrev_b64 v[110:111], 13, v[170:171]
	v_lshl_add_u64 v[110:111], s[0:1], 0, v[110:111]
	v_pk_mul_f32 v[112:113], v[112:113], v[126:127]
	v_lshl_add_u64 v[110:111], v[110:111], 0, v[146:147]
	v_cvt_pk_bf16_f32 v107, v112, v113
	v_cvt_pk_bf16_f32 v108, v108, v109
	v_cvt_pk_bf16_f32 v109, v124, v125
	global_store_dwordx4 v[110:111], v[106:109], off sc1
	v_pk_mul_f32 v[112:113], v[164:165], v[68:69] op_sel_hi:[0,1]
	v_pk_mul_f32 v[124:125], v[164:165], v[66:67] op_sel_hi:[0,1]
	v_pk_mul_f32 v[108:109], v[164:165], v[70:71] op_sel_hi:[0,1]
	v_pk_mul_f32 v[102:103], v[108:109], v[102:103]
	s_waitcnt vmcnt(5)
	v_lshlrev_b32_e32 v108, 16, v130
	v_mul_f32_e32 v108, 0xbfb8aa3b, v108
	v_exp_f32_e32 v108, v108
	v_pk_mul_f32 v[106:107], v[164:165], v[72:73] op_sel_hi:[0,1]
	v_pk_mul_f32 v[104:105], v[106:107], v[104:105]
	v_pk_mul_f32 v[98:99], v[124:125], v[98:99]
	v_pk_mul_f32 v[100:101], v[112:113], v[100:101]
	v_add_f32_e32 v106, 1.0, v108
	v_and_b32_e32 v107, 0xffff0000, v130
	v_lshlrev_b32_e32 v108, 16, v131
	v_and_b32_e32 v109, 0xffff0000, v131
	v_lshlrev_b32_e32 v112, 16, v132
	v_and_b32_e32 v113, 0xffff0000, v132
	v_lshlrev_b32_e32 v124, 16, v133
	v_and_b32_e32 v125, 0xffff0000, v133
	v_mul_f32_e32 v107, 0xbfb8aa3b, v107
	v_mul_f32_e32 v108, 0xbfb8aa3b, v108
	v_mul_f32_e32 v109, 0xbfb8aa3b, v109
	v_mul_f32_e32 v112, 0xbfb8aa3b, v112
	v_mul_f32_e32 v113, 0xbfb8aa3b, v113
	v_mul_f32_e32 v124, 0xbfb8aa3b, v124
	v_mul_f32_e32 v125, 0xbfb8aa3b, v125
	v_exp_f32_e32 v107, v107
	v_exp_f32_e32 v108, v108
	v_exp_f32_e32 v109, v109
	v_exp_f32_e32 v112, v112
	v_exp_f32_e32 v113, v113
	v_exp_f32_e32 v124, v124
	v_exp_f32_e32 v125, v125
	v_add_f32_e32 v107, 1.0, v107
	v_add_f32_e32 v108, 1.0, v108
	v_add_f32_e32 v109, 1.0, v109
	v_add_f32_e32 v112, 1.0, v112
	v_add_f32_e32 v113, 1.0, v113
	v_add_f32_e32 v124, 1.0, v124
	v_add_f32_e32 v125, 1.0, v125
	v_rcp_f32_e32 v106, v106
	v_rcp_f32_e32 v107, v107
	v_rcp_f32_e32 v108, v108
	v_rcp_f32_e32 v109, v109
	v_rcp_f32_e32 v112, v112
	v_rcp_f32_e32 v124, v124
	v_rcp_f32_e32 v125, v125
	v_rcp_f32_e32 v113, v113
	v_pk_mul_f32 v[104:105], v[104:105], v[108:109]
	v_pk_mul_f32 v[102:103], v[102:103], v[106:107]
	v_pk_mul_f32 v[106:107], v[100:101], v[124:125]
	v_pk_mul_f32 v[100:101], v[98:99], v[112:113]
	v_cvt_pk_bf16_f32 v98, v102, v103
	v_cvt_pk_bf16_f32 v99, v104, v105
	v_pk_mul_f32 v[108:109], v[162:163], v[78:79] op_sel_hi:[0,1]
	v_cvt_pk_bf16_f32 v100, v100, v101
	v_cvt_pk_bf16_f32 v101, v106, v107
	global_store_dwordx4 v[110:111], v[98:101], off offset:256 sc1
	v_pk_mul_f32 v[94:95], v[108:109], v[94:95]
	s_waitcnt vmcnt(3)
;     __device__ __forceinline__ void operator()(const f32x4 (&acc)[2][2][4][2], const Unit& u, int wr, int wc, int fr, int fq) const {
;     ...
;         EPB_LOAD(0);
; #pragma unroll
;         for (int kb = 0; kb < 8; ++kb) { const int ai = kb >> 2, m = kb & 3;
;             if (kb < 7) EPB_LOAD(kb + 1);
;             { const int row = row0 + ai * HALF + m * 16; float rmx = 0.f;
; #pragma unroll
;                 for (int bj = 0; bj < 2; ++bj) { const int col = col0 + bj * HALF; f32x4 v0 = acc[ai][bj][m][0], v1 = acc[ai][bj][m][1];
;                     if (QI8) { const f32x4 c0 = cb[bj][0] * ra[ai][m], c1 = cb[bj][1] * ra[ai][m]; const i32x4 i0 = __builtin_bit_cast(i32x4, v0), i1 = __builtin_bit_cast(i32x4, v1);
;                         v0 = (f32x4){(float)i0[0], (float)i0[1], (float)i0[2], (float)i0[3]} * c0; v1 = (f32x4){(float)i1[0], (float)i1[1], (float)i1[2], (float)i1[3]} * c1; }
;                     else if (MODE == 0) { v0 = v0 * tsc; v1 = v1 * tsc; }
;                     if (!QI8 && MODE == 1) { v0 = v0 * cb[bj][0]; v1 = v1 * cb[bj][1]; }
;                     if (MODE == 2 || MODE == 3) { const u32x4 g = gq[kb & 1][bj];
;                         f32x4 g0 = {sigmoidf_(bflo(g.x)), sigmoidf_(bfhi(g.x)), sigmoidf_(bflo(g.y)), sigmoidf_(bfhi(g.y))};
;                         f32x4 g1 = {sigmoidf_(bflo(g.z)), sigmoidf_(bfhi(g.z)), sigmoidf_(bflo(g.w)), sigmoidf_(bfhi(g.w))};
;                         v0 = v0 * g0; v1 = v1 * g1;
;                         if (MODE == 3) { const u32x4 q = aq[kb & 1][bj];
;                             v0 = v0 + (f32x4){bflo(q.x), bfhi(q.x), bflo(q.y), bfhi(q.y)}; v1 = v1 + (f32x4){bflo(q.z), bfhi(q.z), bflo(q.w), bfhi(q.w)}; } }
;                     if (MODE == 4) { v0 = v0 + rs[kb & 1][bj][0]; v1 = v1 + rs[kb & 1][bj][1]; }
;                     if (MODE == 5) { const u32x4 c = gq[kb & 1][bj], q = aq[kb & 1][bj];
;                         v0 = (f32x4){bflo(c.x) + sigmoidf_(v0[0]) * bflo(q.x), bfhi(c.x) + sigmoidf_(v0[1]) * bfhi(q.x), bflo(c.y) + sigmoidf_(v0[2]) * bflo(q.y), bfhi(c.y) + sigmoidf_(v0[3]) * bfhi(q.y)};
;                         v1 = (f32x4){bflo(c.z) + sigmoidf_(v1[0]) * bflo(q.z), bfhi(c.z) + sigmoidf_(v1[1]) * bfhi(q.z), bflo(c.w) + sigmoidf_(v1[2]) * bflo(q.w), bfhi(c.w) + sigmoidf_(v1[3]) * bfhi(q.w)}; }
	v_lshlrev_b32_e32 v108, 16, v118
	v_mad_i64_i32 v[98:99], s[34:35], v160, s64, v[154:155]
	v_lshl_add_u64 v[98:99], v[98:99], 0, v[146:147]
	global_load_dwordx4 v[102:105], v[98:99], off nt
	s_nop 0
	global_load_dwordx4 v[98:101], v[98:99], off offset:256 nt
	v_mul_f32_e32 v108, 0xbfb8aa3b, v108
	v_pk_mul_f32 v[106:107], v[162:163], v[80:81] op_sel_hi:[0,1]
	v_exp_f32_e32 v108, v108
	v_pk_mul_f32 v[110:111], v[162:163], v[76:77] op_sel_hi:[0,1]
	v_pk_mul_f32 v[112:113], v[162:163], v[74:75] op_sel_hi:[0,1]
	v_pk_mul_f32 v[96:97], v[106:107], v[96:97]
	v_and_b32_e32 v107, 0xffff0000, v118
	v_pk_mul_f32 v[90:91], v[112:113], v[90:91]
	v_pk_mul_f32 v[92:93], v[110:111], v[92:93]
	v_mul_f32_e32 v107, 0xbfb8aa3b, v107
	v_lshlrev_b32_e32 v110, 16, v120
	v_and_b32_e32 v111, 0xffff0000, v120
	v_lshlrev_b32_e32 v112, 16, v121
	v_and_b32_e32 v113, 0xffff0000, v121
	v_exp_f32_e32 v107, v107
	v_mul_f32_e32 v110, 0xbfb8aa3b, v110
	v_mul_f32_e32 v111, 0xbfb8aa3b, v111
	v_mul_f32_e32 v112, 0xbfb8aa3b, v112
	v_mul_f32_e32 v113, 0xbfb8aa3b, v113
	v_add_f32_e32 v106, 1.0, v108
	v_lshlrev_b32_e32 v108, 16, v119
	v_and_b32_e32 v109, 0xffff0000, v119
	v_exp_f32_e32 v110, v110
	v_exp_f32_e32 v111, v111
	v_exp_f32_e32 v112, v112
	v_exp_f32_e32 v113, v113
	v_mul_f32_e32 v108, 0xbfb8aa3b, v108
	v_mul_f32_e32 v109, 0xbfb8aa3b, v109
	v_exp_f32_e32 v108, v108
	v_exp_f32_e32 v109, v109
	v_add_f32_e32 v107, 1.0, v107
	v_rcp_f32_e32 v106, v106
	v_rcp_f32_e32 v107, v107
	v_add_f32_e32 v110, 1.0, v110
	v_add_f32_e32 v111, 1.0, v111
	v_add_f32_e32 v112, 1.0, v112
	v_add_f32_e32 v113, 1.0, v113
	v_rcp_f32_e32 v110, v110
	v_rcp_f32_e32 v112, v112
	v_rcp_f32_e32 v113, v113
	v_rcp_f32_e32 v111, v111
	v_add_f32_e32 v108, 1.0, v108
	v_add_f32_e32 v109, 1.0, v109
	v_rcp_f32_e32 v108, v108
	v_rcp_f32_e32 v109, v109
	v_ashrrev_i32_e32 v123, 31, v122
	v_pk_mul_f32 v[94:95], v[94:95], v[106:107]
	v_pk_mul_f32 v[106:107], v[92:93], v[112:113]
	v_pk_mul_f32 v[92:93], v[90:91], v[110:111]
	v_cvt_pk_bf16_f32 v90, v94, v95
	v_lshlrev_b64 v[94:95], 13, v[122:123]
	v_lshl_add_u64 v[94:95], s[0:1], 0, v[94:95]
	v_pk_mul_f32 v[96:97], v[96:97], v[108:109]
	v_lshl_add_u64 v[94:95], v[94:95], 0, v[146:147]
	v_cvt_pk_bf16_f32 v91, v96, v97
	v_cvt_pk_bf16_f32 v92, v92, v93
	v_cvt_pk_bf16_f32 v93, v106, v107
	global_store_dwordx4 v[94:95], v[90:93], off sc1
	v_pk_mul_f32 v[96:97], v[162:163], v[68:69] op_sel_hi:[0,1]
	v_pk_mul_f32 v[106:107], v[162:163], v[66:67] op_sel_hi:[0,1]
	v_pk_mul_f32 v[92:93], v[162:163], v[70:71] op_sel_hi:[0,1]
	v_pk_mul_f32 v[86:87], v[92:93], v[86:87]
	s_waitcnt vmcnt(5)
	v_lshlrev_b32_e32 v92, 16, v114
	v_mul_f32_e32 v92, 0xbfb8aa3b, v92
	v_exp_f32_e32 v92, v92
	v_pk_mul_f32 v[90:91], v[162:163], v[72:73] op_sel_hi:[0,1]
	v_pk_mul_f32 v[88:89], v[90:91], v[88:89]
	v_pk_mul_f32 v[82:83], v[106:107], v[82:83]
	v_pk_mul_f32 v[84:85], v[96:97], v[84:85]
	v_and_b32_e32 v91, 0xffff0000, v114
	v_lshlrev_b32_e32 v96, 16, v116
	v_and_b32_e32 v97, 0xffff0000, v116
	v_lshlrev_b32_e32 v106, 16, v117
	v_and_b32_e32 v107, 0xffff0000, v117
	v_add_f32_e32 v90, 1.0, v92
	v_mul_f32_e32 v91, 0xbfb8aa3b, v91
	v_lshlrev_b32_e32 v92, 16, v115
	v_and_b32_e32 v93, 0xffff0000, v115
	v_mul_f32_e32 v96, 0xbfb8aa3b, v96
	v_mul_f32_e32 v97, 0xbfb8aa3b, v97
	v_mul_f32_e32 v106, 0xbfb8aa3b, v106
	v_mul_f32_e32 v107, 0xbfb8aa3b, v107
	v_exp_f32_e32 v91, v91
	v_mul_f32_e32 v92, 0xbfb8aa3b, v92
	v_mul_f32_e32 v93, 0xbfb8aa3b, v93
	v_exp_f32_e32 v96, v96
	v_exp_f32_e32 v97, v97
	v_exp_f32_e32 v106, v106
	v_exp_f32_e32 v107, v107
	v_exp_f32_e32 v92, v92
	v_exp_f32_e32 v93, v93
	v_add_f32_e32 v91, 1.0, v91
	v_add_f32_e32 v96, 1.0, v96
	v_add_f32_e32 v97, 1.0, v97
	v_add_f32_e32 v106, 1.0, v106
	v_add_f32_e32 v107, 1.0, v107
	v_rcp_f32_e32 v90, v90
	v_rcp_f32_e32 v91, v91
	v_add_f32_e32 v92, 1.0, v92
	v_add_f32_e32 v93, 1.0, v93
	v_rcp_f32_e32 v96, v96
	v_rcp_f32_e32 v106, v106
	v_rcp_f32_e32 v107, v107
	v_rcp_f32_e32 v97, v97
	v_rcp_f32_e32 v92, v92
	v_rcp_f32_e32 v93, v93
	v_pk_mul_f32 v[86:87], v[86:87], v[90:91]
	v_pk_mul_f32 v[90:91], v[84:85], v[106:107]
	v_pk_mul_f32 v[84:85], v[82:83], v[96:97]
	v_pk_mul_f32 v[88:89], v[88:89], v[92:93]
	v_cvt_pk_bf16_f32 v82, v86, v87
	v_cvt_f32_i32_e32 v61, v61
	v_cvt_pk_bf16_f32 v83, v88, v89
	v_cvt_pk_bf16_f32 v84, v84, v85
	v_cvt_pk_bf16_f32 v85, v90, v91
	v_add_u32_e32 v90, 0x90, v152
	global_store_dwordx4 v[94:95], v[82:85], off offset:256 sc1
	v_pk_mul_f32 v[94:95], v[158:159], v[78:79] op_sel_hi:[0,1]
	v_pk_mul_f32 v[62:63], v[94:95], v[62:63]
	v_mad_i64_i32 v[82:83], s[34:35], v90, s64, v[154:155]
	v_lshl_add_u64 v[82:83], v[82:83], 0, v[146:147]
	global_load_dwordx4 v[86:89], v[82:83], off nt
	s_nop 0
	global_load_dwordx4 v[82:85], v[82:83], off offset:256 nt
	s_waitcnt vmcnt(5)
;     __device__ __forceinline__ void operator()(const f32x4 (&acc)[2][2][4][2], const Unit& u, int wr, int wc, int fr, int fq) const {
;     ...
;         EPB_LOAD(0);
; #pragma unroll
;         for (int kb = 0; kb < 8; ++kb) { const int ai = kb >> 2, m = kb & 3;
;             if (kb < 7) EPB_LOAD(kb + 1);
;             { const int row = row0 + ai * HALF + m * 16; float rmx = 0.f;
; #pragma unroll
;                 for (int bj = 0; bj < 2; ++bj) { const int col = col0 + bj * HALF; f32x4 v0 = acc[ai][bj][m][0], v1 = acc[ai][bj][m][1];
;                     if (QI8) { const f32x4 c0 = cb[bj][0] * ra[ai][m], c1 = cb[bj][1] * ra[ai][m]; const i32x4 i0 = __builtin_bit_cast(i32x4, v0), i1 = __builtin_bit_cast(i32x4, v1);
;                         v0 = (f32x4){(float)i0[0], (float)i0[1], (float)i0[2], (float)i0[3]} * c0; v1 = (f32x4){(float)i1[0], (float)i1[1], (float)i1[2], (float)i1[3]} * c1; }
;                     else if (MODE == 0) { v0 = v0 * tsc; v1 = v1 * tsc; }
;                     if (!QI8 && MODE == 1) { v0 = v0 * cb[bj][0]; v1 = v1 * cb[bj][1]; }
;                     if (MODE == 2 || MODE == 3) { const u32x4 g = gq[kb & 1][bj];
;                         f32x4 g0 = {sigmoidf_(bflo(g.x)), sigmoidf_(bfhi(g.x)), sigmoidf_(bflo(g.y)), sigmoidf_(bfhi(g.y))};
;                         f32x4 g1 = {sigmoidf_(bflo(g.z)), sigmoidf_(bfhi(g.z)), sigmoidf_(bflo(g.w)), sigmoidf_(bfhi(g.w))};
;                         v0 = v0 * g0; v1 = v1 * g1;
;                         if (MODE == 3) { const u32x4 q = aq[kb & 1][bj];
;                             v0 = v0 + (f32x4){bflo(q.x), bfhi(q.x), bflo(q.y), bfhi(q.y)}; v1 = v1 + (f32x4){bflo(q.z), bfhi(q.z), bflo(q.w), bfhi(q.w)}; } }
;                     if (MODE == 4) { v0 = v0 + rs[kb & 1][bj][0]; v1 = v1 + rs[kb & 1][bj][1]; }
;                     if (MODE == 5) { const u32x4 c = gq[kb & 1][bj], q = aq[kb & 1][bj];
;                         v0 = (f32x4){bflo(c.x) + sigmoidf_(v0[0]) * bflo(q.x), bfhi(c.x) + sigmoidf_(v0[1]) * bfhi(q.x), bflo(c.y) + sigmoidf_(v0[2]) * bflo(q.y), bfhi(c.y) + sigmoidf_(v0[3]) * bfhi(q.y)};
;                         v1 = (f32x4){bflo(c.z) + sigmoidf_(v1[0]) * bflo(q.z), bfhi(c.z) + sigmoidf_(v1[1]) * bfhi(q.z), bflo(c.w) + sigmoidf_(v1[2]) * bflo(q.w), bfhi(c.w) + sigmoidf_(v1[3]) * bfhi(q.w)}; }
	v_lshlrev_b32_e32 v94, 16, v102
	v_mul_f32_e32 v94, 0xbfb8aa3b, v94
	v_cvt_f32_i32_e32 v60, v60
	v_exp_f32_e32 v94, v94
	v_pk_mul_f32 v[92:93], v[158:159], v[80:81] op_sel_hi:[0,1]
	v_pk_mul_f32 v[96:97], v[158:159], v[76:77] op_sel_hi:[0,1]
	v_pk_mul_f32 v[64:65], v[92:93], v[64:65]
	v_and_b32_e32 v93, 0xffff0000, v102
	v_pk_mul_f32 v[60:61], v[96:97], v[60:61]
	v_add_f32_e32 v92, 1.0, v94
	v_mul_f32_e32 v93, 0xbfb8aa3b, v93
	v_lshlrev_b32_e32 v94, 16, v103
	v_and_b32_e32 v95, 0xffff0000, v103
	v_lshlrev_b32_e32 v96, 16, v104
	v_and_b32_e32 v97, 0xffff0000, v104
	v_lshlrev_b32_e32 v102, 16, v105
	v_and_b32_e32 v103, 0xffff0000, v105
	v_exp_f32_e32 v93, v93
	v_mul_f32_e32 v96, 0xbfb8aa3b, v96
	v_mul_f32_e32 v97, 0xbfb8aa3b, v97
	v_mul_f32_e32 v102, 0xbfb8aa3b, v102
	v_mul_f32_e32 v103, 0xbfb8aa3b, v103
	v_exp_f32_e32 v96, v96
	v_exp_f32_e32 v97, v97
	v_exp_f32_e32 v102, v102
	v_exp_f32_e32 v103, v103
	v_mul_f32_e32 v94, 0xbfb8aa3b, v94
	v_mul_f32_e32 v95, 0xbfb8aa3b, v95
	v_exp_f32_e32 v94, v94
	v_exp_f32_e32 v95, v95
	v_add_f32_e32 v93, 1.0, v93
	v_cvt_f32_i32_e32 v59, v59
	v_cvt_f32_i32_e32 v58, v58
	v_rcp_f32_e32 v92, v92
	v_rcp_f32_e32 v93, v93
	v_add_f32_e32 v96, 1.0, v96
	v_add_f32_e32 v97, 1.0, v97
	v_add_f32_e32 v102, 1.0, v102
	v_add_f32_e32 v103, 1.0, v103
	v_rcp_f32_e32 v96, v96
	v_rcp_f32_e32 v102, v102
	v_rcp_f32_e32 v103, v103
	v_rcp_f32_e32 v97, v97
	v_add_f32_e32 v94, 1.0, v94
	v_add_f32_e32 v95, 1.0, v95
	v_pk_mul_f32 v[106:107], v[158:159], v[74:75] op_sel_hi:[0,1]
	v_rcp_f32_e32 v94, v94
	v_rcp_f32_e32 v95, v95
	v_ashrrev_i32_e32 v161, 31, v160
	v_pk_mul_f32 v[58:59], v[106:107], v[58:59]
	v_pk_mul_f32 v[62:63], v[62:63], v[92:93]
	v_pk_mul_f32 v[92:93], v[60:61], v[102:103]
	v_pk_mul_f32 v[60:61], v[58:59], v[96:97]
	v_cvt_pk_bf16_f32 v58, v62, v63
	v_lshlrev_b64 v[62:63], 13, v[160:161]
	v_cvt_f32_i32_e32 v55, v55
	v_cvt_f32_i32_e32 v54, v54
	v_lshl_add_u64 v[62:63], s[0:1], 0, v[62:63]
	v_pk_mul_f32 v[64:65], v[64:65], v[94:95]
	v_lshl_add_u64 v[62:63], v[62:63], 0, v[146:147]
	v_cvt_pk_bf16_f32 v59, v64, v65
	v_cvt_pk_bf16_f32 v60, v60, v61
	v_cvt_pk_bf16_f32 v61, v92, v93
	global_store_dwordx4 v[62:63], v[58:61], off sc1
	v_cvt_f32_i32_e32 v57, v57
	v_cvt_f32_i32_e32 v56, v56
	v_pk_mul_f32 v[60:61], v[158:159], v[70:71] op_sel_hi:[0,1]
	v_pk_mul_f32 v[54:55], v[60:61], v[54:55]
	s_waitcnt vmcnt(5)
	v_lshlrev_b32_e32 v60, 16, v98
	v_cvt_f32_i32_e32 v53, v53
	v_cvt_f32_i32_e32 v52, v52
	v_cvt_f32_i32_e32 v51, v51
	v_cvt_f32_i32_e32 v50, v50
	v_mul_f32_e32 v60, 0xbfb8aa3b, v60
	v_exp_f32_e32 v60, v60
	v_pk_mul_f32 v[58:59], v[158:159], v[72:73] op_sel_hi:[0,1]
	v_pk_mul_f32 v[64:65], v[158:159], v[68:69] op_sel_hi:[0,1]
	v_pk_mul_f32 v[92:93], v[158:159], v[66:67] op_sel_hi:[0,1]
	v_pk_mul_f32 v[56:57], v[58:59], v[56:57]
	v_pk_mul_f32 v[50:51], v[92:93], v[50:51]
	v_pk_mul_f32 v[52:53], v[64:65], v[52:53]
	v_and_b32_e32 v59, 0xffff0000, v98
	v_lshlrev_b32_e32 v64, 16, v100
	v_and_b32_e32 v65, 0xffff0000, v100
	v_lshlrev_b32_e32 v92, 16, v101
	v_and_b32_e32 v93, 0xffff0000, v101
	v_add_f32_e32 v58, 1.0, v60
	v_mul_f32_e32 v59, 0xbfb8aa3b, v59
	v_lshlrev_b32_e32 v60, 16, v99
	v_and_b32_e32 v61, 0xffff0000, v99
	v_mul_f32_e32 v64, 0xbfb8aa3b, v64
	v_mul_f32_e32 v65, 0xbfb8aa3b, v65
	v_mul_f32_e32 v92, 0xbfb8aa3b, v92
	v_mul_f32_e32 v93, 0xbfb8aa3b, v93
	v_exp_f32_e32 v59, v59
	v_mul_f32_e32 v60, 0xbfb8aa3b, v60
	v_mul_f32_e32 v61, 0xbfb8aa3b, v61
	v_exp_f32_e32 v64, v64
	v_exp_f32_e32 v65, v65
	v_exp_f32_e32 v92, v92
	v_exp_f32_e32 v93, v93
	v_exp_f32_e32 v60, v60
	v_exp_f32_e32 v61, v61
	v_add_f32_e32 v59, 1.0, v59
	v_add_f32_e32 v64, 1.0, v64
	v_add_f32_e32 v65, 1.0, v65
	v_add_f32_e32 v92, 1.0, v92
	v_add_f32_e32 v93, 1.0, v93
	v_rcp_f32_e32 v58, v58
	v_rcp_f32_e32 v59, v59
	v_add_f32_e32 v60, 1.0, v60
	v_add_f32_e32 v61, 1.0, v61
	v_rcp_f32_e32 v64, v64
	v_rcp_f32_e32 v92, v92
	v_rcp_f32_e32 v93, v93
	v_rcp_f32_e32 v65, v65
	v_rcp_f32_e32 v60, v60
	v_rcp_f32_e32 v61, v61
	v_cvt_f32_i32_e32 v47, v47
	v_cvt_f32_i32_e32 v46, v46
	v_pk_mul_f32 v[54:55], v[54:55], v[58:59]
	v_pk_mul_f32 v[58:59], v[52:53], v[92:93]
	v_pk_mul_f32 v[52:53], v[50:51], v[64:65]
	v_pk_mul_f32 v[56:57], v[56:57], v[60:61]
	v_cvt_pk_bf16_f32 v50, v54, v55
	v_cvt_f32_i32_e32 v49, v49
	v_cvt_pk_bf16_f32 v51, v56, v57
	v_cvt_pk_bf16_f32 v52, v52, v53
	v_cvt_pk_bf16_f32 v53, v58, v59
	v_add_u32_e32 v58, 0xa0, v152
	global_store_dwordx4 v[62:63], v[50:53], off offset:256 sc1
	v_pk_mul_f32 v[62:63], v[156:157], v[78:79] op_sel_hi:[0,1]
	v_pk_mul_f32 v[46:47], v[62:63], v[46:47]
	v_mad_i64_i32 v[50:51], s[34:35], v58, s64, v[154:155]
	v_lshl_add_u64 v[50:51], v[50:51], 0, v[146:147]
	s_waitcnt vmcnt(3)
;     __device__ __forceinline__ void operator()(const f32x4 (&acc)[2][2][4][2], const Unit& u, int wr, int wc, int fr, int fq) const {
;     ...
;         EPB_LOAD(0);
; #pragma unroll
;         for (int kb = 0; kb < 8; ++kb) { const int ai = kb >> 2, m = kb & 3;
;             if (kb < 7) EPB_LOAD(kb + 1);
;             { const int row = row0 + ai * HALF + m * 16; float rmx = 0.f;
; #pragma unroll
;                 for (int bj = 0; bj < 2; ++bj) { const int col = col0 + bj * HALF; f32x4 v0 = acc[ai][bj][m][0], v1 = acc[ai][bj][m][1];
;                     if (QI8) { const f32x4 c0 = cb[bj][0] * ra[ai][m], c1 = cb[bj][1] * ra[ai][m]; const i32x4 i0 = __builtin_bit_cast(i32x4, v0), i1 = __builtin_bit_cast(i32x4, v1);
;                         v0 = (f32x4){(float)i0[0], (float)i0[1], (float)i0[2], (float)i0[3]} * c0; v1 = (f32x4){(float)i1[0], (float)i1[1], (float)i1[2], (float)i1[3]} * c1; }
;                     else if (MODE == 0) { v0 = v0 * tsc; v1 = v1 * tsc; }
;                     if (!QI8 && MODE == 1) { v0 = v0 * cb[bj][0]; v1 = v1 * cb[bj][1]; }
;                     if (MODE == 2 || MODE == 3) { const u32x4 g = gq[kb & 1][bj];
;                         f32x4 g0 = {sigmoidf_(bflo(g.x)), sigmoidf_(bfhi(g.x)), sigmoidf_(bflo(g.y)), sigmoidf_(bfhi(g.y))};
;                         f32x4 g1 = {sigmoidf_(bflo(g.z)), sigmoidf_(bfhi(g.z)), sigmoidf_(bflo(g.w)), sigmoidf_(bfhi(g.w))};
;                         v0 = v0 * g0; v1 = v1 * g1;
;                         if (MODE == 3) { const u32x4 q = aq[kb & 1][bj];
;                             v0 = v0 + (f32x4){bflo(q.x), bfhi(q.x), bflo(q.y), bfhi(q.y)}; v1 = v1 + (f32x4){bflo(q.z), bfhi(q.z), bflo(q.w), bfhi(q.w)}; } }
;                     if (MODE == 4) { v0 = v0 + rs[kb & 1][bj][0]; v1 = v1 + rs[kb & 1][bj][1]; }
;                     if (MODE == 5) { const u32x4 c = gq[kb & 1][bj], q = aq[kb & 1][bj];
;                         v0 = (f32x4){bflo(c.x) + sigmoidf_(v0[0]) * bflo(q.x), bfhi(c.x) + sigmoidf_(v0[1]) * bfhi(q.x), bflo(c.y) + sigmoidf_(v0[2]) * bflo(q.y), bfhi(c.y) + sigmoidf_(v0[3]) * bfhi(q.y)};
;                         v1 = (f32x4){bflo(c.z) + sigmoidf_(v1[0]) * bflo(q.z), bfhi(c.z) + sigmoidf_(v1[1]) * bfhi(q.z), bflo(c.w) + sigmoidf_(v1[2]) * bflo(q.w), bfhi(c.w) + sigmoidf_(v1[3]) * bfhi(q.w)}; }
	v_lshlrev_b32_e32 v62, 16, v86
	global_load_dwordx4 v[54:57], v[50:51], off nt
	s_nop 0
	global_load_dwordx4 v[50:53], v[50:51], off offset:256 nt
	v_cvt_f32_i32_e32 v48, v48
	v_mul_f32_e32 v62, 0xbfb8aa3b, v62
	v_cvt_f32_i32_e32 v45, v45
	v_cvt_f32_i32_e32 v44, v44
	v_exp_f32_e32 v62, v62
	v_pk_mul_f32 v[60:61], v[156:157], v[80:81] op_sel_hi:[0,1]
	v_pk_mul_f32 v[64:65], v[156:157], v[76:77] op_sel_hi:[0,1]
	v_pk_mul_f32 v[48:49], v[60:61], v[48:49]
	v_and_b32_e32 v61, 0xffff0000, v86
	v_pk_mul_f32 v[44:45], v[64:65], v[44:45]
	v_add_f32_e32 v60, 1.0, v62
	v_mul_f32_e32 v61, 0xbfb8aa3b, v61
	v_lshlrev_b32_e32 v62, 16, v87
	v_and_b32_e32 v63, 0xffff0000, v87
	v_lshlrev_b32_e32 v64, 16, v88
	v_and_b32_e32 v65, 0xffff0000, v88
	v_lshlrev_b32_e32 v86, 16, v89
	v_and_b32_e32 v87, 0xffff0000, v89
	v_exp_f32_e32 v61, v61
	v_mul_f32_e32 v64, 0xbfb8aa3b, v64
	v_mul_f32_e32 v65, 0xbfb8aa3b, v65
	v_mul_f32_e32 v86, 0xbfb8aa3b, v86
	v_mul_f32_e32 v87, 0xbfb8aa3b, v87
	v_exp_f32_e32 v64, v64
	v_exp_f32_e32 v65, v65
	v_exp_f32_e32 v86, v86
	v_exp_f32_e32 v87, v87
	v_mul_f32_e32 v62, 0xbfb8aa3b, v62
	v_mul_f32_e32 v63, 0xbfb8aa3b, v63
	v_exp_f32_e32 v62, v62
	v_exp_f32_e32 v63, v63
	v_add_f32_e32 v61, 1.0, v61
	v_cvt_f32_i32_e32 v43, v43
	v_cvt_f32_i32_e32 v42, v42
	v_rcp_f32_e32 v60, v60
	v_rcp_f32_e32 v61, v61
	v_add_f32_e32 v64, 1.0, v64
	v_add_f32_e32 v65, 1.0, v65
	v_add_f32_e32 v86, 1.0, v86
	v_add_f32_e32 v87, 1.0, v87
	v_rcp_f32_e32 v64, v64
	v_rcp_f32_e32 v86, v86
	v_rcp_f32_e32 v87, v87
	v_rcp_f32_e32 v65, v65
	v_add_f32_e32 v62, 1.0, v62
	v_add_f32_e32 v63, 1.0, v63
	v_pk_mul_f32 v[92:93], v[156:157], v[74:75] op_sel_hi:[0,1]
	v_rcp_f32_e32 v62, v62
	v_rcp_f32_e32 v63, v63
	v_ashrrev_i32_e32 v91, 31, v90
	v_pk_mul_f32 v[42:43], v[92:93], v[42:43]
	v_pk_mul_f32 v[46:47], v[46:47], v[60:61]
	v_pk_mul_f32 v[60:61], v[44:45], v[86:87]
	v_pk_mul_f32 v[44:45], v[42:43], v[64:65]
	v_cvt_pk_bf16_f32 v42, v46, v47
	v_lshlrev_b64 v[46:47], 13, v[90:91]
	v_cvt_f32_i32_e32 v39, v39
	v_cvt_f32_i32_e32 v38, v38
	v_lshl_add_u64 v[46:47], s[0:1], 0, v[46:47]
	v_pk_mul_f32 v[48:49], v[48:49], v[62:63]
	v_lshl_add_u64 v[46:47], v[46:47], 0, v[146:147]
	v_cvt_pk_bf16_f32 v43, v48, v49
	v_cvt_pk_bf16_f32 v44, v44, v45
	v_cvt_pk_bf16_f32 v45, v60, v61
	global_store_dwordx4 v[46:47], v[42:45], off sc1
	v_cvt_f32_i32_e32 v41, v41
	v_cvt_f32_i32_e32 v40, v40
	v_pk_mul_f32 v[44:45], v[156:157], v[70:71] op_sel_hi:[0,1]
	v_pk_mul_f32 v[38:39], v[44:45], v[38:39]
	s_waitcnt vmcnt(5)
	v_lshlrev_b32_e32 v44, 16, v82
	v_cvt_f32_i32_e32 v37, v37
	v_cvt_f32_i32_e32 v36, v36
	v_cvt_f32_i32_e32 v35, v35
	v_cvt_f32_i32_e32 v34, v34
	v_mul_f32_e32 v44, 0xbfb8aa3b, v44
	v_exp_f32_e32 v44, v44
	v_pk_mul_f32 v[42:43], v[156:157], v[72:73] op_sel_hi:[0,1]
	v_pk_mul_f32 v[48:49], v[156:157], v[68:69] op_sel_hi:[0,1]
	v_pk_mul_f32 v[60:61], v[156:157], v[66:67] op_sel_hi:[0,1]
	v_pk_mul_f32 v[40:41], v[42:43], v[40:41]
	v_pk_mul_f32 v[34:35], v[60:61], v[34:35]
	v_pk_mul_f32 v[36:37], v[48:49], v[36:37]
	v_and_b32_e32 v43, 0xffff0000, v82
	v_lshlrev_b32_e32 v48, 16, v84
	v_and_b32_e32 v49, 0xffff0000, v84
	v_lshlrev_b32_e32 v60, 16, v85
	v_and_b32_e32 v61, 0xffff0000, v85
	v_add_f32_e32 v42, 1.0, v44
	v_mul_f32_e32 v43, 0xbfb8aa3b, v43
	v_lshlrev_b32_e32 v44, 16, v83
	v_and_b32_e32 v45, 0xffff0000, v83
	v_mul_f32_e32 v48, 0xbfb8aa3b, v48
	v_mul_f32_e32 v49, 0xbfb8aa3b, v49
	v_mul_f32_e32 v60, 0xbfb8aa3b, v60
	v_mul_f32_e32 v61, 0xbfb8aa3b, v61
	v_exp_f32_e32 v43, v43
	v_mul_f32_e32 v44, 0xbfb8aa3b, v44
	v_mul_f32_e32 v45, 0xbfb8aa3b, v45
	v_exp_f32_e32 v48, v48
	v_exp_f32_e32 v49, v49
	v_exp_f32_e32 v60, v60
	v_exp_f32_e32 v61, v61
	v_exp_f32_e32 v44, v44
	v_exp_f32_e32 v45, v45
	v_add_f32_e32 v43, 1.0, v43
	v_add_f32_e32 v48, 1.0, v48
	v_add_f32_e32 v49, 1.0, v49
	v_add_f32_e32 v60, 1.0, v60
	v_add_f32_e32 v61, 1.0, v61
	v_rcp_f32_e32 v42, v42
	v_rcp_f32_e32 v43, v43
	v_add_f32_e32 v44, 1.0, v44
	v_add_f32_e32 v45, 1.0, v45
	v_rcp_f32_e32 v48, v48
	v_rcp_f32_e32 v60, v60
	v_rcp_f32_e32 v61, v61
	v_rcp_f32_e32 v49, v49
	v_rcp_f32_e32 v44, v44
	v_rcp_f32_e32 v45, v45
	v_pk_mul_f32 v[38:39], v[38:39], v[42:43]
	v_pk_mul_f32 v[42:43], v[36:37], v[60:61]
	v_pk_mul_f32 v[36:37], v[34:35], v[48:49]
	v_pk_mul_f32 v[40:41], v[40:41], v[44:45]
	v_cvt_pk_bf16_f32 v34, v38, v39
	v_cvt_f32_i32_e32 v31, v31
	v_cvt_pk_bf16_f32 v35, v40, v41
	v_cvt_pk_bf16_f32 v36, v36, v37
	v_cvt_pk_bf16_f32 v37, v42, v43
	v_add_u32_e32 v42, 0xb0, v152
	global_store_dwordx4 v[46:47], v[34:37], off offset:256 sc1
	v_cvt_f32_i32_e32 v30, v30
	v_pk_mul_f32 v[46:47], v[150:151], v[78:79] op_sel_hi:[0,1]
	v_mad_i64_i32 v[34:35], s[34:35], v42, s64, v[154:155]
	v_lshl_add_u64 v[34:35], v[34:35], 0, v[146:147]
	global_load_dwordx4 v[38:41], v[34:35], off nt
	s_nop 0
	global_load_dwordx4 v[34:37], v[34:35], off offset:256 nt
	v_pk_mul_f32 v[30:31], v[46:47], v[30:31]
	s_waitcnt vmcnt(5)
;     __device__ __forceinline__ void operator()(const f32x4 (&acc)[2][2][4][2], const Unit& u, int wr, int wc, int fr, int fq) const {
;     ...
;         EPB_LOAD(0);
; #pragma unroll
;         for (int kb = 0; kb < 8; ++kb) { const int ai = kb >> 2, m = kb & 3;
;             if (kb < 7) EPB_LOAD(kb + 1);
;             { const int row = row0 + ai * HALF + m * 16; float rmx = 0.f;
; #pragma unroll
;                 for (int bj = 0; bj < 2; ++bj) { const int col = col0 + bj * HALF; f32x4 v0 = acc[ai][bj][m][0], v1 = acc[ai][bj][m][1];
;                     if (QI8) { const f32x4 c0 = cb[bj][0] * ra[ai][m], c1 = cb[bj][1] * ra[ai][m]; const i32x4 i0 = __builtin_bit_cast(i32x4, v0), i1 = __builtin_bit_cast(i32x4, v1);
;                         v0 = (f32x4){(float)i0[0], (float)i0[1], (float)i0[2], (float)i0[3]} * c0; v1 = (f32x4){(float)i1[0], (float)i1[1], (float)i1[2], (float)i1[3]} * c1; }
;                     else if (MODE == 0) { v0 = v0 * tsc; v1 = v1 * tsc; }
;                     if (!QI8 && MODE == 1) { v0 = v0 * cb[bj][0]; v1 = v1 * cb[bj][1]; }
;                     if (MODE == 2 || MODE == 3) { const u32x4 g = gq[kb & 1][bj];
;                         f32x4 g0 = {sigmoidf_(bflo(g.x)), sigmoidf_(bfhi(g.x)), sigmoidf_(bflo(g.y)), sigmoidf_(bfhi(g.y))};
;                         f32x4 g1 = {sigmoidf_(bflo(g.z)), sigmoidf_(bfhi(g.z)), sigmoidf_(bflo(g.w)), sigmoidf_(bfhi(g.w))};
;                         v0 = v0 * g0; v1 = v1 * g1;
;                         if (MODE == 3) { const u32x4 q = aq[kb & 1][bj];
;                             v0 = v0 + (f32x4){bflo(q.x), bfhi(q.x), bflo(q.y), bfhi(q.y)}; v1 = v1 + (f32x4){bflo(q.z), bfhi(q.z), bflo(q.w), bfhi(q.w)}; } }
;                     if (MODE == 4) { v0 = v0 + rs[kb & 1][bj][0]; v1 = v1 + rs[kb & 1][bj][1]; }
;                     if (MODE == 5) { const u32x4 c = gq[kb & 1][bj], q = aq[kb & 1][bj];
;                         v0 = (f32x4){bflo(c.x) + sigmoidf_(v0[0]) * bflo(q.x), bfhi(c.x) + sigmoidf_(v0[1]) * bfhi(q.x), bflo(c.y) + sigmoidf_(v0[2]) * bflo(q.y), bfhi(c.y) + sigmoidf_(v0[3]) * bfhi(q.y)};
;                         v1 = (f32x4){bflo(c.z) + sigmoidf_(v1[0]) * bflo(q.z), bfhi(c.z) + sigmoidf_(v1[1]) * bfhi(q.z), bflo(c.w) + sigmoidf_(v1[2]) * bflo(q.w), bfhi(c.w) + sigmoidf_(v1[3]) * bfhi(q.w)}; }
	v_lshlrev_b32_e32 v46, 16, v54
	v_cvt_f32_i32_e32 v33, v33
	v_cvt_f32_i32_e32 v32, v32
	v_mul_f32_e32 v46, 0xbfb8aa3b, v46
	v_cvt_f32_i32_e32 v29, v29
	v_cvt_f32_i32_e32 v28, v28
	v_exp_f32_e32 v46, v46
	v_pk_mul_f32 v[44:45], v[150:151], v[80:81] op_sel_hi:[0,1]
	v_pk_mul_f32 v[48:49], v[150:151], v[76:77] op_sel_hi:[0,1]
	v_pk_mul_f32 v[32:33], v[44:45], v[32:33]
	v_and_b32_e32 v45, 0xffff0000, v54
	v_pk_mul_f32 v[28:29], v[48:49], v[28:29]
	v_add_f32_e32 v44, 1.0, v46
	v_mul_f32_e32 v45, 0xbfb8aa3b, v45
	v_lshlrev_b32_e32 v46, 16, v55
	v_and_b32_e32 v47, 0xffff0000, v55
	v_lshlrev_b32_e32 v48, 16, v56
	v_and_b32_e32 v49, 0xffff0000, v56
	v_lshlrev_b32_e32 v54, 16, v57
	v_and_b32_e32 v55, 0xffff0000, v57
	v_exp_f32_e32 v45, v45
	v_mul_f32_e32 v48, 0xbfb8aa3b, v48
	v_mul_f32_e32 v49, 0xbfb8aa3b, v49
	v_mul_f32_e32 v54, 0xbfb8aa3b, v54
	v_mul_f32_e32 v55, 0xbfb8aa3b, v55
	v_exp_f32_e32 v48, v48
	v_exp_f32_e32 v49, v49
	v_exp_f32_e32 v54, v54
	v_exp_f32_e32 v55, v55
	v_mul_f32_e32 v46, 0xbfb8aa3b, v46
	v_mul_f32_e32 v47, 0xbfb8aa3b, v47
	v_exp_f32_e32 v46, v46
	v_exp_f32_e32 v47, v47
	v_add_f32_e32 v45, 1.0, v45
	v_cvt_f32_i32_e32 v27, v27
	v_cvt_f32_i32_e32 v26, v26
	v_rcp_f32_e32 v44, v44
	v_rcp_f32_e32 v45, v45
	v_add_f32_e32 v48, 1.0, v48
	v_add_f32_e32 v49, 1.0, v49
	v_add_f32_e32 v54, 1.0, v54
	v_add_f32_e32 v55, 1.0, v55
	v_rcp_f32_e32 v48, v48
	v_rcp_f32_e32 v54, v54
	v_rcp_f32_e32 v55, v55
	v_rcp_f32_e32 v49, v49
	v_add_f32_e32 v46, 1.0, v46
	v_add_f32_e32 v47, 1.0, v47
	v_pk_mul_f32 v[60:61], v[150:151], v[74:75] op_sel_hi:[0,1]
	v_rcp_f32_e32 v46, v46
	v_rcp_f32_e32 v47, v47
	v_ashrrev_i32_e32 v59, 31, v58
	v_pk_mul_f32 v[26:27], v[60:61], v[26:27]
	v_pk_mul_f32 v[30:31], v[30:31], v[44:45]
	v_pk_mul_f32 v[44:45], v[28:29], v[54:55]
	v_pk_mul_f32 v[28:29], v[26:27], v[48:49]
	v_cvt_pk_bf16_f32 v26, v30, v31
	v_lshlrev_b64 v[30:31], 13, v[58:59]
	v_cvt_f32_i32_e32 v23, v23
	v_cvt_f32_i32_e32 v22, v22
	v_lshl_add_u64 v[30:31], s[0:1], 0, v[30:31]
	v_pk_mul_f32 v[32:33], v[32:33], v[46:47]
	v_lshl_add_u64 v[30:31], v[30:31], 0, v[146:147]
	v_cvt_pk_bf16_f32 v27, v32, v33
	v_cvt_pk_bf16_f32 v28, v28, v29
	v_cvt_pk_bf16_f32 v29, v44, v45
	global_store_dwordx4 v[30:31], v[26:29], off sc1
	v_cvt_f32_i32_e32 v25, v25
	v_cvt_f32_i32_e32 v24, v24
	v_pk_mul_f32 v[28:29], v[150:151], v[70:71] op_sel_hi:[0,1]
	v_pk_mul_f32 v[22:23], v[28:29], v[22:23]
	s_waitcnt vmcnt(5)
	v_lshlrev_b32_e32 v28, 16, v50
	v_cvt_f32_i32_e32 v21, v21
	v_cvt_f32_i32_e32 v20, v20
	v_cvt_f32_i32_e32 v19, v19
	v_cvt_f32_i32_e32 v18, v18
	v_mul_f32_e32 v28, 0xbfb8aa3b, v28
	v_exp_f32_e32 v28, v28
	v_pk_mul_f32 v[26:27], v[150:151], v[72:73] op_sel_hi:[0,1]
	v_pk_mul_f32 v[32:33], v[150:151], v[68:69] op_sel_hi:[0,1]
	v_pk_mul_f32 v[44:45], v[150:151], v[66:67] op_sel_hi:[0,1]
	v_pk_mul_f32 v[24:25], v[26:27], v[24:25]
	v_pk_mul_f32 v[18:19], v[44:45], v[18:19]
	v_pk_mul_f32 v[20:21], v[32:33], v[20:21]
	v_and_b32_e32 v27, 0xffff0000, v50
	v_lshlrev_b32_e32 v32, 16, v52
	v_and_b32_e32 v33, 0xffff0000, v52
	v_lshlrev_b32_e32 v44, 16, v53
	v_and_b32_e32 v45, 0xffff0000, v53
	v_add_f32_e32 v26, 1.0, v28
	v_mul_f32_e32 v27, 0xbfb8aa3b, v27
	v_lshlrev_b32_e32 v28, 16, v51
	v_and_b32_e32 v29, 0xffff0000, v51
	v_mul_f32_e32 v32, 0xbfb8aa3b, v32
	v_mul_f32_e32 v33, 0xbfb8aa3b, v33
	v_mul_f32_e32 v44, 0xbfb8aa3b, v44
	v_mul_f32_e32 v45, 0xbfb8aa3b, v45
	v_exp_f32_e32 v27, v27
	v_mul_f32_e32 v28, 0xbfb8aa3b, v28
	v_mul_f32_e32 v29, 0xbfb8aa3b, v29
	v_exp_f32_e32 v32, v32
	v_exp_f32_e32 v33, v33
	v_exp_f32_e32 v44, v44
	v_exp_f32_e32 v45, v45
	v_exp_f32_e32 v28, v28
	v_exp_f32_e32 v29, v29
	v_add_f32_e32 v27, 1.0, v27
	v_add_f32_e32 v32, 1.0, v32
	v_add_f32_e32 v33, 1.0, v33
	v_add_f32_e32 v44, 1.0, v44
	v_add_f32_e32 v45, 1.0, v45
	v_rcp_f32_e32 v26, v26
	v_rcp_f32_e32 v27, v27
	v_add_f32_e32 v28, 1.0, v28
	v_add_f32_e32 v29, 1.0, v29
	v_rcp_f32_e32 v32, v32
	v_rcp_f32_e32 v44, v44
	v_rcp_f32_e32 v45, v45
	v_rcp_f32_e32 v33, v33
	v_rcp_f32_e32 v28, v28
	v_rcp_f32_e32 v29, v29
	v_cvt_f32_i32_e32 v15, v15
	v_cvt_f32_i32_e32 v14, v14
	v_pk_mul_f32 v[22:23], v[22:23], v[26:27]
	v_pk_mul_f32 v[26:27], v[20:21], v[44:45]
	v_pk_mul_f32 v[20:21], v[18:19], v[32:33]
	v_pk_mul_f32 v[24:25], v[24:25], v[28:29]
	v_cvt_pk_bf16_f32 v18, v22, v23
	v_cvt_f32_i32_e32 v17, v17
	v_cvt_pk_bf16_f32 v19, v24, v25
	v_cvt_pk_bf16_f32 v20, v20, v21
	v_cvt_pk_bf16_f32 v21, v26, v27
	global_store_dwordx4 v[30:31], v[18:21], off offset:256 sc1
	v_cvt_f32_i32_e32 v16, v16
	v_cvt_f32_i32_e32 v13, v13
	v_pk_mul_f32 v[20:21], v[78:79], v[148:149] op_sel_hi:[1,0]
	v_cvt_f32_i32_e32 v12, v12
	v_pk_mul_f32 v[14:15], v[20:21], v[14:15]
	v_cvt_f32_i32_e32 v11, v11
	v_cvt_f32_i32_e32 v10, v10
	s_waitcnt vmcnt(3)
;     __device__ __forceinline__ void operator()(const f32x4 (&acc)[2][2][4][2], const Unit& u, int wr, int wc, int fr, int fq) const {
;     ...
;             { const int row = row0 + ai * HALF + m * 16; float rmx = 0.f;
; #pragma unroll
;                 for (int bj = 0; bj < 2; ++bj) { const int col = col0 + bj * HALF; f32x4 v0 = acc[ai][bj][m][0], v1 = acc[ai][bj][m][1];
;                     if (QI8) { const f32x4 c0 = cb[bj][0] * ra[ai][m], c1 = cb[bj][1] * ra[ai][m]; const i32x4 i0 = __builtin_bit_cast(i32x4, v0), i1 = __builtin_bit_cast(i32x4, v1);
;                         v0 = (f32x4){(float)i0[0], (float)i0[1], (float)i0[2], (float)i0[3]} * c0; v1 = (f32x4){(float)i1[0], (float)i1[1], (float)i1[2], (float)i1[3]} * c1; }
;                     else if (MODE == 0) { v0 = v0 * tsc; v1 = v1 * tsc; }
;                     if (!QI8 && MODE == 1) { v0 = v0 * cb[bj][0]; v1 = v1 * cb[bj][1]; }
;                     if (MODE == 2 || MODE == 3) { const u32x4 g = gq[kb & 1][bj];
;                         f32x4 g0 = {sigmoidf_(bflo(g.x)), sigmoidf_(bfhi(g.x)), sigmoidf_(bflo(g.y)), sigmoidf_(bfhi(g.y))};
;                         f32x4 g1 = {sigmoidf_(bflo(g.z)), sigmoidf_(bfhi(g.z)), sigmoidf_(bflo(g.w)), sigmoidf_(bfhi(g.w))};
;                         v0 = v0 * g0; v1 = v1 * g1;
;                         if (MODE == 3) { const u32x4 q = aq[kb & 1][bj];
;                             v0 = v0 + (f32x4){bflo(q.x), bfhi(q.x), bflo(q.y), bfhi(q.y)}; v1 = v1 + (f32x4){bflo(q.z), bfhi(q.z), bflo(q.w), bfhi(q.w)}; } }
;                     if (MODE == 4) { v0 = v0 + rs[kb & 1][bj][0]; v1 = v1 + rs[kb & 1][bj][1]; }
;                     if (MODE == 5) { const u32x4 c = gq[kb & 1][bj], q = aq[kb & 1][bj];
;                         v0 = (f32x4){bflo(c.x) + sigmoidf_(v0[0]) * bflo(q.x), bfhi(c.x) + sigmoidf_(v0[1]) * bfhi(q.x), bflo(c.y) + sigmoidf_(v0[2]) * bflo(q.y), bfhi(c.y) + sigmoidf_(v0[3]) * bfhi(q.y)};
;                         v1 = (f32x4){bflo(c.z) + sigmoidf_(v1[0]) * bflo(q.z), bfhi(c.z) + sigmoidf_(v1[1]) * bfhi(q.z), bflo(c.w) + sigmoidf_(v1[2]) * bflo(q.w), bfhi(c.w) + sigmoidf_(v1[3]) * bfhi(q.w)}; }
;                     u32x4 w; w.x = cvtpk(v0[0], v0[1]); w.y = cvtpk(v0[2], v0[3]); w.z = cvtpk(v1[0], v1[1]); w.w = cvtpk(v1[2], v1[3]);
;                     *(u32x4*)(O + (size_t)row * ldo + col) = w;
	v_lshlrev_b32_e32 v20, 16, v38
	v_mul_f32_e32 v20, 0xbfb8aa3b, v20
	v_pk_mul_f32 v[18:19], v[80:81], v[148:149] op_sel_hi:[1,0]
	v_exp_f32_e32 v20, v20
	v_pk_mul_f32 v[22:23], v[148:149], v[76:77] op_sel_hi:[0,1]
	v_pk_mul_f32 v[24:25], v[148:149], v[74:75] op_sel_hi:[0,1]
	v_pk_mul_f32 v[16:17], v[18:19], v[16:17]
	v_and_b32_e32 v19, 0xffff0000, v38
	v_pk_mul_f32 v[10:11], v[24:25], v[10:11]
	v_pk_mul_f32 v[12:13], v[22:23], v[12:13]
	v_mul_f32_e32 v19, 0xbfb8aa3b, v19
	v_lshlrev_b32_e32 v22, 16, v40
	v_and_b32_e32 v23, 0xffff0000, v40
	v_lshlrev_b32_e32 v24, 16, v41
	v_and_b32_e32 v25, 0xffff0000, v41
	v_exp_f32_e32 v19, v19
	v_mul_f32_e32 v22, 0xbfb8aa3b, v22
	v_mul_f32_e32 v23, 0xbfb8aa3b, v23
	v_mul_f32_e32 v24, 0xbfb8aa3b, v24
	v_mul_f32_e32 v25, 0xbfb8aa3b, v25
	v_add_f32_e32 v18, 1.0, v20
	v_lshlrev_b32_e32 v20, 16, v39
	v_and_b32_e32 v21, 0xffff0000, v39
	v_exp_f32_e32 v22, v22
	v_exp_f32_e32 v23, v23
	v_exp_f32_e32 v24, v24
	v_exp_f32_e32 v25, v25
	v_mul_f32_e32 v20, 0xbfb8aa3b, v20
	v_mul_f32_e32 v21, 0xbfb8aa3b, v21
	v_exp_f32_e32 v20, v20
	v_exp_f32_e32 v21, v21
	v_add_f32_e32 v19, 1.0, v19
	v_rcp_f32_e32 v18, v18
	v_rcp_f32_e32 v19, v19
	v_add_f32_e32 v22, 1.0, v22
	v_add_f32_e32 v23, 1.0, v23
	v_add_f32_e32 v24, 1.0, v24
	v_add_f32_e32 v25, 1.0, v25
	v_rcp_f32_e32 v22, v22
	v_rcp_f32_e32 v24, v24
	v_rcp_f32_e32 v25, v25
	v_rcp_f32_e32 v23, v23
	v_add_f32_e32 v20, 1.0, v20
	v_add_f32_e32 v21, 1.0, v21
	v_rcp_f32_e32 v20, v20
	v_rcp_f32_e32 v21, v21
	v_ashrrev_i32_e32 v43, 31, v42
	v_pk_mul_f32 v[14:15], v[14:15], v[18:19]
	v_pk_mul_f32 v[18:19], v[12:13], v[24:25]
	v_pk_mul_f32 v[12:13], v[10:11], v[22:23]
	v_cvt_pk_bf16_f32 v10, v14, v15
	v_lshlrev_b64 v[14:15], 13, v[42:43]
	v_cvt_f32_i32_e32 v7, v7
	v_cvt_f32_i32_e32 v6, v6
	v_lshl_add_u64 v[14:15], s[0:1], 0, v[14:15]
	v_pk_mul_f32 v[16:17], v[16:17], v[20:21]
	v_lshl_add_u64 v[14:15], v[14:15], 0, v[146:147]
	v_cvt_pk_bf16_f32 v11, v16, v17
	v_cvt_pk_bf16_f32 v12, v12, v13
	v_cvt_pk_bf16_f32 v13, v18, v19
	global_store_dwordx4 v[14:15], v[10:13], off sc1
	v_cvt_f32_i32_e32 v9, v9
	v_cvt_f32_i32_e32 v8, v8
	v_pk_mul_f32 v[12:13], v[148:149], v[70:71] op_sel_hi:[0,1]
	v_pk_mul_f32 v[6:7], v[12:13], v[6:7]
	s_waitcnt vmcnt(3)
	v_lshlrev_b32_e32 v12, 16, v34
	v_cvt_f32_i32_e32 v5, v5
	v_cvt_f32_i32_e32 v4, v4
	v_cvt_f32_i32_e32 v3, v3
	v_cvt_f32_i32_e32 v2, v2
	v_mul_f32_e32 v12, 0xbfb8aa3b, v12
	v_exp_f32_e32 v12, v12
	v_pk_mul_f32 v[10:11], v[148:149], v[72:73] op_sel_hi:[0,1]
	v_pk_mul_f32 v[16:17], v[148:149], v[68:69] op_sel_hi:[0,1]
	v_pk_mul_f32 v[18:19], v[148:149], v[66:67] op_sel_hi:[0,1]
	v_pk_mul_f32 v[8:9], v[10:11], v[8:9]
	v_pk_mul_f32 v[2:3], v[18:19], v[2:3]
	v_pk_mul_f32 v[4:5], v[16:17], v[4:5]
	v_and_b32_e32 v11, 0xffff0000, v34
	v_lshlrev_b32_e32 v16, 16, v36
	v_and_b32_e32 v17, 0xffff0000, v36
	v_lshlrev_b32_e32 v18, 16, v37
	v_and_b32_e32 v19, 0xffff0000, v37
	v_add_f32_e32 v10, 1.0, v12
	v_mul_f32_e32 v11, 0xbfb8aa3b, v11
	v_lshlrev_b32_e32 v12, 16, v35
	v_and_b32_e32 v13, 0xffff0000, v35
	v_mul_f32_e32 v16, 0xbfb8aa3b, v16
	v_mul_f32_e32 v17, 0xbfb8aa3b, v17
	v_mul_f32_e32 v18, 0xbfb8aa3b, v18
	v_mul_f32_e32 v19, 0xbfb8aa3b, v19
	v_exp_f32_e32 v11, v11
	v_mul_f32_e32 v12, 0xbfb8aa3b, v12
	v_mul_f32_e32 v13, 0xbfb8aa3b, v13
	v_exp_f32_e32 v16, v16
	v_exp_f32_e32 v17, v17
	v_exp_f32_e32 v18, v18
	v_exp_f32_e32 v19, v19
	v_exp_f32_e32 v12, v12
	v_exp_f32_e32 v13, v13
	v_add_f32_e32 v11, 1.0, v11
	v_add_f32_e32 v16, 1.0, v16
	v_add_f32_e32 v17, 1.0, v17
	v_add_f32_e32 v18, 1.0, v18
	v_add_f32_e32 v19, 1.0, v19
	v_rcp_f32_e32 v10, v10
	v_rcp_f32_e32 v11, v11
	v_add_f32_e32 v12, 1.0, v12
	v_add_f32_e32 v13, 1.0, v13
	v_rcp_f32_e32 v16, v16
	v_rcp_f32_e32 v18, v18
	v_rcp_f32_e32 v19, v19
	v_rcp_f32_e32 v17, v17
	v_rcp_f32_e32 v12, v12
	v_rcp_f32_e32 v13, v13
	v_pk_mul_f32 v[6:7], v[6:7], v[10:11]
	v_pk_mul_f32 v[10:11], v[4:5], v[18:19]
	v_pk_mul_f32 v[4:5], v[2:3], v[16:17]
	s_andn2_b64 vcc, exec, s[6:7]
	s_mov_b64 s[6:7], -1
	v_pk_mul_f32 v[8:9], v[8:9], v[12:13]
	v_cvt_pk_bf16_f32 v2, v6, v7
	s_nop 0
	v_cvt_pk_bf16_f32 v3, v8, v9
	v_cvt_pk_bf16_f32 v4, v4, v5
	v_cvt_pk_bf16_f32 v5, v10, v11
	global_store_dwordx4 v[14:15], v[2:5], off offset:256 sc1
	s_cbranch_vccnz .LBB0_988
	s_andn2_b64 vcc, exec, s[8:9]
	s_cbranch_vccnz .LBB0_987
	s_barrier
	s_branch .LBB0_987

;     __device__ __forceinline__ void operator()(const f32x4 (&acc)[2][2][4][2], const Unit& u, int wr, int wc, int fr, int fq) const {
;     ...
;         if (QI8) {
; #pragma unroll
;             for (int ai = 0; ai < 2; ++ai)
; #pragma unroll
;                 for (int m = 0; m < 4; ++m) ra[ai][m] = sa[row0 + ai * HALF + m * 16];
; #pragma unroll
;             for (int bj = 0; bj < 2; ++bj) { cb[bj][0] = *(const f32x4*)(sb + col0 + bj * HALF) * tsc; cb[bj][1] = *(const f32x4*)(sb + col0 + bj * HALF + 4) * tsc; } }
;         else if (MODE == 1) {
; #pragma unroll
;             for (int bj = 0; bj < 2; ++bj) { cb[bj][0] = *(const f32x4*)(colscale + col0 + bj * HALF); cb[bj][1] = *(const f32x4*)(colscale + col0 + bj * HALF + 4); } }
;         const bool dual = (MODE == 0) && aux != nullptr && u.pn >= ZC_KV / 256 && u.pn < ZC_KV / 256 + 4;
;         u32x4 gq[2][2], aq[2][2]; f32x4 rs[2][2][2];
;     ...
;         EPB_LOAD(0);
; #pragma unroll
;         for (int kb = 0; kb < 8; ++kb) { const int ai = kb >> 2, m = kb & 3;
;             if (kb < 7) EPB_LOAD(kb + 1);
;             { const int row = row0 + ai * HALF + m * 16; float rmx = 0.f;
; #pragma unroll
;                 for (int bj = 0; bj < 2; ++bj) { const int col = col0 + bj * HALF; f32x4 v0 = acc[ai][bj][m][0], v1 = acc[ai][bj][m][1];
;                     if (QI8) { const f32x4 c0 = cb[bj][0] * ra[ai][m], c1 = cb[bj][1] * ra[ai][m]; const i32x4 i0 = __builtin_bit_cast(i32x4, v0), i1 = __builtin_bit_cast(i32x4, v1);
;                         v0 = (f32x4){(float)i0[0], (float)i0[1], (float)i0[2], (float)i0[3]} * c0; v1 = (f32x4){(float)i1[0], (float)i1[1], (float)i1[2], (float)i1[3]} * c1; }
;                     else if (MODE == 0) { v0 = v0 * tsc; v1 = v1 * tsc; }
;                     if (!QI8 && MODE == 1) { v0 = v0 * cb[bj][0]; v1 = v1 * cb[bj][1]; }
;                     if (MODE == 2 || MODE == 3) { const u32x4 g = gq[kb & 1][bj];
;                         f32x4 g0 = {sigmoidf_(bflo(g.x)), sigmoidf_(bfhi(g.x)), sigmoidf_(bflo(g.y)), sigmoidf_(bfhi(g.y))};
;                         f32x4 g1 = {sigmoidf_(bflo(g.z)), sigmoidf_(bfhi(g.z)), sigmoidf_(bflo(g.w)), sigmoidf_(bfhi(g.w))};
;                         v0 = v0 * g0; v1 = v1 * g1;
;                         if (MODE == 3) { const u32x4 q = aq[kb & 1][bj];
.LBB0_1030:
	v_lshl_or_b32 v162, s34, 8, v224
	v_lshl_add_u32 v176, s36, 8, v1
	v_ashrrev_i32_e32 v163, 31, v162
	v_mov_b64_e32 v[142:143], s[14:15]
	v_ashrrev_i32_e32 v177, 31, v176
	v_mad_i64_i32 v[144:145], s[34:35], v176, s65, v[142:143]
	v_lshlrev_b64 v[166:167], 1, v[162:163]
	v_lshl_add_u64 v[138:139], v[176:177], 2, s[4:5]
	v_lshl_add_u64 v[140:141], v[162:163], 2, s[10:11]
	v_lshl_add_u64 v[144:145], v[144:145], 0, v[166:167]
	global_load_dword v182, v[138:139], off
	global_load_dwordx4 v[66:69], v[140:141], off
	global_load_dwordx4 v[62:65], v[140:141], off offset:16
	global_load_dwordx4 v[158:161], v[144:145], off
	v_lshlrev_b64 v[212:213], 13, v[176:177]
	v_lshl_add_u64 v[146:147], s[0:1], 0, v[212:213]
	v_lshl_add_u64 v[146:147], v[146:147], 0, v[166:167]
	global_load_dwordx4 v[186:189], v[146:147], off
	v_cvt_f32_i32_e32 v215, v57
	v_cvt_f32_i32_e32 v214, v56
	v_cvt_f32_i32_e32 v217, v55
	v_cvt_f32_i32_e32 v216, v54
	v_cvt_f32_i32_e32 v219, v53
	v_cvt_f32_i32_e32 v218, v52
	v_cvt_f32_i32_e32 v221, v51
	v_cvt_f32_i32_e32 v220, v50
	global_load_dword v184, v[138:139], off offset:64
	global_load_dword v178, v[138:139], off offset:128
	global_load_dword v174, v[138:139], off offset:192
	global_load_dword v172, v[138:139], off offset:512
	global_load_dword v170, v[138:139], off offset:576
	global_load_dword v168, v[138:139], off offset:640
	global_load_dword v164, v[138:139], off offset:704
	global_load_dwordx4 v[50:53], v[140:141], off offset:528
	global_load_dwordx4 v[54:57], v[140:141], off offset:512
	global_load_dwordx4 v[190:193], v[144:145], off offset:256
	v_or_b32_e32 v180, 16, v176
	v_mad_i64_i32 v[142:143], s[34:35], v180, s65, v[142:143]
	v_lshl_add_u64 v[140:141], v[142:143], 0, v[166:167]
	global_load_dwordx4 v[154:157], v[140:141], off
	global_load_dwordx4 v[142:145], v[140:141], off offset:256
	global_load_dwordx4 v[150:153], v[146:147], off offset:256
	v_ashrrev_i32_e32 v181, 31, v180
	v_lshlrev_b64 v[138:139], 13, v[180:181]
	v_lshl_add_u64 v[138:139], s[0:1], 0, v[138:139]
	v_lshl_add_u64 v[138:139], v[138:139], 0, v[166:167]
	global_load_dwordx4 v[146:149], v[138:139], off
	s_nop 0
	global_load_dwordx4 v[138:141], v[138:139], off offset:256
	v_cvt_f32_i32_e32 v135, v135
	v_cvt_f32_i32_e32 v134, v134
	v_cvt_f32_i32_e32 v137, v137
	v_cvt_f32_i32_e32 v136, v136
	v_cvt_f32_i32_e32 v131, v131
	v_cvt_f32_i32_e32 v130, v130
	v_cvt_f32_i32_e32 v133, v133
	v_cvt_f32_i32_e32 v132, v132
	s_waitcnt vmcnt(0)
	v_pk_mul_f32 v[222:223], v[182:183], v[68:69] op_sel_hi:[0,1]
	v_pk_mul_f32 v[230:231], v[182:183], v[66:67] op_sel_hi:[0,1]
	v_lshlrev_b32_e32 v165, 16, v158
	v_lshlrev_b32_e32 v169, 16, v159
	v_lshlrev_b32_e32 v171, 16, v160
	v_and_b32_e32 v160, 0xffff0000, v160
	v_lshlrev_b32_e32 v173, 16, v161
	v_and_b32_e32 v161, 0xffff0000, v161
	v_mul_f32_e32 v165, 0xbfb8aa3b, v165
	v_mul_f32_e32 v169, 0xbfb8aa3b, v169
	v_and_b32_e32 v159, 0xffff0000, v159
	v_mul_f32_e32 v160, 0xbfb8aa3b, v160
	v_mul_f32_e32 v175, 0xbfb8aa3b, v161
	v_exp_f32_e32 v161, v165
	v_exp_f32_e32 v165, v169
	v_and_b32_e32 v158, 0xffff0000, v158
	v_mul_f32_e32 v159, 0xbfb8aa3b, v159
	v_exp_f32_e32 v160, v160
	v_mul_f32_e32 v158, 0xbfb8aa3b, v158
	v_mul_f32_e32 v171, 0xbfb8aa3b, v171
	v_exp_f32_e32 v159, v159
	v_exp_f32_e32 v158, v158
	v_exp_f32_e32 v169, v171
	v_mul_f32_e32 v173, 0xbfb8aa3b, v173
	v_add_f32_e32 v165, 1.0, v165
	v_pk_mul_f32 v[232:233], v[182:183], v[64:65] op_sel_hi:[0,1]
	v_pk_mul_f32 v[234:235], v[182:183], v[62:63] op_sel_hi:[0,1]
	v_exp_f32_e32 v171, v173
	v_add_f32_e32 v183, 1.0, v160
	v_rcp_f32_e32 v160, v165
	v_exp_f32_e32 v165, v175
	v_add_f32_e32 v161, 1.0, v161
	v_add_f32_e32 v179, 1.0, v159
	v_add_f32_e32 v173, 1.0, v158
	v_add_f32_e32 v169, 1.0, v169
	v_rcp_f32_e32 v158, v161
	v_rcp_f32_e32 v161, v179
	v_pk_mul_f32 v[214:215], v[222:223], v[214:215]
	v_rcp_f32_e32 v159, v173
	v_rcp_f32_e32 v222, v169
	v_rcp_f32_e32 v223, v183
	v_add_f32_e32 v169, 1.0, v171
	v_add_f32_e32 v165, 1.0, v165
	v_pk_mul_f32 v[216:217], v[230:231], v[216:217]
	v_pk_mul_f32 v[218:219], v[232:233], v[218:219]
	v_rcp_f32_e32 v230, v169
	v_rcp_f32_e32 v231, v165
	v_lshlrev_b32_e32 v232, 16, v186
	v_and_b32_e32 v233, 0xffff0000, v186
	v_lshlrev_b32_e32 v186, 16, v187
	v_and_b32_e32 v187, 0xffff0000, v187
	v_pk_mul_f32 v[220:221], v[234:235], v[220:221]
	v_pk_fma_f32 v[160:161], v[214:215], v[160:161], v[186:187]
	v_lshlrev_b32_e32 v186, 16, v188
	v_and_b32_e32 v187, 0xffff0000, v188
	v_pk_fma_f32 v[158:159], v[216:217], v[158:159], v[232:233]
	v_pk_fma_f32 v[186:187], v[220:221], v[222:223], v[186:187]
	v_lshlrev_b32_e32 v188, 16, v189
	v_and_b32_e32 v189, 0xffff0000, v189
	v_cvt_pk_bf16_f32 v158, v158, v159
	v_cvt_pk_bf16_f32 v159, v160, v161
	v_cvt_pk_bf16_f32 v160, v186, v187
	v_lshl_add_u64 v[186:187], s[12:13], 0, v[212:213]
	v_pk_fma_f32 v[188:189], v[218:219], v[230:231], v[188:189]
	v_lshl_add_u64 v[186:187], v[186:187], 0, v[166:167]
	v_cvt_pk_bf16_f32 v161, v188, v189
	global_store_dwordx4 v[186:187], v[158:161], off sc1
	v_lshlrev_b32_e32 v169, 16, v161
	v_lshlrev_b32_e32 v165, 16, v158
	v_and_b32_e32 v161, 0xffff0000, v161
	v_and_b32_e32 v158, 0xffff0000, v158
	v_max_f32_e64 v161, |v161|, |v161|
	v_max_f32_e64 v169, |v169|, |v169|
	v_max_f32_e64 v158, |v158|, |v158|
	v_max_f32_e64 v165, |v165|, |v165|
	v_max_f32_e32 v161, v169, v161
	v_lshlrev_b32_e32 v169, 16, v192
	v_max_f32_e32 v158, v165, v158
	v_lshlrev_b32_e32 v165, 16, v159
	v_and_b32_e32 v159, 0xffff0000, v159
	v_mul_f32_e32 v169, 0xbfb8aa3b, v169
	v_and_b32_e32 v171, 0xffff0000, v192
	v_max_f32_e64 v159, |v159|, |v159|
	v_max_f32_e64 v165, |v165|, |v165|
	v_exp_f32_e32 v169, v169
;     __device__ __forceinline__ void operator()(const f32x4 (&acc)[2][2][4][2], const Unit& u, int wr, int wc, int fr, int fq) const {
;     ...
;         EPB_LOAD(0);
; #pragma unroll
;         for (int kb = 0; kb < 8; ++kb) { const int ai = kb >> 2, m = kb & 3;
;             if (kb < 7) EPB_LOAD(kb + 1);
;             { const int row = row0 + ai * HALF + m * 16; float rmx = 0.f;
; #pragma unroll
;                 for (int bj = 0; bj < 2; ++bj) { const int col = col0 + bj * HALF; f32x4 v0 = acc[ai][bj][m][0], v1 = acc[ai][bj][m][1];
;                     if (QI8) { const f32x4 c0 = cb[bj][0] * ra[ai][m], c1 = cb[bj][1] * ra[ai][m]; const i32x4 i0 = __builtin_bit_cast(i32x4, v0), i1 = __builtin_bit_cast(i32x4, v1);
;                         v0 = (f32x4){(float)i0[0], (float)i0[1], (float)i0[2], (float)i0[3]} * c0; v1 = (f32x4){(float)i1[0], (float)i1[1], (float)i1[2], (float)i1[3]} * c1; }
;                     else if (MODE == 0) { v0 = v0 * tsc; v1 = v1 * tsc; }
;                     if (!QI8 && MODE == 1) { v0 = v0 * cb[bj][0]; v1 = v1 * cb[bj][1]; }
;                     if (MODE == 2 || MODE == 3) { const u32x4 g = gq[kb & 1][bj];
;                         f32x4 g0 = {sigmoidf_(bflo(g.x)), sigmoidf_(bfhi(g.x)), sigmoidf_(bflo(g.y)), sigmoidf_(bfhi(g.y))};
;                         f32x4 g1 = {sigmoidf_(bflo(g.z)), sigmoidf_(bfhi(g.z)), sigmoidf_(bflo(g.w)), sigmoidf_(bfhi(g.w))};
;                         v0 = v0 * g0; v1 = v1 * g1;
;                         if (MODE == 3) { const u32x4 q = aq[kb & 1][bj];
;                             v0 = v0 + (f32x4){bflo(q.x), bfhi(q.x), bflo(q.y), bfhi(q.y)}; v1 = v1 + (f32x4){bflo(q.z), bfhi(q.z), bflo(q.w), bfhi(q.w)}; } }
;                     if (MODE == 4) { v0 = v0 + rs[kb & 1][bj][0]; v1 = v1 + rs[kb & 1][bj][1]; }
;                     if (MODE == 5) { const u32x4 c = gq[kb & 1][bj], q = aq[kb & 1][bj];
;                         v0 = (f32x4){bflo(c.x) + sigmoidf_(v0[0]) * bflo(q.x), bfhi(c.x) + sigmoidf_(v0[1]) * bfhi(q.x), bflo(c.y) + sigmoidf_(v0[2]) * bflo(q.y), bfhi(c.y) + sigmoidf_(v0[3]) * bfhi(q.y)};
;                         v1 = (f32x4){bflo(c.z) + sigmoidf_(v1[0]) * bflo(q.z), bfhi(c.z) + sigmoidf_(v1[1]) * bfhi(q.z), bflo(c.w) + sigmoidf_(v1[2]) * bflo(q.w), bfhi(c.w) + sigmoidf_(v1[3]) * bfhi(q.w)}; }
	v_mul_f32_e32 v171, 0xbfb8aa3b, v171
	v_max_f32_e32 v159, v165, v159
	v_lshlrev_b32_e32 v165, 16, v160
	v_and_b32_e32 v160, 0xffff0000, v160
	v_exp_f32_e32 v171, v171
	v_max3_f32 v160, |v165|, |v160|, v161
	v_max3_f32 v165, v158, v159, v160
	v_pk_mul_f32 v[160:161], v[182:183], v[54:55] op_sel_hi:[0,1]
	v_pk_mul_f32 v[158:159], v[182:183], v[56:57] op_sel_hi:[0,1]
	v_pk_mul_f32 v[188:189], v[182:183], v[52:53] op_sel_hi:[0,1]
	v_pk_mul_f32 v[182:183], v[182:183], v[50:51] op_sel_hi:[0,1]
	v_pk_mul_f32 v[134:135], v[160:161], v[134:135]
	v_lshlrev_b32_e32 v160, 16, v191
	v_and_b32_e32 v161, 0xffff0000, v191
	v_add_f32_e32 v169, 1.0, v169
	v_pk_mul_f32 v[136:137], v[158:159], v[136:137]
	v_pk_mul_f32 v[130:131], v[182:183], v[130:131]
	v_lshlrev_b32_e32 v158, 16, v190
	v_and_b32_e32 v159, 0xffff0000, v190
	v_mul_f32_e32 v160, 0xbfb8aa3b, v160
	v_mul_f32_e32 v161, 0xbfb8aa3b, v161
	v_rcp_f32_e32 v182, v169
	v_add_f32_e32 v169, 1.0, v171
	v_lshlrev_b32_e32 v171, 16, v193
	v_mul_f32_e32 v158, 0xbfb8aa3b, v158
	v_mul_f32_e32 v159, 0xbfb8aa3b, v159
	v_exp_f32_e32 v160, v160
	v_exp_f32_e32 v161, v161
	v_mul_f32_e32 v171, 0xbfb8aa3b, v171
	v_and_b32_e32 v173, 0xffff0000, v193
	v_exp_f32_e32 v158, v158
	v_exp_f32_e32 v159, v159
	v_exp_f32_e32 v171, v171
	v_mul_f32_e32 v173, 0xbfb8aa3b, v173
	v_exp_f32_e32 v173, v173
	v_add_f32_e32 v160, 1.0, v160
	v_add_f32_e32 v161, 1.0, v161
	v_add_f32_e32 v158, 1.0, v158
	v_add_f32_e32 v159, 1.0, v159
	v_rcp_f32_e32 v160, v160
	v_rcp_f32_e32 v161, v161
	v_rcp_f32_e32 v183, v169
	v_add_f32_e32 v169, 1.0, v171
	v_pk_mul_f32 v[132:133], v[188:189], v[132:133]
	v_rcp_f32_e32 v158, v158
	v_rcp_f32_e32 v159, v159
	v_rcp_f32_e32 v188, v169
	v_add_f32_e32 v169, 1.0, v173
	v_rcp_f32_e32 v189, v169
	v_lshlrev_b32_e32 v190, 16, v150
	v_and_b32_e32 v191, 0xffff0000, v150
	v_lshlrev_b32_e32 v150, 16, v151
	v_and_b32_e32 v151, 0xffff0000, v151
	v_pk_fma_f32 v[136:137], v[136:137], v[160:161], v[150:151]
	v_lshlrev_b32_e32 v150, 16, v152
	v_and_b32_e32 v151, 0xffff0000, v152
	v_pk_fma_f32 v[134:135], v[134:135], v[158:159], v[190:191]
	v_lshlrev_b32_e32 v152, 16, v153
	v_and_b32_e32 v153, 0xffff0000, v153
	v_pk_fma_f32 v[130:131], v[130:131], v[182:183], v[150:151]
	v_pk_fma_f32 v[152:153], v[132:133], v[188:189], v[152:153]
	v_cvt_pk_bf16_f32 v132, v134, v135
	v_cvt_pk_bf16_f32 v133, v136, v137
	v_cvt_pk_bf16_f32 v134, v130, v131
	s_nop 0
	v_lshlrev_b32_e32 v130, 16, v132
	v_and_b32_e32 v131, 0xffff0000, v132
	v_max_f32_e64 v131, |v131|, |v131|
	v_max_f32_e64 v130, |v130|, |v130|
	v_cvt_pk_bf16_f32 v135, v152, v153
	v_max_f32_e32 v130, v130, v131
	v_lshlrev_b32_e32 v131, 16, v133
	v_and_b32_e32 v136, 0xffff0000, v133
	v_lshlrev_b32_e32 v150, 16, v135
	v_and_b32_e32 v151, 0xffff0000, v135
	v_max_f32_e64 v136, |v136|, |v136|
	v_max_f32_e64 v131, |v131|, |v131|
	v_max_f32_e64 v151, |v151|, |v151|
	v_max_f32_e64 v150, |v150|, |v150|
	v_max_f32_e32 v131, v131, v136
	v_lshlrev_b32_e32 v136, 16, v134
	v_and_b32_e32 v137, 0xffff0000, v134
	v_max_f32_e32 v150, v150, v151
	v_max3_f32 v136, |v136|, |v137|, v150
	v_max3_f32 v130, v130, v131, v136
	v_and_b32_e32 v136, 64, v228
	v_xor_b32_e32 v131, 16, v228
	v_add_u32_e32 v136, 64, v136
	v_cmp_lt_i32_e32 vcc, v131, v136
	v_max3_f32 v130, v165, 0, v130
	global_store_dwordx4 v[186:187], v[132:135], off offset:256 sc1
	v_cndmask_b32_e32 v131, v228, v131, vcc
	v_lshlrev_b32_e32 v165, 2, v131
	ds_bpermute_b32 v131, v165, v130
	s_waitcnt lgkmcnt(0)
	v_max_f32_e32 v131, v131, v131
	v_max_f32_e32 v130, v130, v131
	v_xor_b32_e32 v131, 32, v228
	v_cmp_lt_i32_e32 vcc, v131, v136
	s_nop 1
	v_cndmask_b32_e32 v131, v228, v131, vcc
	v_lshlrev_b32_e32 v169, 2, v131
	ds_bpermute_b32 v131, v169, v130
	s_and_saveexec_b64 s[34:35], s[6:7]
	s_cbranch_execz .LBB0_1032
	s_waitcnt lgkmcnt(0)
	v_max_f32_e32 v131, v131, v131
	v_max_f32_e32 v130, v130, v130
	v_lshl_add_u64 v[132:133], v[176:177], 2, s[16:17]
	v_max_f32_e32 v130, v130, v131
	global_atomic_umax v[132:133], v130, off
.LBB0_1032:
	s_or_b64 exec, exec, s[34:35]
	v_or_b32_e32 v182, 32, v176
	v_ashrrev_i32_e32 v183, 31, v182
	s_waitcnt lgkmcnt(0)
	v_mov_b64_e32 v[130:131], s[14:15]
	v_lshlrev_b64 v[132:133], 13, v[182:183]
	v_mad_i64_i32 v[130:131], s[34:35], v182, s65, v[130:131]
	v_lshl_add_u64 v[132:133], s[0:1], 0, v[132:133]
	v_lshl_add_u64 v[130:131], v[130:131], 0, v[166:167]
	v_lshl_add_u64 v[132:133], v[132:133], 0, v[166:167]
	global_load_dwordx4 v[158:161], v[130:131], off
	global_load_dwordx4 v[134:137], v[130:131], off offset:256
	global_load_dwordx4 v[150:153], v[132:133], off
	s_nop 0
	global_load_dwordx4 v[130:133], v[132:133], off offset:256
	v_lshlrev_b32_e32 v171, 16, v154
	v_and_b32_e32 v154, 0xffff0000, v154
	v_mul_f32_e32 v171, 0xbfb8aa3b, v171
	v_mul_f32_e32 v154, 0xbfb8aa3b, v154
	v_exp_f32_e32 v171, v171
	v_exp_f32_e32 v173, v154
	v_cvt_f32_i32_e32 v129, v129
	v_cvt_f32_i32_e32 v128, v128
	v_add_f32_e32 v154, 1.0, v171
	v_add_f32_e32 v171, 1.0, v173
	v_lshlrev_b32_e32 v173, 16, v155
	v_mul_f32_e32 v173, 0xbfb8aa3b, v173
	v_exp_f32_e32 v173, v173
	v_and_b32_e32 v155, 0xffff0000, v155
	v_mul_f32_e32 v155, 0xbfb8aa3b, v155
	v_exp_f32_e32 v175, v155
	v_rcp_f32_e32 v155, v171
	v_add_f32_e32 v171, 1.0, v173
	v_lshlrev_b32_e32 v173, 16, v156
	v_mul_f32_e32 v173, 0xbfb8aa3b, v173
	v_exp_f32_e32 v173, v173
	v_and_b32_e32 v156, 0xffff0000, v156
	v_pk_mul_f32 v[188:189], v[184:185], v[68:69] op_sel_hi:[0,1]
	v_mul_f32_e32 v156, 0xbfb8aa3b, v156
	v_pk_mul_f32 v[128:129], v[188:189], v[128:129]
	v_rcp_f32_e32 v188, v171
	v_add_f32_e32 v171, 1.0, v175
	v_exp_f32_e32 v175, v156
	v_add_f32_e32 v156, 1.0, v173
	v_lshlrev_b32_e32 v173, 16, v157
;     __device__ __forceinline__ void operator()(const f32x4 (&acc)[2][2][4][2], const Unit& u, int wr, int wc, int fr, int fq) const {
;     ...
;             { const int row = row0 + ai * HALF + m * 16; float rmx = 0.f;
; #pragma unroll
;                 for (int bj = 0; bj < 2; ++bj) { const int col = col0 + bj * HALF; f32x4 v0 = acc[ai][bj][m][0], v1 = acc[ai][bj][m][1];
;                     if (QI8) { const f32x4 c0 = cb[bj][0] * ra[ai][m], c1 = cb[bj][1] * ra[ai][m]; const i32x4 i0 = __builtin_bit_cast(i32x4, v0), i1 = __builtin_bit_cast(i32x4, v1);
;                         v0 = (f32x4){(float)i0[0], (float)i0[1], (float)i0[2], (float)i0[3]} * c0; v1 = (f32x4){(float)i1[0], (float)i1[1], (float)i1[2], (float)i1[3]} * c1; }
;                     else if (MODE == 0) { v0 = v0 * tsc; v1 = v1 * tsc; }
;                     if (!QI8 && MODE == 1) { v0 = v0 * cb[bj][0]; v1 = v1 * cb[bj][1]; }
;                     if (MODE == 2 || MODE == 3) { const u32x4 g = gq[kb & 1][bj];
;                         f32x4 g0 = {sigmoidf_(bflo(g.x)), sigmoidf_(bfhi(g.x)), sigmoidf_(bflo(g.y)), sigmoidf_(bfhi(g.y))};
;                         f32x4 g1 = {sigmoidf_(bflo(g.z)), sigmoidf_(bfhi(g.z)), sigmoidf_(bflo(g.w)), sigmoidf_(bfhi(g.w))};
;                         v0 = v0 * g0; v1 = v1 * g1;
;                         if (MODE == 3) { const u32x4 q = aq[kb & 1][bj];
;                             v0 = v0 + (f32x4){bflo(q.x), bfhi(q.x), bflo(q.y), bfhi(q.y)}; v1 = v1 + (f32x4){bflo(q.z), bfhi(q.z), bflo(q.w), bfhi(q.w)}; } }
;                     if (MODE == 4) { v0 = v0 + rs[kb & 1][bj][0]; v1 = v1 + rs[kb & 1][bj][1]; }
;                     if (MODE == 5) { const u32x4 c = gq[kb & 1][bj], q = aq[kb & 1][bj];
;                         v0 = (f32x4){bflo(c.x) + sigmoidf_(v0[0]) * bflo(q.x), bfhi(c.x) + sigmoidf_(v0[1]) * bfhi(q.x), bflo(c.y) + sigmoidf_(v0[2]) * bflo(q.y), bfhi(c.y) + sigmoidf_(v0[3]) * bfhi(q.y)};
;                         v1 = (f32x4){bflo(c.z) + sigmoidf_(v1[0]) * bflo(q.z), bfhi(c.z) + sigmoidf_(v1[1]) * bfhi(q.z), bflo(c.w) + sigmoidf_(v1[2]) * bflo(q.w), bfhi(c.w) + sigmoidf_(v1[3]) * bfhi(q.w)}; }
;                     u32x4 w; w.x = cvtpk(v0[0], v0[1]); w.y = cvtpk(v0[2], v0[3]); w.z = cvtpk(v1[0], v1[1]); w.w = cvtpk(v1[2], v1[3]);
;                     *(u32x4*)(O + (size_t)row * ldo + col) = w;
	v_mul_f32_e32 v173, 0xbfb8aa3b, v173
	v_and_b32_e32 v157, 0xffff0000, v157
	v_exp_f32_e32 v173, v173
	v_mul_f32_e32 v157, 0xbfb8aa3b, v157
	v_cvt_f32_i32_e32 v127, v127
	v_cvt_f32_i32_e32 v126, v126
	v_rcp_f32_e32 v189, v171
	v_add_f32_e32 v171, 1.0, v175
	v_exp_f32_e32 v175, v157
	v_pk_mul_f32 v[190:191], v[184:185], v[66:67] op_sel_hi:[0,1]
	v_cvt_f32_i32_e32 v125, v125
	v_cvt_f32_i32_e32 v124, v124
	v_rcp_f32_e32 v157, v171
	v_add_f32_e32 v171, 1.0, v173
	v_pk_mul_f32 v[126:127], v[190:191], v[126:127]
	v_cvt_f32_i32_e32 v123, v123
	v_cvt_f32_i32_e32 v122, v122
	v_rcp_f32_e32 v154, v154
	v_rcp_f32_e32 v190, v171
	v_add_f32_e32 v171, 1.0, v175
	v_rcp_f32_e32 v156, v156
	v_rcp_f32_e32 v191, v171
	v_pk_mul_f32 v[192:193], v[184:185], v[64:65] op_sel_hi:[0,1]
	v_pk_mul_f32 v[212:213], v[184:185], v[62:63] op_sel_hi:[0,1]
	v_pk_mul_f32 v[124:125], v[192:193], v[124:125]
	v_lshlrev_b32_e32 v192, 16, v146
	v_and_b32_e32 v193, 0xffff0000, v146
	v_lshlrev_b32_e32 v146, 16, v147
	v_and_b32_e32 v147, 0xffff0000, v147
	v_lshlrev_b64 v[186:187], 12, v[180:181]
	v_pk_mul_f32 v[122:123], v[212:213], v[122:123]
	v_pk_fma_f32 v[128:129], v[128:129], v[188:189], v[146:147]
	v_pk_fma_f32 v[126:127], v[126:127], v[154:155], v[192:193]
	v_lshlrev_b32_e32 v146, 16, v148
	v_and_b32_e32 v147, 0xffff0000, v148
	v_lshlrev_b32_e32 v148, 16, v149
	v_and_b32_e32 v149, 0xffff0000, v149
	v_pk_fma_f32 v[148:149], v[124:125], v[190:191], v[148:149]
	v_pk_fma_f32 v[124:125], v[122:123], v[156:157], v[146:147]
	v_cvt_pk_bf16_f32 v122, v126, v127
	v_lshl_add_u64 v[126:127], v[186:187], 1, s[12:13]
	v_lshl_add_u64 v[126:127], v[126:127], 0, v[166:167]
	v_cvt_pk_bf16_f32 v123, v128, v129
	v_cvt_pk_bf16_f32 v124, v124, v125
	v_cvt_pk_bf16_f32 v125, v148, v149
	global_store_dwordx4 v[126:127], v[122:125], off sc1
	v_lshlrev_b32_e32 v128, 16, v122
	v_max_f32_e64 v128, |v128|, |v128|
	v_and_b32_e32 v122, 0xffff0000, v122
	v_max_f32_e64 v122, |v122|, |v122|
	v_max_f32_e32 v122, v128, v122
	v_lshlrev_b32_e32 v128, 16, v123
	v_and_b32_e32 v123, 0xffff0000, v123
	v_lshlrev_b32_e32 v129, 16, v125
	v_and_b32_e32 v125, 0xffff0000, v125
	v_max_f32_e64 v123, |v123|, |v123|
	v_max_f32_e64 v128, |v128|, |v128|
	v_max_f32_e64 v125, |v125|, |v125|
	v_max_f32_e64 v129, |v129|, |v129|
	v_cvt_f32_i32_e32 v121, v121
	v_cvt_f32_i32_e32 v120, v120
	v_max_f32_e32 v123, v128, v123
	v_lshlrev_b32_e32 v128, 16, v124
	v_and_b32_e32 v124, 0xffff0000, v124
	v_max_f32_e32 v125, v129, v125
	v_cvt_f32_i32_e32 v119, v119
	v_cvt_f32_i32_e32 v118, v118
	v_cvt_f32_i32_e32 v117, v117
	v_cvt_f32_i32_e32 v116, v116
	v_max3_f32 v124, |v128|, |v124|, v125
	v_max3_f32 v148, v122, v123, v124
	v_pk_mul_f32 v[122:123], v[184:185], v[56:57] op_sel_hi:[0,1]
	v_pk_mul_f32 v[124:125], v[184:185], v[54:55] op_sel_hi:[0,1]
	v_pk_mul_f32 v[128:129], v[184:185], v[52:53] op_sel_hi:[0,1]
	v_pk_mul_f32 v[120:121], v[122:123], v[120:121]
	v_lshlrev_b32_e32 v122, 16, v142
	v_and_b32_e32 v123, 0xffff0000, v142
	v_pk_mul_f32 v[118:119], v[124:125], v[118:119]
	v_mul_f32_e32 v122, 0xbfb8aa3b, v122
	v_mul_f32_e32 v123, 0xbfb8aa3b, v123
	v_pk_mul_f32 v[116:117], v[128:129], v[116:117]
	v_lshlrev_b32_e32 v124, 16, v143
	v_and_b32_e32 v125, 0xffff0000, v143
	v_lshlrev_b32_e32 v128, 16, v144
	v_and_b32_e32 v129, 0xffff0000, v144
	v_exp_f32_e32 v122, v122
	v_exp_f32_e32 v123, v123
	v_mul_f32_e32 v124, 0xbfb8aa3b, v124
	v_mul_f32_e32 v125, 0xbfb8aa3b, v125
	v_mul_f32_e32 v128, 0xbfb8aa3b, v128
	v_mul_f32_e32 v129, 0xbfb8aa3b, v129
	v_lshlrev_b32_e32 v142, 16, v145
	v_and_b32_e32 v143, 0xffff0000, v145
	v_exp_f32_e32 v124, v124
	v_exp_f32_e32 v125, v125
	v_exp_f32_e32 v128, v128
	v_exp_f32_e32 v129, v129
	v_mul_f32_e32 v142, 0xbfb8aa3b, v142
	v_mul_f32_e32 v143, 0xbfb8aa3b, v143
	v_exp_f32_e32 v142, v142
	v_exp_f32_e32 v143, v143
	v_add_f32_e32 v122, 1.0, v122
	v_add_f32_e32 v123, 1.0, v123
	v_cvt_f32_i32_e32 v115, v115
	v_cvt_f32_i32_e32 v114, v114
	v_rcp_f32_e32 v122, v122
	v_rcp_f32_e32 v123, v123
	v_add_f32_e32 v124, 1.0, v124
	v_add_f32_e32 v125, 1.0, v125
	v_add_f32_e32 v128, 1.0, v128
	v_add_f32_e32 v129, 1.0, v129
	v_rcp_f32_e32 v124, v124
	v_rcp_f32_e32 v125, v125
	v_rcp_f32_e32 v128, v128
	v_rcp_f32_e32 v129, v129
	v_add_f32_e32 v142, 1.0, v142
	v_add_f32_e32 v143, 1.0, v143
	v_rcp_f32_e32 v142, v142
	v_rcp_f32_e32 v143, v143
	v_pk_mul_f32 v[146:147], v[184:185], v[50:51] op_sel_hi:[0,1]
	v_lshlrev_b32_e32 v144, 16, v138
	v_and_b32_e32 v145, 0xffff0000, v138
	v_pk_mul_f32 v[114:115], v[146:147], v[114:115]
	v_lshlrev_b32_e32 v138, 16, v139
	v_and_b32_e32 v139, 0xffff0000, v139
	v_pk_fma_f32 v[118:119], v[118:119], v[122:123], v[144:145]
	v_lshlrev_b32_e32 v122, 16, v140
	v_and_b32_e32 v123, 0xffff0000, v140
	v_pk_fma_f32 v[120:121], v[120:121], v[124:125], v[138:139]
	v_lshlrev_b32_e32 v124, 16, v141
	v_and_b32_e32 v125, 0xffff0000, v141
	v_pk_fma_f32 v[114:115], v[114:115], v[128:129], v[122:123]
	v_pk_fma_f32 v[124:125], v[116:117], v[142:143], v[124:125]
	v_cvt_pk_bf16_f32 v116, v118, v119
	v_cvt_pk_bf16_f32 v117, v120, v121
	v_cvt_pk_bf16_f32 v118, v114, v115
	s_nop 0
	v_lshlrev_b32_e32 v114, 16, v116
	v_and_b32_e32 v115, 0xffff0000, v116
	v_max_f32_e64 v115, |v115|, |v115|
	v_max_f32_e64 v114, |v114|, |v114|
	v_cvt_pk_bf16_f32 v119, v124, v125
	v_max_f32_e32 v114, v114, v115
	v_lshlrev_b32_e32 v115, 16, v117
	v_and_b32_e32 v120, 0xffff0000, v117
	v_lshlrev_b32_e32 v122, 16, v119
	v_and_b32_e32 v123, 0xffff0000, v119
	v_max_f32_e64 v120, |v120|, |v120|
	v_max_f32_e64 v115, |v115|, |v115|
	v_max_f32_e64 v123, |v123|, |v123|
	v_max_f32_e64 v122, |v122|, |v122|
	v_max_f32_e32 v115, v115, v120
	v_lshlrev_b32_e32 v120, 16, v118
	v_and_b32_e32 v121, 0xffff0000, v118
	v_max_f32_e32 v122, v122, v123
	v_max3_f32 v120, |v120|, |v121|, v122
	v_max3_f32 v114, v114, v115, v120
	v_max3_f32 v114, v148, 0, v114
	ds_bpermute_b32 v115, v165, v114
	global_store_dwordx4 v[126:127], v[116:119], off offset:256 sc1
	s_waitcnt lgkmcnt(0)
	v_max_f32_e32 v115, v115, v115
	v_max_f32_e32 v114, v114, v115
	ds_bpermute_b32 v115, v169, v114
	s_and_saveexec_b64 s[34:35], s[6:7]
	s_cbranch_execz .LBB0_1034
	s_waitcnt lgkmcnt(0)
	v_max_f32_e32 v115, v115, v115
	v_max_f32_e32 v114, v114, v114
	v_lshl_add_u64 v[116:117], v[180:181], 2, s[16:17]
	v_max_f32_e32 v114, v114, v115
	global_atomic_umax v[116:117], v114, off
;     __device__ __forceinline__ void operator()(const f32x4 (&acc)[2][2][4][2], const Unit& u, int wr, int wc, int fr, int fq) const {
;     ...
;         EPB_LOAD(0);
; #pragma unroll
;         for (int kb = 0; kb < 8; ++kb) { const int ai = kb >> 2, m = kb & 3;
;             if (kb < 7) EPB_LOAD(kb + 1);
;             { const int row = row0 + ai * HALF + m * 16; float rmx = 0.f;
; #pragma unroll
;                 for (int bj = 0; bj < 2; ++bj) { const int col = col0 + bj * HALF; f32x4 v0 = acc[ai][bj][m][0], v1 = acc[ai][bj][m][1];
;                     if (QI8) { const f32x4 c0 = cb[bj][0] * ra[ai][m], c1 = cb[bj][1] * ra[ai][m]; const i32x4 i0 = __builtin_bit_cast(i32x4, v0), i1 = __builtin_bit_cast(i32x4, v1);
;                         v0 = (f32x4){(float)i0[0], (float)i0[1], (float)i0[2], (float)i0[3]} * c0; v1 = (f32x4){(float)i1[0], (float)i1[1], (float)i1[2], (float)i1[3]} * c1; }
;                     else if (MODE == 0) { v0 = v0 * tsc; v1 = v1 * tsc; }
;                     if (!QI8 && MODE == 1) { v0 = v0 * cb[bj][0]; v1 = v1 * cb[bj][1]; }
;                     if (MODE == 2 || MODE == 3) { const u32x4 g = gq[kb & 1][bj];
;                         f32x4 g0 = {sigmoidf_(bflo(g.x)), sigmoidf_(bfhi(g.x)), sigmoidf_(bflo(g.y)), sigmoidf_(bfhi(g.y))};
;                         f32x4 g1 = {sigmoidf_(bflo(g.z)), sigmoidf_(bfhi(g.z)), sigmoidf_(bflo(g.w)), sigmoidf_(bfhi(g.w))};
;                         v0 = v0 * g0; v1 = v1 * g1;
;                         if (MODE == 3) { const u32x4 q = aq[kb & 1][bj];
;                             v0 = v0 + (f32x4){bflo(q.x), bfhi(q.x), bflo(q.y), bfhi(q.y)}; v1 = v1 + (f32x4){bflo(q.z), bfhi(q.z), bflo(q.w), bfhi(q.w)}; } }
;                     if (MODE == 4) { v0 = v0 + rs[kb & 1][bj][0]; v1 = v1 + rs[kb & 1][bj][1]; }
;                     if (MODE == 5) { const u32x4 c = gq[kb & 1][bj], q = aq[kb & 1][bj];
;                         v0 = (f32x4){bflo(c.x) + sigmoidf_(v0[0]) * bflo(q.x), bfhi(c.x) + sigmoidf_(v0[1]) * bfhi(q.x), bflo(c.y) + sigmoidf_(v0[2]) * bflo(q.y), bfhi(c.y) + sigmoidf_(v0[3]) * bfhi(q.y)};
;                         v1 = (f32x4){bflo(c.z) + sigmoidf_(v1[0]) * bflo(q.z), bfhi(c.z) + sigmoidf_(v1[1]) * bfhi(q.z), bflo(c.w) + sigmoidf_(v1[2]) * bflo(q.w), bfhi(c.w) + sigmoidf_(v1[3]) * bfhi(q.w)}; }
.LBB0_1034:
	s_or_b64 exec, exec, s[34:35]
	v_or_b32_e32 v138, 48, v176
	v_ashrrev_i32_e32 v139, 31, v138
	s_waitcnt lgkmcnt(0)
	v_mov_b64_e32 v[114:115], s[14:15]
	v_lshlrev_b64 v[116:117], 13, v[138:139]
	v_mad_i64_i32 v[114:115], s[34:35], v138, s65, v[114:115]
	v_lshl_add_u64 v[116:117], s[0:1], 0, v[116:117]
	v_lshl_add_u64 v[114:115], v[114:115], 0, v[166:167]
	v_lshl_add_u64 v[116:117], v[116:117], 0, v[166:167]
	global_load_dwordx4 v[126:129], v[114:115], off
	global_load_dwordx4 v[118:121], v[114:115], off offset:256
	global_load_dwordx4 v[122:125], v[116:117], off
	s_nop 0
	global_load_dwordx4 v[114:117], v[116:117], off offset:256
	v_cvt_f32_i32_e32 v111, v111
	v_cvt_f32_i32_e32 v110, v110
	v_cvt_f32_i32_e32 v113, v113
	v_cvt_f32_i32_e32 v112, v112
	v_cvt_f32_i32_e32 v107, v107
	v_cvt_f32_i32_e32 v106, v106
	v_cvt_f32_i32_e32 v109, v109
	v_cvt_f32_i32_e32 v108, v108
	v_pk_mul_f32 v[142:143], v[178:179], v[68:69] op_sel_hi:[0,1]
	v_pk_mul_f32 v[144:145], v[178:179], v[66:67] op_sel_hi:[0,1]
	v_pk_mul_f32 v[146:147], v[178:179], v[64:65] op_sel_hi:[0,1]
	v_pk_mul_f32 v[148:149], v[178:179], v[62:63] op_sel_hi:[0,1]
	v_pk_mul_f32 v[110:111], v[144:145], v[110:111]
	v_pk_mul_f32 v[112:113], v[142:143], v[112:113]
	s_waitcnt vmcnt(9)
	v_lshlrev_b32_e32 v142, 16, v158
	v_and_b32_e32 v143, 0xffff0000, v158
	v_lshlrev_b32_e32 v144, 16, v159
	v_and_b32_e32 v145, 0xffff0000, v159
	v_pk_mul_f32 v[106:107], v[148:149], v[106:107]
	v_mul_f32_e32 v142, 0xbfb8aa3b, v142
	v_mul_f32_e32 v143, 0xbfb8aa3b, v143
	v_pk_mul_f32 v[108:109], v[146:147], v[108:109]
	v_mul_f32_e32 v144, 0xbfb8aa3b, v144
	v_mul_f32_e32 v145, 0xbfb8aa3b, v145
	v_lshlrev_b32_e32 v146, 16, v160
	v_and_b32_e32 v147, 0xffff0000, v160
	v_lshlrev_b32_e32 v148, 16, v161
	v_and_b32_e32 v149, 0xffff0000, v161
	v_exp_f32_e32 v142, v142
	v_exp_f32_e32 v143, v143
	v_exp_f32_e32 v144, v144
	v_exp_f32_e32 v145, v145
	v_mul_f32_e32 v146, 0xbfb8aa3b, v146
	v_mul_f32_e32 v147, 0xbfb8aa3b, v147
	v_mul_f32_e32 v148, 0xbfb8aa3b, v148
	v_mul_f32_e32 v149, 0xbfb8aa3b, v149
	v_exp_f32_e32 v146, v146
	v_exp_f32_e32 v147, v147
	v_exp_f32_e32 v148, v148
	v_exp_f32_e32 v149, v149
	v_add_f32_e32 v142, 1.0, v142
	v_add_f32_e32 v143, 1.0, v143
	v_add_f32_e32 v144, 1.0, v144
	v_add_f32_e32 v145, 1.0, v145
	v_rcp_f32_e32 v142, v142
	v_rcp_f32_e32 v143, v143
	v_rcp_f32_e32 v144, v144
	v_rcp_f32_e32 v145, v145
	v_add_f32_e32 v146, 1.0, v146
	v_add_f32_e32 v147, 1.0, v147
	v_add_f32_e32 v148, 1.0, v148
	v_add_f32_e32 v149, 1.0, v149
	v_rcp_f32_e32 v146, v146
	v_rcp_f32_e32 v147, v147
	v_rcp_f32_e32 v148, v148
	v_rcp_f32_e32 v149, v149
	s_waitcnt vmcnt(7)
	v_lshlrev_b32_e32 v154, 16, v150
	v_and_b32_e32 v155, 0xffff0000, v150
	v_lshlrev_b32_e32 v150, 16, v151
	v_and_b32_e32 v151, 0xffff0000, v151
	v_lshlrev_b64 v[140:141], 12, v[182:183]
	v_pk_fma_f32 v[112:113], v[112:113], v[144:145], v[150:151]
	v_pk_fma_f32 v[110:111], v[110:111], v[142:143], v[154:155]
	v_lshlrev_b32_e32 v142, 16, v152
	v_and_b32_e32 v143, 0xffff0000, v152
	v_lshlrev_b32_e32 v144, 16, v153
	v_and_b32_e32 v145, 0xffff0000, v153
	v_pk_fma_f32 v[144:145], v[108:109], v[148:149], v[144:145]
	v_pk_fma_f32 v[108:109], v[106:107], v[146:147], v[142:143]
	v_cvt_pk_bf16_f32 v106, v110, v111
	v_lshl_add_u64 v[110:111], v[140:141], 1, s[12:13]
	v_lshl_add_u64 v[110:111], v[110:111], 0, v[166:167]
	v_cvt_pk_bf16_f32 v107, v112, v113
	v_cvt_pk_bf16_f32 v108, v108, v109
	v_cvt_pk_bf16_f32 v109, v144, v145
	global_store_dwordx4 v[110:111], v[106:109], off sc1
	v_lshlrev_b32_e32 v112, 16, v106
	v_max_f32_e64 v112, |v112|, |v112|
	v_and_b32_e32 v106, 0xffff0000, v106
	v_max_f32_e64 v106, |v106|, |v106|
	v_max_f32_e32 v106, v112, v106
	v_lshlrev_b32_e32 v112, 16, v107
	v_and_b32_e32 v107, 0xffff0000, v107
	v_lshlrev_b32_e32 v113, 16, v109
	v_and_b32_e32 v109, 0xffff0000, v109
	v_max_f32_e64 v107, |v107|, |v107|
	v_max_f32_e64 v112, |v112|, |v112|
	v_max_f32_e64 v109, |v109|, |v109|
	v_max_f32_e64 v113, |v113|, |v113|
	v_cvt_f32_i32_e32 v105, v105
	v_cvt_f32_i32_e32 v104, v104
	v_max_f32_e32 v107, v112, v107
	v_lshlrev_b32_e32 v112, 16, v108
	v_and_b32_e32 v108, 0xffff0000, v108
	v_max_f32_e32 v109, v113, v109
	v_cvt_f32_i32_e32 v103, v103
	v_cvt_f32_i32_e32 v102, v102
	v_cvt_f32_i32_e32 v101, v101
	v_cvt_f32_i32_e32 v100, v100
	v_max3_f32 v108, |v112|, |v108|, v109
	v_max3_f32 v142, v106, v107, v108
	v_pk_mul_f32 v[106:107], v[178:179], v[56:57] op_sel_hi:[0,1]
	v_pk_mul_f32 v[108:109], v[178:179], v[54:55] op_sel_hi:[0,1]
	v_pk_mul_f32 v[112:113], v[178:179], v[52:53] op_sel_hi:[0,1]
	v_pk_mul_f32 v[104:105], v[106:107], v[104:105]
	v_lshlrev_b32_e32 v106, 16, v134
	v_and_b32_e32 v107, 0xffff0000, v134
	v_pk_mul_f32 v[102:103], v[108:109], v[102:103]
	v_mul_f32_e32 v106, 0xbfb8aa3b, v106
	v_mul_f32_e32 v107, 0xbfb8aa3b, v107
	v_pk_mul_f32 v[100:101], v[112:113], v[100:101]
	v_lshlrev_b32_e32 v108, 16, v135
	v_and_b32_e32 v109, 0xffff0000, v135
	v_lshlrev_b32_e32 v112, 16, v136
	v_and_b32_e32 v113, 0xffff0000, v136
	v_exp_f32_e32 v106, v106
	v_exp_f32_e32 v107, v107
	v_mul_f32_e32 v108, 0xbfb8aa3b, v108
	v_mul_f32_e32 v109, 0xbfb8aa3b, v109
	v_mul_f32_e32 v112, 0xbfb8aa3b, v112
	v_mul_f32_e32 v113, 0xbfb8aa3b, v113
	v_lshlrev_b32_e32 v134, 16, v137
	v_and_b32_e32 v135, 0xffff0000, v137
	v_exp_f32_e32 v108, v108
	v_exp_f32_e32 v109, v109
	v_exp_f32_e32 v112, v112
	v_exp_f32_e32 v113, v113
	v_mul_f32_e32 v134, 0xbfb8aa3b, v134
	v_mul_f32_e32 v135, 0xbfb8aa3b, v135
	v_exp_f32_e32 v134, v134
	v_exp_f32_e32 v135, v135
	v_add_f32_e32 v106, 1.0, v106
	v_add_f32_e32 v107, 1.0, v107
	v_cvt_f32_i32_e32 v99, v99
	v_cvt_f32_i32_e32 v98, v98
	v_rcp_f32_e32 v106, v106
	v_rcp_f32_e32 v107, v107
	v_add_f32_e32 v108, 1.0, v108
	v_add_f32_e32 v109, 1.0, v109
	v_add_f32_e32 v112, 1.0, v112
	v_add_f32_e32 v113, 1.0, v113
	v_rcp_f32_e32 v108, v108
	v_rcp_f32_e32 v109, v109
	v_rcp_f32_e32 v112, v112
	v_rcp_f32_e32 v113, v113
	v_add_f32_e32 v134, 1.0, v134
	v_add_f32_e32 v135, 1.0, v135
	v_rcp_f32_e32 v134, v134
	v_rcp_f32_e32 v135, v135
	v_pk_mul_f32 v[140:141], v[178:179], v[50:51] op_sel_hi:[0,1]
	s_waitcnt vmcnt(7)
;     __device__ __forceinline__ void operator()(const f32x4 (&acc)[2][2][4][2], const Unit& u, int wr, int wc, int fr, int fq) const {
;     ...
;         EPB_LOAD(0);
; #pragma unroll
;         for (int kb = 0; kb < 8; ++kb) { const int ai = kb >> 2, m = kb & 3;
;             if (kb < 7) EPB_LOAD(kb + 1);
;             { const int row = row0 + ai * HALF + m * 16; float rmx = 0.f;
; #pragma unroll
;                 for (int bj = 0; bj < 2; ++bj) { const int col = col0 + bj * HALF; f32x4 v0 = acc[ai][bj][m][0], v1 = acc[ai][bj][m][1];
;                     if (QI8) { const f32x4 c0 = cb[bj][0] * ra[ai][m], c1 = cb[bj][1] * ra[ai][m]; const i32x4 i0 = __builtin_bit_cast(i32x4, v0), i1 = __builtin_bit_cast(i32x4, v1);
;                         v0 = (f32x4){(float)i0[0], (float)i0[1], (float)i0[2], (float)i0[3]} * c0; v1 = (f32x4){(float)i1[0], (float)i1[1], (float)i1[2], (float)i1[3]} * c1; }
;                     else if (MODE == 0) { v0 = v0 * tsc; v1 = v1 * tsc; }
;                     if (!QI8 && MODE == 1) { v0 = v0 * cb[bj][0]; v1 = v1 * cb[bj][1]; }
;                     if (MODE == 2 || MODE == 3) { const u32x4 g = gq[kb & 1][bj];
;                         f32x4 g0 = {sigmoidf_(bflo(g.x)), sigmoidf_(bfhi(g.x)), sigmoidf_(bflo(g.y)), sigmoidf_(bfhi(g.y))};
;                         f32x4 g1 = {sigmoidf_(bflo(g.z)), sigmoidf_(bfhi(g.z)), sigmoidf_(bflo(g.w)), sigmoidf_(bfhi(g.w))};
;                         v0 = v0 * g0; v1 = v1 * g1;
;                         if (MODE == 3) { const u32x4 q = aq[kb & 1][bj];
;                             v0 = v0 + (f32x4){bflo(q.x), bfhi(q.x), bflo(q.y), bfhi(q.y)}; v1 = v1 + (f32x4){bflo(q.z), bfhi(q.z), bflo(q.w), bfhi(q.w)}; } }
;                     if (MODE == 4) { v0 = v0 + rs[kb & 1][bj][0]; v1 = v1 + rs[kb & 1][bj][1]; }
;                     if (MODE == 5) { const u32x4 c = gq[kb & 1][bj], q = aq[kb & 1][bj];
;                         v0 = (f32x4){bflo(c.x) + sigmoidf_(v0[0]) * bflo(q.x), bfhi(c.x) + sigmoidf_(v0[1]) * bfhi(q.x), bflo(c.y) + sigmoidf_(v0[2]) * bflo(q.y), bfhi(c.y) + sigmoidf_(v0[3]) * bfhi(q.y)};
;                         v1 = (f32x4){bflo(c.z) + sigmoidf_(v1[0]) * bflo(q.z), bfhi(c.z) + sigmoidf_(v1[1]) * bfhi(q.z), bflo(c.w) + sigmoidf_(v1[2]) * bflo(q.w), bfhi(c.w) + sigmoidf_(v1[3]) * bfhi(q.w)}; }
	v_lshlrev_b32_e32 v136, 16, v130
	v_and_b32_e32 v137, 0xffff0000, v130
	v_pk_mul_f32 v[98:99], v[140:141], v[98:99]
	v_lshlrev_b32_e32 v130, 16, v131
	v_and_b32_e32 v131, 0xffff0000, v131
	v_pk_fma_f32 v[102:103], v[102:103], v[106:107], v[136:137]
	v_lshlrev_b32_e32 v106, 16, v132
	v_and_b32_e32 v107, 0xffff0000, v132
	v_pk_fma_f32 v[104:105], v[104:105], v[108:109], v[130:131]
	v_lshlrev_b32_e32 v108, 16, v133
	v_and_b32_e32 v109, 0xffff0000, v133
	v_pk_fma_f32 v[98:99], v[98:99], v[112:113], v[106:107]
	v_pk_fma_f32 v[108:109], v[100:101], v[134:135], v[108:109]
	v_cvt_pk_bf16_f32 v100, v102, v103
	v_cvt_pk_bf16_f32 v101, v104, v105
	v_cvt_pk_bf16_f32 v102, v98, v99
	s_nop 0
	v_lshlrev_b32_e32 v98, 16, v100
	v_and_b32_e32 v99, 0xffff0000, v100
	v_max_f32_e64 v99, |v99|, |v99|
	v_max_f32_e64 v98, |v98|, |v98|
	v_cvt_pk_bf16_f32 v103, v108, v109
	v_max_f32_e32 v98, v98, v99
	v_lshlrev_b32_e32 v99, 16, v101
	v_and_b32_e32 v104, 0xffff0000, v101
	v_lshlrev_b32_e32 v106, 16, v103
	v_and_b32_e32 v107, 0xffff0000, v103
	v_max_f32_e64 v104, |v104|, |v104|
	v_max_f32_e64 v99, |v99|, |v99|
	v_max_f32_e64 v107, |v107|, |v107|
	v_max_f32_e64 v106, |v106|, |v106|
	v_max_f32_e32 v99, v99, v104
	v_lshlrev_b32_e32 v104, 16, v102
	v_and_b32_e32 v105, 0xffff0000, v102
	v_max_f32_e32 v106, v106, v107
	v_max3_f32 v104, |v104|, |v105|, v106
	v_max3_f32 v98, v98, v99, v104
	v_max3_f32 v98, v142, 0, v98
	ds_bpermute_b32 v99, v165, v98
	global_store_dwordx4 v[110:111], v[100:103], off offset:256 sc1
	s_waitcnt lgkmcnt(0)
	v_max_f32_e32 v99, v99, v99
	v_max_f32_e32 v98, v98, v99
	ds_bpermute_b32 v99, v169, v98
	s_and_saveexec_b64 s[34:35], s[6:7]
	s_cbranch_execz .LBB0_1036
	s_waitcnt lgkmcnt(0)
	v_max_f32_e32 v99, v99, v99
	v_max_f32_e32 v98, v98, v98
	v_lshl_add_u64 v[100:101], v[182:183], 2, s[16:17]
	v_max_f32_e32 v98, v98, v99
	global_atomic_umax v[100:101], v98, off
.LBB0_1036:
	s_or_b64 exec, exec, s[34:35]
	v_add_u32_e32 v130, 0x80, v176
	v_ashrrev_i32_e32 v131, 31, v130
	s_waitcnt lgkmcnt(0)
	v_mov_b64_e32 v[98:99], s[14:15]
	v_lshlrev_b64 v[100:101], 13, v[130:131]
	v_mad_i64_i32 v[98:99], s[34:35], v130, s65, v[98:99]
	v_lshl_add_u64 v[100:101], s[0:1], 0, v[100:101]
	v_lshl_add_u64 v[98:99], v[98:99], 0, v[166:167]
	v_lshl_add_u64 v[100:101], v[100:101], 0, v[166:167]
	global_load_dwordx4 v[110:113], v[98:99], off
	global_load_dwordx4 v[102:105], v[98:99], off offset:256
	global_load_dwordx4 v[106:109], v[100:101], off
	s_nop 0
	global_load_dwordx4 v[98:101], v[100:101], off offset:256
	v_cvt_f32_i32_e32 v97, v97
	v_cvt_f32_i32_e32 v96, v96
	v_pk_mul_f32 v[134:135], v[174:175], v[68:69] op_sel_hi:[0,1]
	v_cvt_f32_i32_e32 v95, v95
	v_cvt_f32_i32_e32 v94, v94
	v_pk_mul_f32 v[96:97], v[134:135], v[96:97]
	s_waitcnt vmcnt(9)
	v_lshlrev_b32_e32 v134, 16, v126
	v_and_b32_e32 v126, 0xffff0000, v126
	v_mul_f32_e32 v134, 0xbfb8aa3b, v134
	v_mul_f32_e32 v126, 0xbfb8aa3b, v126
	v_exp_f32_e32 v134, v134
	v_exp_f32_e32 v135, v126
	v_pk_mul_f32 v[136:137], v[174:175], v[66:67] op_sel_hi:[0,1]
	v_pk_mul_f32 v[94:95], v[136:137], v[94:95]
	v_add_f32_e32 v126, 1.0, v134
	v_add_f32_e32 v134, 1.0, v135
	v_lshlrev_b32_e32 v135, 16, v127
	v_and_b32_e32 v127, 0xffff0000, v127
	v_mul_f32_e32 v135, 0xbfb8aa3b, v135
	v_mul_f32_e32 v127, 0xbfb8aa3b, v127
	v_exp_f32_e32 v135, v135
	v_exp_f32_e32 v136, v127
	v_rcp_f32_e32 v127, v134
	v_cvt_f32_i32_e32 v93, v93
	v_add_f32_e32 v134, 1.0, v135
	v_add_f32_e32 v135, 1.0, v136
	v_lshlrev_b32_e32 v136, 16, v128
	v_and_b32_e32 v128, 0xffff0000, v128
	v_mul_f32_e32 v136, 0xbfb8aa3b, v136
	v_mul_f32_e32 v128, 0xbfb8aa3b, v128
	v_exp_f32_e32 v136, v136
	v_exp_f32_e32 v137, v128
	v_cvt_f32_i32_e32 v92, v92
	v_pk_mul_f32 v[140:141], v[174:175], v[64:65] op_sel_hi:[0,1]
	v_add_f32_e32 v128, 1.0, v136
	v_add_f32_e32 v136, 1.0, v137
	v_lshlrev_b32_e32 v137, 16, v129
	v_and_b32_e32 v129, 0xffff0000, v129
	v_mul_f32_e32 v137, 0xbfb8aa3b, v137
	v_mul_f32_e32 v129, 0xbfb8aa3b, v129
	v_pk_mul_f32 v[92:93], v[140:141], v[92:93]
	v_exp_f32_e32 v137, v137
	v_exp_f32_e32 v140, v129
	v_cvt_f32_i32_e32 v91, v91
	v_cvt_f32_i32_e32 v90, v90
	v_rcp_f32_e32 v126, v126
	v_rcp_f32_e32 v134, v134
	v_rcp_f32_e32 v135, v135
	v_rcp_f32_e32 v129, v136
	v_add_f32_e32 v136, 1.0, v137
	v_add_f32_e32 v137, 1.0, v140
	v_rcp_f32_e32 v128, v128
	v_rcp_f32_e32 v136, v136
	v_rcp_f32_e32 v137, v137
	v_pk_mul_f32 v[142:143], v[174:175], v[62:63] op_sel_hi:[0,1]
	s_waitcnt vmcnt(7)
;     __device__ __forceinline__ void operator()(const f32x4 (&acc)[2][2][4][2], const Unit& u, int wr, int wc, int fr, int fq) const {
;     ...
;             { const int row = row0 + ai * HALF + m * 16; float rmx = 0.f;
; #pragma unroll
;                 for (int bj = 0; bj < 2; ++bj) { const int col = col0 + bj * HALF; f32x4 v0 = acc[ai][bj][m][0], v1 = acc[ai][bj][m][1];
;                     if (QI8) { const f32x4 c0 = cb[bj][0] * ra[ai][m], c1 = cb[bj][1] * ra[ai][m]; const i32x4 i0 = __builtin_bit_cast(i32x4, v0), i1 = __builtin_bit_cast(i32x4, v1);
;                         v0 = (f32x4){(float)i0[0], (float)i0[1], (float)i0[2], (float)i0[3]} * c0; v1 = (f32x4){(float)i1[0], (float)i1[1], (float)i1[2], (float)i1[3]} * c1; }
;                     else if (MODE == 0) { v0 = v0 * tsc; v1 = v1 * tsc; }
;                     if (!QI8 && MODE == 1) { v0 = v0 * cb[bj][0]; v1 = v1 * cb[bj][1]; }
;                     if (MODE == 2 || MODE == 3) { const u32x4 g = gq[kb & 1][bj];
;                         f32x4 g0 = {sigmoidf_(bflo(g.x)), sigmoidf_(bfhi(g.x)), sigmoidf_(bflo(g.y)), sigmoidf_(bfhi(g.y))};
;                         f32x4 g1 = {sigmoidf_(bflo(g.z)), sigmoidf_(bfhi(g.z)), sigmoidf_(bflo(g.w)), sigmoidf_(bfhi(g.w))};
;                         v0 = v0 * g0; v1 = v1 * g1;
;                         if (MODE == 3) { const u32x4 q = aq[kb & 1][bj];
;                             v0 = v0 + (f32x4){bflo(q.x), bfhi(q.x), bflo(q.y), bfhi(q.y)}; v1 = v1 + (f32x4){bflo(q.z), bfhi(q.z), bflo(q.w), bfhi(q.w)}; } }
;                     if (MODE == 4) { v0 = v0 + rs[kb & 1][bj][0]; v1 = v1 + rs[kb & 1][bj][1]; }
;                     if (MODE == 5) { const u32x4 c = gq[kb & 1][bj], q = aq[kb & 1][bj];
;                         v0 = (f32x4){bflo(c.x) + sigmoidf_(v0[0]) * bflo(q.x), bfhi(c.x) + sigmoidf_(v0[1]) * bfhi(q.x), bflo(c.y) + sigmoidf_(v0[2]) * bflo(q.y), bfhi(c.y) + sigmoidf_(v0[3]) * bfhi(q.y)};
;                         v1 = (f32x4){bflo(c.z) + sigmoidf_(v1[0]) * bflo(q.z), bfhi(c.z) + sigmoidf_(v1[1]) * bfhi(q.z), bflo(c.w) + sigmoidf_(v1[2]) * bflo(q.w), bfhi(c.w) + sigmoidf_(v1[3]) * bfhi(q.w)}; }
;                     u32x4 w; w.x = cvtpk(v0[0], v0[1]); w.y = cvtpk(v0[2], v0[3]); w.z = cvtpk(v1[0], v1[1]); w.w = cvtpk(v1[2], v1[3]);
;                     *(u32x4*)(O + (size_t)row * ldo + col) = w;
	v_lshlrev_b32_e32 v140, 16, v122
	v_and_b32_e32 v141, 0xffff0000, v122
	v_lshlrev_b32_e32 v122, 16, v123
	v_and_b32_e32 v123, 0xffff0000, v123
	v_lshlrev_b64 v[132:133], 12, v[138:139]
	v_pk_mul_f32 v[90:91], v[142:143], v[90:91]
	v_pk_fma_f32 v[96:97], v[96:97], v[134:135], v[122:123]
	v_pk_fma_f32 v[94:95], v[94:95], v[126:127], v[140:141]
	v_lshlrev_b32_e32 v122, 16, v124
	v_and_b32_e32 v123, 0xffff0000, v124
	v_lshlrev_b32_e32 v124, 16, v125
	v_and_b32_e32 v125, 0xffff0000, v125
	v_pk_fma_f32 v[124:125], v[92:93], v[136:137], v[124:125]
	v_pk_fma_f32 v[92:93], v[90:91], v[128:129], v[122:123]
	v_cvt_pk_bf16_f32 v90, v94, v95
	v_lshl_add_u64 v[94:95], v[132:133], 1, s[12:13]
	v_lshl_add_u64 v[94:95], v[94:95], 0, v[166:167]
	v_cvt_pk_bf16_f32 v91, v96, v97
	v_cvt_pk_bf16_f32 v92, v92, v93
	v_cvt_pk_bf16_f32 v93, v124, v125
	global_store_dwordx4 v[94:95], v[90:93], off sc1
	v_lshlrev_b32_e32 v96, 16, v90
	v_max_f32_e64 v96, |v96|, |v96|
	v_and_b32_e32 v90, 0xffff0000, v90
	v_max_f32_e64 v90, |v90|, |v90|
	v_max_f32_e32 v90, v96, v90
	v_lshlrev_b32_e32 v96, 16, v91
	v_and_b32_e32 v91, 0xffff0000, v91
	v_lshlrev_b32_e32 v97, 16, v93
	v_and_b32_e32 v93, 0xffff0000, v93
	v_max_f32_e64 v91, |v91|, |v91|
	v_max_f32_e64 v96, |v96|, |v96|
	v_max_f32_e64 v93, |v93|, |v93|
	v_max_f32_e64 v97, |v97|, |v97|
	v_cvt_f32_i32_e32 v89, v89
	v_cvt_f32_i32_e32 v88, v88
	v_max_f32_e32 v91, v96, v91
	v_lshlrev_b32_e32 v96, 16, v92
	v_and_b32_e32 v92, 0xffff0000, v92
	v_max_f32_e32 v93, v97, v93
	v_cvt_f32_i32_e32 v87, v87
	v_cvt_f32_i32_e32 v86, v86
	v_cvt_f32_i32_e32 v85, v85
	v_cvt_f32_i32_e32 v84, v84
	v_max3_f32 v92, |v96|, |v92|, v93
	v_max3_f32 v124, v90, v91, v92
	v_pk_mul_f32 v[90:91], v[174:175], v[56:57] op_sel_hi:[0,1]
	v_pk_mul_f32 v[92:93], v[174:175], v[54:55] op_sel_hi:[0,1]
	v_pk_mul_f32 v[96:97], v[174:175], v[52:53] op_sel_hi:[0,1]
	v_pk_mul_f32 v[88:89], v[90:91], v[88:89]
	v_lshlrev_b32_e32 v90, 16, v118
	v_and_b32_e32 v91, 0xffff0000, v118
	v_pk_mul_f32 v[86:87], v[92:93], v[86:87]
	v_mul_f32_e32 v90, 0xbfb8aa3b, v90
	v_mul_f32_e32 v91, 0xbfb8aa3b, v91
	v_pk_mul_f32 v[84:85], v[96:97], v[84:85]
	v_lshlrev_b32_e32 v92, 16, v119
	v_and_b32_e32 v93, 0xffff0000, v119
	v_lshlrev_b32_e32 v96, 16, v120
	v_and_b32_e32 v97, 0xffff0000, v120
	v_exp_f32_e32 v90, v90
	v_exp_f32_e32 v91, v91
	v_mul_f32_e32 v92, 0xbfb8aa3b, v92
	v_mul_f32_e32 v93, 0xbfb8aa3b, v93
	v_mul_f32_e32 v96, 0xbfb8aa3b, v96
	v_mul_f32_e32 v97, 0xbfb8aa3b, v97
	v_lshlrev_b32_e32 v118, 16, v121
	v_and_b32_e32 v119, 0xffff0000, v121
	v_exp_f32_e32 v92, v92
	v_exp_f32_e32 v93, v93
	v_exp_f32_e32 v96, v96
	v_exp_f32_e32 v97, v97
	v_mul_f32_e32 v118, 0xbfb8aa3b, v118
	v_mul_f32_e32 v119, 0xbfb8aa3b, v119
	v_exp_f32_e32 v118, v118
	v_exp_f32_e32 v119, v119
	v_add_f32_e32 v90, 1.0, v90
	v_add_f32_e32 v91, 1.0, v91
	v_cvt_f32_i32_e32 v83, v83
	v_cvt_f32_i32_e32 v82, v82
	v_rcp_f32_e32 v90, v90
	v_rcp_f32_e32 v91, v91
	v_add_f32_e32 v92, 1.0, v92
	v_add_f32_e32 v93, 1.0, v93
	v_add_f32_e32 v96, 1.0, v96
	v_add_f32_e32 v97, 1.0, v97
	v_rcp_f32_e32 v92, v92
	v_rcp_f32_e32 v93, v93
	v_rcp_f32_e32 v96, v96
	v_rcp_f32_e32 v97, v97
	v_add_f32_e32 v118, 1.0, v118
	v_add_f32_e32 v119, 1.0, v119
	v_rcp_f32_e32 v118, v118
	v_rcp_f32_e32 v119, v119
	v_pk_mul_f32 v[122:123], v[174:175], v[50:51] op_sel_hi:[0,1]
	s_waitcnt vmcnt(7)
	v_lshlrev_b32_e32 v120, 16, v114
	v_and_b32_e32 v121, 0xffff0000, v114
	v_pk_mul_f32 v[82:83], v[122:123], v[82:83]
	v_lshlrev_b32_e32 v114, 16, v115
	v_and_b32_e32 v115, 0xffff0000, v115
	v_pk_fma_f32 v[86:87], v[86:87], v[90:91], v[120:121]
	v_lshlrev_b32_e32 v90, 16, v116
	v_and_b32_e32 v91, 0xffff0000, v116
	v_pk_fma_f32 v[88:89], v[88:89], v[92:93], v[114:115]
	v_lshlrev_b32_e32 v92, 16, v117
	v_and_b32_e32 v93, 0xffff0000, v117
	v_pk_fma_f32 v[82:83], v[82:83], v[96:97], v[90:91]
	v_pk_fma_f32 v[92:93], v[84:85], v[118:119], v[92:93]
	v_cvt_pk_bf16_f32 v84, v86, v87
	v_cvt_pk_bf16_f32 v85, v88, v89
	v_cvt_pk_bf16_f32 v86, v82, v83
	s_nop 0
	v_lshlrev_b32_e32 v82, 16, v84
	v_and_b32_e32 v83, 0xffff0000, v84
	v_max_f32_e64 v83, |v83|, |v83|
	v_max_f32_e64 v82, |v82|, |v82|
	v_cvt_pk_bf16_f32 v87, v92, v93
	v_max_f32_e32 v82, v82, v83
	v_lshlrev_b32_e32 v83, 16, v85
	v_and_b32_e32 v88, 0xffff0000, v85
	v_lshlrev_b32_e32 v90, 16, v87
	v_and_b32_e32 v91, 0xffff0000, v87
	v_max_f32_e64 v88, |v88|, |v88|
	v_max_f32_e64 v83, |v83|, |v83|
	v_max_f32_e64 v91, |v91|, |v91|
	v_max_f32_e64 v90, |v90|, |v90|
	v_max_f32_e32 v83, v83, v88
	v_lshlrev_b32_e32 v88, 16, v86
	v_and_b32_e32 v89, 0xffff0000, v86
	v_max_f32_e32 v90, v90, v91
	v_max3_f32 v88, |v88|, |v89|, v90
	v_max3_f32 v82, v82, v83, v88
	v_max3_f32 v82, v124, 0, v82
	ds_bpermute_b32 v83, v165, v82
	global_store_dwordx4 v[94:95], v[84:87], off offset:256 sc1
	s_waitcnt lgkmcnt(0)
	v_max_f32_e32 v83, v83, v83
	v_max_f32_e32 v82, v82, v83
	ds_bpermute_b32 v83, v169, v82
	s_and_saveexec_b64 s[34:35], s[6:7]
	s_cbranch_execz .LBB0_1038
	s_waitcnt lgkmcnt(0)
	v_max_f32_e32 v83, v83, v83
	v_max_f32_e32 v82, v82, v82
	v_lshl_add_u64 v[84:85], v[138:139], 2, s[16:17]
	v_max_f32_e32 v82, v82, v83
	global_atomic_umax v[84:85], v82, off
;     __device__ __forceinline__ void operator()(const f32x4 (&acc)[2][2][4][2], const Unit& u, int wr, int wc, int fr, int fq) const {
;     ...
;         EPB_LOAD(0);
; #pragma unroll
;         for (int kb = 0; kb < 8; ++kb) { const int ai = kb >> 2, m = kb & 3;
;             if (kb < 7) EPB_LOAD(kb + 1);
;             { const int row = row0 + ai * HALF + m * 16; float rmx = 0.f;
; #pragma unroll
;                 for (int bj = 0; bj < 2; ++bj) { const int col = col0 + bj * HALF; f32x4 v0 = acc[ai][bj][m][0], v1 = acc[ai][bj][m][1];
;                     if (QI8) { const f32x4 c0 = cb[bj][0] * ra[ai][m], c1 = cb[bj][1] * ra[ai][m]; const i32x4 i0 = __builtin_bit_cast(i32x4, v0), i1 = __builtin_bit_cast(i32x4, v1);
;                         v0 = (f32x4){(float)i0[0], (float)i0[1], (float)i0[2], (float)i0[3]} * c0; v1 = (f32x4){(float)i1[0], (float)i1[1], (float)i1[2], (float)i1[3]} * c1; }
;                     else if (MODE == 0) { v0 = v0 * tsc; v1 = v1 * tsc; }
;                     if (!QI8 && MODE == 1) { v0 = v0 * cb[bj][0]; v1 = v1 * cb[bj][1]; }
;                     if (MODE == 2 || MODE == 3) { const u32x4 g = gq[kb & 1][bj];
;                         f32x4 g0 = {sigmoidf_(bflo(g.x)), sigmoidf_(bfhi(g.x)), sigmoidf_(bflo(g.y)), sigmoidf_(bfhi(g.y))};
;                         f32x4 g1 = {sigmoidf_(bflo(g.z)), sigmoidf_(bfhi(g.z)), sigmoidf_(bflo(g.w)), sigmoidf_(bfhi(g.w))};
;                         v0 = v0 * g0; v1 = v1 * g1;
;                         if (MODE == 3) { const u32x4 q = aq[kb & 1][bj];
;                             v0 = v0 + (f32x4){bflo(q.x), bfhi(q.x), bflo(q.y), bfhi(q.y)}; v1 = v1 + (f32x4){bflo(q.z), bfhi(q.z), bflo(q.w), bfhi(q.w)}; } }
;                     if (MODE == 4) { v0 = v0 + rs[kb & 1][bj][0]; v1 = v1 + rs[kb & 1][bj][1]; }
;                     if (MODE == 5) { const u32x4 c = gq[kb & 1][bj], q = aq[kb & 1][bj];
;                         v0 = (f32x4){bflo(c.x) + sigmoidf_(v0[0]) * bflo(q.x), bfhi(c.x) + sigmoidf_(v0[1]) * bfhi(q.x), bflo(c.y) + sigmoidf_(v0[2]) * bflo(q.y), bfhi(c.y) + sigmoidf_(v0[3]) * bfhi(q.y)};
;                         v1 = (f32x4){bflo(c.z) + sigmoidf_(v1[0]) * bflo(q.z), bfhi(c.z) + sigmoidf_(v1[1]) * bfhi(q.z), bflo(c.w) + sigmoidf_(v1[2]) * bflo(q.w), bfhi(c.w) + sigmoidf_(v1[3]) * bfhi(q.w)}; }
.LBB0_1038:
	s_or_b64 exec, exec, s[34:35]
	v_or_b32_e32 v114, 16, v130
	v_ashrrev_i32_e32 v115, 31, v114
	s_waitcnt lgkmcnt(0)
	v_mov_b64_e32 v[82:83], s[14:15]
	v_lshlrev_b64 v[84:85], 13, v[114:115]
	v_mad_i64_i32 v[82:83], s[34:35], v114, s65, v[82:83]
	v_lshl_add_u64 v[84:85], s[0:1], 0, v[84:85]
	v_lshl_add_u64 v[82:83], v[82:83], 0, v[166:167]
	v_lshl_add_u64 v[84:85], v[84:85], 0, v[166:167]
	global_load_dwordx4 v[94:97], v[82:83], off
	global_load_dwordx4 v[86:89], v[82:83], off offset:256
	global_load_dwordx4 v[90:93], v[84:85], off
	s_nop 0
	global_load_dwordx4 v[82:85], v[84:85], off offset:256
	v_cvt_f32_i32_e32 v81, v81
	v_cvt_f32_i32_e32 v80, v80
	v_pk_mul_f32 v[118:119], v[172:173], v[68:69] op_sel_hi:[0,1]
	v_cvt_f32_i32_e32 v79, v79
	v_cvt_f32_i32_e32 v78, v78
	v_pk_mul_f32 v[80:81], v[118:119], v[80:81]
	s_waitcnt vmcnt(9)
	v_lshlrev_b32_e32 v118, 16, v110
	v_and_b32_e32 v110, 0xffff0000, v110
	v_mul_f32_e32 v118, 0xbfb8aa3b, v118
	v_mul_f32_e32 v110, 0xbfb8aa3b, v110
	v_exp_f32_e32 v118, v118
	v_exp_f32_e32 v119, v110
	v_pk_mul_f32 v[120:121], v[172:173], v[66:67] op_sel_hi:[0,1]
	v_pk_mul_f32 v[78:79], v[120:121], v[78:79]
	v_add_f32_e32 v110, 1.0, v118
	v_add_f32_e32 v118, 1.0, v119
	v_lshlrev_b32_e32 v119, 16, v111
	v_and_b32_e32 v111, 0xffff0000, v111
	v_mul_f32_e32 v119, 0xbfb8aa3b, v119
	v_mul_f32_e32 v111, 0xbfb8aa3b, v111
	v_exp_f32_e32 v119, v119
	v_exp_f32_e32 v120, v111
	v_rcp_f32_e32 v111, v118
	v_cvt_f32_i32_e32 v77, v77
	v_add_f32_e32 v118, 1.0, v119
	v_add_f32_e32 v119, 1.0, v120
	v_lshlrev_b32_e32 v120, 16, v112
	v_and_b32_e32 v112, 0xffff0000, v112
	v_mul_f32_e32 v120, 0xbfb8aa3b, v120
	v_mul_f32_e32 v112, 0xbfb8aa3b, v112
	v_exp_f32_e32 v120, v120
	v_exp_f32_e32 v121, v112
	v_cvt_f32_i32_e32 v76, v76
	v_pk_mul_f32 v[122:123], v[172:173], v[64:65] op_sel_hi:[0,1]
	v_add_f32_e32 v112, 1.0, v120
	v_add_f32_e32 v120, 1.0, v121
	v_lshlrev_b32_e32 v121, 16, v113
	v_and_b32_e32 v113, 0xffff0000, v113
	v_mul_f32_e32 v121, 0xbfb8aa3b, v121
	v_mul_f32_e32 v113, 0xbfb8aa3b, v113
	v_pk_mul_f32 v[76:77], v[122:123], v[76:77]
	v_exp_f32_e32 v121, v121
	v_exp_f32_e32 v122, v113
	v_cvt_f32_i32_e32 v75, v75
	v_cvt_f32_i32_e32 v74, v74
	v_rcp_f32_e32 v110, v110
	v_rcp_f32_e32 v118, v118
	v_rcp_f32_e32 v119, v119
	v_rcp_f32_e32 v113, v120
	v_add_f32_e32 v120, 1.0, v121
	v_add_f32_e32 v121, 1.0, v122
	v_rcp_f32_e32 v112, v112
	v_rcp_f32_e32 v120, v120
	v_rcp_f32_e32 v121, v121
	v_pk_mul_f32 v[124:125], v[172:173], v[62:63] op_sel_hi:[0,1]
	s_waitcnt vmcnt(7)
	v_lshlrev_b32_e32 v122, 16, v106
	v_and_b32_e32 v123, 0xffff0000, v106
	v_lshlrev_b32_e32 v106, 16, v107
	v_and_b32_e32 v107, 0xffff0000, v107
	v_lshlrev_b64 v[116:117], 12, v[130:131]
	v_pk_mul_f32 v[74:75], v[124:125], v[74:75]
	v_pk_fma_f32 v[80:81], v[80:81], v[118:119], v[106:107]
	v_pk_fma_f32 v[78:79], v[78:79], v[110:111], v[122:123]
	v_lshlrev_b32_e32 v106, 16, v108
	v_and_b32_e32 v107, 0xffff0000, v108
	v_lshlrev_b32_e32 v108, 16, v109
	v_and_b32_e32 v109, 0xffff0000, v109
	v_pk_fma_f32 v[108:109], v[76:77], v[120:121], v[108:109]
	v_pk_fma_f32 v[76:77], v[74:75], v[112:113], v[106:107]
	v_cvt_pk_bf16_f32 v74, v78, v79
	v_lshl_add_u64 v[78:79], v[116:117], 1, s[12:13]
	v_lshl_add_u64 v[78:79], v[78:79], 0, v[166:167]
	v_cvt_pk_bf16_f32 v75, v80, v81
	v_cvt_pk_bf16_f32 v76, v76, v77
	v_cvt_pk_bf16_f32 v77, v108, v109
	global_store_dwordx4 v[78:79], v[74:77], off sc1
	v_lshlrev_b32_e32 v80, 16, v74
	v_max_f32_e64 v80, |v80|, |v80|
	v_and_b32_e32 v74, 0xffff0000, v74
	v_max_f32_e64 v74, |v74|, |v74|
	v_max_f32_e32 v74, v80, v74
	v_lshlrev_b32_e32 v80, 16, v75
	v_and_b32_e32 v75, 0xffff0000, v75
	v_lshlrev_b32_e32 v81, 16, v77
	v_and_b32_e32 v77, 0xffff0000, v77
	v_max_f32_e64 v75, |v75|, |v75|
	v_max_f32_e64 v80, |v80|, |v80|
	v_max_f32_e64 v77, |v77|, |v77|
	v_max_f32_e64 v81, |v81|, |v81|
	v_cvt_f32_i32_e32 v73, v73
	v_cvt_f32_i32_e32 v72, v72
	v_max_f32_e32 v75, v80, v75
	v_lshlrev_b32_e32 v80, 16, v76
	v_and_b32_e32 v76, 0xffff0000, v76
	v_max_f32_e32 v77, v81, v77
	v_cvt_f32_i32_e32 v71, v71
	v_cvt_f32_i32_e32 v70, v70
	v_cvt_f32_i32_e32 v61, v61
	v_cvt_f32_i32_e32 v60, v60
	v_max3_f32 v76, |v80|, |v76|, v77
	v_max3_f32 v108, v74, v75, v76
	v_pk_mul_f32 v[74:75], v[172:173], v[56:57] op_sel_hi:[0,1]
	v_pk_mul_f32 v[76:77], v[172:173], v[54:55] op_sel_hi:[0,1]
	v_pk_mul_f32 v[80:81], v[172:173], v[52:53] op_sel_hi:[0,1]
	v_pk_mul_f32 v[72:73], v[74:75], v[72:73]
	v_lshlrev_b32_e32 v74, 16, v102
	v_and_b32_e32 v75, 0xffff0000, v102
	v_pk_mul_f32 v[70:71], v[76:77], v[70:71]
	v_mul_f32_e32 v74, 0xbfb8aa3b, v74
	v_mul_f32_e32 v75, 0xbfb8aa3b, v75
	v_pk_mul_f32 v[60:61], v[80:81], v[60:61]
	v_lshlrev_b32_e32 v76, 16, v103
	v_and_b32_e32 v77, 0xffff0000, v103
	v_lshlrev_b32_e32 v80, 16, v104
	v_and_b32_e32 v81, 0xffff0000, v104
	v_exp_f32_e32 v74, v74
	v_exp_f32_e32 v75, v75
	v_mul_f32_e32 v76, 0xbfb8aa3b, v76
	v_mul_f32_e32 v77, 0xbfb8aa3b, v77
	v_mul_f32_e32 v80, 0xbfb8aa3b, v80
	v_mul_f32_e32 v81, 0xbfb8aa3b, v81
	v_exp_f32_e32 v76, v76
	v_exp_f32_e32 v77, v77
	v_exp_f32_e32 v80, v80
	v_exp_f32_e32 v81, v81
	v_lshlrev_b32_e32 v102, 16, v105
	v_and_b32_e32 v103, 0xffff0000, v105
	v_mul_f32_e32 v102, 0xbfb8aa3b, v102
	v_mul_f32_e32 v103, 0xbfb8aa3b, v103
	v_exp_f32_e32 v102, v102
	v_exp_f32_e32 v103, v103
	v_add_f32_e32 v74, 1.0, v74
	v_add_f32_e32 v75, 1.0, v75
	v_cvt_f32_i32_e32 v59, v59
	v_cvt_f32_i32_e32 v58, v58
	v_rcp_f32_e32 v74, v74
	v_rcp_f32_e32 v75, v75
	v_add_f32_e32 v76, 1.0, v76
	v_add_f32_e32 v77, 1.0, v77
	v_add_f32_e32 v80, 1.0, v80
	v_add_f32_e32 v81, 1.0, v81
	v_rcp_f32_e32 v76, v76
	v_rcp_f32_e32 v77, v77
	v_rcp_f32_e32 v80, v80
	v_rcp_f32_e32 v81, v81
	v_add_f32_e32 v102, 1.0, v102
	v_add_f32_e32 v103, 1.0, v103
	v_pk_mul_f32 v[106:107], v[172:173], v[50:51] op_sel_hi:[0,1]
	v_rcp_f32_e32 v102, v102
	v_rcp_f32_e32 v103, v103
	s_waitcnt vmcnt(7)
;     __device__ __forceinline__ void operator()(const f32x4 (&acc)[2][2][4][2], const Unit& u, int wr, int wc, int fr, int fq) const {
;     ...
;         EPB_LOAD(0);
; #pragma unroll
;         for (int kb = 0; kb < 8; ++kb) { const int ai = kb >> 2, m = kb & 3;
;             if (kb < 7) EPB_LOAD(kb + 1);
;             { const int row = row0 + ai * HALF + m * 16; float rmx = 0.f;
; #pragma unroll
;                 for (int bj = 0; bj < 2; ++bj) { const int col = col0 + bj * HALF; f32x4 v0 = acc[ai][bj][m][0], v1 = acc[ai][bj][m][1];
;                     if (QI8) { const f32x4 c0 = cb[bj][0] * ra[ai][m], c1 = cb[bj][1] * ra[ai][m]; const i32x4 i0 = __builtin_bit_cast(i32x4, v0), i1 = __builtin_bit_cast(i32x4, v1);
;                         v0 = (f32x4){(float)i0[0], (float)i0[1], (float)i0[2], (float)i0[3]} * c0; v1 = (f32x4){(float)i1[0], (float)i1[1], (float)i1[2], (float)i1[3]} * c1; }
;                     else if (MODE == 0) { v0 = v0 * tsc; v1 = v1 * tsc; }
;                     if (!QI8 && MODE == 1) { v0 = v0 * cb[bj][0]; v1 = v1 * cb[bj][1]; }
;                     if (MODE == 2 || MODE == 3) { const u32x4 g = gq[kb & 1][bj];
;                         f32x4 g0 = {sigmoidf_(bflo(g.x)), sigmoidf_(bfhi(g.x)), sigmoidf_(bflo(g.y)), sigmoidf_(bfhi(g.y))};
;                         f32x4 g1 = {sigmoidf_(bflo(g.z)), sigmoidf_(bfhi(g.z)), sigmoidf_(bflo(g.w)), sigmoidf_(bfhi(g.w))};
;                         v0 = v0 * g0; v1 = v1 * g1;
;                         if (MODE == 3) { const u32x4 q = aq[kb & 1][bj];
;                             v0 = v0 + (f32x4){bflo(q.x), bfhi(q.x), bflo(q.y), bfhi(q.y)}; v1 = v1 + (f32x4){bflo(q.z), bfhi(q.z), bflo(q.w), bfhi(q.w)}; } }
;                     if (MODE == 4) { v0 = v0 + rs[kb & 1][bj][0]; v1 = v1 + rs[kb & 1][bj][1]; }
;                     if (MODE == 5) { const u32x4 c = gq[kb & 1][bj], q = aq[kb & 1][bj];
;                         v0 = (f32x4){bflo(c.x) + sigmoidf_(v0[0]) * bflo(q.x), bfhi(c.x) + sigmoidf_(v0[1]) * bfhi(q.x), bflo(c.y) + sigmoidf_(v0[2]) * bflo(q.y), bfhi(c.y) + sigmoidf_(v0[3]) * bfhi(q.y)};
;                         v1 = (f32x4){bflo(c.z) + sigmoidf_(v1[0]) * bflo(q.z), bfhi(c.z) + sigmoidf_(v1[1]) * bfhi(q.z), bflo(c.w) + sigmoidf_(v1[2]) * bflo(q.w), bfhi(c.w) + sigmoidf_(v1[3]) * bfhi(q.w)}; }
	v_lshlrev_b32_e32 v104, 16, v98
	v_and_b32_e32 v105, 0xffff0000, v98
	v_pk_mul_f32 v[58:59], v[106:107], v[58:59]
	v_lshlrev_b32_e32 v98, 16, v99
	v_and_b32_e32 v99, 0xffff0000, v99
	v_pk_fma_f32 v[70:71], v[70:71], v[74:75], v[104:105]
	v_lshlrev_b32_e32 v74, 16, v100
	v_and_b32_e32 v75, 0xffff0000, v100
	v_pk_fma_f32 v[72:73], v[72:73], v[76:77], v[98:99]
	v_pk_fma_f32 v[58:59], v[58:59], v[80:81], v[74:75]
	v_lshlrev_b32_e32 v76, 16, v101
	v_and_b32_e32 v77, 0xffff0000, v101
	v_cvt_pk_bf16_f32 v70, v70, v71
	v_cvt_pk_bf16_f32 v71, v72, v73
	v_cvt_pk_bf16_f32 v72, v58, v59
	v_pk_fma_f32 v[60:61], v[60:61], v[102:103], v[76:77]
	v_lshlrev_b32_e32 v58, 16, v70
	v_and_b32_e32 v59, 0xffff0000, v70
	v_max_f32_e64 v59, |v59|, |v59|
	v_max_f32_e64 v58, |v58|, |v58|
	v_cvt_pk_bf16_f32 v73, v60, v61
	v_max_f32_e32 v58, v58, v59
	v_lshlrev_b32_e32 v59, 16, v71
	v_and_b32_e32 v60, 0xffff0000, v71
	v_lshlrev_b32_e32 v74, 16, v73
	v_and_b32_e32 v75, 0xffff0000, v73
	v_max_f32_e64 v60, |v60|, |v60|
	v_max_f32_e64 v59, |v59|, |v59|
	v_max_f32_e64 v75, |v75|, |v75|
	v_max_f32_e64 v74, |v74|, |v74|
	v_max_f32_e32 v59, v59, v60
	v_lshlrev_b32_e32 v60, 16, v72
	v_and_b32_e32 v61, 0xffff0000, v72
	v_max_f32_e32 v74, v74, v75
	v_max3_f32 v60, |v60|, |v61|, v74
	v_max3_f32 v58, v58, v59, v60
	v_max3_f32 v58, v108, 0, v58
	ds_bpermute_b32 v59, v165, v58
	global_store_dwordx4 v[78:79], v[70:73], off offset:256 sc1
	s_waitcnt lgkmcnt(0)
	v_max_f32_e32 v59, v59, v59
	v_max_f32_e32 v58, v58, v59
	ds_bpermute_b32 v59, v169, v58
	s_and_saveexec_b64 s[34:35], s[6:7]
	s_cbranch_execz .LBB0_1040
	s_waitcnt lgkmcnt(0)
	v_max_f32_e32 v59, v59, v59
	v_max_f32_e32 v58, v58, v58
	v_lshl_add_u64 v[60:61], v[130:131], 2, s[16:17]
	v_max_f32_e32 v58, v58, v59
	global_atomic_umax v[60:61], v58, off
.LBB0_1040:
	s_or_b64 exec, exec, s[34:35]
	v_or_b32_e32 v98, 32, v130
	v_ashrrev_i32_e32 v99, 31, v98
	s_waitcnt lgkmcnt(0)
	v_mov_b64_e32 v[58:59], s[14:15]
	v_lshlrev_b64 v[60:61], 13, v[98:99]
	v_mad_i64_i32 v[58:59], s[34:35], v98, s65, v[58:59]
	v_lshl_add_u64 v[60:61], s[0:1], 0, v[60:61]
	v_lshl_add_u64 v[58:59], v[58:59], 0, v[166:167]
	v_lshl_add_u64 v[60:61], v[60:61], 0, v[166:167]
	global_load_dwordx4 v[78:81], v[58:59], off
	global_load_dwordx4 v[70:73], v[58:59], off offset:256
	global_load_dwordx4 v[74:77], v[60:61], off
	s_nop 0
	global_load_dwordx4 v[58:61], v[60:61], off offset:256
	v_cvt_f32_i32_e32 v49, v49
	v_cvt_f32_i32_e32 v48, v48
	v_pk_mul_f32 v[102:103], v[170:171], v[68:69] op_sel_hi:[0,1]
	v_cvt_f32_i32_e32 v47, v47
	v_cvt_f32_i32_e32 v46, v46
	v_pk_mul_f32 v[48:49], v[102:103], v[48:49]
	s_waitcnt vmcnt(9)
	v_lshlrev_b32_e32 v102, 16, v94
	v_and_b32_e32 v94, 0xffff0000, v94
	v_mul_f32_e32 v102, 0xbfb8aa3b, v102
	v_mul_f32_e32 v94, 0xbfb8aa3b, v94
	v_exp_f32_e32 v102, v102
	v_exp_f32_e32 v103, v94
	v_pk_mul_f32 v[104:105], v[170:171], v[66:67] op_sel_hi:[0,1]
	v_pk_mul_f32 v[46:47], v[104:105], v[46:47]
	v_add_f32_e32 v94, 1.0, v102
	v_add_f32_e32 v102, 1.0, v103
	v_lshlrev_b32_e32 v103, 16, v95
	v_and_b32_e32 v95, 0xffff0000, v95
	v_mul_f32_e32 v103, 0xbfb8aa3b, v103
	v_mul_f32_e32 v95, 0xbfb8aa3b, v95
	v_exp_f32_e32 v103, v103
	v_exp_f32_e32 v104, v95
	v_rcp_f32_e32 v95, v102
	v_cvt_f32_i32_e32 v45, v45
	v_add_f32_e32 v102, 1.0, v103
	v_add_f32_e32 v103, 1.0, v104
	v_lshlrev_b32_e32 v104, 16, v96
	v_and_b32_e32 v96, 0xffff0000, v96
	v_mul_f32_e32 v104, 0xbfb8aa3b, v104
	v_mul_f32_e32 v96, 0xbfb8aa3b, v96
	v_exp_f32_e32 v104, v104
	v_exp_f32_e32 v105, v96
	v_cvt_f32_i32_e32 v44, v44
	v_pk_mul_f32 v[106:107], v[170:171], v[64:65] op_sel_hi:[0,1]
	v_add_f32_e32 v96, 1.0, v104
	v_add_f32_e32 v104, 1.0, v105
	v_lshlrev_b32_e32 v105, 16, v97
	v_and_b32_e32 v97, 0xffff0000, v97
	v_mul_f32_e32 v105, 0xbfb8aa3b, v105
	v_mul_f32_e32 v97, 0xbfb8aa3b, v97
	v_pk_mul_f32 v[44:45], v[106:107], v[44:45]
	v_exp_f32_e32 v105, v105
	v_exp_f32_e32 v106, v97
	v_cvt_f32_i32_e32 v43, v43
	v_cvt_f32_i32_e32 v42, v42
	v_rcp_f32_e32 v94, v94
	v_rcp_f32_e32 v102, v102
	v_rcp_f32_e32 v103, v103
	v_rcp_f32_e32 v97, v104
	v_add_f32_e32 v104, 1.0, v105
	v_add_f32_e32 v105, 1.0, v106
	v_rcp_f32_e32 v96, v96
	v_rcp_f32_e32 v104, v104
	v_rcp_f32_e32 v105, v105
	v_pk_mul_f32 v[108:109], v[170:171], v[62:63] op_sel_hi:[0,1]
	s_waitcnt vmcnt(7)
;     __device__ __forceinline__ void operator()(const f32x4 (&acc)[2][2][4][2], const Unit& u, int wr, int wc, int fr, int fq) const {
;     ...
;             { const int row = row0 + ai * HALF + m * 16; float rmx = 0.f;
; #pragma unroll
;                 for (int bj = 0; bj < 2; ++bj) { const int col = col0 + bj * HALF; f32x4 v0 = acc[ai][bj][m][0], v1 = acc[ai][bj][m][1];
;                     if (QI8) { const f32x4 c0 = cb[bj][0] * ra[ai][m], c1 = cb[bj][1] * ra[ai][m]; const i32x4 i0 = __builtin_bit_cast(i32x4, v0), i1 = __builtin_bit_cast(i32x4, v1);
;                         v0 = (f32x4){(float)i0[0], (float)i0[1], (float)i0[2], (float)i0[3]} * c0; v1 = (f32x4){(float)i1[0], (float)i1[1], (float)i1[2], (float)i1[3]} * c1; }
;                     else if (MODE == 0) { v0 = v0 * tsc; v1 = v1 * tsc; }
;                     if (!QI8 && MODE == 1) { v0 = v0 * cb[bj][0]; v1 = v1 * cb[bj][1]; }
;                     if (MODE == 2 || MODE == 3) { const u32x4 g = gq[kb & 1][bj];
;                         f32x4 g0 = {sigmoidf_(bflo(g.x)), sigmoidf_(bfhi(g.x)), sigmoidf_(bflo(g.y)), sigmoidf_(bfhi(g.y))};
;                         f32x4 g1 = {sigmoidf_(bflo(g.z)), sigmoidf_(bfhi(g.z)), sigmoidf_(bflo(g.w)), sigmoidf_(bfhi(g.w))};
;                         v0 = v0 * g0; v1 = v1 * g1;
;                         if (MODE == 3) { const u32x4 q = aq[kb & 1][bj];
;                             v0 = v0 + (f32x4){bflo(q.x), bfhi(q.x), bflo(q.y), bfhi(q.y)}; v1 = v1 + (f32x4){bflo(q.z), bfhi(q.z), bflo(q.w), bfhi(q.w)}; } }
;                     if (MODE == 4) { v0 = v0 + rs[kb & 1][bj][0]; v1 = v1 + rs[kb & 1][bj][1]; }
;                     if (MODE == 5) { const u32x4 c = gq[kb & 1][bj], q = aq[kb & 1][bj];
;                         v0 = (f32x4){bflo(c.x) + sigmoidf_(v0[0]) * bflo(q.x), bfhi(c.x) + sigmoidf_(v0[1]) * bfhi(q.x), bflo(c.y) + sigmoidf_(v0[2]) * bflo(q.y), bfhi(c.y) + sigmoidf_(v0[3]) * bfhi(q.y)};
;                         v1 = (f32x4){bflo(c.z) + sigmoidf_(v1[0]) * bflo(q.z), bfhi(c.z) + sigmoidf_(v1[1]) * bfhi(q.z), bflo(c.w) + sigmoidf_(v1[2]) * bflo(q.w), bfhi(c.w) + sigmoidf_(v1[3]) * bfhi(q.w)}; }
;                     u32x4 w; w.x = cvtpk(v0[0], v0[1]); w.y = cvtpk(v0[2], v0[3]); w.z = cvtpk(v1[0], v1[1]); w.w = cvtpk(v1[2], v1[3]);
;                     *(u32x4*)(O + (size_t)row * ldo + col) = w;
	v_lshlrev_b32_e32 v106, 16, v90
	v_and_b32_e32 v107, 0xffff0000, v90
	v_lshlrev_b32_e32 v90, 16, v91
	v_and_b32_e32 v91, 0xffff0000, v91
	v_lshlrev_b64 v[100:101], 12, v[114:115]
	v_pk_mul_f32 v[42:43], v[108:109], v[42:43]
	v_pk_fma_f32 v[48:49], v[48:49], v[102:103], v[90:91]
	v_pk_fma_f32 v[46:47], v[46:47], v[94:95], v[106:107]
	v_lshlrev_b32_e32 v90, 16, v92
	v_and_b32_e32 v91, 0xffff0000, v92
	v_lshlrev_b32_e32 v92, 16, v93
	v_and_b32_e32 v93, 0xffff0000, v93
	v_pk_fma_f32 v[92:93], v[44:45], v[104:105], v[92:93]
	v_pk_fma_f32 v[44:45], v[42:43], v[96:97], v[90:91]
	v_cvt_pk_bf16_f32 v42, v46, v47
	v_lshl_add_u64 v[46:47], v[100:101], 1, s[12:13]
	v_lshl_add_u64 v[46:47], v[46:47], 0, v[166:167]
	v_cvt_pk_bf16_f32 v43, v48, v49
	v_cvt_pk_bf16_f32 v44, v44, v45
	v_cvt_pk_bf16_f32 v45, v92, v93
	global_store_dwordx4 v[46:47], v[42:45], off sc1
	v_lshlrev_b32_e32 v48, 16, v42
	v_max_f32_e64 v48, |v48|, |v48|
	v_and_b32_e32 v42, 0xffff0000, v42
	v_max_f32_e64 v42, |v42|, |v42|
	v_max_f32_e32 v42, v48, v42
	v_lshlrev_b32_e32 v48, 16, v43
	v_and_b32_e32 v43, 0xffff0000, v43
	v_lshlrev_b32_e32 v49, 16, v45
	v_and_b32_e32 v45, 0xffff0000, v45
	v_max_f32_e64 v43, |v43|, |v43|
	v_max_f32_e64 v48, |v48|, |v48|
	v_max_f32_e64 v45, |v45|, |v45|
	v_max_f32_e64 v49, |v49|, |v49|
	v_cvt_f32_i32_e32 v41, v41
	v_cvt_f32_i32_e32 v40, v40
	v_max_f32_e32 v43, v48, v43
	v_lshlrev_b32_e32 v48, 16, v44
	v_and_b32_e32 v44, 0xffff0000, v44
	v_max_f32_e32 v45, v49, v45
	v_cvt_f32_i32_e32 v39, v39
	v_cvt_f32_i32_e32 v38, v38
	v_cvt_f32_i32_e32 v37, v37
	v_cvt_f32_i32_e32 v36, v36
	v_max3_f32 v44, |v48|, |v44|, v45
	v_max3_f32 v92, v42, v43, v44
	v_pk_mul_f32 v[42:43], v[170:171], v[56:57] op_sel_hi:[0,1]
	v_pk_mul_f32 v[44:45], v[170:171], v[54:55] op_sel_hi:[0,1]
	v_pk_mul_f32 v[48:49], v[170:171], v[52:53] op_sel_hi:[0,1]
	v_pk_mul_f32 v[40:41], v[42:43], v[40:41]
	v_lshlrev_b32_e32 v42, 16, v86
	v_and_b32_e32 v43, 0xffff0000, v86
	v_pk_mul_f32 v[38:39], v[44:45], v[38:39]
	v_mul_f32_e32 v42, 0xbfb8aa3b, v42
	v_mul_f32_e32 v43, 0xbfb8aa3b, v43
	v_pk_mul_f32 v[36:37], v[48:49], v[36:37]
	v_lshlrev_b32_e32 v44, 16, v87
	v_and_b32_e32 v45, 0xffff0000, v87
	v_lshlrev_b32_e32 v48, 16, v88
	v_and_b32_e32 v49, 0xffff0000, v88
	v_exp_f32_e32 v42, v42
	v_exp_f32_e32 v43, v43
	v_mul_f32_e32 v44, 0xbfb8aa3b, v44
	v_mul_f32_e32 v45, 0xbfb8aa3b, v45
	v_mul_f32_e32 v48, 0xbfb8aa3b, v48
	v_mul_f32_e32 v49, 0xbfb8aa3b, v49
	v_lshlrev_b32_e32 v86, 16, v89
	v_and_b32_e32 v87, 0xffff0000, v89
	v_exp_f32_e32 v44, v44
	v_exp_f32_e32 v45, v45
	v_exp_f32_e32 v48, v48
	v_exp_f32_e32 v49, v49
	v_mul_f32_e32 v86, 0xbfb8aa3b, v86
	v_mul_f32_e32 v87, 0xbfb8aa3b, v87
	v_exp_f32_e32 v86, v86
	v_exp_f32_e32 v87, v87
	v_add_f32_e32 v42, 1.0, v42
	v_add_f32_e32 v43, 1.0, v43
	v_cvt_f32_i32_e32 v35, v35
	v_cvt_f32_i32_e32 v34, v34
	v_rcp_f32_e32 v42, v42
	v_rcp_f32_e32 v43, v43
	v_add_f32_e32 v44, 1.0, v44
	v_add_f32_e32 v45, 1.0, v45
	v_add_f32_e32 v48, 1.0, v48
	v_add_f32_e32 v49, 1.0, v49
	v_rcp_f32_e32 v44, v44
	v_rcp_f32_e32 v45, v45
	v_rcp_f32_e32 v48, v48
	v_rcp_f32_e32 v49, v49
	v_add_f32_e32 v86, 1.0, v86
	v_add_f32_e32 v87, 1.0, v87
	v_rcp_f32_e32 v86, v86
	v_rcp_f32_e32 v87, v87
	v_pk_mul_f32 v[90:91], v[170:171], v[50:51] op_sel_hi:[0,1]
	s_waitcnt vmcnt(7)
	v_lshlrev_b32_e32 v88, 16, v82
	v_and_b32_e32 v89, 0xffff0000, v82
	v_pk_mul_f32 v[34:35], v[90:91], v[34:35]
	v_lshlrev_b32_e32 v82, 16, v83
	v_and_b32_e32 v83, 0xffff0000, v83
	v_pk_fma_f32 v[38:39], v[38:39], v[42:43], v[88:89]
	v_lshlrev_b32_e32 v42, 16, v84
	v_and_b32_e32 v43, 0xffff0000, v84
	v_pk_fma_f32 v[40:41], v[40:41], v[44:45], v[82:83]
	v_lshlrev_b32_e32 v44, 16, v85
	v_and_b32_e32 v45, 0xffff0000, v85
	v_pk_fma_f32 v[34:35], v[34:35], v[48:49], v[42:43]
	v_pk_fma_f32 v[44:45], v[36:37], v[86:87], v[44:45]
	v_cvt_pk_bf16_f32 v36, v38, v39
	v_cvt_pk_bf16_f32 v37, v40, v41
	v_cvt_pk_bf16_f32 v38, v34, v35
	s_nop 0
	v_lshlrev_b32_e32 v34, 16, v36
	v_and_b32_e32 v35, 0xffff0000, v36
	v_max_f32_e64 v35, |v35|, |v35|
	v_max_f32_e64 v34, |v34|, |v34|
	v_cvt_pk_bf16_f32 v39, v44, v45
	v_max_f32_e32 v34, v34, v35
	v_lshlrev_b32_e32 v35, 16, v37
	v_and_b32_e32 v40, 0xffff0000, v37
	v_lshlrev_b32_e32 v42, 16, v39
	v_and_b32_e32 v43, 0xffff0000, v39
	v_max_f32_e64 v40, |v40|, |v40|
	v_max_f32_e64 v35, |v35|, |v35|
	v_max_f32_e64 v43, |v43|, |v43|
	v_max_f32_e64 v42, |v42|, |v42|
	v_max_f32_e32 v35, v35, v40
	v_lshlrev_b32_e32 v40, 16, v38
	v_and_b32_e32 v41, 0xffff0000, v38
	v_max_f32_e32 v42, v42, v43
	v_max3_f32 v40, |v40|, |v41|, v42
	v_max3_f32 v34, v34, v35, v40
	v_max3_f32 v34, v92, 0, v34
	ds_bpermute_b32 v35, v165, v34
	global_store_dwordx4 v[46:47], v[36:39], off offset:256 sc1
	s_waitcnt lgkmcnt(0)
	v_max_f32_e32 v35, v35, v35
	v_max_f32_e32 v34, v34, v35
	ds_bpermute_b32 v35, v169, v34
	s_and_saveexec_b64 s[34:35], s[6:7]
	s_cbranch_execz .LBB0_1042
	s_waitcnt lgkmcnt(0)
	v_max_f32_e32 v35, v35, v35
	v_max_f32_e32 v34, v34, v34
	v_lshl_add_u64 v[36:37], v[114:115], 2, s[16:17]
	v_max_f32_e32 v34, v34, v35
	global_atomic_umax v[36:37], v34, off
;     __device__ __forceinline__ void operator()(const f32x4 (&acc)[2][2][4][2], const Unit& u, int wr, int wc, int fr, int fq) const {
;     ...
;         EPB_LOAD(0);
; #pragma unroll
;         for (int kb = 0; kb < 8; ++kb) { const int ai = kb >> 2, m = kb & 3;
;             if (kb < 7) EPB_LOAD(kb + 1);
;             { const int row = row0 + ai * HALF + m * 16; float rmx = 0.f;
; #pragma unroll
;                 for (int bj = 0; bj < 2; ++bj) { const int col = col0 + bj * HALF; f32x4 v0 = acc[ai][bj][m][0], v1 = acc[ai][bj][m][1];
;                     if (QI8) { const f32x4 c0 = cb[bj][0] * ra[ai][m], c1 = cb[bj][1] * ra[ai][m]; const i32x4 i0 = __builtin_bit_cast(i32x4, v0), i1 = __builtin_bit_cast(i32x4, v1);
;                         v0 = (f32x4){(float)i0[0], (float)i0[1], (float)i0[2], (float)i0[3]} * c0; v1 = (f32x4){(float)i1[0], (float)i1[1], (float)i1[2], (float)i1[3]} * c1; }
;                     else if (MODE == 0) { v0 = v0 * tsc; v1 = v1 * tsc; }
;                     if (!QI8 && MODE == 1) { v0 = v0 * cb[bj][0]; v1 = v1 * cb[bj][1]; }
;                     if (MODE == 2 || MODE == 3) { const u32x4 g = gq[kb & 1][bj];
;                         f32x4 g0 = {sigmoidf_(bflo(g.x)), sigmoidf_(bfhi(g.x)), sigmoidf_(bflo(g.y)), sigmoidf_(bfhi(g.y))};
;                         f32x4 g1 = {sigmoidf_(bflo(g.z)), sigmoidf_(bfhi(g.z)), sigmoidf_(bflo(g.w)), sigmoidf_(bfhi(g.w))};
;                         v0 = v0 * g0; v1 = v1 * g1;
;                         if (MODE == 3) { const u32x4 q = aq[kb & 1][bj];
;                             v0 = v0 + (f32x4){bflo(q.x), bfhi(q.x), bflo(q.y), bfhi(q.y)}; v1 = v1 + (f32x4){bflo(q.z), bfhi(q.z), bflo(q.w), bfhi(q.w)}; } }
;                     if (MODE == 4) { v0 = v0 + rs[kb & 1][bj][0]; v1 = v1 + rs[kb & 1][bj][1]; }
;                     if (MODE == 5) { const u32x4 c = gq[kb & 1][bj], q = aq[kb & 1][bj];
;                         v0 = (f32x4){bflo(c.x) + sigmoidf_(v0[0]) * bflo(q.x), bfhi(c.x) + sigmoidf_(v0[1]) * bfhi(q.x), bflo(c.y) + sigmoidf_(v0[2]) * bflo(q.y), bfhi(c.y) + sigmoidf_(v0[3]) * bfhi(q.y)};
;                         v1 = (f32x4){bflo(c.z) + sigmoidf_(v1[0]) * bflo(q.z), bfhi(c.z) + sigmoidf_(v1[1]) * bfhi(q.z), bflo(c.w) + sigmoidf_(v1[2]) * bflo(q.w), bfhi(c.w) + sigmoidf_(v1[3]) * bfhi(q.w)}; }
.LBB0_1042:
	s_or_b64 exec, exec, s[34:35]
	v_or_b32_e32 v82, 48, v130
	v_ashrrev_i32_e32 v83, 31, v82
	s_waitcnt lgkmcnt(0)
	v_mov_b64_e32 v[34:35], s[14:15]
	v_lshlrev_b64 v[36:37], 13, v[82:83]
	v_mad_i64_i32 v[34:35], s[34:35], v82, s65, v[34:35]
	v_lshl_add_u64 v[36:37], s[0:1], 0, v[36:37]
	v_lshl_add_u64 v[34:35], v[34:35], 0, v[166:167]
	v_lshl_add_u64 v[36:37], v[36:37], 0, v[166:167]
	global_load_dwordx4 v[46:49], v[34:35], off
	global_load_dwordx4 v[38:41], v[34:35], off offset:256
	global_load_dwordx4 v[42:45], v[36:37], off
	s_nop 0
	global_load_dwordx4 v[34:37], v[36:37], off offset:256
	v_cvt_f32_i32_e32 v33, v33
	v_cvt_f32_i32_e32 v32, v32
	v_pk_mul_f32 v[86:87], v[168:169], v[68:69] op_sel_hi:[0,1]
	v_cvt_f32_i32_e32 v31, v31
	v_cvt_f32_i32_e32 v30, v30
	v_pk_mul_f32 v[32:33], v[86:87], v[32:33]
	s_waitcnt vmcnt(9)
	v_lshlrev_b32_e32 v86, 16, v78
	v_and_b32_e32 v78, 0xffff0000, v78
	v_mul_f32_e32 v86, 0xbfb8aa3b, v86
	v_mul_f32_e32 v78, 0xbfb8aa3b, v78
	v_exp_f32_e32 v86, v86
	v_exp_f32_e32 v87, v78
	v_pk_mul_f32 v[88:89], v[168:169], v[66:67] op_sel_hi:[0,1]
	v_pk_mul_f32 v[30:31], v[88:89], v[30:31]
	v_add_f32_e32 v78, 1.0, v86
	v_add_f32_e32 v86, 1.0, v87
	v_lshlrev_b32_e32 v87, 16, v79
	v_and_b32_e32 v79, 0xffff0000, v79
	v_mul_f32_e32 v87, 0xbfb8aa3b, v87
	v_mul_f32_e32 v79, 0xbfb8aa3b, v79
	v_exp_f32_e32 v87, v87
	v_exp_f32_e32 v88, v79
	v_rcp_f32_e32 v79, v86
	v_cvt_f32_i32_e32 v29, v29
	v_add_f32_e32 v86, 1.0, v87
	v_add_f32_e32 v87, 1.0, v88
	v_lshlrev_b32_e32 v88, 16, v80
	v_and_b32_e32 v80, 0xffff0000, v80
	v_mul_f32_e32 v88, 0xbfb8aa3b, v88
	v_mul_f32_e32 v80, 0xbfb8aa3b, v80
	v_exp_f32_e32 v88, v88
	v_exp_f32_e32 v89, v80
	v_cvt_f32_i32_e32 v28, v28
	v_pk_mul_f32 v[90:91], v[168:169], v[64:65] op_sel_hi:[0,1]
	v_add_f32_e32 v80, 1.0, v88
	v_add_f32_e32 v88, 1.0, v89
	v_lshlrev_b32_e32 v89, 16, v81
	v_and_b32_e32 v81, 0xffff0000, v81
	v_mul_f32_e32 v89, 0xbfb8aa3b, v89
	v_mul_f32_e32 v81, 0xbfb8aa3b, v81
	v_pk_mul_f32 v[28:29], v[90:91], v[28:29]
	v_exp_f32_e32 v89, v89
	v_exp_f32_e32 v90, v81
	v_cvt_f32_i32_e32 v27, v27
	v_cvt_f32_i32_e32 v26, v26
	v_rcp_f32_e32 v78, v78
	v_rcp_f32_e32 v86, v86
	v_rcp_f32_e32 v87, v87
	v_rcp_f32_e32 v81, v88
	v_add_f32_e32 v88, 1.0, v89
	v_add_f32_e32 v89, 1.0, v90
	v_rcp_f32_e32 v80, v80
	v_rcp_f32_e32 v88, v88
	v_rcp_f32_e32 v89, v89
	v_pk_mul_f32 v[92:93], v[168:169], v[62:63] op_sel_hi:[0,1]
	s_waitcnt vmcnt(7)
	v_lshlrev_b32_e32 v90, 16, v74
	v_and_b32_e32 v91, 0xffff0000, v74
	v_lshlrev_b32_e32 v74, 16, v75
	v_and_b32_e32 v75, 0xffff0000, v75
	v_lshlrev_b64 v[84:85], 12, v[98:99]
	v_pk_mul_f32 v[26:27], v[92:93], v[26:27]
	v_pk_fma_f32 v[32:33], v[32:33], v[86:87], v[74:75]
	v_pk_fma_f32 v[30:31], v[30:31], v[78:79], v[90:91]
	v_lshlrev_b32_e32 v74, 16, v76
	v_and_b32_e32 v75, 0xffff0000, v76
	v_lshlrev_b32_e32 v76, 16, v77
	v_and_b32_e32 v77, 0xffff0000, v77
	v_pk_fma_f32 v[76:77], v[28:29], v[88:89], v[76:77]
	v_pk_fma_f32 v[28:29], v[26:27], v[80:81], v[74:75]
	v_cvt_pk_bf16_f32 v26, v30, v31
	v_lshl_add_u64 v[30:31], v[84:85], 1, s[12:13]
	v_lshl_add_u64 v[30:31], v[30:31], 0, v[166:167]
	v_cvt_pk_bf16_f32 v27, v32, v33
	v_cvt_pk_bf16_f32 v28, v28, v29
	v_cvt_pk_bf16_f32 v29, v76, v77
	global_store_dwordx4 v[30:31], v[26:29], off sc1
	v_lshlrev_b32_e32 v32, 16, v26
	v_max_f32_e64 v32, |v32|, |v32|
	v_and_b32_e32 v26, 0xffff0000, v26
	v_max_f32_e64 v26, |v26|, |v26|
	v_max_f32_e32 v26, v32, v26
	v_lshlrev_b32_e32 v32, 16, v27
	v_and_b32_e32 v27, 0xffff0000, v27
	v_lshlrev_b32_e32 v33, 16, v29
	v_and_b32_e32 v29, 0xffff0000, v29
	v_max_f32_e64 v27, |v27|, |v27|
	v_max_f32_e64 v32, |v32|, |v32|
	v_max_f32_e64 v29, |v29|, |v29|
	v_max_f32_e64 v33, |v33|, |v33|
	v_cvt_f32_i32_e32 v25, v25
	v_cvt_f32_i32_e32 v24, v24
	v_max_f32_e32 v27, v32, v27
	v_lshlrev_b32_e32 v32, 16, v28
	v_and_b32_e32 v28, 0xffff0000, v28
	v_max_f32_e32 v29, v33, v29
	v_cvt_f32_i32_e32 v23, v23
	v_cvt_f32_i32_e32 v22, v22
	v_cvt_f32_i32_e32 v21, v21
	v_cvt_f32_i32_e32 v20, v20
	v_max3_f32 v28, |v32|, |v28|, v29
	v_max3_f32 v76, v26, v27, v28
	v_pk_mul_f32 v[26:27], v[168:169], v[56:57] op_sel_hi:[0,1]
	v_pk_mul_f32 v[28:29], v[168:169], v[54:55] op_sel_hi:[0,1]
	v_pk_mul_f32 v[32:33], v[168:169], v[52:53] op_sel_hi:[0,1]
	v_pk_mul_f32 v[24:25], v[26:27], v[24:25]
	v_lshlrev_b32_e32 v26, 16, v70
	v_and_b32_e32 v27, 0xffff0000, v70
	v_pk_mul_f32 v[22:23], v[28:29], v[22:23]
	v_mul_f32_e32 v26, 0xbfb8aa3b, v26
	v_mul_f32_e32 v27, 0xbfb8aa3b, v27
	v_pk_mul_f32 v[20:21], v[32:33], v[20:21]
	v_lshlrev_b32_e32 v28, 16, v71
	v_and_b32_e32 v29, 0xffff0000, v71
	v_lshlrev_b32_e32 v32, 16, v72
	v_and_b32_e32 v33, 0xffff0000, v72
	v_exp_f32_e32 v26, v26
	v_exp_f32_e32 v27, v27
	v_mul_f32_e32 v28, 0xbfb8aa3b, v28
	v_mul_f32_e32 v29, 0xbfb8aa3b, v29
	v_mul_f32_e32 v32, 0xbfb8aa3b, v32
	v_mul_f32_e32 v33, 0xbfb8aa3b, v33
	v_lshlrev_b32_e32 v70, 16, v73
	v_and_b32_e32 v71, 0xffff0000, v73
	v_exp_f32_e32 v28, v28
	v_exp_f32_e32 v29, v29
	v_exp_f32_e32 v32, v32
	v_exp_f32_e32 v33, v33
	v_mul_f32_e32 v70, 0xbfb8aa3b, v70
	v_mul_f32_e32 v71, 0xbfb8aa3b, v71
	v_exp_f32_e32 v70, v70
	v_exp_f32_e32 v71, v71
	v_add_f32_e32 v26, 1.0, v26
	v_add_f32_e32 v27, 1.0, v27
	v_cvt_f32_i32_e32 v19, v19
	v_cvt_f32_i32_e32 v18, v18
	v_rcp_f32_e32 v26, v26
	v_rcp_f32_e32 v27, v27
	v_add_f32_e32 v28, 1.0, v28
	v_add_f32_e32 v29, 1.0, v29
	v_add_f32_e32 v32, 1.0, v32
	v_add_f32_e32 v33, 1.0, v33
	v_rcp_f32_e32 v28, v28
	v_rcp_f32_e32 v29, v29
	v_rcp_f32_e32 v32, v32
	v_rcp_f32_e32 v33, v33
	v_add_f32_e32 v70, 1.0, v70
	v_add_f32_e32 v71, 1.0, v71
	v_rcp_f32_e32 v70, v70
	v_rcp_f32_e32 v71, v71
	v_pk_mul_f32 v[74:75], v[168:169], v[50:51] op_sel_hi:[0,1]
	s_waitcnt vmcnt(7)
; __device__ __forceinline__ unsigned cvtpk(float lo, float hi) { unsigned r; asm volatile("v_cvt_pk_bf16_f32 %0, %1, %2" : "=v"(r) : "v"(lo), "v"(hi)); return r; }
;     __device__ __forceinline__ void operator()(const f32x4 (&acc)[2][2][4][2], const Unit& u, int wr, int wc, int fr, int fq) const {
;     ...
;                     if (MODE == 2 || MODE == 3) { const u32x4 g = gq[kb & 1][bj];
;                         f32x4 g0 = {sigmoidf_(bflo(g.x)), sigmoidf_(bfhi(g.x)), sigmoidf_(bflo(g.y)), sigmoidf_(bfhi(g.y))};
;                         f32x4 g1 = {sigmoidf_(bflo(g.z)), sigmoidf_(bfhi(g.z)), sigmoidf_(bflo(g.w)), sigmoidf_(bfhi(g.w))};
;                         v0 = v0 * g0; v1 = v1 * g1;
;                         if (MODE == 3) { const u32x4 q = aq[kb & 1][bj];
;                             v0 = v0 + (f32x4){bflo(q.x), bfhi(q.x), bflo(q.y), bfhi(q.y)}; v1 = v1 + (f32x4){bflo(q.z), bfhi(q.z), bflo(q.w), bfhi(q.w)}; } }
;                     if (MODE == 4) { v0 = v0 + rs[kb & 1][bj][0]; v1 = v1 + rs[kb & 1][bj][1]; }
;                     if (MODE == 5) { const u32x4 c = gq[kb & 1][bj], q = aq[kb & 1][bj];
;                         v0 = (f32x4){bflo(c.x) + sigmoidf_(v0[0]) * bflo(q.x), bfhi(c.x) + sigmoidf_(v0[1]) * bfhi(q.x), bflo(c.y) + sigmoidf_(v0[2]) * bflo(q.y), bfhi(c.y) + sigmoidf_(v0[3]) * bfhi(q.y)};
;                         v1 = (f32x4){bflo(c.z) + sigmoidf_(v1[0]) * bflo(q.z), bfhi(c.z) + sigmoidf_(v1[1]) * bfhi(q.z), bflo(c.w) + sigmoidf_(v1[2]) * bflo(q.w), bfhi(c.w) + sigmoidf_(v1[3]) * bfhi(q.w)}; }
;                     u32x4 w; w.x = cvtpk(v0[0], v0[1]); w.y = cvtpk(v0[2], v0[3]); w.z = cvtpk(v1[0], v1[1]); w.w = cvtpk(v1[2], v1[3]);
;                     *(u32x4*)(O + (size_t)row * ldo + col) = w;
;                     if (MODE == 0) { if (dual) { const int kc = col - ZC_KV;
;                         *(u32x4*)((bf16_t*)aux + (size_t)((kc >> 7) * 512 + (row >> 4)) * 2048 + (row & 15) * 128 + (kc & 127)) = w; } }
;                     if (RMAX) rmx = fmaxf(rmx, fmaxf(fmaxf(fmaxf(fabsf(bflo(w.x)), fabsf(bfhi(w.x))), fmaxf(fabsf(bflo(w.y)), fabsf(bfhi(w.y)))), fmaxf(fmaxf(fabsf(bflo(w.z)), fabsf(bfhi(w.z))), fmaxf(fabsf(bflo(w.w)), fabsf(bfhi(w.w)))))); }
;                 if (RMAX) { rmx = fmaxf(rmx, __shfl_xor(rmx, 16)); rmx = fmaxf(rmx, __shfl_xor(rmx, 32)); if (fq == 0) atomicMax(rowmax + row, __float_as_uint(rmx)); } } }
	v_lshlrev_b32_e32 v72, 16, v58
	v_and_b32_e32 v73, 0xffff0000, v58
	v_pk_mul_f32 v[18:19], v[74:75], v[18:19]
	v_lshlrev_b32_e32 v58, 16, v59
	v_and_b32_e32 v59, 0xffff0000, v59
	v_pk_fma_f32 v[22:23], v[22:23], v[26:27], v[72:73]
	v_lshlrev_b32_e32 v26, 16, v60
	v_and_b32_e32 v27, 0xffff0000, v60
	v_pk_fma_f32 v[24:25], v[24:25], v[28:29], v[58:59]
	v_lshlrev_b32_e32 v28, 16, v61
	v_and_b32_e32 v29, 0xffff0000, v61
	v_pk_fma_f32 v[18:19], v[18:19], v[32:33], v[26:27]
	v_pk_fma_f32 v[28:29], v[20:21], v[70:71], v[28:29]
	v_cvt_pk_bf16_f32 v20, v22, v23
	v_cvt_pk_bf16_f32 v21, v24, v25
	v_cvt_pk_bf16_f32 v22, v18, v19
	s_nop 0
	v_lshlrev_b32_e32 v18, 16, v20
	v_and_b32_e32 v19, 0xffff0000, v20
	v_max_f32_e64 v19, |v19|, |v19|
	v_max_f32_e64 v18, |v18|, |v18|
	v_cvt_pk_bf16_f32 v23, v28, v29
	v_max_f32_e32 v18, v18, v19
	v_lshlrev_b32_e32 v19, 16, v21
	v_and_b32_e32 v24, 0xffff0000, v21
	v_lshlrev_b32_e32 v26, 16, v23
	v_and_b32_e32 v27, 0xffff0000, v23
	v_max_f32_e64 v24, |v24|, |v24|
	v_max_f32_e64 v19, |v19|, |v19|
	v_max_f32_e64 v27, |v27|, |v27|
	v_max_f32_e64 v26, |v26|, |v26|
	v_max_f32_e32 v19, v19, v24
	v_lshlrev_b32_e32 v24, 16, v22
	v_and_b32_e32 v25, 0xffff0000, v22
	v_max_f32_e32 v26, v26, v27
	v_max3_f32 v24, |v24|, |v25|, v26
	v_max3_f32 v18, v18, v19, v24
	v_max3_f32 v18, v76, 0, v18
	ds_bpermute_b32 v19, v165, v18
	global_store_dwordx4 v[30:31], v[20:23], off offset:256 sc1
	s_waitcnt lgkmcnt(0)
	v_max_f32_e32 v19, v19, v19
	v_max_f32_e32 v18, v18, v19
	ds_bpermute_b32 v19, v169, v18
	s_and_saveexec_b64 s[34:35], s[6:7]
	s_cbranch_execz .LBB0_1044
	s_waitcnt lgkmcnt(0)
	v_max_f32_e32 v19, v19, v19
	v_max_f32_e32 v18, v18, v18
	v_lshl_add_u64 v[20:21], v[98:99], 2, s[16:17]
	v_max_f32_e32 v18, v18, v19
	global_atomic_umax v[20:21], v18, off
;     __device__ __forceinline__ void operator()(const f32x4 (&acc)[2][2][4][2], const Unit& u, int wr, int wc, int fr, int fq) const {
;     ...
;             { const int row = row0 + ai * HALF + m * 16; float rmx = 0.f;
; #pragma unroll
;                 for (int bj = 0; bj < 2; ++bj) { const int col = col0 + bj * HALF; f32x4 v0 = acc[ai][bj][m][0], v1 = acc[ai][bj][m][1];
;                     if (QI8) { const f32x4 c0 = cb[bj][0] * ra[ai][m], c1 = cb[bj][1] * ra[ai][m]; const i32x4 i0 = __builtin_bit_cast(i32x4, v0), i1 = __builtin_bit_cast(i32x4, v1);
;                         v0 = (f32x4){(float)i0[0], (float)i0[1], (float)i0[2], (float)i0[3]} * c0; v1 = (f32x4){(float)i1[0], (float)i1[1], (float)i1[2], (float)i1[3]} * c1; }
;                     else if (MODE == 0) { v0 = v0 * tsc; v1 = v1 * tsc; }
;                     if (!QI8 && MODE == 1) { v0 = v0 * cb[bj][0]; v1 = v1 * cb[bj][1]; }
;                     if (MODE == 2 || MODE == 3) { const u32x4 g = gq[kb & 1][bj];
;                         f32x4 g0 = {sigmoidf_(bflo(g.x)), sigmoidf_(bfhi(g.x)), sigmoidf_(bflo(g.y)), sigmoidf_(bfhi(g.y))};
;                         f32x4 g1 = {sigmoidf_(bflo(g.z)), sigmoidf_(bfhi(g.z)), sigmoidf_(bflo(g.w)), sigmoidf_(bfhi(g.w))};
;                         v0 = v0 * g0; v1 = v1 * g1;
;                         if (MODE == 3) { const u32x4 q = aq[kb & 1][bj];
;                             v0 = v0 + (f32x4){bflo(q.x), bfhi(q.x), bflo(q.y), bfhi(q.y)}; v1 = v1 + (f32x4){bflo(q.z), bfhi(q.z), bflo(q.w), bfhi(q.w)}; } }
;                     if (MODE == 4) { v0 = v0 + rs[kb & 1][bj][0]; v1 = v1 + rs[kb & 1][bj][1]; }
;                     if (MODE == 5) { const u32x4 c = gq[kb & 1][bj], q = aq[kb & 1][bj];
;                         v0 = (f32x4){bflo(c.x) + sigmoidf_(v0[0]) * bflo(q.x), bfhi(c.x) + sigmoidf_(v0[1]) * bfhi(q.x), bflo(c.y) + sigmoidf_(v0[2]) * bflo(q.y), bfhi(c.y) + sigmoidf_(v0[3]) * bfhi(q.y)};
;                         v1 = (f32x4){bflo(c.z) + sigmoidf_(v1[0]) * bflo(q.z), bfhi(c.z) + sigmoidf_(v1[1]) * bfhi(q.z), bflo(c.w) + sigmoidf_(v1[2]) * bflo(q.w), bfhi(c.w) + sigmoidf_(v1[3]) * bfhi(q.w)}; }
;                     u32x4 w; w.x = cvtpk(v0[0], v0[1]); w.y = cvtpk(v0[2], v0[3]); w.z = cvtpk(v1[0], v1[1]); w.w = cvtpk(v1[2], v1[3]);
;                     *(u32x4*)(O + (size_t)row * ldo + col) = w;
.LBB0_1044:
	s_or_b64 exec, exec, s[34:35]
	v_cvt_f32_i32_e32 v15, v15
	v_cvt_f32_i32_e32 v14, v14
	v_cvt_f32_i32_e32 v17, v17
	v_cvt_f32_i32_e32 v16, v16
	v_cvt_f32_i32_e32 v11, v11
	v_cvt_f32_i32_e32 v10, v10
	v_cvt_f32_i32_e32 v13, v13
	v_cvt_f32_i32_e32 v12, v12
	v_pk_mul_f32 v[20:21], v[68:69], v[164:165] op_sel_hi:[1,0]
	v_pk_mul_f32 v[22:23], v[66:67], v[164:165] op_sel_hi:[1,0]
	v_pk_mul_f32 v[24:25], v[164:165], v[64:65] op_sel_hi:[0,1]
	v_pk_mul_f32 v[26:27], v[164:165], v[62:63] op_sel_hi:[0,1]
	v_pk_mul_f32 v[14:15], v[22:23], v[14:15]
	v_pk_mul_f32 v[16:17], v[20:21], v[16:17]
	s_waitcnt vmcnt(5)
	v_lshlrev_b32_e32 v20, 16, v46
	v_and_b32_e32 v21, 0xffff0000, v46
	v_lshlrev_b32_e32 v22, 16, v47
	v_and_b32_e32 v23, 0xffff0000, v47
	v_pk_mul_f32 v[10:11], v[26:27], v[10:11]
	v_mul_f32_e32 v20, 0xbfb8aa3b, v20
	v_mul_f32_e32 v21, 0xbfb8aa3b, v21
	v_pk_mul_f32 v[12:13], v[24:25], v[12:13]
	v_mul_f32_e32 v22, 0xbfb8aa3b, v22
	v_mul_f32_e32 v23, 0xbfb8aa3b, v23
	v_lshlrev_b32_e32 v24, 16, v48
	v_and_b32_e32 v25, 0xffff0000, v48
	v_lshlrev_b32_e32 v26, 16, v49
	v_and_b32_e32 v27, 0xffff0000, v49
	v_exp_f32_e32 v20, v20
	v_exp_f32_e32 v21, v21
	v_exp_f32_e32 v22, v22
	v_exp_f32_e32 v23, v23
	v_mul_f32_e32 v24, 0xbfb8aa3b, v24
	v_mul_f32_e32 v25, 0xbfb8aa3b, v25
	v_mul_f32_e32 v26, 0xbfb8aa3b, v26
	v_mul_f32_e32 v27, 0xbfb8aa3b, v27
	v_exp_f32_e32 v24, v24
	v_exp_f32_e32 v25, v25
	v_exp_f32_e32 v26, v26
	v_exp_f32_e32 v27, v27
	v_add_f32_e32 v20, 1.0, v20
	v_add_f32_e32 v21, 1.0, v21
	v_add_f32_e32 v22, 1.0, v22
	v_add_f32_e32 v23, 1.0, v23
	v_rcp_f32_e32 v20, v20
	v_rcp_f32_e32 v21, v21
	v_rcp_f32_e32 v22, v22
	v_rcp_f32_e32 v23, v23
	v_add_f32_e32 v24, 1.0, v24
	v_add_f32_e32 v25, 1.0, v25
	v_add_f32_e32 v26, 1.0, v26
	v_add_f32_e32 v27, 1.0, v27
	v_rcp_f32_e32 v24, v24
	v_rcp_f32_e32 v25, v25
	v_rcp_f32_e32 v26, v26
	v_rcp_f32_e32 v27, v27
	s_waitcnt vmcnt(3)
	v_lshlrev_b32_e32 v28, 16, v42
	v_and_b32_e32 v29, 0xffff0000, v42
	v_lshlrev_b32_e32 v30, 16, v43
	v_and_b32_e32 v31, 0xffff0000, v43
	s_waitcnt lgkmcnt(0)
	v_lshlrev_b64 v[18:19], 12, v[82:83]
	v_pk_fma_f32 v[16:17], v[16:17], v[22:23], v[30:31]
	v_pk_fma_f32 v[14:15], v[14:15], v[20:21], v[28:29]
	v_lshlrev_b32_e32 v20, 16, v44
	v_and_b32_e32 v21, 0xffff0000, v44
	v_lshlrev_b32_e32 v22, 16, v45
	v_and_b32_e32 v23, 0xffff0000, v45
	v_pk_fma_f32 v[22:23], v[12:13], v[26:27], v[22:23]
	v_pk_fma_f32 v[12:13], v[10:11], v[24:25], v[20:21]
	v_cvt_pk_bf16_f32 v10, v14, v15
	v_lshl_add_u64 v[14:15], v[18:19], 1, s[12:13]
	v_lshl_add_u64 v[14:15], v[162:163], 1, v[14:15]
	v_cvt_pk_bf16_f32 v11, v16, v17
	v_cvt_pk_bf16_f32 v12, v12, v13
	v_cvt_pk_bf16_f32 v13, v22, v23
	global_store_dwordx4 v[14:15], v[10:13], off sc1
	v_lshlrev_b32_e32 v16, 16, v10
	v_max_f32_e64 v16, |v16|, |v16|
	v_and_b32_e32 v10, 0xffff0000, v10
	v_max_f32_e64 v10, |v10|, |v10|
	v_max_f32_e32 v10, v16, v10
	v_lshlrev_b32_e32 v16, 16, v11
	v_and_b32_e32 v11, 0xffff0000, v11
	v_lshlrev_b32_e32 v17, 16, v13
	v_and_b32_e32 v13, 0xffff0000, v13
	v_max_f32_e64 v11, |v11|, |v11|
	v_max_f32_e64 v16, |v16|, |v16|
	v_max_f32_e64 v13, |v13|, |v13|
	v_max_f32_e64 v17, |v17|, |v17|
	v_cvt_f32_i32_e32 v9, v9
	v_cvt_f32_i32_e32 v8, v8
	v_max_f32_e32 v11, v16, v11
	v_lshlrev_b32_e32 v16, 16, v12
	v_and_b32_e32 v12, 0xffff0000, v12
	v_max_f32_e32 v13, v17, v13
	v_cvt_f32_i32_e32 v7, v7
	v_cvt_f32_i32_e32 v6, v6
	v_cvt_f32_i32_e32 v5, v5
	v_cvt_f32_i32_e32 v4, v4
	v_max3_f32 v12, |v16|, |v12|, v13
	v_cvt_f32_i32_e32 v3, v3
	v_cvt_f32_i32_e32 v2, v2
	v_max3_f32 v24, v10, v11, v12
	v_pk_mul_f32 v[10:11], v[164:165], v[56:57] op_sel_hi:[0,1]
	v_pk_mul_f32 v[12:13], v[164:165], v[54:55] op_sel_hi:[0,1]
	v_pk_mul_f32 v[16:17], v[164:165], v[52:53] op_sel_hi:[0,1]
	v_pk_mul_f32 v[8:9], v[10:11], v[8:9]
	v_lshlrev_b32_e32 v10, 16, v38
	v_and_b32_e32 v11, 0xffff0000, v38
	v_pk_mul_f32 v[18:19], v[164:165], v[50:51] op_sel_hi:[0,1]
	v_pk_mul_f32 v[6:7], v[12:13], v[6:7]
	v_mul_f32_e32 v10, 0xbfb8aa3b, v10
	v_mul_f32_e32 v11, 0xbfb8aa3b, v11
	v_pk_mul_f32 v[4:5], v[16:17], v[4:5]
	v_lshlrev_b32_e32 v12, 16, v39
	v_and_b32_e32 v13, 0xffff0000, v39
	v_lshlrev_b32_e32 v16, 16, v40
	v_and_b32_e32 v17, 0xffff0000, v40
	v_pk_mul_f32 v[2:3], v[18:19], v[2:3]
	v_exp_f32_e32 v10, v10
	v_exp_f32_e32 v11, v11
	v_mul_f32_e32 v12, 0xbfb8aa3b, v12
	v_mul_f32_e32 v13, 0xbfb8aa3b, v13
	v_mul_f32_e32 v16, 0xbfb8aa3b, v16
	v_mul_f32_e32 v17, 0xbfb8aa3b, v17
	v_lshlrev_b32_e32 v18, 16, v41
	v_and_b32_e32 v19, 0xffff0000, v41
	v_exp_f32_e32 v12, v12
	v_exp_f32_e32 v13, v13
	v_exp_f32_e32 v16, v16
	v_exp_f32_e32 v17, v17
	v_mul_f32_e32 v18, 0xbfb8aa3b, v18
	v_mul_f32_e32 v19, 0xbfb8aa3b, v19
	v_exp_f32_e32 v18, v18
	v_exp_f32_e32 v19, v19
	v_add_f32_e32 v10, 1.0, v10
	v_add_f32_e32 v11, 1.0, v11
	v_rcp_f32_e32 v10, v10
	v_rcp_f32_e32 v11, v11
	v_add_f32_e32 v12, 1.0, v12
	v_add_f32_e32 v13, 1.0, v13
	v_add_f32_e32 v16, 1.0, v16
	v_add_f32_e32 v17, 1.0, v17
	v_rcp_f32_e32 v12, v12
	v_rcp_f32_e32 v13, v13
	v_rcp_f32_e32 v16, v16
	v_rcp_f32_e32 v17, v17
	v_add_f32_e32 v18, 1.0, v18
	v_add_f32_e32 v19, 1.0, v19
	v_rcp_f32_e32 v18, v18
	v_rcp_f32_e32 v19, v19
	s_waitcnt vmcnt(3)
	v_lshlrev_b32_e32 v20, 16, v34
	v_and_b32_e32 v21, 0xffff0000, v34
	v_lshlrev_b32_e32 v22, 16, v35
	v_and_b32_e32 v23, 0xffff0000, v35
	v_pk_fma_f32 v[6:7], v[6:7], v[10:11], v[20:21]
	v_lshlrev_b32_e32 v10, 16, v36
	v_and_b32_e32 v11, 0xffff0000, v36
	v_pk_fma_f32 v[8:9], v[8:9], v[12:13], v[22:23]
	v_lshlrev_b32_e32 v12, 16, v37
	v_and_b32_e32 v13, 0xffff0000, v37
	v_pk_fma_f32 v[2:3], v[2:3], v[16:17], v[10:11]
	v_pk_fma_f32 v[12:13], v[4:5], v[18:19], v[12:13]
	v_cvt_pk_bf16_f32 v4, v6, v7
	v_cvt_pk_bf16_f32 v5, v8, v9
	v_cvt_pk_bf16_f32 v6, v2, v3
	s_nop 0
	v_lshlrev_b32_e32 v2, 16, v4
	v_and_b32_e32 v3, 0xffff0000, v4
	v_max_f32_e64 v3, |v3|, |v3|
	v_max_f32_e64 v2, |v2|, |v2|
	v_cvt_pk_bf16_f32 v7, v12, v13
	v_max_f32_e32 v2, v2, v3
	v_lshlrev_b32_e32 v3, 16, v5
	v_and_b32_e32 v8, 0xffff0000, v5
	v_lshlrev_b32_e32 v10, 16, v7
	v_and_b32_e32 v11, 0xffff0000, v7
	v_max_f32_e64 v8, |v8|, |v8|
	v_max_f32_e64 v3, |v3|, |v3|
	v_max_f32_e64 v11, |v11|, |v11|
	v_max_f32_e64 v10, |v10|, |v10|
	v_max_f32_e32 v3, v3, v8
	v_lshlrev_b32_e32 v8, 16, v6
	v_and_b32_e32 v9, 0xffff0000, v6
	v_max_f32_e32 v10, v10, v11
	v_max3_f32 v8, |v8|, |v9|, v10
	v_max3_f32 v2, v2, v3, v8
	v_max3_f32 v2, v24, 0, v2
	ds_bpermute_b32 v3, v165, v2
	global_store_dwordx4 v[14:15], v[4:7], off offset:256 sc1
	s_waitcnt lgkmcnt(0)
	v_max_f32_e32 v3, v3, v3
	v_max_f32_e32 v2, v2, v3
	ds_bpermute_b32 v3, v169, v2
	s_and_saveexec_b64 s[34:35], s[6:7]
	s_cbranch_execz .LBB0_1046
	s_waitcnt lgkmcnt(0)
	v_max_f32_e32 v3, v3, v3
	v_max_f32_e32 v2, v2, v2
	v_lshl_add_u64 v[4:5], v[82:83], 2, s[16:17]
	v_max_f32_e32 v2, v2, v3
	global_atomic_umax v[4:5], v2, off

; __device__ __forceinline__ float sigmoidf_(float x) { return __builtin_amdgcn_rcpf(1.f + __builtin_amdgcn_exp2f(-1.4426950408889634f * x)); }
;     __device__ __forceinline__ void operator()(const f32x4 (&acc)[2][2][4][2], const Unit& u, int wr, int wc, int fr, int fq) const {
;     ...
;         if (QI8) {
; #pragma unroll
;             for (int ai = 0; ai < 2; ++ai)
; #pragma unroll
;                 for (int m = 0; m < 4; ++m) ra[ai][m] = sa[row0 + ai * HALF + m * 16];
; #pragma unroll
;             for (int bj = 0; bj < 2; ++bj) { cb[bj][0] = *(const f32x4*)(sb + col0 + bj * HALF) * tsc; cb[bj][1] = *(const f32x4*)(sb + col0 + bj * HALF + 4) * tsc; } }
;     ...
;         EPB_LOAD(0);
; #pragma unroll
;         for (int kb = 0; kb < 8; ++kb) { const int ai = kb >> 2, m = kb & 3;
;             if (kb < 7) EPB_LOAD(kb + 1);
;             { const int row = row0 + ai * HALF + m * 16; float rmx = 0.f;
; #pragma unroll
;                 for (int bj = 0; bj < 2; ++bj) { const int col = col0 + bj * HALF; f32x4 v0 = acc[ai][bj][m][0], v1 = acc[ai][bj][m][1];
;                     if (QI8) { const f32x4 c0 = cb[bj][0] * ra[ai][m], c1 = cb[bj][1] * ra[ai][m]; const i32x4 i0 = __builtin_bit_cast(i32x4, v0), i1 = __builtin_bit_cast(i32x4, v1);
;                         v0 = (f32x4){(float)i0[0], (float)i0[1], (float)i0[2], (float)i0[3]} * c0; v1 = (f32x4){(float)i1[0], (float)i1[1], (float)i1[2], (float)i1[3]} * c1; }
;                     else if (MODE == 0) { v0 = v0 * tsc; v1 = v1 * tsc; }
;                     if (!QI8 && MODE == 1) { v0 = v0 * cb[bj][0]; v1 = v1 * cb[bj][1]; }
;                     if (MODE == 2 || MODE == 3) { const u32x4 g = gq[kb & 1][bj];
;                         f32x4 g0 = {sigmoidf_(bflo(g.x)), sigmoidf_(bfhi(g.x)), sigmoidf_(bflo(g.y)), sigmoidf_(bfhi(g.y))};
;                         f32x4 g1 = {sigmoidf_(bflo(g.z)), sigmoidf_(bfhi(g.z)), sigmoidf_(bflo(g.w)), sigmoidf_(bfhi(g.w))};
;                         v0 = v0 * g0; v1 = v1 * g1;
;                         if (MODE == 3) { const u32x4 q = aq[kb & 1][bj];
;                             v0 = v0 + (f32x4){bflo(q.x), bfhi(q.x), bflo(q.y), bfhi(q.y)}; v1 = v1 + (f32x4){bflo(q.z), bfhi(q.z), bflo(q.w), bfhi(q.w)}; } }
;                     if (MODE == 4) { v0 = v0 + rs[kb & 1][bj][0]; v1 = v1 + rs[kb & 1][bj][1]; }
;                     if (MODE == 5) { const u32x4 c = gq[kb & 1][bj], q = aq[kb & 1][bj];
.LBB0_1188:
	v_lshl_add_u32 v146, s26, 8, v1
	v_ashrrev_i32_e32 v147, 31, v146
	v_lshl_or_b32 v182, s58, 8, v224
	v_lshl_add_u64 v[178:179], v[146:147], 2, s[4:5]
	v_ashrrev_i32_e32 v183, 31, v182
	global_load_dword v180, v[178:179], off
	v_lshlrev_b64 v[148:149], 2, v[182:183]
	v_lshlrev_b64 v[150:151], 14, v[146:147]
	v_or_b32_e32 v186, 16, v146
	v_lshl_add_u64 v[110:111], s[8:9], 0, v[148:149]
	v_lshl_add_u64 v[150:151], s[0:1], 0, v[150:151]
	v_ashrrev_i32_e32 v187, 31, v186
	global_load_dwordx4 v[126:129], v[110:111], off nt
	global_load_dwordx4 v[122:125], v[110:111], off offset:16 nt
	global_load_dwordx4 v[106:109], v[110:111], off offset:528 nt
	s_nop 0
	global_load_dwordx4 v[110:113], v[110:111], off offset:512 nt
	v_lshl_add_u64 v[162:163], v[150:151], 0, v[148:149]
	v_lshlrev_b64 v[166:167], 14, v[186:187]
	global_load_dwordx4 v[150:153], v[162:163], off nt
	global_load_dwordx4 v[154:157], v[162:163], off offset:16 nt
	global_load_dwordx4 v[158:161], v[162:163], off offset:512 nt
	s_nop 0
	global_load_dwordx4 v[162:165], v[162:163], off offset:528 nt
	s_nop 0
	global_load_dword v184, v[178:179], off offset:64
	v_lshl_add_u64 v[166:167], s[0:1], 0, v[166:167]
	v_lshl_add_u64 v[174:175], v[166:167], 0, v[148:149]
	global_load_dwordx4 v[166:169], v[174:175], off nt
	global_load_dwordx4 v[170:173], v[174:175], off offset:16 nt
	v_cvt_f32_i32_e32 v189, v143
	v_cvt_f32_i32_e32 v188, v142
	v_cvt_f32_i32_e32 v191, v145
	v_cvt_f32_i32_e32 v190, v144
	global_load_dwordx4 v[142:145], v[174:175], off offset:528 nt
	s_nop 0
	global_load_dwordx4 v[174:177], v[174:175], off offset:512 nt
	v_cvt_f32_i32_e32 v193, v139
	v_cvt_f32_i32_e32 v192, v138
	v_cvt_f32_i32_e32 v213, v141
	v_cvt_f32_i32_e32 v212, v140
	v_cvt_f32_i32_e32 v215, v135
	v_cvt_f32_i32_e32 v214, v134
	v_cvt_f32_i32_e32 v217, v137
	v_cvt_f32_i32_e32 v216, v136
	v_cvt_f32_i32_e32 v219, v131
	v_cvt_f32_i32_e32 v218, v130
	v_cvt_f32_i32_e32 v221, v133
	v_cvt_f32_i32_e32 v220, v132
	v_or_b32_e32 v222, 32, v146
	v_lshlrev_b64 v[228:229], 13, v[146:147]
	v_cvt_f32_i32_e32 v119, v119
	v_cvt_f32_i32_e32 v118, v118
	v_lshlrev_b64 v[130:131], 1, v[182:183]
	v_ashrrev_i32_e32 v223, 31, v222
	global_load_dword v182, v[178:179], off offset:128
	global_load_dword v140, v[178:179], off offset:192
	global_load_dword v138, v[178:179], off offset:512
	global_load_dword v136, v[178:179], off offset:576
	global_load_dword v134, v[178:179], off offset:640
	global_load_dword v132, v[178:179], off offset:704
	v_lshl_add_u64 v[178:179], s[10:11], 0, v[228:229]
	v_cvt_f32_i32_e32 v115, v115
	v_cvt_f32_i32_e32 v117, v117
	v_cvt_f32_i32_e32 v116, v116
	v_cvt_f32_i32_e32 v114, v114
	v_lshlrev_b64 v[228:229], 14, v[222:223]
	v_lshl_add_u64 v[178:179], v[178:179], 0, v[130:131]
	v_lshl_add_u64 v[228:229], s[0:1], 0, v[228:229]
	v_cvt_f32_i32_e32 v121, v121
	v_cvt_f32_i32_e32 v120, v120
	v_lshl_add_u64 v[228:229], v[228:229], 0, v[148:149]
	v_cvt_f32_i32_e32 v103, v103
	v_cvt_f32_i32_e32 v102, v102
	v_cvt_f32_i32_e32 v101, v101
	v_cvt_f32_i32_e32 v100, v100
	v_cvt_f32_i32_e32 v105, v105
	v_cvt_f32_i32_e32 v104, v104
	v_cvt_f32_i32_e32 v99, v99
	v_cvt_f32_i32_e32 v98, v98
	v_cvt_f32_i32_e32 v97, v97
	v_cvt_f32_i32_e32 v96, v96
	v_cvt_f32_i32_e32 v87, v87
	v_cvt_f32_i32_e32 v86, v86
	v_cvt_f32_i32_e32 v89, v89
	v_cvt_f32_i32_e32 v88, v88
	v_cvt_f32_i32_e32 v83, v83
	v_cvt_f32_i32_e32 v85, v85
	v_cvt_f32_i32_e32 v84, v84
	v_cvt_f32_i32_e32 v82, v82
	v_cvt_f32_i32_e32 v79, v79
	v_cvt_f32_i32_e32 v78, v78
	v_cvt_f32_i32_e32 v75, v75
	v_cvt_f32_i32_e32 v77, v77
	v_cvt_f32_i32_e32 v76, v76
	v_cvt_f32_i32_e32 v74, v74
	v_cvt_f32_i32_e32 v81, v81
	v_cvt_f32_i32_e32 v80, v80
	v_cvt_f32_i32_e32 v71, v71
	v_cvt_f32_i32_e32 v70, v70
	v_cvt_f32_i32_e32 v67, v67
	v_cvt_f32_i32_e32 v69, v69
	v_cvt_f32_i32_e32 v68, v68
	v_cvt_f32_i32_e32 v66, v66
	v_cvt_f32_i32_e32 v73, v73
	v_cvt_f32_i32_e32 v72, v72
	v_cvt_f32_i32_e32 v63, v63
	s_waitcnt vmcnt(0)
	v_pk_mul_f32 v[230:231], v[180:181], v[126:127] op_sel_hi:[0,1]
	v_pk_mul_f32 v[232:233], v[180:181], v[128:129] op_sel_hi:[0,1]
	v_pk_mul_f32 v[234:235], v[180:181], v[122:123] op_sel_hi:[0,1]
	v_pk_mul_f32 v[236:237], v[180:181], v[124:125] op_sel_hi:[0,1]
	v_pk_fma_f32 v[152:153], v[232:233], v[190:191], v[152:153]
	v_pk_fma_f32 v[150:151], v[230:231], v[188:189], v[150:151]
	v_pk_mul_f32 v[238:239], v[180:181], v[110:111] op_sel_hi:[0,1]
	v_pk_mul_f32 v[240:241], v[180:181], v[112:113] op_sel_hi:[0,1]
	v_pk_mul_f32 v[242:243], v[180:181], v[106:107] op_sel_hi:[0,1]
	v_pk_mul_f32 v[180:181], v[180:181], v[108:109] op_sel_hi:[0,1]
	v_pk_fma_f32 v[156:157], v[236:237], v[212:213], v[156:157]
	v_pk_fma_f32 v[154:155], v[234:235], v[192:193], v[154:155]
	v_cvt_pk_bf16_f32 v150, v150, v151
	v_cvt_pk_bf16_f32 v151, v152, v153
	v_pk_fma_f32 v[160:161], v[240:241], v[216:217], v[160:161]
	v_cvt_pk_bf16_f32 v152, v154, v155
	v_cvt_pk_bf16_f32 v153, v156, v157
	v_pk_fma_f32 v[158:159], v[238:239], v[214:215], v[158:159]
	v_pk_fma_f32 v[164:165], v[180:181], v[220:221], v[164:165]
	v_pk_fma_f32 v[162:163], v[242:243], v[218:219], v[162:163]
	global_store_dwordx4 v[178:179], v[150:153], off sc1
	v_pk_mul_f32 v[188:189], v[184:185], v[122:123] op_sel_hi:[0,1]
	v_pk_mul_f32 v[190:191], v[184:185], v[124:125] op_sel_hi:[0,1]
	v_cvt_pk_bf16_f32 v150, v158, v159
	v_cvt_pk_bf16_f32 v151, v160, v161
	v_cvt_pk_bf16_f32 v152, v162, v163
	v_cvt_pk_bf16_f32 v153, v164, v165
	global_store_dwordx4 v[178:179], v[150:153], off offset:256 sc1
	v_pk_mul_f32 v[178:179], v[184:185], v[126:127] op_sel_hi:[0,1]
	v_pk_fma_f32 v[118:119], v[178:179], v[118:119], v[166:167]
	global_load_dwordx4 v[150:153], v[228:229], off offset:16 nt
;     __device__ __forceinline__ void operator()(const f32x4 (&acc)[2][2][4][2], const Unit& u, int wr, int wc, int fr, int fq) const {
;     ...
;         EPB_LOAD(0);
; #pragma unroll
;         for (int kb = 0; kb < 8; ++kb) { const int ai = kb >> 2, m = kb & 3;
;             if (kb < 7) EPB_LOAD(kb + 1);
;             { const int row = row0 + ai * HALF + m * 16; float rmx = 0.f;
; #pragma unroll
;                 for (int bj = 0; bj < 2; ++bj) { const int col = col0 + bj * HALF; f32x4 v0 = acc[ai][bj][m][0], v1 = acc[ai][bj][m][1];
;                     if (QI8) { const f32x4 c0 = cb[bj][0] * ra[ai][m], c1 = cb[bj][1] * ra[ai][m]; const i32x4 i0 = __builtin_bit_cast(i32x4, v0), i1 = __builtin_bit_cast(i32x4, v1);
;                         v0 = (f32x4){(float)i0[0], (float)i0[1], (float)i0[2], (float)i0[3]} * c0; v1 = (f32x4){(float)i1[0], (float)i1[1], (float)i1[2], (float)i1[3]} * c1; }
;                     else if (MODE == 0) { v0 = v0 * tsc; v1 = v1 * tsc; }
;                     if (!QI8 && MODE == 1) { v0 = v0 * cb[bj][0]; v1 = v1 * cb[bj][1]; }
;                     if (MODE == 2 || MODE == 3) { const u32x4 g = gq[kb & 1][bj];
;                         f32x4 g0 = {sigmoidf_(bflo(g.x)), sigmoidf_(bfhi(g.x)), sigmoidf_(bflo(g.y)), sigmoidf_(bfhi(g.y))};
;                         f32x4 g1 = {sigmoidf_(bflo(g.z)), sigmoidf_(bfhi(g.z)), sigmoidf_(bflo(g.w)), sigmoidf_(bfhi(g.w))};
;                         v0 = v0 * g0; v1 = v1 * g1;
;                         if (MODE == 3) { const u32x4 q = aq[kb & 1][bj];
;                             v0 = v0 + (f32x4){bflo(q.x), bfhi(q.x), bflo(q.y), bfhi(q.y)}; v1 = v1 + (f32x4){bflo(q.z), bfhi(q.z), bflo(q.w), bfhi(q.w)}; } }
;                     if (MODE == 4) { v0 = v0 + rs[kb & 1][bj][0]; v1 = v1 + rs[kb & 1][bj][1]; }
;                     if (MODE == 5) { const u32x4 c = gq[kb & 1][bj], q = aq[kb & 1][bj];
;                         v0 = (f32x4){bflo(c.x) + sigmoidf_(v0[0]) * bflo(q.x), bfhi(c.x) + sigmoidf_(v0[1]) * bfhi(q.x), bflo(c.y) + sigmoidf_(v0[2]) * bflo(q.y), bfhi(c.y) + sigmoidf_(v0[3]) * bfhi(q.y)};
;                         v1 = (f32x4){bflo(c.z) + sigmoidf_(v1[0]) * bflo(q.z), bfhi(c.z) + sigmoidf_(v1[1]) * bfhi(q.z), bflo(c.w) + sigmoidf_(v1[2]) * bflo(q.w), bfhi(c.w) + sigmoidf_(v1[3]) * bfhi(q.w)}; }
	global_load_dwordx4 v[154:157], v[228:229], off nt
	global_load_dwordx4 v[158:161], v[228:229], off offset:528 nt
	global_load_dwordx4 v[162:165], v[228:229], off offset:512 nt
	v_pk_fma_f32 v[166:167], v[190:191], v[116:117], v[172:173]
	v_pk_fma_f32 v[116:117], v[188:189], v[114:115], v[170:171]
	v_cvt_pk_bf16_f32 v114, v118, v119
	v_lshlrev_b64 v[118:119], 13, v[186:187]
	v_pk_mul_f32 v[180:181], v[184:185], v[128:129] op_sel_hi:[0,1]
	v_lshl_add_u64 v[118:119], s[10:11], 0, v[118:119]
	v_pk_fma_f32 v[120:121], v[180:181], v[120:121], v[168:169]
	v_lshl_add_u64 v[118:119], v[118:119], 0, v[130:131]
	v_cvt_pk_bf16_f32 v115, v120, v121
	v_cvt_pk_bf16_f32 v116, v116, v117
	v_cvt_pk_bf16_f32 v117, v166, v167
	global_store_dwordx4 v[118:119], v[114:117], off sc1
	v_pk_mul_f32 v[166:167], v[184:185], v[108:109] op_sel_hi:[0,1]
	v_pk_mul_f32 v[120:121], v[184:185], v[106:107] op_sel_hi:[0,1]
	v_pk_mul_f32 v[114:115], v[184:185], v[110:111] op_sel_hi:[0,1]
	v_pk_mul_f32 v[116:117], v[184:185], v[112:113] op_sel_hi:[0,1]
	v_pk_fma_f32 v[102:103], v[114:115], v[102:103], v[174:175]
	v_pk_fma_f32 v[114:115], v[166:167], v[100:101], v[144:145]
	v_or_b32_e32 v166, 48, v146
	v_pk_fma_f32 v[104:105], v[116:117], v[104:105], v[176:177]
	v_pk_fma_f32 v[100:101], v[120:121], v[98:99], v[142:143]
	v_cvt_pk_bf16_f32 v98, v102, v103
	v_cvt_pk_bf16_f32 v99, v104, v105
	v_ashrrev_i32_e32 v167, 31, v166
	v_cvt_pk_bf16_f32 v100, v100, v101
	v_cvt_pk_bf16_f32 v101, v114, v115
	global_store_dwordx4 v[118:119], v[98:101], off offset:256 sc1
	v_cvt_f32_i32_e32 v119, v95
	v_cvt_f32_i32_e32 v118, v94
	v_lshlrev_b64 v[98:99], 14, v[166:167]
	v_lshl_add_u64 v[98:99], s[0:1], 0, v[98:99]
	v_lshl_add_u64 v[114:115], v[98:99], 0, v[148:149]
	global_load_dwordx4 v[98:101], v[114:115], off nt
	global_load_dwordx4 v[102:105], v[114:115], off offset:16 nt
	v_cvt_f32_i32_e32 v143, v93
	v_cvt_f32_i32_e32 v142, v92
	global_load_dwordx4 v[92:95], v[114:115], off offset:528 nt
	s_nop 0
	global_load_dwordx4 v[114:117], v[114:115], off offset:512 nt
	v_cvt_f32_i32_e32 v121, v91
	v_cvt_f32_i32_e32 v120, v90
	v_lshlrev_b64 v[144:145], 13, v[222:223]
	v_pk_mul_f32 v[168:169], v[182:183], v[126:127] op_sel_hi:[0,1]
	v_lshl_add_u64 v[144:145], s[10:11], 0, v[144:145]
	v_pk_mul_f32 v[170:171], v[182:183], v[128:129] op_sel_hi:[0,1]
	v_pk_mul_f32 v[172:173], v[182:183], v[122:123] op_sel_hi:[0,1]
	v_lshl_add_u64 v[144:145], v[144:145], 0, v[130:131]
	v_pk_mul_f32 v[174:175], v[182:183], v[124:125] op_sel_hi:[0,1]
	v_add_u32_e32 v90, 0x80, v146
	v_pk_mul_f32 v[176:177], v[182:183], v[110:111] op_sel_hi:[0,1]
	v_pk_mul_f32 v[178:179], v[182:183], v[112:113] op_sel_hi:[0,1]
	v_ashrrev_i32_e32 v91, 31, v90
	v_cvt_f32_i32_e32 v62, v62
	v_cvt_f32_i32_e32 v59, v59
	v_cvt_f32_i32_e32 v61, v61
	v_cvt_f32_i32_e32 v60, v60
	v_cvt_f32_i32_e32 v58, v58
	v_cvt_f32_i32_e32 v65, v65
	v_cvt_f32_i32_e32 v64, v64
	v_cvt_f32_i32_e32 v55, v55
	v_cvt_f32_i32_e32 v54, v54
	v_cvt_f32_i32_e32 v53, v53
	v_cvt_f32_i32_e32 v52, v52
	v_cvt_f32_i32_e32 v57, v57
	v_cvt_f32_i32_e32 v56, v56
	v_cvt_f32_i32_e32 v51, v51
	v_cvt_f32_i32_e32 v50, v50
	v_cvt_f32_i32_e32 v47, v47
	v_cvt_f32_i32_e32 v46, v46
	v_cvt_f32_i32_e32 v43, v43
	v_cvt_f32_i32_e32 v45, v45
	v_cvt_f32_i32_e32 v44, v44
	v_cvt_f32_i32_e32 v42, v42
	v_cvt_f32_i32_e32 v49, v49
	v_cvt_f32_i32_e32 v48, v48
	v_cvt_f32_i32_e32 v39, v39
	v_cvt_f32_i32_e32 v38, v38
	v_cvt_f32_i32_e32 v37, v37
	v_cvt_f32_i32_e32 v36, v36
	s_waitcnt vmcnt(9)
	v_pk_fma_f32 v[120:121], v[172:173], v[120:121], v[150:151]
	s_waitcnt vmcnt(8)
	v_pk_fma_f32 v[118:119], v[168:169], v[118:119], v[154:155]
	v_pk_fma_f32 v[96:97], v[170:171], v[96:97], v[156:157]
	v_cvt_pk_bf16_f32 v118, v118, v119
	v_pk_fma_f32 v[142:143], v[174:175], v[142:143], v[152:153]
	v_cvt_pk_bf16_f32 v119, v96, v97
	v_cvt_pk_bf16_f32 v120, v120, v121
	v_pk_mul_f32 v[96:97], v[182:183], v[106:107] op_sel_hi:[0,1]
	v_cvt_pk_bf16_f32 v121, v142, v143
	global_store_dwordx4 v[144:145], v[118:121], off sc1
	s_waitcnt vmcnt(7)
	v_pk_fma_f32 v[88:89], v[178:179], v[88:89], v[164:165]
	v_pk_fma_f32 v[86:87], v[176:177], v[86:87], v[162:163]
	v_pk_mul_f32 v[118:119], v[182:183], v[108:109] op_sel_hi:[0,1]
	v_pk_fma_f32 v[118:119], v[118:119], v[84:85], v[160:161]
	v_pk_fma_f32 v[84:85], v[96:97], v[82:83], v[158:159]
	v_cvt_pk_bf16_f32 v82, v86, v87
	v_cvt_pk_bf16_f32 v83, v88, v89
	v_pk_mul_f32 v[152:153], v[140:141], v[122:123] op_sel_hi:[0,1]
	v_cvt_pk_bf16_f32 v84, v84, v85
	v_cvt_pk_bf16_f32 v85, v118, v119
	global_store_dwordx4 v[144:145], v[82:85], off offset:256 sc1
	v_pk_mul_f32 v[154:155], v[140:141], v[124:125] op_sel_hi:[0,1]
	v_pk_mul_f32 v[150:151], v[140:141], v[128:129] op_sel_hi:[0,1]
	v_lshlrev_b64 v[82:83], 14, v[90:91]
	v_lshl_add_u64 v[82:83], s[0:1], 0, v[82:83]
	v_lshl_add_u64 v[96:97], v[82:83], 0, v[148:149]
	global_load_dwordx4 v[82:85], v[96:97], off nt
	global_load_dwordx4 v[86:89], v[96:97], off offset:16 nt
	global_load_dwordx4 v[118:121], v[96:97], off offset:528 nt
	global_load_dwordx4 v[142:145], v[96:97], off offset:512 nt
	v_pk_mul_f32 v[96:97], v[140:141], v[126:127] op_sel_hi:[0,1]
	v_cvt_f32_i32_e32 v41, v41
	v_cvt_f32_i32_e32 v40, v40
	v_cvt_f32_i32_e32 v35, v35
	v_cvt_f32_i32_e32 v34, v34
	v_cvt_f32_i32_e32 v31, v31
	v_cvt_f32_i32_e32 v30, v30
	v_cvt_f32_i32_e32 v27, v27
	s_waitcnt vmcnt(9)
	v_pk_fma_f32 v[78:79], v[96:97], v[78:79], v[98:99]
	s_waitcnt vmcnt(8)
;     __device__ __forceinline__ void operator()(const f32x4 (&acc)[2][2][4][2], const Unit& u, int wr, int wc, int fr, int fq) const {
;     ...
;         EPB_LOAD(0);
; #pragma unroll
;         for (int kb = 0; kb < 8; ++kb) { const int ai = kb >> 2, m = kb & 3;
;             if (kb < 7) EPB_LOAD(kb + 1);
;             { const int row = row0 + ai * HALF + m * 16; float rmx = 0.f;
; #pragma unroll
;                 for (int bj = 0; bj < 2; ++bj) { const int col = col0 + bj * HALF; f32x4 v0 = acc[ai][bj][m][0], v1 = acc[ai][bj][m][1];
;                     if (QI8) { const f32x4 c0 = cb[bj][0] * ra[ai][m], c1 = cb[bj][1] * ra[ai][m]; const i32x4 i0 = __builtin_bit_cast(i32x4, v0), i1 = __builtin_bit_cast(i32x4, v1);
;                         v0 = (f32x4){(float)i0[0], (float)i0[1], (float)i0[2], (float)i0[3]} * c0; v1 = (f32x4){(float)i1[0], (float)i1[1], (float)i1[2], (float)i1[3]} * c1; }
;                     else if (MODE == 0) { v0 = v0 * tsc; v1 = v1 * tsc; }
;                     if (!QI8 && MODE == 1) { v0 = v0 * cb[bj][0]; v1 = v1 * cb[bj][1]; }
;                     if (MODE == 2 || MODE == 3) { const u32x4 g = gq[kb & 1][bj];
;                         f32x4 g0 = {sigmoidf_(bflo(g.x)), sigmoidf_(bfhi(g.x)), sigmoidf_(bflo(g.y)), sigmoidf_(bfhi(g.y))};
;                         f32x4 g1 = {sigmoidf_(bflo(g.z)), sigmoidf_(bfhi(g.z)), sigmoidf_(bflo(g.w)), sigmoidf_(bfhi(g.w))};
;                         v0 = v0 * g0; v1 = v1 * g1;
;                         if (MODE == 3) { const u32x4 q = aq[kb & 1][bj];
;                             v0 = v0 + (f32x4){bflo(q.x), bfhi(q.x), bflo(q.y), bfhi(q.y)}; v1 = v1 + (f32x4){bflo(q.z), bfhi(q.z), bflo(q.w), bfhi(q.w)}; } }
;                     if (MODE == 4) { v0 = v0 + rs[kb & 1][bj][0]; v1 = v1 + rs[kb & 1][bj][1]; }
;                     if (MODE == 5) { const u32x4 c = gq[kb & 1][bj], q = aq[kb & 1][bj];
;                         v0 = (f32x4){bflo(c.x) + sigmoidf_(v0[0]) * bflo(q.x), bfhi(c.x) + sigmoidf_(v0[1]) * bfhi(q.x), bflo(c.y) + sigmoidf_(v0[2]) * bflo(q.y), bfhi(c.y) + sigmoidf_(v0[3]) * bfhi(q.y)};
;                         v1 = (f32x4){bflo(c.z) + sigmoidf_(v1[0]) * bflo(q.z), bfhi(c.z) + sigmoidf_(v1[1]) * bfhi(q.z), bflo(c.w) + sigmoidf_(v1[2]) * bflo(q.w), bfhi(c.w) + sigmoidf_(v1[3]) * bfhi(q.w)}; }
	v_pk_fma_f32 v[96:97], v[154:155], v[76:77], v[104:105]
	v_pk_fma_f32 v[76:77], v[152:153], v[74:75], v[102:103]
	v_cvt_pk_bf16_f32 v74, v78, v79
	v_lshlrev_b64 v[78:79], 13, v[166:167]
	v_lshl_add_u64 v[78:79], s[10:11], 0, v[78:79]
	v_pk_fma_f32 v[80:81], v[150:151], v[80:81], v[100:101]
	v_lshl_add_u64 v[78:79], v[78:79], 0, v[130:131]
	v_cvt_pk_bf16_f32 v75, v80, v81
	v_cvt_pk_bf16_f32 v76, v76, v77
	v_cvt_pk_bf16_f32 v77, v96, v97
	global_store_dwordx4 v[78:79], v[74:77], off sc1
	v_pk_mul_f32 v[80:81], v[140:141], v[106:107] op_sel_hi:[0,1]
	v_pk_mul_f32 v[96:97], v[140:141], v[108:109] op_sel_hi:[0,1]
	v_pk_mul_f32 v[74:75], v[140:141], v[110:111] op_sel_hi:[0,1]
	v_pk_mul_f32 v[76:77], v[140:141], v[112:113] op_sel_hi:[0,1]
	s_waitcnt vmcnt(7)
	v_pk_fma_f32 v[70:71], v[74:75], v[70:71], v[114:115]
	v_pk_fma_f32 v[74:75], v[96:97], v[68:69], v[94:95]
	v_pk_fma_f32 v[68:69], v[80:81], v[66:67], v[92:93]
	v_add_u32_e32 v92, 0x90, v146
	v_pk_fma_f32 v[72:73], v[76:77], v[72:73], v[116:117]
	v_cvt_pk_bf16_f32 v66, v70, v71
	v_ashrrev_i32_e32 v93, 31, v92
	v_cvt_pk_bf16_f32 v67, v72, v73
	v_cvt_pk_bf16_f32 v68, v68, v69
	v_cvt_pk_bf16_f32 v69, v74, v75
	global_store_dwordx4 v[78:79], v[66:69], off offset:256 sc1
	v_pk_mul_f32 v[94:95], v[138:139], v[126:127] op_sel_hi:[0,1]
	v_pk_mul_f32 v[98:99], v[138:139], v[122:123] op_sel_hi:[0,1]
	v_lshlrev_b64 v[66:67], 14, v[92:93]
	v_lshl_add_u64 v[66:67], s[0:1], 0, v[66:67]
	v_lshl_add_u64 v[78:79], v[66:67], 0, v[148:149]
	global_load_dwordx4 v[66:69], v[78:79], off nt
	global_load_dwordx4 v[70:73], v[78:79], off offset:16 nt
	global_load_dwordx4 v[74:77], v[78:79], off offset:528 nt
	s_nop 0
	global_load_dwordx4 v[78:81], v[78:79], off offset:512 nt
	v_pk_mul_f32 v[100:101], v[138:139], v[124:125] op_sel_hi:[0,1]
	v_pk_mul_f32 v[96:97], v[138:139], v[128:129] op_sel_hi:[0,1]
	v_cvt_f32_i32_e32 v29, v29
	v_cvt_f32_i32_e32 v28, v28
	v_cvt_f32_i32_e32 v26, v26
	v_cvt_f32_i32_e32 v33, v33
	v_cvt_f32_i32_e32 v32, v32
	v_cvt_f32_i32_e32 v23, v23
	v_cvt_f32_i32_e32 v22, v22
	v_cvt_f32_i32_e32 v25, v25
	v_cvt_f32_i32_e32 v24, v24
	v_cvt_f32_i32_e32 v19, v19
	v_cvt_f32_i32_e32 v21, v21
	v_cvt_f32_i32_e32 v20, v20
	v_cvt_f32_i32_e32 v18, v18
	v_cvt_f32_i32_e32 v15, v15
	v_cvt_f32_i32_e32 v14, v14
	v_cvt_f32_i32_e32 v11, v11
	v_cvt_f32_i32_e32 v13, v13
	v_cvt_f32_i32_e32 v12, v12
	v_cvt_f32_i32_e32 v10, v10
	v_cvt_f32_i32_e32 v17, v17
	v_cvt_f32_i32_e32 v16, v16
	v_cvt_f32_i32_e32 v7, v7
	v_cvt_f32_i32_e32 v6, v6
	v_cvt_f32_i32_e32 v3, v3
	v_cvt_f32_i32_e32 v5, v5
	v_cvt_f32_i32_e32 v4, v4
	v_cvt_f32_i32_e32 v2, v2
	v_cvt_f32_i32_e32 v9, v9
	v_cvt_f32_i32_e32 v8, v8
	s_andn2_b64 vcc, exec, s[6:7]
	s_mov_b64 s[6:7], -1
	s_waitcnt vmcnt(9)
	v_pk_fma_f32 v[62:63], v[94:95], v[62:63], v[82:83]
	s_waitcnt vmcnt(8)
	v_pk_fma_f32 v[82:83], v[100:101], v[60:61], v[88:89]
	v_pk_fma_f32 v[60:61], v[98:99], v[58:59], v[86:87]
	v_cvt_pk_bf16_f32 v58, v62, v63
	v_lshlrev_b64 v[62:63], 13, v[90:91]
	v_lshl_add_u64 v[62:63], s[10:11], 0, v[62:63]
	v_pk_fma_f32 v[64:65], v[96:97], v[64:65], v[84:85]
	v_lshl_add_u64 v[62:63], v[62:63], 0, v[130:131]
	v_cvt_pk_bf16_f32 v59, v64, v65
	v_cvt_pk_bf16_f32 v60, v60, v61
	v_cvt_pk_bf16_f32 v61, v82, v83
	global_store_dwordx4 v[62:63], v[58:61], off sc1
	v_pk_mul_f32 v[82:83], v[138:139], v[108:109] op_sel_hi:[0,1]
	v_pk_mul_f32 v[64:65], v[138:139], v[106:107] op_sel_hi:[0,1]
	v_pk_mul_f32 v[58:59], v[138:139], v[110:111] op_sel_hi:[0,1]
	v_pk_mul_f32 v[60:61], v[138:139], v[112:113] op_sel_hi:[0,1]
	s_waitcnt vmcnt(7)
	v_pk_fma_f32 v[54:55], v[58:59], v[54:55], v[142:143]
	v_pk_fma_f32 v[58:59], v[82:83], v[52:53], v[120:121]
	v_add_u32_e32 v82, 0xa0, v146
	v_pk_fma_f32 v[56:57], v[60:61], v[56:57], v[144:145]
	v_pk_fma_f32 v[52:53], v[64:65], v[50:51], v[118:119]
	v_cvt_pk_bf16_f32 v50, v54, v55
	v_cvt_pk_bf16_f32 v51, v56, v57
	v_ashrrev_i32_e32 v83, 31, v82
	v_cvt_pk_bf16_f32 v52, v52, v53
	v_cvt_pk_bf16_f32 v53, v58, v59
	global_store_dwordx4 v[62:63], v[50:53], off offset:256 sc1
	v_pk_mul_f32 v[84:85], v[136:137], v[126:127] op_sel_hi:[0,1]
	v_pk_mul_f32 v[88:89], v[136:137], v[122:123] op_sel_hi:[0,1]
	v_lshlrev_b64 v[50:51], 14, v[82:83]
	v_lshl_add_u64 v[50:51], s[0:1], 0, v[50:51]
	v_lshl_add_u64 v[62:63], v[50:51], 0, v[148:149]
	v_pk_mul_f32 v[90:91], v[136:137], v[124:125] op_sel_hi:[0,1]
	global_load_dwordx4 v[50:53], v[62:63], off offset:16 nt
	global_load_dwordx4 v[54:57], v[62:63], off nt
	global_load_dwordx4 v[58:61], v[62:63], off offset:528 nt
	s_nop 0
	global_load_dwordx4 v[62:65], v[62:63], off offset:512 nt
	v_pk_mul_f32 v[86:87], v[136:137], v[128:129] op_sel_hi:[0,1]
	s_waitcnt vmcnt(9)
	v_pk_fma_f32 v[46:47], v[84:85], v[46:47], v[66:67]
	s_waitcnt vmcnt(8)
;     __device__ __forceinline__ void operator()(const f32x4 (&acc)[2][2][4][2], const Unit& u, int wr, int wc, int fr, int fq) const {
;     ...
;         EPB_LOAD(0);
; #pragma unroll
;         for (int kb = 0; kb < 8; ++kb) { const int ai = kb >> 2, m = kb & 3;
;             if (kb < 7) EPB_LOAD(kb + 1);
;             { const int row = row0 + ai * HALF + m * 16; float rmx = 0.f;
; #pragma unroll
;                 for (int bj = 0; bj < 2; ++bj) { const int col = col0 + bj * HALF; f32x4 v0 = acc[ai][bj][m][0], v1 = acc[ai][bj][m][1];
;                     if (QI8) { const f32x4 c0 = cb[bj][0] * ra[ai][m], c1 = cb[bj][1] * ra[ai][m]; const i32x4 i0 = __builtin_bit_cast(i32x4, v0), i1 = __builtin_bit_cast(i32x4, v1);
;                         v0 = (f32x4){(float)i0[0], (float)i0[1], (float)i0[2], (float)i0[3]} * c0; v1 = (f32x4){(float)i1[0], (float)i1[1], (float)i1[2], (float)i1[3]} * c1; }
;                     else if (MODE == 0) { v0 = v0 * tsc; v1 = v1 * tsc; }
;                     if (!QI8 && MODE == 1) { v0 = v0 * cb[bj][0]; v1 = v1 * cb[bj][1]; }
;                     if (MODE == 2 || MODE == 3) { const u32x4 g = gq[kb & 1][bj];
;                         f32x4 g0 = {sigmoidf_(bflo(g.x)), sigmoidf_(bfhi(g.x)), sigmoidf_(bflo(g.y)), sigmoidf_(bfhi(g.y))};
;                         f32x4 g1 = {sigmoidf_(bflo(g.z)), sigmoidf_(bfhi(g.z)), sigmoidf_(bflo(g.w)), sigmoidf_(bfhi(g.w))};
;                         v0 = v0 * g0; v1 = v1 * g1;
;                         if (MODE == 3) { const u32x4 q = aq[kb & 1][bj];
;                             v0 = v0 + (f32x4){bflo(q.x), bfhi(q.x), bflo(q.y), bfhi(q.y)}; v1 = v1 + (f32x4){bflo(q.z), bfhi(q.z), bflo(q.w), bfhi(q.w)}; } }
;                     if (MODE == 4) { v0 = v0 + rs[kb & 1][bj][0]; v1 = v1 + rs[kb & 1][bj][1]; }
;                     if (MODE == 5) { const u32x4 c = gq[kb & 1][bj], q = aq[kb & 1][bj];
;                         v0 = (f32x4){bflo(c.x) + sigmoidf_(v0[0]) * bflo(q.x), bfhi(c.x) + sigmoidf_(v0[1]) * bfhi(q.x), bflo(c.y) + sigmoidf_(v0[2]) * bflo(q.y), bfhi(c.y) + sigmoidf_(v0[3]) * bfhi(q.y)};
;                         v1 = (f32x4){bflo(c.z) + sigmoidf_(v1[0]) * bflo(q.z), bfhi(c.z) + sigmoidf_(v1[1]) * bfhi(q.z), bflo(c.w) + sigmoidf_(v1[2]) * bflo(q.w), bfhi(c.w) + sigmoidf_(v1[3]) * bfhi(q.w)}; }
	v_pk_fma_f32 v[66:67], v[90:91], v[44:45], v[72:73]
	v_pk_fma_f32 v[44:45], v[88:89], v[42:43], v[70:71]
	v_cvt_pk_bf16_f32 v42, v46, v47
	v_lshlrev_b64 v[46:47], 13, v[92:93]
	v_lshl_add_u64 v[46:47], s[10:11], 0, v[46:47]
	v_pk_fma_f32 v[48:49], v[86:87], v[48:49], v[68:69]
	v_lshl_add_u64 v[46:47], v[46:47], 0, v[130:131]
	v_cvt_pk_bf16_f32 v43, v48, v49
	v_cvt_pk_bf16_f32 v44, v44, v45
	v_cvt_pk_bf16_f32 v45, v66, v67
	global_store_dwordx4 v[46:47], v[42:45], off sc1
	v_pk_mul_f32 v[66:67], v[136:137], v[108:109] op_sel_hi:[0,1]
	v_pk_mul_f32 v[48:49], v[136:137], v[106:107] op_sel_hi:[0,1]
	v_pk_mul_f32 v[42:43], v[136:137], v[110:111] op_sel_hi:[0,1]
	v_pk_mul_f32 v[44:45], v[136:137], v[112:113] op_sel_hi:[0,1]
	s_waitcnt vmcnt(7)
	v_pk_fma_f32 v[38:39], v[42:43], v[38:39], v[78:79]
	v_pk_fma_f32 v[42:43], v[66:67], v[36:37], v[76:77]
	v_add_u32_e32 v66, 0xb0, v146
	v_pk_fma_f32 v[40:41], v[44:45], v[40:41], v[80:81]
	v_pk_fma_f32 v[36:37], v[48:49], v[34:35], v[74:75]
	v_cvt_pk_bf16_f32 v34, v38, v39
	v_cvt_pk_bf16_f32 v35, v40, v41
	v_ashrrev_i32_e32 v67, 31, v66
	v_cvt_pk_bf16_f32 v36, v36, v37
	v_cvt_pk_bf16_f32 v37, v42, v43
	global_store_dwordx4 v[46:47], v[34:37], off offset:256 sc1
	v_pk_mul_f32 v[68:69], v[134:135], v[126:127] op_sel_hi:[0,1]
	v_pk_mul_f32 v[72:73], v[134:135], v[122:123] op_sel_hi:[0,1]
	v_lshlrev_b64 v[34:35], 14, v[66:67]
	v_lshl_add_u64 v[34:35], s[0:1], 0, v[34:35]
	v_lshl_add_u64 v[46:47], v[34:35], 0, v[148:149]
	global_load_dwordx4 v[34:37], v[46:47], off nt
	global_load_dwordx4 v[38:41], v[46:47], off offset:16 nt
	global_load_dwordx4 v[42:45], v[46:47], off offset:528 nt
	s_nop 0
	global_load_dwordx4 v[46:49], v[46:47], off offset:512 nt
	v_pk_mul_f32 v[74:75], v[134:135], v[124:125] op_sel_hi:[0,1]
	v_pk_mul_f32 v[70:71], v[134:135], v[128:129] op_sel_hi:[0,1]
	s_waitcnt vmcnt(9)
	v_pk_fma_f32 v[52:53], v[74:75], v[28:29], v[52:53]
	s_waitcnt vmcnt(8)
	v_pk_fma_f32 v[30:31], v[68:69], v[30:31], v[54:55]
	v_pk_fma_f32 v[28:29], v[72:73], v[26:27], v[50:51]
	v_cvt_pk_bf16_f32 v26, v30, v31
	v_lshlrev_b64 v[30:31], 13, v[82:83]
	v_lshl_add_u64 v[30:31], s[10:11], 0, v[30:31]
	v_pk_fma_f32 v[32:33], v[70:71], v[32:33], v[56:57]
	v_lshl_add_u64 v[30:31], v[30:31], 0, v[130:131]
	v_cvt_pk_bf16_f32 v27, v32, v33
	v_cvt_pk_bf16_f32 v28, v28, v29
	v_cvt_pk_bf16_f32 v29, v52, v53
	global_store_dwordx4 v[30:31], v[26:29], off sc1
	v_pk_mul_f32 v[32:33], v[134:135], v[106:107] op_sel_hi:[0,1]
	v_pk_mul_f32 v[50:51], v[134:135], v[108:109] op_sel_hi:[0,1]
	v_pk_mul_f32 v[26:27], v[134:135], v[110:111] op_sel_hi:[0,1]
	v_pk_mul_f32 v[28:29], v[134:135], v[112:113] op_sel_hi:[0,1]
	s_waitcnt vmcnt(7)
	v_pk_fma_f32 v[24:25], v[28:29], v[24:25], v[64:65]
	v_pk_fma_f32 v[22:23], v[26:27], v[22:23], v[62:63]
	v_pk_fma_f32 v[26:27], v[50:51], v[20:21], v[60:61]
	v_pk_fma_f32 v[20:21], v[32:33], v[18:19], v[58:59]
	v_cvt_pk_bf16_f32 v18, v22, v23
	v_cvt_pk_bf16_f32 v19, v24, v25
	v_pk_mul_f32 v[22:23], v[132:133], v[122:123] op_sel_hi:[0,1]
	v_cvt_pk_bf16_f32 v20, v20, v21
	v_cvt_pk_bf16_f32 v21, v26, v27
	global_store_dwordx4 v[30:31], v[18:21], off offset:256 sc1
	v_pk_mul_f32 v[24:25], v[132:133], v[124:125] op_sel_hi:[0,1]
	s_nop 0
	v_pk_mul_f32 v[18:19], v[126:127], v[132:133] op_sel_hi:[1,0]
	v_pk_mul_f32 v[20:21], v[128:129], v[132:133] op_sel_hi:[1,0]
	s_waitcnt vmcnt(5)
	v_pk_fma_f32 v[14:15], v[18:19], v[14:15], v[34:35]
	s_waitcnt vmcnt(4)
	v_pk_fma_f32 v[18:19], v[24:25], v[12:13], v[40:41]
	v_pk_fma_f32 v[12:13], v[22:23], v[10:11], v[38:39]
	v_cvt_pk_bf16_f32 v10, v14, v15
	v_lshlrev_b64 v[14:15], 13, v[66:67]
	v_lshl_add_u64 v[14:15], s[10:11], 0, v[14:15]
	v_pk_fma_f32 v[16:17], v[20:21], v[16:17], v[36:37]
	v_lshl_add_u64 v[14:15], v[14:15], 0, v[130:131]
	v_cvt_pk_bf16_f32 v11, v16, v17
	v_cvt_pk_bf16_f32 v12, v12, v13
	v_cvt_pk_bf16_f32 v13, v18, v19
	global_store_dwordx4 v[14:15], v[10:13], off sc1
	v_pk_mul_f32 v[16:17], v[132:133], v[106:107] op_sel_hi:[0,1]
	v_pk_mul_f32 v[18:19], v[132:133], v[108:109] op_sel_hi:[0,1]
	v_pk_mul_f32 v[10:11], v[132:133], v[110:111] op_sel_hi:[0,1]
	v_pk_mul_f32 v[12:13], v[132:133], v[112:113] op_sel_hi:[0,1]
	s_waitcnt vmcnt(3)
	v_pk_fma_f32 v[6:7], v[10:11], v[6:7], v[46:47]
	v_pk_fma_f32 v[10:11], v[18:19], v[4:5], v[44:45]
	v_pk_fma_f32 v[4:5], v[16:17], v[2:3], v[42:43]
	v_pk_fma_f32 v[8:9], v[12:13], v[8:9], v[48:49]
	v_cvt_pk_bf16_f32 v2, v6, v7
	s_nop 0
	v_cvt_pk_bf16_f32 v3, v8, v9
	v_cvt_pk_bf16_f32 v4, v4, v5
	v_cvt_pk_bf16_f32 v5, v10, v11
	global_store_dwordx4 v[14:15], v[2:5], off offset:256 sc1
	s_cbranch_vccnz .LBB0_1173
	s_andn2_b64 vcc, exec, s[2:3]
	s_cbranch_vccnz .LBB0_1172
	s_barrier
	s_branch .LBB0_1172

;     __device__ __forceinline__ void operator()(const f32x4 (&acc)[2][2][4][2], const Unit& u, int wr, int wc, int fr, int fq) const {
;     ...
;         if (QI8) {
; #pragma unroll
;             for (int ai = 0; ai < 2; ++ai)
; #pragma unroll
;                 for (int m = 0; m < 4; ++m) ra[ai][m] = sa[row0 + ai * HALF + m * 16];
; #pragma unroll
;             for (int bj = 0; bj < 2; ++bj) { cb[bj][0] = *(const f32x4*)(sb + col0 + bj * HALF) * tsc; cb[bj][1] = *(const f32x4*)(sb + col0 + bj * HALF + 4) * tsc; } }
;     ...
;             { const int row = row0 + ai * HALF + m * 16; float rmx = 0.f;
; #pragma unroll
;                 for (int bj = 0; bj < 2; ++bj) { const int col = col0 + bj * HALF; f32x4 v0 = acc[ai][bj][m][0], v1 = acc[ai][bj][m][1];
;                     if (QI8) { const f32x4 c0 = cb[bj][0] * ra[ai][m], c1 = cb[bj][1] * ra[ai][m]; const i32x4 i0 = __builtin_bit_cast(i32x4, v0), i1 = __builtin_bit_cast(i32x4, v1);
;                         v0 = (f32x4){(float)i0[0], (float)i0[1], (float)i0[2], (float)i0[3]} * c0; v1 = (f32x4){(float)i1[0], (float)i1[1], (float)i1[2], (float)i1[3]} * c1; }
;                     else if (MODE == 0) { v0 = v0 * tsc; v1 = v1 * tsc; }
;                     if (!QI8 && MODE == 1) { v0 = v0 * cb[bj][0]; v1 = v1 * cb[bj][1]; }
;                     if (MODE == 2 || MODE == 3) { const u32x4 g = gq[kb & 1][bj];
;                         f32x4 g0 = {sigmoidf_(bflo(g.x)), sigmoidf_(bfhi(g.x)), sigmoidf_(bflo(g.y)), sigmoidf_(bfhi(g.y))};
;                         f32x4 g1 = {sigmoidf_(bflo(g.z)), sigmoidf_(bfhi(g.z)), sigmoidf_(bflo(g.w)), sigmoidf_(bfhi(g.w))};
;                         v0 = v0 * g0; v1 = v1 * g1;
;                         if (MODE == 3) { const u32x4 q = aq[kb & 1][bj];
;                             v0 = v0 + (f32x4){bflo(q.x), bfhi(q.x), bflo(q.y), bfhi(q.y)}; v1 = v1 + (f32x4){bflo(q.z), bfhi(q.z), bflo(q.w), bfhi(q.w)}; } }
;                     if (MODE == 4) { v0 = v0 + rs[kb & 1][bj][0]; v1 = v1 + rs[kb & 1][bj][1]; }
;                     if (MODE == 5) { const u32x4 c = gq[kb & 1][bj], q = aq[kb & 1][bj];
;                         v0 = (f32x4){bflo(c.x) + sigmoidf_(v0[0]) * bflo(q.x), bfhi(c.x) + sigmoidf_(v0[1]) * bfhi(q.x), bflo(c.y) + sigmoidf_(v0[2]) * bflo(q.y), bfhi(c.y) + sigmoidf_(v0[3]) * bfhi(q.y)};
.LBB0_1332:
	v_lshl_add_u32 v146, s26, 8, v1
	v_ashrrev_i32_e32 v147, 31, v146
	v_lshl_add_u64 v[148:149], v[146:147], 2, s[4:5]
	v_lshl_or_b32 v152, s59, 8, v224
	global_load_dword v150, v[148:149], off
	v_ashrrev_i32_e32 v153, 31, v152
	v_lshl_add_u64 v[114:115], v[152:153], 2, s[8:9]
	global_load_dwordx4 v[134:137], v[114:115], off
	global_load_dwordx4 v[130:133], v[114:115], off offset:16
	global_load_dwordx4 v[122:125], v[114:115], off offset:512
	s_nop 0
	global_load_dwordx4 v[114:117], v[114:115], off offset:528
	s_nop 0
	global_load_dword v154, v[148:149], off offset:64
	global_load_dword v168, v[148:149], off offset:128
	v_cvt_f32_i32_e32 v156, v126
	v_cvt_f32_i32_e32 v158, v118
	v_cvt_f32_i32_e32 v162, v110
	v_cvt_f32_i32_e32 v164, v112
	v_cvt_f32_i32_e32 v170, v108
	global_load_dword v126, v[148:149], off offset:192
	global_load_dword v118, v[148:149], off offset:512
	global_load_dword v112, v[148:149], off offset:576
	global_load_dword v110, v[148:149], off offset:640
	global_load_dword v108, v[148:149], off offset:704
	v_cvt_f32_i32_e32 v143, v143
	v_cvt_f32_i32_e32 v142, v142
	v_cvt_f32_i32_e32 v145, v145
	v_cvt_f32_i32_e32 v144, v144
	v_cvt_f32_i32_e32 v139, v139
	v_cvt_f32_i32_e32 v138, v138
	v_cvt_f32_i32_e32 v141, v141
	v_cvt_f32_i32_e32 v140, v140
	v_cvt_f32_i32_e32 v160, v120
	v_or_b32_e32 v120, 16, v146
	v_cvt_f32_i32_e32 v157, v127
	v_cvt_f32_i32_e32 v129, v129
	v_cvt_f32_i32_e32 v128, v128
	v_cvt_f32_i32_e32 v161, v121
	v_lshlrev_b64 v[172:173], 12, v[146:147]
	v_ashrrev_i32_e32 v121, 31, v120
	v_cvt_f32_i32_e32 v159, v119
	v_cvt_f32_i32_e32 v163, v111
	v_cvt_f32_i32_e32 v165, v113
	v_cvt_f32_i32_e32 v167, v107
	v_cvt_f32_i32_e32 v166, v106
	v_lshlrev_b64 v[106:107], 1, v[152:153]
	v_lshl_add_u64 v[148:149], s[10:11], 0, v[172:173]
	v_lshlrev_b64 v[152:153], 12, v[120:121]
	v_cvt_f32_i32_e32 v171, v109
	v_lshl_add_u64 v[120:121], v[148:149], 0, v[106:107]
	v_lshl_add_u64 v[148:149], s[10:11], 0, v[152:153]
	v_cvt_f32_i32_e32 v103, v103
	v_cvt_f32_i32_e32 v102, v102
	v_cvt_f32_i32_e32 v99, v99
	v_cvt_f32_i32_e32 v101, v101
	v_cvt_f32_i32_e32 v100, v100
	v_cvt_f32_i32_e32 v98, v98
	v_cvt_f32_i32_e32 v105, v105
	v_cvt_f32_i32_e32 v104, v104
	v_cvt_f32_i32_e32 v95, v95
	v_cvt_f32_i32_e32 v94, v94
	v_cvt_f32_i32_e32 v91, v91
	v_cvt_f32_i32_e32 v93, v93
	v_cvt_f32_i32_e32 v92, v92
	v_cvt_f32_i32_e32 v90, v90
	v_cvt_f32_i32_e32 v97, v97
	v_cvt_f32_i32_e32 v96, v96
	v_cvt_f32_i32_e32 v87, v87
	v_cvt_f32_i32_e32 v86, v86
	v_cvt_f32_i32_e32 v83, v83
	v_cvt_f32_i32_e32 v85, v85
	v_cvt_f32_i32_e32 v84, v84
	v_cvt_f32_i32_e32 v82, v82
	v_cvt_f32_i32_e32 v89, v89
	v_cvt_f32_i32_e32 v88, v88
	v_cvt_f32_i32_e32 v79, v79
	v_cvt_f32_i32_e32 v78, v78
	v_cvt_f32_i32_e32 v75, v75
	v_cvt_f32_i32_e32 v77, v77
	v_cvt_f32_i32_e32 v76, v76
	v_cvt_f32_i32_e32 v74, v74
	v_cvt_f32_i32_e32 v81, v81
	v_cvt_f32_i32_e32 v80, v80
	v_cvt_f32_i32_e32 v71, v71
	v_cvt_f32_i32_e32 v70, v70
	v_cvt_f32_i32_e32 v67, v67
	v_cvt_f32_i32_e32 v69, v69
	v_cvt_f32_i32_e32 v68, v68
	v_cvt_f32_i32_e32 v66, v66
	v_cvt_f32_i32_e32 v73, v73
	v_cvt_f32_i32_e32 v72, v72
	v_cvt_f32_i32_e32 v65, v65
	v_cvt_f32_i32_e32 v64, v64
	s_waitcnt vmcnt(0)
	v_pk_mul_f32 v[152:153], v[150:151], v[134:135] op_sel_hi:[0,1]
	v_pk_mul_f32 v[172:173], v[150:151], v[136:137] op_sel_hi:[0,1]
	v_pk_mul_f32 v[174:175], v[150:151], v[130:131] op_sel_hi:[0,1]
	v_pk_mul_f32 v[176:177], v[150:151], v[132:133] op_sel_hi:[0,1]
	v_pk_mul_f32 v[178:179], v[150:151], v[122:123] op_sel_hi:[0,1]
	v_pk_mul_f32 v[180:181], v[150:151], v[124:125] op_sel_hi:[0,1]
	v_pk_mul_f32 v[144:145], v[172:173], v[144:145]
	v_pk_mul_f32 v[142:143], v[152:153], v[142:143]
	v_pk_mul_f32 v[152:153], v[176:177], v[140:141]
	v_pk_mul_f32 v[140:141], v[174:175], v[138:139]
	v_cvt_pk_bf16_f32 v138, v142, v143
	v_cvt_pk_bf16_f32 v139, v144, v145
	v_pk_mul_f32 v[182:183], v[150:151], v[114:115] op_sel_hi:[0,1]
	v_pk_mul_f32 v[150:151], v[150:151], v[116:117] op_sel_hi:[0,1]
	v_pk_mul_f32 v[184:185], v[154:155], v[134:135] op_sel_hi:[0,1]
	v_pk_mul_f32 v[186:187], v[154:155], v[136:137] op_sel_hi:[0,1]
	v_pk_mul_f32 v[128:129], v[180:181], v[128:129]
	v_pk_mul_f32 v[156:157], v[178:179], v[156:157]
	v_cvt_pk_bf16_f32 v140, v140, v141
	v_cvt_pk_bf16_f32 v141, v152, v153
	global_store_dwordx4 v[120:121], v[138:141], off sc1
	v_pk_mul_f32 v[188:189], v[154:155], v[130:131] op_sel_hi:[0,1]
	v_pk_mul_f32 v[190:191], v[154:155], v[132:133] op_sel_hi:[0,1]
	v_cvt_pk_bf16_f32 v138, v156, v157
	v_cvt_pk_bf16_f32 v139, v128, v129
	v_pk_mul_f32 v[150:151], v[150:151], v[160:161]
	v_pk_mul_f32 v[158:159], v[182:183], v[158:159]
	v_pk_mul_f32 v[160:161], v[186:187], v[164:165]
	v_pk_mul_f32 v[162:163], v[184:185], v[162:163]
	v_cvt_pk_bf16_f32 v140, v158, v159
	v_cvt_pk_bf16_f32 v141, v150, v151
	global_store_dwordx4 v[120:121], v[138:141], off offset:256 sc1
	v_lshl_add_u64 v[128:129], v[148:149], 0, v[106:107]
	v_pk_mul_f32 v[164:165], v[190:191], v[170:171]
	v_cvt_pk_bf16_f32 v138, v162, v163
	v_cvt_pk_bf16_f32 v139, v160, v161
	v_pk_mul_f32 v[166:167], v[188:189], v[166:167]
	v_pk_mul_f32 v[142:143], v[154:155], v[114:115] op_sel_hi:[0,1]
	v_cvt_pk_bf16_f32 v140, v166, v167
	v_cvt_pk_bf16_f32 v141, v164, v165
	global_store_dwordx4 v[128:129], v[138:141], off sc1
	v_pk_mul_f32 v[144:145], v[154:155], v[116:117] op_sel_hi:[0,1]
	v_cvt_f32_i32_e32 v63, v63
	v_pk_mul_f32 v[138:139], v[154:155], v[122:123] op_sel_hi:[0,1]
	v_pk_mul_f32 v[140:141], v[154:155], v[124:125] op_sel_hi:[0,1]
	v_pk_mul_f32 v[102:103], v[138:139], v[102:103]
	v_pk_mul_f32 v[138:139], v[144:145], v[100:101]
	v_pk_mul_f32 v[100:101], v[142:143], v[98:99]
;     __device__ __forceinline__ void operator()(const f32x4 (&acc)[2][2][4][2], const Unit& u, int wr, int wc, int fr, int fq) const {
;     ...
;             { const int row = row0 + ai * HALF + m * 16; float rmx = 0.f;
; #pragma unroll
;                 for (int bj = 0; bj < 2; ++bj) { const int col = col0 + bj * HALF; f32x4 v0 = acc[ai][bj][m][0], v1 = acc[ai][bj][m][1];
;                     if (QI8) { const f32x4 c0 = cb[bj][0] * ra[ai][m], c1 = cb[bj][1] * ra[ai][m]; const i32x4 i0 = __builtin_bit_cast(i32x4, v0), i1 = __builtin_bit_cast(i32x4, v1);
;                         v0 = (f32x4){(float)i0[0], (float)i0[1], (float)i0[2], (float)i0[3]} * c0; v1 = (f32x4){(float)i1[0], (float)i1[1], (float)i1[2], (float)i1[3]} * c1; }
;                     else if (MODE == 0) { v0 = v0 * tsc; v1 = v1 * tsc; }
;                     if (!QI8 && MODE == 1) { v0 = v0 * cb[bj][0]; v1 = v1 * cb[bj][1]; }
;                     if (MODE == 2 || MODE == 3) { const u32x4 g = gq[kb & 1][bj];
;                         f32x4 g0 = {sigmoidf_(bflo(g.x)), sigmoidf_(bfhi(g.x)), sigmoidf_(bflo(g.y)), sigmoidf_(bfhi(g.y))};
;                         f32x4 g1 = {sigmoidf_(bflo(g.z)), sigmoidf_(bfhi(g.z)), sigmoidf_(bflo(g.w)), sigmoidf_(bfhi(g.w))};
;                         v0 = v0 * g0; v1 = v1 * g1;
;                         if (MODE == 3) { const u32x4 q = aq[kb & 1][bj];
;                             v0 = v0 + (f32x4){bflo(q.x), bfhi(q.x), bflo(q.y), bfhi(q.y)}; v1 = v1 + (f32x4){bflo(q.z), bfhi(q.z), bflo(q.w), bfhi(q.w)}; } }
;                     if (MODE == 4) { v0 = v0 + rs[kb & 1][bj][0]; v1 = v1 + rs[kb & 1][bj][1]; }
;                     if (MODE == 5) { const u32x4 c = gq[kb & 1][bj], q = aq[kb & 1][bj];
;                         v0 = (f32x4){bflo(c.x) + sigmoidf_(v0[0]) * bflo(q.x), bfhi(c.x) + sigmoidf_(v0[1]) * bfhi(q.x), bflo(c.y) + sigmoidf_(v0[2]) * bflo(q.y), bfhi(c.y) + sigmoidf_(v0[3]) * bfhi(q.y)};
;                         v1 = (f32x4){bflo(c.z) + sigmoidf_(v1[0]) * bflo(q.z), bfhi(c.z) + sigmoidf_(v1[1]) * bfhi(q.z), bflo(c.w) + sigmoidf_(v1[2]) * bflo(q.w), bfhi(c.w) + sigmoidf_(v1[3]) * bfhi(q.w)}; }
;                     u32x4 w; w.x = cvtpk(v0[0], v0[1]); w.y = cvtpk(v0[2], v0[3]); w.z = cvtpk(v1[0], v1[1]); w.w = cvtpk(v1[2], v1[3]);
;                     *(u32x4*)(O + (size_t)row * ldo + col) = w;
	v_pk_mul_f32 v[104:105], v[140:141], v[104:105]
	v_cvt_pk_bf16_f32 v98, v102, v103
	v_pk_mul_f32 v[102:103], v[168:169], v[136:137] op_sel_hi:[0,1]
	v_cvt_pk_bf16_f32 v99, v104, v105
	v_cvt_pk_bf16_f32 v100, v100, v101
	v_cvt_pk_bf16_f32 v101, v138, v139
	global_store_dwordx4 v[128:129], v[98:101], off offset:256 sc1
	v_pk_mul_f32 v[104:105], v[168:169], v[130:131] op_sel_hi:[0,1]
	v_pk_mul_f32 v[128:129], v[168:169], v[132:133] op_sel_hi:[0,1]
	v_or_b32_e32 v98, 32, v146
	v_pk_mul_f32 v[100:101], v[168:169], v[134:135] op_sel_hi:[0,1]
	v_ashrrev_i32_e32 v99, 31, v98
	v_pk_mul_f32 v[94:95], v[100:101], v[94:95]
	v_pk_mul_f32 v[100:101], v[128:129], v[92:93]
	v_pk_mul_f32 v[92:93], v[104:105], v[90:91]
	v_cvt_pk_bf16_f32 v90, v94, v95
	v_lshlrev_b64 v[94:95], 12, v[98:99]
	v_lshl_add_u64 v[94:95], s[10:11], 0, v[94:95]
	v_pk_mul_f32 v[96:97], v[102:103], v[96:97]
	v_lshl_add_u64 v[94:95], v[94:95], 0, v[106:107]
	v_cvt_pk_bf16_f32 v91, v96, v97
	v_cvt_pk_bf16_f32 v92, v92, v93
	v_cvt_pk_bf16_f32 v93, v100, v101
	global_store_dwordx4 v[94:95], v[90:93], off sc1
	v_pk_mul_f32 v[96:97], v[168:169], v[114:115] op_sel_hi:[0,1]
	v_pk_mul_f32 v[98:99], v[168:169], v[116:117] op_sel_hi:[0,1]
	v_pk_mul_f32 v[90:91], v[168:169], v[122:123] op_sel_hi:[0,1]
	v_pk_mul_f32 v[92:93], v[168:169], v[124:125] op_sel_hi:[0,1]
	v_pk_mul_f32 v[86:87], v[90:91], v[86:87]
	v_pk_mul_f32 v[90:91], v[98:99], v[84:85]
	v_pk_mul_f32 v[84:85], v[96:97], v[82:83]
	v_pk_mul_f32 v[88:89], v[92:93], v[88:89]
	v_cvt_pk_bf16_f32 v82, v86, v87
	v_pk_mul_f32 v[86:87], v[126:127], v[136:137] op_sel_hi:[0,1]
	v_cvt_pk_bf16_f32 v83, v88, v89
	v_cvt_pk_bf16_f32 v84, v84, v85
	v_cvt_pk_bf16_f32 v85, v90, v91
	global_store_dwordx4 v[94:95], v[82:85], off offset:256 sc1
	v_pk_mul_f32 v[88:89], v[126:127], v[130:131] op_sel_hi:[0,1]
	v_pk_mul_f32 v[90:91], v[126:127], v[132:133] op_sel_hi:[0,1]
	v_or_b32_e32 v82, 48, v146
	v_pk_mul_f32 v[84:85], v[126:127], v[134:135] op_sel_hi:[0,1]
	v_ashrrev_i32_e32 v83, 31, v82
	v_pk_mul_f32 v[78:79], v[84:85], v[78:79]
	v_pk_mul_f32 v[84:85], v[90:91], v[76:77]
	v_pk_mul_f32 v[76:77], v[88:89], v[74:75]
	v_cvt_pk_bf16_f32 v74, v78, v79
	v_lshlrev_b64 v[78:79], 12, v[82:83]
	v_lshl_add_u64 v[78:79], s[10:11], 0, v[78:79]
	v_pk_mul_f32 v[80:81], v[86:87], v[80:81]
	v_lshl_add_u64 v[78:79], v[78:79], 0, v[106:107]
	v_cvt_pk_bf16_f32 v75, v80, v81
	v_cvt_pk_bf16_f32 v76, v76, v77
	v_cvt_pk_bf16_f32 v77, v84, v85
	global_store_dwordx4 v[78:79], v[74:77], off sc1
	v_pk_mul_f32 v[80:81], v[126:127], v[114:115] op_sel_hi:[0,1]
	v_pk_mul_f32 v[82:83], v[126:127], v[116:117] op_sel_hi:[0,1]
	v_pk_mul_f32 v[74:75], v[126:127], v[122:123] op_sel_hi:[0,1]
	v_pk_mul_f32 v[76:77], v[126:127], v[124:125] op_sel_hi:[0,1]
	v_pk_mul_f32 v[70:71], v[74:75], v[70:71]
	v_pk_mul_f32 v[74:75], v[82:83], v[68:69]
	v_pk_mul_f32 v[68:69], v[80:81], v[66:67]
	v_cvt_f32_i32_e32 v62, v62
	v_cvt_f32_i32_e32 v59, v59
	v_cvt_f32_i32_e32 v61, v61
	v_cvt_f32_i32_e32 v60, v60
	v_cvt_f32_i32_e32 v58, v58
	v_pk_mul_f32 v[72:73], v[76:77], v[72:73]
	v_cvt_pk_bf16_f32 v66, v70, v71
	v_pk_mul_f32 v[70:71], v[118:119], v[130:131] op_sel_hi:[0,1]
	v_cvt_pk_bf16_f32 v67, v72, v73
	v_cvt_pk_bf16_f32 v68, v68, v69
	v_cvt_pk_bf16_f32 v69, v74, v75
	global_store_dwordx4 v[78:79], v[66:69], off offset:256 sc1
	v_pk_mul_f32 v[72:73], v[118:119], v[132:133] op_sel_hi:[0,1]
	v_cvt_f32_i32_e32 v55, v55
	v_pk_mul_f32 v[68:69], v[118:119], v[136:137] op_sel_hi:[0,1]
	v_pk_mul_f32 v[66:67], v[118:119], v[134:135] op_sel_hi:[0,1]
	v_pk_mul_f32 v[64:65], v[68:69], v[64:65]
	v_cvt_f32_i32_e32 v54, v54
	v_cvt_f32_i32_e32 v51, v51
	v_cvt_f32_i32_e32 v53, v53
	v_cvt_f32_i32_e32 v52, v52
	v_cvt_f32_i32_e32 v50, v50
	v_pk_mul_f32 v[62:63], v[66:67], v[62:63]
	v_pk_mul_f32 v[66:67], v[72:73], v[60:61]
	v_pk_mul_f32 v[60:61], v[70:71], v[58:59]
	v_cvt_pk_bf16_f32 v58, v62, v63
	v_cvt_pk_bf16_f32 v59, v64, v65
	v_add_co_u32_e32 v64, vcc, s57, v120
	v_cvt_f32_i32_e32 v57, v57
	v_cvt_f32_i32_e32 v56, v56
	v_addc_co_u32_e32 v65, vcc, 0, v121, vcc
	v_cvt_pk_bf16_f32 v60, v60, v61
	v_cvt_pk_bf16_f32 v61, v66, v67
	global_store_dwordx4 v[64:65], v[58:61], off sc1
	v_pk_mul_f32 v[64:65], v[118:119], v[114:115] op_sel_hi:[0,1]
	v_pk_mul_f32 v[66:67], v[118:119], v[116:117] op_sel_hi:[0,1]
	v_pk_mul_f32 v[58:59], v[118:119], v[122:123] op_sel_hi:[0,1]
	v_cvt_f32_i32_e32 v47, v47
	v_cvt_f32_i32_e32 v46, v46
	v_pk_mul_f32 v[60:61], v[118:119], v[124:125] op_sel_hi:[0,1]
	v_pk_mul_f32 v[54:55], v[58:59], v[54:55]
	v_pk_mul_f32 v[58:59], v[66:67], v[52:53]
	v_pk_mul_f32 v[52:53], v[64:65], v[50:51]
	v_cvt_f32_i32_e32 v43, v43
	v_cvt_f32_i32_e32 v45, v45
	v_cvt_f32_i32_e32 v44, v44
	v_cvt_f32_i32_e32 v42, v42
	v_lshl_add_u64 v[62:63], v[120:121], 0, s[0:1]
	v_pk_mul_f32 v[56:57], v[60:61], v[56:57]
	v_cvt_pk_bf16_f32 v50, v54, v55
	v_cvt_f32_i32_e32 v49, v49
	v_cvt_pk_bf16_f32 v51, v56, v57
	v_cvt_pk_bf16_f32 v52, v52, v53
	v_cvt_pk_bf16_f32 v53, v58, v59
	global_store_dwordx4 v[62:63], v[50:53], off offset:256 sc1
	v_cvt_f32_i32_e32 v48, v48
	v_pk_mul_f32 v[56:57], v[112:113], v[130:131] op_sel_hi:[0,1]
	v_add_u32_e32 v50, 0x90, v146
	v_pk_mul_f32 v[52:53], v[112:113], v[134:135] op_sel_hi:[0,1]
	v_ashrrev_i32_e32 v51, 31, v50
	v_pk_mul_f32 v[58:59], v[112:113], v[132:133] op_sel_hi:[0,1]
;     __device__ __forceinline__ void operator()(const f32x4 (&acc)[2][2][4][2], const Unit& u, int wr, int wc, int fr, int fq) const {
;     ...
;             { const int row = row0 + ai * HALF + m * 16; float rmx = 0.f;
; #pragma unroll
;                 for (int bj = 0; bj < 2; ++bj) { const int col = col0 + bj * HALF; f32x4 v0 = acc[ai][bj][m][0], v1 = acc[ai][bj][m][1];
;                     if (QI8) { const f32x4 c0 = cb[bj][0] * ra[ai][m], c1 = cb[bj][1] * ra[ai][m]; const i32x4 i0 = __builtin_bit_cast(i32x4, v0), i1 = __builtin_bit_cast(i32x4, v1);
;                         v0 = (f32x4){(float)i0[0], (float)i0[1], (float)i0[2], (float)i0[3]} * c0; v1 = (f32x4){(float)i1[0], (float)i1[1], (float)i1[2], (float)i1[3]} * c1; }
;                     else if (MODE == 0) { v0 = v0 * tsc; v1 = v1 * tsc; }
;                     if (!QI8 && MODE == 1) { v0 = v0 * cb[bj][0]; v1 = v1 * cb[bj][1]; }
;                     if (MODE == 2 || MODE == 3) { const u32x4 g = gq[kb & 1][bj];
;                         f32x4 g0 = {sigmoidf_(bflo(g.x)), sigmoidf_(bfhi(g.x)), sigmoidf_(bflo(g.y)), sigmoidf_(bfhi(g.y))};
;                         f32x4 g1 = {sigmoidf_(bflo(g.z)), sigmoidf_(bfhi(g.z)), sigmoidf_(bflo(g.w)), sigmoidf_(bfhi(g.w))};
;                         v0 = v0 * g0; v1 = v1 * g1;
;                         if (MODE == 3) { const u32x4 q = aq[kb & 1][bj];
;                             v0 = v0 + (f32x4){bflo(q.x), bfhi(q.x), bflo(q.y), bfhi(q.y)}; v1 = v1 + (f32x4){bflo(q.z), bfhi(q.z), bflo(q.w), bfhi(q.w)}; } }
;                     if (MODE == 4) { v0 = v0 + rs[kb & 1][bj][0]; v1 = v1 + rs[kb & 1][bj][1]; }
;                     if (MODE == 5) { const u32x4 c = gq[kb & 1][bj], q = aq[kb & 1][bj];
;                         v0 = (f32x4){bflo(c.x) + sigmoidf_(v0[0]) * bflo(q.x), bfhi(c.x) + sigmoidf_(v0[1]) * bfhi(q.x), bflo(c.y) + sigmoidf_(v0[2]) * bflo(q.y), bfhi(c.y) + sigmoidf_(v0[3]) * bfhi(q.y)};
;                         v1 = (f32x4){bflo(c.z) + sigmoidf_(v1[0]) * bflo(q.z), bfhi(c.z) + sigmoidf_(v1[1]) * bfhi(q.z), bflo(c.w) + sigmoidf_(v1[2]) * bflo(q.w), bfhi(c.w) + sigmoidf_(v1[3]) * bfhi(q.w)}; }
;                     u32x4 w; w.x = cvtpk(v0[0], v0[1]); w.y = cvtpk(v0[2], v0[3]); w.z = cvtpk(v1[0], v1[1]); w.w = cvtpk(v1[2], v1[3]);
;                     *(u32x4*)(O + (size_t)row * ldo + col) = w;
	v_pk_mul_f32 v[46:47], v[52:53], v[46:47]
	v_pk_mul_f32 v[52:53], v[58:59], v[44:45]
	v_pk_mul_f32 v[44:45], v[56:57], v[42:43]
	v_cvt_pk_bf16_f32 v42, v46, v47
	v_lshlrev_b64 v[46:47], 12, v[50:51]
	v_cvt_f32_i32_e32 v39, v39
	v_cvt_f32_i32_e32 v38, v38
	v_cvt_f32_i32_e32 v35, v35
	v_cvt_f32_i32_e32 v37, v37
	v_cvt_f32_i32_e32 v36, v36
	v_cvt_f32_i32_e32 v34, v34
	v_pk_mul_f32 v[54:55], v[112:113], v[136:137] op_sel_hi:[0,1]
	v_lshl_add_u64 v[46:47], s[10:11], 0, v[46:47]
	v_cvt_f32_i32_e32 v41, v41
	v_cvt_f32_i32_e32 v40, v40
	v_pk_mul_f32 v[48:49], v[54:55], v[48:49]
	v_lshl_add_u64 v[46:47], v[46:47], 0, v[106:107]
	v_cvt_pk_bf16_f32 v43, v48, v49
	v_cvt_pk_bf16_f32 v44, v44, v45
	v_cvt_pk_bf16_f32 v45, v52, v53
	global_store_dwordx4 v[46:47], v[42:45], off sc1
	v_pk_mul_f32 v[48:49], v[112:113], v[114:115] op_sel_hi:[0,1]
	v_pk_mul_f32 v[50:51], v[112:113], v[116:117] op_sel_hi:[0,1]
	v_pk_mul_f32 v[42:43], v[112:113], v[122:123] op_sel_hi:[0,1]
	v_cvt_f32_i32_e32 v31, v31
	v_cvt_f32_i32_e32 v30, v30
	v_pk_mul_f32 v[44:45], v[112:113], v[124:125] op_sel_hi:[0,1]
	v_pk_mul_f32 v[38:39], v[42:43], v[38:39]
	v_pk_mul_f32 v[42:43], v[50:51], v[36:37]
	v_pk_mul_f32 v[36:37], v[48:49], v[34:35]
	v_cvt_f32_i32_e32 v27, v27
	v_cvt_f32_i32_e32 v29, v29
	v_cvt_f32_i32_e32 v28, v28
	v_cvt_f32_i32_e32 v26, v26
	v_pk_mul_f32 v[40:41], v[44:45], v[40:41]
	v_cvt_pk_bf16_f32 v34, v38, v39
	v_cvt_f32_i32_e32 v33, v33
	v_cvt_pk_bf16_f32 v35, v40, v41
	v_cvt_pk_bf16_f32 v36, v36, v37
	v_cvt_pk_bf16_f32 v37, v42, v43
	global_store_dwordx4 v[46:47], v[34:37], off offset:256 sc1
	v_cvt_f32_i32_e32 v32, v32
	v_pk_mul_f32 v[40:41], v[110:111], v[130:131] op_sel_hi:[0,1]
	v_add_u32_e32 v34, 0xa0, v146
	v_pk_mul_f32 v[36:37], v[110:111], v[134:135] op_sel_hi:[0,1]
	v_ashrrev_i32_e32 v35, 31, v34
	v_pk_mul_f32 v[42:43], v[110:111], v[132:133] op_sel_hi:[0,1]
	v_pk_mul_f32 v[30:31], v[36:37], v[30:31]
	v_pk_mul_f32 v[36:37], v[42:43], v[28:29]
	v_pk_mul_f32 v[28:29], v[40:41], v[26:27]
	v_cvt_pk_bf16_f32 v26, v30, v31
	v_lshlrev_b64 v[30:31], 12, v[34:35]
	v_cvt_f32_i32_e32 v23, v23
	v_cvt_f32_i32_e32 v22, v22
	v_cvt_f32_i32_e32 v19, v19
	v_cvt_f32_i32_e32 v21, v21
	v_cvt_f32_i32_e32 v20, v20
	v_cvt_f32_i32_e32 v18, v18
	v_pk_mul_f32 v[38:39], v[110:111], v[136:137] op_sel_hi:[0,1]
	v_lshl_add_u64 v[30:31], s[10:11], 0, v[30:31]
	v_cvt_f32_i32_e32 v25, v25
	v_cvt_f32_i32_e32 v24, v24
	v_pk_mul_f32 v[32:33], v[38:39], v[32:33]
	v_lshl_add_u64 v[30:31], v[30:31], 0, v[106:107]
	v_cvt_pk_bf16_f32 v27, v32, v33
	v_cvt_pk_bf16_f32 v28, v28, v29
	v_cvt_pk_bf16_f32 v29, v36, v37
	global_store_dwordx4 v[30:31], v[26:29], off sc1
	v_pk_mul_f32 v[32:33], v[110:111], v[114:115] op_sel_hi:[0,1]
	v_pk_mul_f32 v[34:35], v[110:111], v[116:117] op_sel_hi:[0,1]
	v_pk_mul_f32 v[26:27], v[110:111], v[122:123] op_sel_hi:[0,1]
	v_cvt_f32_i32_e32 v15, v15
	v_cvt_f32_i32_e32 v14, v14
	v_pk_mul_f32 v[28:29], v[110:111], v[124:125] op_sel_hi:[0,1]
	v_pk_mul_f32 v[22:23], v[26:27], v[22:23]
	v_pk_mul_f32 v[26:27], v[34:35], v[20:21]
	v_pk_mul_f32 v[20:21], v[32:33], v[18:19]
	v_cvt_f32_i32_e32 v11, v11
	v_cvt_f32_i32_e32 v13, v13
	v_cvt_f32_i32_e32 v12, v12
	v_cvt_f32_i32_e32 v10, v10
	v_pk_mul_f32 v[24:25], v[28:29], v[24:25]
	v_cvt_pk_bf16_f32 v18, v22, v23
	v_cvt_f32_i32_e32 v17, v17
	v_cvt_pk_bf16_f32 v19, v24, v25
	v_cvt_pk_bf16_f32 v20, v20, v21
	v_cvt_pk_bf16_f32 v21, v26, v27
	global_store_dwordx4 v[30:31], v[18:21], off offset:256 sc1
	v_cvt_f32_i32_e32 v16, v16
	v_pk_mul_f32 v[24:25], v[108:109], v[130:131] op_sel_hi:[0,1]
	v_add_u32_e32 v18, 0xb0, v146
	v_pk_mul_f32 v[20:21], v[134:135], v[108:109] op_sel_hi:[1,0]
	v_ashrrev_i32_e32 v19, 31, v18
	v_pk_mul_f32 v[26:27], v[108:109], v[132:133] op_sel_hi:[0,1]
	v_pk_mul_f32 v[14:15], v[20:21], v[14:15]
	v_pk_mul_f32 v[20:21], v[26:27], v[12:13]
	v_pk_mul_f32 v[12:13], v[24:25], v[10:11]
	v_cvt_pk_bf16_f32 v10, v14, v15
	v_lshlrev_b64 v[14:15], 12, v[18:19]
	v_cvt_f32_i32_e32 v7, v7
	v_cvt_f32_i32_e32 v6, v6
	v_cvt_f32_i32_e32 v3, v3
	v_cvt_f32_i32_e32 v5, v5
	v_cvt_f32_i32_e32 v4, v4
	v_cvt_f32_i32_e32 v2, v2
	v_pk_mul_f32 v[22:23], v[136:137], v[108:109] op_sel_hi:[1,0]
	v_lshl_add_u64 v[14:15], s[10:11], 0, v[14:15]
	v_cvt_f32_i32_e32 v9, v9
	v_cvt_f32_i32_e32 v8, v8
	v_pk_mul_f32 v[16:17], v[22:23], v[16:17]
	v_lshl_add_u64 v[14:15], v[14:15], 0, v[106:107]
	v_cvt_pk_bf16_f32 v11, v16, v17
	v_cvt_pk_bf16_f32 v12, v12, v13
	v_cvt_pk_bf16_f32 v13, v20, v21
	global_store_dwordx4 v[14:15], v[10:13], off sc1
	v_pk_mul_f32 v[16:17], v[108:109], v[114:115] op_sel_hi:[0,1]
	v_pk_mul_f32 v[18:19], v[108:109], v[116:117] op_sel_hi:[0,1]
	v_pk_mul_f32 v[10:11], v[108:109], v[122:123] op_sel_hi:[0,1]
	v_pk_mul_f32 v[12:13], v[108:109], v[124:125] op_sel_hi:[0,1]
	v_pk_mul_f32 v[6:7], v[10:11], v[6:7]
	v_pk_mul_f32 v[10:11], v[18:19], v[4:5]
	v_pk_mul_f32 v[4:5], v[16:17], v[2:3]
	s_andn2_b64 vcc, exec, s[6:7]
	s_mov_b64 s[6:7], -1
	v_pk_mul_f32 v[8:9], v[12:13], v[8:9]
	v_cvt_pk_bf16_f32 v2, v6, v7
	s_nop 0
	v_cvt_pk_bf16_f32 v3, v8, v9
	v_cvt_pk_bf16_f32 v4, v4, v5
	v_cvt_pk_bf16_f32 v5, v10, v11
	global_store_dwordx4 v[14:15], v[2:5], off offset:256 sc1
	s_cbranch_vccnz .LBB0_1317
	s_andn2_b64 vcc, exec, s[2:3]
	s_cbranch_vccnz .LBB0_1316
	s_barrier
	s_branch .LBB0_1316

; __device__ __forceinline__ float sigmoidf_(float x) { return __builtin_amdgcn_rcpf(1.f + __builtin_amdgcn_exp2f(-1.4426950408889634f * x)); }
;     __device__ __forceinline__ void operator()(const f32x4 (&acc)[2][2][4][2], const Unit& u, int wr, int wc, int fr, int fq) const {
;     ...
;         if (QI8) {
; #pragma unroll
;             for (int ai = 0; ai < 2; ++ai)
; #pragma unroll
;                 for (int m = 0; m < 4; ++m) ra[ai][m] = sa[row0 + ai * HALF + m * 16];
; #pragma unroll
;             for (int bj = 0; bj < 2; ++bj) { cb[bj][0] = *(const f32x4*)(sb + col0 + bj * HALF) * tsc; cb[bj][1] = *(const f32x4*)(sb + col0 + bj * HALF + 4) * tsc; } }
;     ...
;         EPB_LOAD(0);
; #pragma unroll
;         for (int kb = 0; kb < 8; ++kb) { const int ai = kb >> 2, m = kb & 3;
;             if (kb < 7) EPB_LOAD(kb + 1);
;             { const int row = row0 + ai * HALF + m * 16; float rmx = 0.f;
; #pragma unroll
;                 for (int bj = 0; bj < 2; ++bj) { const int col = col0 + bj * HALF; f32x4 v0 = acc[ai][bj][m][0], v1 = acc[ai][bj][m][1];
;                     if (QI8) { const f32x4 c0 = cb[bj][0] * ra[ai][m], c1 = cb[bj][1] * ra[ai][m]; const i32x4 i0 = __builtin_bit_cast(i32x4, v0), i1 = __builtin_bit_cast(i32x4, v1);
;                         v0 = (f32x4){(float)i0[0], (float)i0[1], (float)i0[2], (float)i0[3]} * c0; v1 = (f32x4){(float)i1[0], (float)i1[1], (float)i1[2], (float)i1[3]} * c1; }
;                     else if (MODE == 0) { v0 = v0 * tsc; v1 = v1 * tsc; }
;                     if (!QI8 && MODE == 1) { v0 = v0 * cb[bj][0]; v1 = v1 * cb[bj][1]; }
;                     if (MODE == 2 || MODE == 3) { const u32x4 g = gq[kb & 1][bj];
;                         f32x4 g0 = {sigmoidf_(bflo(g.x)), sigmoidf_(bfhi(g.x)), sigmoidf_(bflo(g.y)), sigmoidf_(bfhi(g.y))};
;                         f32x4 g1 = {sigmoidf_(bflo(g.z)), sigmoidf_(bfhi(g.z)), sigmoidf_(bflo(g.w)), sigmoidf_(bfhi(g.w))};
;                         v0 = v0 * g0; v1 = v1 * g1;
;                         if (MODE == 3) { const u32x4 q = aq[kb & 1][bj];
;                             v0 = v0 + (f32x4){bflo(q.x), bfhi(q.x), bflo(q.y), bfhi(q.y)}; v1 = v1 + (f32x4){bflo(q.z), bfhi(q.z), bflo(q.w), bfhi(q.w)}; } }
;                     if (MODE == 4) { v0 = v0 + rs[kb & 1][bj][0]; v1 = v1 + rs[kb & 1][bj][1]; }
;                     if (MODE == 5) { const u32x4 c = gq[kb & 1][bj], q = aq[kb & 1][bj];
.LBB0_1737:
	v_lshl_add_u32 v166, s28, 8, v195
	v_ashrrev_i32_e32 v167, 31, v166
	v_lshl_or_b32 v138, s60, 8, v223
	v_lshl_add_u64 v[136:137], v[166:167], 2, s[2:3]
	v_ashrrev_i32_e32 v139, 31, v138
	global_load_dword v180, v[136:137], off
	v_lshl_add_u64 v[140:141], v[138:139], 2, s[4:5]
	global_load_dwordx4 v[76:79], v[140:141], off
	global_load_dwordx4 v[72:75], v[140:141], off offset:16
	v_lshlrev_b64 v[210:211], 13, v[166:167]
	v_lshl_add_u64 v[142:143], s[8:9], 0, v[210:211]
	v_lshl_add_u64 v[148:149], s[10:11], 0, v[210:211]
	v_lshlrev_b64 v[160:161], 1, v[138:139]
	v_lshl_add_u64 v[138:139], v[142:143], 0, v[160:161]
	v_lshl_add_u64 v[142:143], v[148:149], 0, v[160:161]
	global_load_dwordx4 v[144:147], v[138:139], off
	global_load_dwordx4 v[148:151], v[142:143], off
	v_cvt_f32_i32_e32 v213, v61
	v_cvt_f32_i32_e32 v212, v60
	v_cvt_f32_i32_e32 v215, v63
	v_cvt_f32_i32_e32 v214, v62
	v_cvt_f32_i32_e32 v217, v57
	v_cvt_f32_i32_e32 v216, v56
	v_cvt_f32_i32_e32 v219, v59
	v_cvt_f32_i32_e32 v218, v58
	global_load_dword v178, v[136:137], off offset:64
	global_load_dword v176, v[136:137], off offset:128
	global_load_dword v174, v[136:137], off offset:192
	global_load_dword v170, v[136:137], off offset:512
	global_load_dword v168, v[136:137], off offset:576
	global_load_dword v164, v[136:137], off offset:640
	global_load_dword v162, v[136:137], off offset:704
	global_load_dwordx4 v[56:59], v[140:141], off offset:528
	global_load_dwordx4 v[60:63], v[140:141], off offset:512
	global_load_dwordx4 v[184:187], v[138:139], off offset:256
	global_load_dwordx4 v[188:191], v[142:143], off offset:256
	v_or_b32_e32 v152, 16, v166
	v_ashrrev_i32_e32 v153, 31, v152
	v_lshlrev_b64 v[182:183], 13, v[152:153]
	v_lshl_add_u64 v[136:137], s[8:9], 0, v[182:183]
	v_lshl_add_u64 v[140:141], s[10:11], 0, v[182:183]
	v_lshl_add_u64 v[136:137], v[136:137], 0, v[160:161]
	v_lshl_add_u64 v[140:141], v[140:141], 0, v[160:161]
	global_load_dwordx4 v[152:155], v[136:137], off
	s_nop 0
	global_load_dwordx4 v[136:139], v[136:137], off offset:256
	s_nop 0
	global_load_dwordx4 v[156:159], v[140:141], off
	s_nop 0
	global_load_dwordx4 v[140:143], v[140:141], off offset:256
	v_readlane_b32 s30, v245, 9
	v_readlane_b32 s31, v245, 10
	v_cvt_f32_i32_e32 v133, v133
	v_cvt_f32_i32_e32 v132, v132
	v_cvt_f32_i32_e32 v135, v135
	v_cvt_f32_i32_e32 v134, v134
	v_cvt_f32_i32_e32 v129, v129
	v_cvt_f32_i32_e32 v128, v128
	v_cvt_f32_i32_e32 v131, v131
	v_cvt_f32_i32_e32 v130, v130
	v_cvt_f32_i32_e32 v125, v125
	v_cvt_f32_i32_e32 v124, v124
	v_cvt_f32_i32_e32 v127, v127
	v_cvt_f32_i32_e32 v126, v126
	v_cvt_f32_i32_e32 v121, v121
	v_cvt_f32_i32_e32 v120, v120
	v_cvt_f32_i32_e32 v123, v123
	v_cvt_f32_i32_e32 v122, v122
	v_cvt_f32_i32_e32 v117, v117
	v_cvt_f32_i32_e32 v116, v116
	v_cvt_f32_i32_e32 v119, v119
	v_cvt_f32_i32_e32 v118, v118
	v_cvt_f32_i32_e32 v113, v113
	v_cvt_f32_i32_e32 v112, v112
	v_cvt_f32_i32_e32 v115, v115
	v_cvt_f32_i32_e32 v114, v114
	v_cvt_f32_i32_e32 v109, v109
	v_cvt_f32_i32_e32 v108, v108
	v_cvt_f32_i32_e32 v111, v111
	v_cvt_f32_i32_e32 v110, v110
	v_cvt_f32_i32_e32 v105, v105
	v_cvt_f32_i32_e32 v104, v104
	v_cvt_f32_i32_e32 v107, v107
	v_cvt_f32_i32_e32 v106, v106
	v_cvt_f32_i32_e32 v101, v101
	v_cvt_f32_i32_e32 v100, v100
	v_cvt_f32_i32_e32 v103, v103
	v_cvt_f32_i32_e32 v102, v102
	v_cvt_f32_i32_e32 v97, v97
	v_cvt_f32_i32_e32 v96, v96
	v_cvt_f32_i32_e32 v99, v99
	v_cvt_f32_i32_e32 v98, v98
	v_cvt_f32_i32_e32 v93, v93
	v_cvt_f32_i32_e32 v92, v92
	v_lshl_add_u64 v[172:173], v[210:211], 0, s[16:17]
	v_cvt_f32_i32_e32 v95, v95
	v_cvt_f32_i32_e32 v94, v94
	v_cvt_f32_i32_e32 v89, v89
	v_cvt_f32_i32_e32 v88, v88
	v_cvt_f32_i32_e32 v91, v91
	v_cvt_f32_i32_e32 v90, v90
	v_cvt_f32_i32_e32 v85, v85
	s_waitcnt vmcnt(0)
	v_pk_mul_f32 v[220:221], v[180:181], v[76:77] op_sel_hi:[0,1]
	v_pk_mul_f32 v[228:229], v[180:181], v[78:79] op_sel_hi:[0,1]
	v_pk_mul_f32 v[230:231], v[180:181], v[72:73] op_sel_hi:[0,1]
	v_pk_mul_f32 v[212:213], v[220:221], v[212:213]
	v_pk_mul_f32 v[214:215], v[228:229], v[214:215]
	v_pk_mul_f32 v[216:217], v[230:231], v[216:217]
	v_mul_f32_e32 v169, 0xbfb8aa3b, v213
	v_mul_f32_e32 v175, 0xbfb8aa3b, v214
	v_mul_f32_e32 v214, 0xbfb8aa3b, v217
	v_exp_f32_e32 v169, v169
	v_exp_f32_e32 v214, v214
	v_pk_mul_f32 v[232:233], v[180:181], v[74:75] op_sel_hi:[0,1]
	v_lshlrev_b32_e32 v163, 16, v144
	v_add_f32_e32 v169, 1.0, v169
	v_add_f32_e32 v214, 1.0, v214
	v_rcp_f32_e32 v169, v169
	v_rcp_f32_e32 v214, v214
	v_lshlrev_b32_e32 v167, 16, v148
	v_and_b32_e32 v144, 0xffff0000, v144
	v_and_b32_e32 v148, 0xffff0000, v148
	v_pk_mul_f32 v[218:219], v[232:233], v[218:219]
	v_mul_f32_e32 v165, 0xbfb8aa3b, v212
	v_mul_f32_e32 v179, 0xbfb8aa3b, v215
	v_lshlrev_b32_e32 v181, 16, v146
	v_and_b32_e32 v146, 0xffff0000, v146
	v_fmac_f32_e32 v144, v169, v148
	v_and_b32_e32 v148, 0xffff0000, v150
	v_exp_f32_e32 v165, v165
	v_exp_f32_e32 v179, v179
	v_fmac_f32_e32 v146, v214, v148
	v_mul_f32_e32 v148, 0xbfb8aa3b, v218
	v_lshlrev_b32_e32 v213, 16, v150
	v_exp_f32_e32 v148, v148
	v_mul_f32_e32 v150, 0xbfb8aa3b, v219
	v_mul_f32_e32 v212, 0xbfb8aa3b, v216
	v_exp_f32_e32 v150, v150
	v_exp_f32_e32 v175, v175
	v_exp_f32_e32 v212, v212
	v_add_f32_e32 v165, 1.0, v165
	v_add_f32_e32 v179, 1.0, v179
	v_rcp_f32_e32 v165, v165
	v_rcp_f32_e32 v179, v179
	v_add_f32_e32 v148, 1.0, v148
	v_rcp_f32_e32 v148, v148
	v_add_f32_e32 v150, 1.0, v150
	v_add_f32_e32 v175, 1.0, v175
	v_add_f32_e32 v212, 1.0, v212
	v_rcp_f32_e32 v150, v150
	v_lshlrev_b32_e32 v171, 16, v145
	v_lshlrev_b32_e32 v177, 16, v149
	v_and_b32_e32 v145, 0xffff0000, v145
	v_and_b32_e32 v149, 0xffff0000, v149
	v_rcp_f32_e32 v175, v175
;     __device__ __forceinline__ void operator()(const f32x4 (&acc)[2][2][4][2], const Unit& u, int wr, int wc, int fr, int fq) const {
;     ...
;         EPB_LOAD(0);
; #pragma unroll
;         for (int kb = 0; kb < 8; ++kb) { const int ai = kb >> 2, m = kb & 3;
;             if (kb < 7) EPB_LOAD(kb + 1);
;             { const int row = row0 + ai * HALF + m * 16; float rmx = 0.f;
; #pragma unroll
;                 for (int bj = 0; bj < 2; ++bj) { const int col = col0 + bj * HALF; f32x4 v0 = acc[ai][bj][m][0], v1 = acc[ai][bj][m][1];
;                     if (QI8) { const f32x4 c0 = cb[bj][0] * ra[ai][m], c1 = cb[bj][1] * ra[ai][m]; const i32x4 i0 = __builtin_bit_cast(i32x4, v0), i1 = __builtin_bit_cast(i32x4, v1);
;                         v0 = (f32x4){(float)i0[0], (float)i0[1], (float)i0[2], (float)i0[3]} * c0; v1 = (f32x4){(float)i1[0], (float)i1[1], (float)i1[2], (float)i1[3]} * c1; }
;                     else if (MODE == 0) { v0 = v0 * tsc; v1 = v1 * tsc; }
;                     if (!QI8 && MODE == 1) { v0 = v0 * cb[bj][0]; v1 = v1 * cb[bj][1]; }
;                     if (MODE == 2 || MODE == 3) { const u32x4 g = gq[kb & 1][bj];
;                         f32x4 g0 = {sigmoidf_(bflo(g.x)), sigmoidf_(bfhi(g.x)), sigmoidf_(bflo(g.y)), sigmoidf_(bfhi(g.y))};
;                         f32x4 g1 = {sigmoidf_(bflo(g.z)), sigmoidf_(bfhi(g.z)), sigmoidf_(bflo(g.w)), sigmoidf_(bfhi(g.w))};
;                         v0 = v0 * g0; v1 = v1 * g1;
;                         if (MODE == 3) { const u32x4 q = aq[kb & 1][bj];
;                             v0 = v0 + (f32x4){bflo(q.x), bfhi(q.x), bflo(q.y), bfhi(q.y)}; v1 = v1 + (f32x4){bflo(q.z), bfhi(q.z), bflo(q.w), bfhi(q.w)}; } }
;                     if (MODE == 4) { v0 = v0 + rs[kb & 1][bj][0]; v1 = v1 + rs[kb & 1][bj][1]; }
;                     if (MODE == 5) { const u32x4 c = gq[kb & 1][bj], q = aq[kb & 1][bj];
;                         v0 = (f32x4){bflo(c.x) + sigmoidf_(v0[0]) * bflo(q.x), bfhi(c.x) + sigmoidf_(v0[1]) * bfhi(q.x), bflo(c.y) + sigmoidf_(v0[2]) * bflo(q.y), bfhi(c.y) + sigmoidf_(v0[3]) * bfhi(q.y)};
;                         v1 = (f32x4){bflo(c.z) + sigmoidf_(v1[0]) * bflo(q.z), bfhi(c.z) + sigmoidf_(v1[1]) * bfhi(q.z), bflo(c.w) + sigmoidf_(v1[2]) * bflo(q.w), bfhi(c.w) + sigmoidf_(v1[3]) * bfhi(q.w)}; }
	v_rcp_f32_e32 v212, v212
	v_fmac_f32_e32 v163, v165, v167
	v_fmac_f32_e32 v145, v179, v149
	v_lshlrev_b32_e32 v149, 16, v147
	v_lshlrev_b32_e32 v165, 16, v151
	v_fmac_f32_e32 v149, v148, v165
	v_and_b32_e32 v147, 0xffff0000, v147
	v_and_b32_e32 v148, 0xffff0000, v151
	v_fmac_f32_e32 v147, v150, v148
	v_fmac_f32_e32 v171, v175, v177
	v_fmac_f32_e32 v181, v212, v213
	v_cvt_pk_bf16_f32 v144, v163, v144
	v_cvt_pk_bf16_f32 v145, v171, v145
	v_cvt_pk_bf16_f32 v146, v181, v146
	v_cvt_pk_bf16_f32 v147, v149, v147
	v_lshl_add_u64 v[148:149], s[30:31], 0, v[210:211]
	v_lshl_add_u64 v[148:149], v[148:149], 0, v[160:161]
	global_store_dwordx4 v[148:149], v[144:147], off sc1
	v_pk_mul_f32 v[150:151], v[180:181], v[56:57] op_sel_hi:[0,1]
	v_pk_mul_f32 v[128:129], v[150:151], v[128:129]
	v_pk_mul_f32 v[144:145], v[180:181], v[60:61] op_sel_hi:[0,1]
	v_pk_mul_f32 v[132:133], v[144:145], v[132:133]
	v_pk_mul_f32 v[146:147], v[180:181], v[62:63] op_sel_hi:[0,1]
	v_mul_f32_e32 v132, 0xbfb8aa3b, v132
	v_exp_f32_e32 v132, v132
	v_mul_f32_e32 v133, 0xbfb8aa3b, v133
	v_exp_f32_e32 v133, v133
	v_lshlrev_b32_e32 v144, 16, v184
	v_add_f32_e32 v132, 1.0, v132
	v_rcp_f32_e32 v132, v132
	v_add_f32_e32 v133, 1.0, v133
	v_rcp_f32_e32 v133, v133
	v_lshlrev_b32_e32 v145, 16, v188
	v_pk_mul_f32 v[134:135], v[146:147], v[134:135]
	v_fmac_f32_e32 v144, v132, v145
	v_and_b32_e32 v132, 0xffff0000, v184
	v_and_b32_e32 v145, 0xffff0000, v188
	v_fmac_f32_e32 v132, v133, v145
	v_mul_f32_e32 v133, 0xbfb8aa3b, v134
	v_exp_f32_e32 v133, v133
	v_mul_f32_e32 v135, 0xbfb8aa3b, v135
	v_exp_f32_e32 v135, v135
	v_mul_f32_e32 v128, 0xbfb8aa3b, v128
	v_exp_f32_e32 v128, v128
	v_mul_f32_e32 v129, 0xbfb8aa3b, v129
	v_exp_f32_e32 v129, v129
	v_add_f32_e32 v133, 1.0, v133
	v_rcp_f32_e32 v133, v133
	v_add_f32_e32 v135, 1.0, v135
	v_rcp_f32_e32 v135, v135
	v_add_f32_e32 v128, 1.0, v128
	v_rcp_f32_e32 v128, v128
	v_add_f32_e32 v129, 1.0, v129
	v_lshlrev_b32_e32 v134, 16, v185
	v_lshlrev_b32_e32 v145, 16, v189
	v_rcp_f32_e32 v129, v129
	v_fmac_f32_e32 v134, v133, v145
	v_and_b32_e32 v133, 0xffff0000, v185
	v_and_b32_e32 v145, 0xffff0000, v189
	v_pk_mul_f32 v[180:181], v[180:181], v[58:59] op_sel_hi:[0,1]
	v_fmac_f32_e32 v133, v135, v145
	v_lshlrev_b32_e32 v135, 16, v186
	v_lshlrev_b32_e32 v145, 16, v190
	v_pk_mul_f32 v[130:131], v[180:181], v[130:131]
	v_fmac_f32_e32 v135, v128, v145
	v_and_b32_e32 v145, 0xffff0000, v186
	v_and_b32_e32 v128, 0xffff0000, v190
	v_fmac_f32_e32 v145, v129, v128
	v_mul_f32_e32 v128, 0xbfb8aa3b, v130
	v_exp_f32_e32 v128, v128
	v_mul_f32_e32 v129, 0xbfb8aa3b, v131
	v_exp_f32_e32 v129, v129
	v_lshlrev_b32_e32 v146, 16, v187
	v_add_f32_e32 v128, 1.0, v128
	v_rcp_f32_e32 v128, v128
	v_add_f32_e32 v129, 1.0, v129
	v_rcp_f32_e32 v129, v129
	v_lshlrev_b32_e32 v130, 16, v191
	v_fmac_f32_e32 v146, v128, v130
	v_and_b32_e32 v131, 0xffff0000, v187
	v_and_b32_e32 v128, 0xffff0000, v191
	v_pk_mul_f32 v[184:185], v[178:179], v[76:77] op_sel_hi:[0,1]
	v_fmac_f32_e32 v131, v129, v128
	v_cvt_pk_bf16_f32 v128, v144, v132
	v_pk_mul_f32 v[124:125], v[184:185], v[124:125]
	v_cvt_pk_bf16_f32 v129, v134, v133
	v_cvt_pk_bf16_f32 v130, v135, v145
	v_cvt_pk_bf16_f32 v131, v146, v131
	global_store_dwordx4 v[148:149], v[128:131], off offset:256 sc1
	v_mul_f32_e32 v124, 0xbfb8aa3b, v124
	v_exp_f32_e32 v124, v124
	v_or_b32_e32 v128, 32, v166
	v_ashrrev_i32_e32 v129, 31, v128
	v_mul_f32_e32 v125, 0xbfb8aa3b, v125
	v_lshlrev_b64 v[180:181], 13, v[128:129]
	v_exp_f32_e32 v125, v125
	v_lshl_add_u64 v[128:129], s[8:9], 0, v[180:181]
	v_lshl_add_u64 v[130:131], s[10:11], 0, v[180:181]
	v_lshl_add_u64 v[128:129], v[128:129], 0, v[160:161]
	v_lshl_add_u64 v[132:133], v[130:131], 0, v[160:161]
	global_load_dwordx4 v[144:147], v[128:129], off
	s_nop 0
	global_load_dwordx4 v[128:131], v[128:129], off offset:256
	s_nop 0
	global_load_dwordx4 v[148:151], v[132:133], off
	s_nop 0
	global_load_dwordx4 v[132:135], v[132:133], off offset:256
	v_add_f32_e32 v124, 1.0, v124
	v_rcp_f32_e32 v124, v124
	v_add_f32_e32 v125, 1.0, v125
	v_rcp_f32_e32 v125, v125
	v_pk_mul_f32 v[186:187], v[178:179], v[78:79] op_sel_hi:[0,1]
	v_lshlrev_b32_e32 v163, 16, v152
	v_lshlrev_b32_e32 v165, 16, v156
	v_pk_mul_f32 v[126:127], v[186:187], v[126:127]
	v_fmac_f32_e32 v163, v124, v165
	v_and_b32_e32 v124, 0xffff0000, v152
	v_and_b32_e32 v152, 0xffff0000, v156
	v_pk_mul_f32 v[188:189], v[178:179], v[72:73] op_sel_hi:[0,1]
	v_fmac_f32_e32 v124, v125, v152
	v_mul_f32_e32 v125, 0xbfb8aa3b, v126
	v_pk_mul_f32 v[120:121], v[188:189], v[120:121]
	v_exp_f32_e32 v125, v125
	v_mul_f32_e32 v127, 0xbfb8aa3b, v127
	v_exp_f32_e32 v127, v127
	v_mul_f32_e32 v120, 0xbfb8aa3b, v120
	v_exp_f32_e32 v120, v120
	v_mul_f32_e32 v121, 0xbfb8aa3b, v121
	v_exp_f32_e32 v121, v121
	v_add_f32_e32 v125, 1.0, v125
	v_rcp_f32_e32 v125, v125
	v_add_f32_e32 v127, 1.0, v127
	v_rcp_f32_e32 v127, v127
	v_add_f32_e32 v120, 1.0, v120
	v_rcp_f32_e32 v120, v120
	v_add_f32_e32 v121, 1.0, v121
	v_lshlrev_b32_e32 v126, 16, v153
	v_lshlrev_b32_e32 v152, 16, v157
	v_rcp_f32_e32 v121, v121
	v_fmac_f32_e32 v126, v125, v152
	v_and_b32_e32 v125, 0xffff0000, v153
	v_and_b32_e32 v152, 0xffff0000, v157
	v_pk_mul_f32 v[190:191], v[178:179], v[74:75] op_sel_hi:[0,1]
	v_fmac_f32_e32 v125, v127, v152
	v_lshlrev_b32_e32 v127, 16, v154
	v_lshlrev_b32_e32 v152, 16, v158
	v_pk_mul_f32 v[122:123], v[190:191], v[122:123]
	v_fmac_f32_e32 v127, v120, v152
	v_and_b32_e32 v152, 0xffff0000, v154
	v_and_b32_e32 v120, 0xffff0000, v158
	v_fmac_f32_e32 v152, v121, v120
	v_mul_f32_e32 v120, 0xbfb8aa3b, v122
	v_exp_f32_e32 v120, v120
	v_mul_f32_e32 v121, 0xbfb8aa3b, v123
	v_exp_f32_e32 v121, v121
;     __device__ __forceinline__ void operator()(const f32x4 (&acc)[2][2][4][2], const Unit& u, int wr, int wc, int fr, int fq) const {
;     ...
;         EPB_LOAD(0);
; #pragma unroll
;         for (int kb = 0; kb < 8; ++kb) { const int ai = kb >> 2, m = kb & 3;
;             if (kb < 7) EPB_LOAD(kb + 1);
;             { const int row = row0 + ai * HALF + m * 16; float rmx = 0.f;
; #pragma unroll
;                 for (int bj = 0; bj < 2; ++bj) { const int col = col0 + bj * HALF; f32x4 v0 = acc[ai][bj][m][0], v1 = acc[ai][bj][m][1];
;                     if (QI8) { const f32x4 c0 = cb[bj][0] * ra[ai][m], c1 = cb[bj][1] * ra[ai][m]; const i32x4 i0 = __builtin_bit_cast(i32x4, v0), i1 = __builtin_bit_cast(i32x4, v1);
;                         v0 = (f32x4){(float)i0[0], (float)i0[1], (float)i0[2], (float)i0[3]} * c0; v1 = (f32x4){(float)i1[0], (float)i1[1], (float)i1[2], (float)i1[3]} * c1; }
;                     else if (MODE == 0) { v0 = v0 * tsc; v1 = v1 * tsc; }
;                     if (!QI8 && MODE == 1) { v0 = v0 * cb[bj][0]; v1 = v1 * cb[bj][1]; }
;                     if (MODE == 2 || MODE == 3) { const u32x4 g = gq[kb & 1][bj];
;                         f32x4 g0 = {sigmoidf_(bflo(g.x)), sigmoidf_(bfhi(g.x)), sigmoidf_(bflo(g.y)), sigmoidf_(bfhi(g.y))};
;                         f32x4 g1 = {sigmoidf_(bflo(g.z)), sigmoidf_(bfhi(g.z)), sigmoidf_(bflo(g.w)), sigmoidf_(bfhi(g.w))};
;                         v0 = v0 * g0; v1 = v1 * g1;
;                         if (MODE == 3) { const u32x4 q = aq[kb & 1][bj];
;                             v0 = v0 + (f32x4){bflo(q.x), bfhi(q.x), bflo(q.y), bfhi(q.y)}; v1 = v1 + (f32x4){bflo(q.z), bfhi(q.z), bflo(q.w), bfhi(q.w)}; } }
;                     if (MODE == 4) { v0 = v0 + rs[kb & 1][bj][0]; v1 = v1 + rs[kb & 1][bj][1]; }
;                     if (MODE == 5) { const u32x4 c = gq[kb & 1][bj], q = aq[kb & 1][bj];
;                         v0 = (f32x4){bflo(c.x) + sigmoidf_(v0[0]) * bflo(q.x), bfhi(c.x) + sigmoidf_(v0[1]) * bfhi(q.x), bflo(c.y) + sigmoidf_(v0[2]) * bflo(q.y), bfhi(c.y) + sigmoidf_(v0[3]) * bfhi(q.y)};
;                         v1 = (f32x4){bflo(c.z) + sigmoidf_(v1[0]) * bflo(q.z), bfhi(c.z) + sigmoidf_(v1[1]) * bfhi(q.z), bflo(c.w) + sigmoidf_(v1[2]) * bflo(q.w), bfhi(c.w) + sigmoidf_(v1[3]) * bfhi(q.w)}; }
	v_lshlrev_b32_e32 v153, 16, v155
	v_add_f32_e32 v120, 1.0, v120
	v_rcp_f32_e32 v120, v120
	v_add_f32_e32 v121, 1.0, v121
	v_rcp_f32_e32 v121, v121
	v_lshlrev_b32_e32 v122, 16, v159
	v_fmac_f32_e32 v153, v120, v122
	v_and_b32_e32 v123, 0xffff0000, v155
	v_and_b32_e32 v120, 0xffff0000, v159
	v_fmac_f32_e32 v123, v121, v120
	v_cvt_pk_bf16_f32 v120, v163, v124
	v_cvt_pk_bf16_f32 v121, v126, v125
	v_lshl_add_u64 v[124:125], s[30:31], 0, v[182:183]
	v_lshl_add_u64 v[124:125], v[124:125], 0, v[160:161]
	v_cvt_pk_bf16_f32 v122, v127, v152
	v_cvt_pk_bf16_f32 v123, v153, v123
	global_store_dwordx4 v[124:125], v[120:123], off sc1
	v_pk_mul_f32 v[126:127], v[178:179], v[56:57] op_sel_hi:[0,1]
	v_pk_mul_f32 v[112:113], v[126:127], v[112:113]
	v_pk_mul_f32 v[120:121], v[178:179], v[60:61] op_sel_hi:[0,1]
	v_pk_mul_f32 v[116:117], v[120:121], v[116:117]
	v_pk_mul_f32 v[122:123], v[178:179], v[62:63] op_sel_hi:[0,1]
	v_mul_f32_e32 v116, 0xbfb8aa3b, v116
	v_exp_f32_e32 v116, v116
	v_mul_f32_e32 v117, 0xbfb8aa3b, v117
	v_exp_f32_e32 v117, v117
	v_lshlrev_b32_e32 v120, 16, v136
	v_add_f32_e32 v116, 1.0, v116
	v_rcp_f32_e32 v116, v116
	v_add_f32_e32 v117, 1.0, v117
	v_rcp_f32_e32 v117, v117
	v_lshlrev_b32_e32 v121, 16, v140
	v_pk_mul_f32 v[118:119], v[122:123], v[118:119]
	v_fmac_f32_e32 v120, v116, v121
	v_and_b32_e32 v116, 0xffff0000, v136
	v_and_b32_e32 v121, 0xffff0000, v140
	v_fmac_f32_e32 v116, v117, v121
	v_mul_f32_e32 v117, 0xbfb8aa3b, v118
	v_exp_f32_e32 v117, v117
	v_mul_f32_e32 v119, 0xbfb8aa3b, v119
	v_exp_f32_e32 v119, v119
	v_mul_f32_e32 v112, 0xbfb8aa3b, v112
	v_exp_f32_e32 v112, v112
	v_mul_f32_e32 v113, 0xbfb8aa3b, v113
	v_exp_f32_e32 v113, v113
	v_add_f32_e32 v117, 1.0, v117
	v_rcp_f32_e32 v117, v117
	v_add_f32_e32 v119, 1.0, v119
	v_rcp_f32_e32 v119, v119
	v_add_f32_e32 v112, 1.0, v112
	v_rcp_f32_e32 v112, v112
	v_add_f32_e32 v113, 1.0, v113
	v_lshlrev_b32_e32 v118, 16, v137
	v_lshlrev_b32_e32 v121, 16, v141
	v_rcp_f32_e32 v113, v113
	v_fmac_f32_e32 v118, v117, v121
	v_and_b32_e32 v117, 0xffff0000, v137
	v_and_b32_e32 v121, 0xffff0000, v141
	v_pk_mul_f32 v[152:153], v[178:179], v[58:59] op_sel_hi:[0,1]
	v_fmac_f32_e32 v117, v119, v121
	v_lshlrev_b32_e32 v119, 16, v138
	v_lshlrev_b32_e32 v121, 16, v142
	v_pk_mul_f32 v[114:115], v[152:153], v[114:115]
	v_fmac_f32_e32 v119, v112, v121
	v_and_b32_e32 v121, 0xffff0000, v138
	v_and_b32_e32 v112, 0xffff0000, v142
	v_fmac_f32_e32 v121, v113, v112
	v_mul_f32_e32 v112, 0xbfb8aa3b, v114
	v_exp_f32_e32 v112, v112
	v_mul_f32_e32 v113, 0xbfb8aa3b, v115
	v_exp_f32_e32 v113, v113
	v_lshlrev_b32_e32 v122, 16, v139
	v_add_f32_e32 v112, 1.0, v112
	v_rcp_f32_e32 v112, v112
	v_add_f32_e32 v113, 1.0, v113
	v_rcp_f32_e32 v113, v113
	v_lshlrev_b32_e32 v114, 16, v143
	v_fmac_f32_e32 v122, v112, v114
	v_and_b32_e32 v115, 0xffff0000, v139
	v_and_b32_e32 v112, 0xffff0000, v143
	v_pk_mul_f32 v[138:139], v[176:177], v[76:77] op_sel_hi:[0,1]
	v_fmac_f32_e32 v115, v113, v112
	v_cvt_pk_bf16_f32 v112, v120, v116
	v_pk_mul_f32 v[108:109], v[138:139], v[108:109]
	v_cvt_pk_bf16_f32 v113, v118, v117
	v_cvt_pk_bf16_f32 v114, v119, v121
	v_cvt_pk_bf16_f32 v115, v122, v115
	global_store_dwordx4 v[124:125], v[112:115], off offset:256 sc1
	v_mul_f32_e32 v108, 0xbfb8aa3b, v108
	v_exp_f32_e32 v108, v108
	v_or_b32_e32 v112, 48, v166
	v_ashrrev_i32_e32 v113, 31, v112
	v_mul_f32_e32 v109, 0xbfb8aa3b, v109
	v_lshlrev_b64 v[136:137], 13, v[112:113]
	v_exp_f32_e32 v109, v109
	v_lshl_add_u64 v[112:113], s[8:9], 0, v[136:137]
	v_lshl_add_u64 v[114:115], s[10:11], 0, v[136:137]
	v_lshl_add_u64 v[112:113], v[112:113], 0, v[160:161]
	v_lshl_add_u64 v[116:117], v[114:115], 0, v[160:161]
	global_load_dwordx4 v[120:123], v[112:113], off
	s_nop 0
	global_load_dwordx4 v[112:115], v[112:113], off offset:256
	s_nop 0
	global_load_dwordx4 v[124:127], v[116:117], off
	s_nop 0
	global_load_dwordx4 v[116:119], v[116:117], off offset:256
	v_add_f32_e32 v108, 1.0, v108
	v_rcp_f32_e32 v108, v108
	v_add_f32_e32 v109, 1.0, v109
	v_rcp_f32_e32 v109, v109
	v_pk_mul_f32 v[140:141], v[176:177], v[78:79] op_sel_hi:[0,1]
	s_waitcnt vmcnt(9)
	v_lshlrev_b32_e32 v138, 16, v144
	s_waitcnt vmcnt(7)
	v_lshlrev_b32_e32 v139, 16, v148
	v_pk_mul_f32 v[110:111], v[140:141], v[110:111]
	v_fmac_f32_e32 v138, v108, v139
	v_and_b32_e32 v108, 0xffff0000, v144
	v_and_b32_e32 v139, 0xffff0000, v148
	v_pk_mul_f32 v[142:143], v[176:177], v[72:73] op_sel_hi:[0,1]
	v_fmac_f32_e32 v108, v109, v139
	v_mul_f32_e32 v109, 0xbfb8aa3b, v110
	v_pk_mul_f32 v[104:105], v[142:143], v[104:105]
	v_exp_f32_e32 v109, v109
	v_mul_f32_e32 v111, 0xbfb8aa3b, v111
	v_exp_f32_e32 v111, v111
	v_mul_f32_e32 v104, 0xbfb8aa3b, v104
	v_exp_f32_e32 v104, v104
	v_mul_f32_e32 v105, 0xbfb8aa3b, v105
	v_exp_f32_e32 v105, v105
	v_add_f32_e32 v109, 1.0, v109
	v_rcp_f32_e32 v109, v109
	v_add_f32_e32 v111, 1.0, v111
	v_rcp_f32_e32 v111, v111
	v_add_f32_e32 v104, 1.0, v104
	v_rcp_f32_e32 v104, v104
	v_add_f32_e32 v105, 1.0, v105
	v_lshlrev_b32_e32 v110, 16, v145
	v_lshlrev_b32_e32 v139, 16, v149
	v_rcp_f32_e32 v105, v105
	v_fmac_f32_e32 v110, v109, v139
	v_and_b32_e32 v109, 0xffff0000, v145
	v_and_b32_e32 v139, 0xffff0000, v149
	v_pk_mul_f32 v[152:153], v[176:177], v[74:75] op_sel_hi:[0,1]
	v_fmac_f32_e32 v109, v111, v139
	v_lshlrev_b32_e32 v111, 16, v146
	v_lshlrev_b32_e32 v139, 16, v150
	v_pk_mul_f32 v[106:107], v[152:153], v[106:107]
	v_fmac_f32_e32 v111, v104, v139
	v_and_b32_e32 v139, 0xffff0000, v146
	v_and_b32_e32 v104, 0xffff0000, v150
	v_fmac_f32_e32 v139, v105, v104
	v_mul_f32_e32 v104, 0xbfb8aa3b, v106
	v_exp_f32_e32 v104, v104
	v_mul_f32_e32 v105, 0xbfb8aa3b, v107
	v_exp_f32_e32 v105, v105
	v_lshlrev_b32_e32 v140, 16, v147
	v_add_f32_e32 v104, 1.0, v104
	v_rcp_f32_e32 v104, v104
	v_add_f32_e32 v105, 1.0, v105
	v_rcp_f32_e32 v105, v105
	v_lshlrev_b32_e32 v106, 16, v151
	v_fmac_f32_e32 v140, v104, v106
	v_and_b32_e32 v107, 0xffff0000, v147
	v_and_b32_e32 v104, 0xffff0000, v151
	v_fmac_f32_e32 v107, v105, v104
	v_cvt_pk_bf16_f32 v104, v138, v108
	v_cvt_pk_bf16_f32 v105, v110, v109
	v_lshl_add_u64 v[108:109], s[30:31], 0, v[180:181]
	v_lshl_add_u64 v[108:109], v[108:109], 0, v[160:161]
	v_cvt_pk_bf16_f32 v106, v111, v139
	v_cvt_pk_bf16_f32 v107, v140, v107
	global_store_dwordx4 v[108:109], v[104:107], off sc1
	v_pk_mul_f32 v[110:111], v[176:177], v[56:57] op_sel_hi:[0,1]
	v_pk_mul_f32 v[96:97], v[110:111], v[96:97]
	v_pk_mul_f32 v[104:105], v[176:177], v[60:61] op_sel_hi:[0,1]
	v_pk_mul_f32 v[100:101], v[104:105], v[100:101]
	v_pk_mul_f32 v[106:107], v[176:177], v[62:63] op_sel_hi:[0,1]
	v_mul_f32_e32 v100, 0xbfb8aa3b, v100
	v_exp_f32_e32 v100, v100
	v_mul_f32_e32 v101, 0xbfb8aa3b, v101
	v_exp_f32_e32 v101, v101
	v_lshlrev_b32_e32 v104, 16, v128
	v_add_f32_e32 v100, 1.0, v100
	v_rcp_f32_e32 v100, v100
	v_add_f32_e32 v101, 1.0, v101
	v_rcp_f32_e32 v101, v101
	s_waitcnt vmcnt(7)
;     __device__ __forceinline__ void operator()(const f32x4 (&acc)[2][2][4][2], const Unit& u, int wr, int wc, int fr, int fq) const {
;     ...
;         EPB_LOAD(0);
; #pragma unroll
;         for (int kb = 0; kb < 8; ++kb) { const int ai = kb >> 2, m = kb & 3;
;             if (kb < 7) EPB_LOAD(kb + 1);
;             { const int row = row0 + ai * HALF + m * 16; float rmx = 0.f;
; #pragma unroll
;                 for (int bj = 0; bj < 2; ++bj) { const int col = col0 + bj * HALF; f32x4 v0 = acc[ai][bj][m][0], v1 = acc[ai][bj][m][1];
;                     if (QI8) { const f32x4 c0 = cb[bj][0] * ra[ai][m], c1 = cb[bj][1] * ra[ai][m]; const i32x4 i0 = __builtin_bit_cast(i32x4, v0), i1 = __builtin_bit_cast(i32x4, v1);
;                         v0 = (f32x4){(float)i0[0], (float)i0[1], (float)i0[2], (float)i0[3]} * c0; v1 = (f32x4){(float)i1[0], (float)i1[1], (float)i1[2], (float)i1[3]} * c1; }
;                     else if (MODE == 0) { v0 = v0 * tsc; v1 = v1 * tsc; }
;                     if (!QI8 && MODE == 1) { v0 = v0 * cb[bj][0]; v1 = v1 * cb[bj][1]; }
;                     if (MODE == 2 || MODE == 3) { const u32x4 g = gq[kb & 1][bj];
;                         f32x4 g0 = {sigmoidf_(bflo(g.x)), sigmoidf_(bfhi(g.x)), sigmoidf_(bflo(g.y)), sigmoidf_(bfhi(g.y))};
;                         f32x4 g1 = {sigmoidf_(bflo(g.z)), sigmoidf_(bfhi(g.z)), sigmoidf_(bflo(g.w)), sigmoidf_(bfhi(g.w))};
;                         v0 = v0 * g0; v1 = v1 * g1;
;                         if (MODE == 3) { const u32x4 q = aq[kb & 1][bj];
;                             v0 = v0 + (f32x4){bflo(q.x), bfhi(q.x), bflo(q.y), bfhi(q.y)}; v1 = v1 + (f32x4){bflo(q.z), bfhi(q.z), bflo(q.w), bfhi(q.w)}; } }
;                     if (MODE == 4) { v0 = v0 + rs[kb & 1][bj][0]; v1 = v1 + rs[kb & 1][bj][1]; }
;                     if (MODE == 5) { const u32x4 c = gq[kb & 1][bj], q = aq[kb & 1][bj];
;                         v0 = (f32x4){bflo(c.x) + sigmoidf_(v0[0]) * bflo(q.x), bfhi(c.x) + sigmoidf_(v0[1]) * bfhi(q.x), bflo(c.y) + sigmoidf_(v0[2]) * bflo(q.y), bfhi(c.y) + sigmoidf_(v0[3]) * bfhi(q.y)};
;                         v1 = (f32x4){bflo(c.z) + sigmoidf_(v1[0]) * bflo(q.z), bfhi(c.z) + sigmoidf_(v1[1]) * bfhi(q.z), bflo(c.w) + sigmoidf_(v1[2]) * bflo(q.w), bfhi(c.w) + sigmoidf_(v1[3]) * bfhi(q.w)}; }
	v_lshlrev_b32_e32 v105, 16, v132
	v_pk_mul_f32 v[102:103], v[106:107], v[102:103]
	v_fmac_f32_e32 v104, v100, v105
	v_and_b32_e32 v100, 0xffff0000, v128
	v_and_b32_e32 v105, 0xffff0000, v132
	v_fmac_f32_e32 v100, v101, v105
	v_mul_f32_e32 v101, 0xbfb8aa3b, v102
	v_exp_f32_e32 v101, v101
	v_mul_f32_e32 v103, 0xbfb8aa3b, v103
	v_exp_f32_e32 v103, v103
	v_mul_f32_e32 v96, 0xbfb8aa3b, v96
	v_exp_f32_e32 v96, v96
	v_mul_f32_e32 v97, 0xbfb8aa3b, v97
	v_exp_f32_e32 v97, v97
	v_add_f32_e32 v101, 1.0, v101
	v_rcp_f32_e32 v101, v101
	v_add_f32_e32 v103, 1.0, v103
	v_rcp_f32_e32 v103, v103
	v_add_f32_e32 v96, 1.0, v96
	v_rcp_f32_e32 v96, v96
	v_add_f32_e32 v97, 1.0, v97
	v_lshlrev_b32_e32 v102, 16, v129
	v_lshlrev_b32_e32 v105, 16, v133
	v_rcp_f32_e32 v97, v97
	v_fmac_f32_e32 v102, v101, v105
	v_and_b32_e32 v101, 0xffff0000, v129
	v_and_b32_e32 v105, 0xffff0000, v133
	v_pk_mul_f32 v[138:139], v[176:177], v[58:59] op_sel_hi:[0,1]
	v_fmac_f32_e32 v101, v103, v105
	v_lshlrev_b32_e32 v103, 16, v130
	v_lshlrev_b32_e32 v105, 16, v134
	v_pk_mul_f32 v[98:99], v[138:139], v[98:99]
	v_fmac_f32_e32 v103, v96, v105
	v_and_b32_e32 v105, 0xffff0000, v130
	v_and_b32_e32 v96, 0xffff0000, v134
	v_fmac_f32_e32 v105, v97, v96
	v_mul_f32_e32 v96, 0xbfb8aa3b, v98
	v_exp_f32_e32 v96, v96
	v_mul_f32_e32 v97, 0xbfb8aa3b, v99
	v_exp_f32_e32 v97, v97
	v_lshlrev_b32_e32 v106, 16, v131
	v_add_f32_e32 v96, 1.0, v96
	v_rcp_f32_e32 v96, v96
	v_add_f32_e32 v97, 1.0, v97
	v_rcp_f32_e32 v97, v97
	v_lshlrev_b32_e32 v98, 16, v135
	v_fmac_f32_e32 v106, v96, v98
	v_and_b32_e32 v99, 0xffff0000, v131
	v_and_b32_e32 v96, 0xffff0000, v135
	v_pk_mul_f32 v[128:129], v[174:175], v[76:77] op_sel_hi:[0,1]
	v_fmac_f32_e32 v99, v97, v96
	v_pk_mul_f32 v[92:93], v[128:129], v[92:93]
	v_cvt_pk_bf16_f32 v96, v104, v100
	v_cvt_pk_bf16_f32 v97, v102, v101
	v_cvt_pk_bf16_f32 v98, v103, v105
	v_cvt_pk_bf16_f32 v99, v106, v99
	global_store_dwordx4 v[108:109], v[96:99], off offset:256 sc1
	v_mul_f32_e32 v92, 0xbfb8aa3b, v92
	v_exp_f32_e32 v92, v92
	v_lshl_add_u64 v[96:97], s[8:9], 0, v[172:173]
	v_lshl_add_u64 v[98:99], s[10:11], 0, v[172:173]
	v_mul_f32_e32 v93, 0xbfb8aa3b, v93
	v_lshl_add_u64 v[96:97], v[96:97], 0, v[160:161]
	v_lshl_add_u64 v[100:101], v[98:99], 0, v[160:161]
	v_exp_f32_e32 v93, v93
	global_load_dwordx4 v[104:107], v[96:97], off
	s_nop 0
	global_load_dwordx4 v[96:99], v[96:97], off offset:256
	s_nop 0
	global_load_dwordx4 v[108:111], v[100:101], off
	s_nop 0
	global_load_dwordx4 v[100:103], v[100:101], off offset:256
	v_add_f32_e32 v92, 1.0, v92
	v_rcp_f32_e32 v92, v92
	v_add_f32_e32 v93, 1.0, v93
	v_rcp_f32_e32 v93, v93
	v_pk_mul_f32 v[130:131], v[174:175], v[78:79] op_sel_hi:[0,1]
	s_waitcnt vmcnt(9)
	v_lshlrev_b32_e32 v128, 16, v120
	s_waitcnt vmcnt(7)
	v_lshlrev_b32_e32 v129, 16, v124
	v_pk_mul_f32 v[94:95], v[130:131], v[94:95]
	v_fmac_f32_e32 v128, v92, v129
	v_and_b32_e32 v92, 0xffff0000, v120
	v_and_b32_e32 v120, 0xffff0000, v124
	v_pk_mul_f32 v[132:133], v[174:175], v[72:73] op_sel_hi:[0,1]
	v_fmac_f32_e32 v92, v93, v120
	v_mul_f32_e32 v93, 0xbfb8aa3b, v94
	v_pk_mul_f32 v[88:89], v[132:133], v[88:89]
	v_exp_f32_e32 v93, v93
	v_mul_f32_e32 v95, 0xbfb8aa3b, v95
	v_exp_f32_e32 v95, v95
	v_mul_f32_e32 v88, 0xbfb8aa3b, v88
	v_exp_f32_e32 v88, v88
	v_mul_f32_e32 v89, 0xbfb8aa3b, v89
	v_exp_f32_e32 v89, v89
	v_add_f32_e32 v93, 1.0, v93
	v_rcp_f32_e32 v93, v93
	v_add_f32_e32 v95, 1.0, v95
	v_rcp_f32_e32 v95, v95
	v_add_f32_e32 v88, 1.0, v88
	v_rcp_f32_e32 v88, v88
	v_add_f32_e32 v89, 1.0, v89
	v_lshlrev_b32_e32 v94, 16, v121
	v_lshlrev_b32_e32 v120, 16, v125
	v_rcp_f32_e32 v89, v89
	v_fmac_f32_e32 v94, v93, v120
	v_and_b32_e32 v93, 0xffff0000, v121
	v_and_b32_e32 v120, 0xffff0000, v125
	v_pk_mul_f32 v[134:135], v[174:175], v[74:75] op_sel_hi:[0,1]
	v_fmac_f32_e32 v93, v95, v120
	v_lshlrev_b32_e32 v95, 16, v122
	v_lshlrev_b32_e32 v120, 16, v126
	v_pk_mul_f32 v[90:91], v[134:135], v[90:91]
	v_fmac_f32_e32 v95, v88, v120
	v_and_b32_e32 v120, 0xffff0000, v122
	v_and_b32_e32 v88, 0xffff0000, v126
	v_fmac_f32_e32 v120, v89, v88
	v_mul_f32_e32 v88, 0xbfb8aa3b, v90
	v_exp_f32_e32 v88, v88
	v_mul_f32_e32 v89, 0xbfb8aa3b, v91
	v_exp_f32_e32 v89, v89
	v_lshlrev_b32_e32 v121, 16, v123
	v_add_f32_e32 v88, 1.0, v88
	v_rcp_f32_e32 v88, v88
	v_add_f32_e32 v89, 1.0, v89
	v_rcp_f32_e32 v89, v89
	v_lshlrev_b32_e32 v90, 16, v127
	v_fmac_f32_e32 v121, v88, v90
	v_and_b32_e32 v91, 0xffff0000, v123
	v_and_b32_e32 v88, 0xffff0000, v127
	v_cvt_f32_i32_e32 v84, v84
	v_fmac_f32_e32 v91, v89, v88
	v_cvt_pk_bf16_f32 v88, v128, v92
	v_cvt_pk_bf16_f32 v89, v94, v93
	v_lshl_add_u64 v[92:93], s[30:31], 0, v[136:137]
	v_lshl_add_u64 v[92:93], v[92:93], 0, v[160:161]
	v_cvt_pk_bf16_f32 v90, v95, v120
	v_cvt_pk_bf16_f32 v91, v121, v91
	global_store_dwordx4 v[92:93], v[88:91], off sc1
	v_cvt_f32_i32_e32 v87, v87
	v_cvt_f32_i32_e32 v86, v86
	v_pk_mul_f32 v[88:89], v[174:175], v[60:61] op_sel_hi:[0,1]
	v_pk_mul_f32 v[84:85], v[88:89], v[84:85]
	v_cvt_f32_i32_e32 v81, v81
	v_mul_f32_e32 v84, 0xbfb8aa3b, v84
	v_exp_f32_e32 v84, v84
	v_mul_f32_e32 v85, 0xbfb8aa3b, v85
	v_exp_f32_e32 v85, v85
	v_cvt_f32_i32_e32 v80, v80
	v_add_f32_e32 v84, 1.0, v84
	v_rcp_f32_e32 v84, v84
	v_add_f32_e32 v85, 1.0, v85
	v_rcp_f32_e32 v85, v85
	v_pk_mul_f32 v[90:91], v[174:175], v[62:63] op_sel_hi:[0,1]
	v_lshlrev_b32_e32 v88, 16, v112
	s_waitcnt vmcnt(7)
;     __device__ __forceinline__ void operator()(const f32x4 (&acc)[2][2][4][2], const Unit& u, int wr, int wc, int fr, int fq) const {
;     ...
;         EPB_LOAD(0);
; #pragma unroll
;         for (int kb = 0; kb < 8; ++kb) { const int ai = kb >> 2, m = kb & 3;
;             if (kb < 7) EPB_LOAD(kb + 1);
;             { const int row = row0 + ai * HALF + m * 16; float rmx = 0.f;
; #pragma unroll
;                 for (int bj = 0; bj < 2; ++bj) { const int col = col0 + bj * HALF; f32x4 v0 = acc[ai][bj][m][0], v1 = acc[ai][bj][m][1];
;                     if (QI8) { const f32x4 c0 = cb[bj][0] * ra[ai][m], c1 = cb[bj][1] * ra[ai][m]; const i32x4 i0 = __builtin_bit_cast(i32x4, v0), i1 = __builtin_bit_cast(i32x4, v1);
;                         v0 = (f32x4){(float)i0[0], (float)i0[1], (float)i0[2], (float)i0[3]} * c0; v1 = (f32x4){(float)i1[0], (float)i1[1], (float)i1[2], (float)i1[3]} * c1; }
;                     else if (MODE == 0) { v0 = v0 * tsc; v1 = v1 * tsc; }
;                     if (!QI8 && MODE == 1) { v0 = v0 * cb[bj][0]; v1 = v1 * cb[bj][1]; }
;                     if (MODE == 2 || MODE == 3) { const u32x4 g = gq[kb & 1][bj];
;                         f32x4 g0 = {sigmoidf_(bflo(g.x)), sigmoidf_(bfhi(g.x)), sigmoidf_(bflo(g.y)), sigmoidf_(bfhi(g.y))};
;                         f32x4 g1 = {sigmoidf_(bflo(g.z)), sigmoidf_(bfhi(g.z)), sigmoidf_(bflo(g.w)), sigmoidf_(bfhi(g.w))};
;                         v0 = v0 * g0; v1 = v1 * g1;
;                         if (MODE == 3) { const u32x4 q = aq[kb & 1][bj];
;                             v0 = v0 + (f32x4){bflo(q.x), bfhi(q.x), bflo(q.y), bfhi(q.y)}; v1 = v1 + (f32x4){bflo(q.z), bfhi(q.z), bflo(q.w), bfhi(q.w)}; } }
;                     if (MODE == 4) { v0 = v0 + rs[kb & 1][bj][0]; v1 = v1 + rs[kb & 1][bj][1]; }
;                     if (MODE == 5) { const u32x4 c = gq[kb & 1][bj], q = aq[kb & 1][bj];
;                         v0 = (f32x4){bflo(c.x) + sigmoidf_(v0[0]) * bflo(q.x), bfhi(c.x) + sigmoidf_(v0[1]) * bfhi(q.x), bflo(c.y) + sigmoidf_(v0[2]) * bflo(q.y), bfhi(c.y) + sigmoidf_(v0[3]) * bfhi(q.y)};
;                         v1 = (f32x4){bflo(c.z) + sigmoidf_(v1[0]) * bflo(q.z), bfhi(c.z) + sigmoidf_(v1[1]) * bfhi(q.z), bflo(c.w) + sigmoidf_(v1[2]) * bflo(q.w), bfhi(c.w) + sigmoidf_(v1[3]) * bfhi(q.w)}; }
	v_lshlrev_b32_e32 v89, 16, v116
	v_pk_mul_f32 v[86:87], v[90:91], v[86:87]
	v_fmac_f32_e32 v88, v84, v89
	v_and_b32_e32 v84, 0xffff0000, v112
	v_and_b32_e32 v89, 0xffff0000, v116
	v_pk_mul_f32 v[94:95], v[174:175], v[56:57] op_sel_hi:[0,1]
	v_fmac_f32_e32 v84, v85, v89
	v_mul_f32_e32 v85, 0xbfb8aa3b, v86
	v_pk_mul_f32 v[80:81], v[94:95], v[80:81]
	v_exp_f32_e32 v85, v85
	v_mul_f32_e32 v87, 0xbfb8aa3b, v87
	v_exp_f32_e32 v87, v87
	v_mul_f32_e32 v80, 0xbfb8aa3b, v80
	v_exp_f32_e32 v80, v80
	v_mul_f32_e32 v81, 0xbfb8aa3b, v81
	v_exp_f32_e32 v81, v81
	v_add_f32_e32 v85, 1.0, v85
	v_rcp_f32_e32 v85, v85
	v_add_f32_e32 v87, 1.0, v87
	v_rcp_f32_e32 v87, v87
	v_add_f32_e32 v80, 1.0, v80
	v_cvt_f32_i32_e32 v83, v83
	v_cvt_f32_i32_e32 v82, v82
	v_rcp_f32_e32 v80, v80
	v_add_f32_e32 v81, 1.0, v81
	v_lshlrev_b32_e32 v86, 16, v113
	v_lshlrev_b32_e32 v89, 16, v117
	v_rcp_f32_e32 v81, v81
	v_fmac_f32_e32 v86, v85, v89
	v_and_b32_e32 v85, 0xffff0000, v113
	v_and_b32_e32 v89, 0xffff0000, v117
	v_pk_mul_f32 v[120:121], v[174:175], v[58:59] op_sel_hi:[0,1]
	v_fmac_f32_e32 v85, v87, v89
	v_lshlrev_b32_e32 v87, 16, v114
	v_lshlrev_b32_e32 v89, 16, v118
	v_pk_mul_f32 v[82:83], v[120:121], v[82:83]
	v_fmac_f32_e32 v87, v80, v89
	v_and_b32_e32 v89, 0xffff0000, v114
	v_and_b32_e32 v80, 0xffff0000, v118
	v_fmac_f32_e32 v89, v81, v80
	v_mul_f32_e32 v80, 0xbfb8aa3b, v82
	v_exp_f32_e32 v80, v80
	v_mul_f32_e32 v81, 0xbfb8aa3b, v83
	v_exp_f32_e32 v81, v81
	v_cvt_f32_i32_e32 v69, v69
	v_add_f32_e32 v80, 1.0, v80
	v_cvt_f32_i32_e32 v68, v68
	v_rcp_f32_e32 v80, v80
	v_add_f32_e32 v81, 1.0, v81
	v_rcp_f32_e32 v81, v81
	v_lshlrev_b32_e32 v90, 16, v115
	v_and_b32_e32 v83, 0xffff0000, v115
	v_pk_mul_f32 v[114:115], v[170:171], v[76:77] op_sel_hi:[0,1]
	v_lshlrev_b32_e32 v82, 16, v119
	v_pk_mul_f32 v[68:69], v[114:115], v[68:69]
	v_fmac_f32_e32 v90, v80, v82
	v_and_b32_e32 v80, 0xffff0000, v119
	v_mul_f32_e32 v68, 0xbfb8aa3b, v68
	v_fmac_f32_e32 v83, v81, v80
	v_cvt_pk_bf16_f32 v80, v88, v84
	v_exp_f32_e32 v68, v68
	v_mul_f32_e32 v69, 0xbfb8aa3b, v69
	v_cvt_pk_bf16_f32 v81, v86, v85
	v_cvt_pk_bf16_f32 v82, v87, v89
	v_cvt_pk_bf16_f32 v83, v90, v83
	global_store_dwordx4 v[92:93], v[80:83], off offset:256 sc1
	v_exp_f32_e32 v69, v69
	v_add_f32_e32 v68, 1.0, v68
	v_add_u32_e32 v80, 0x90, v166
	v_ashrrev_i32_e32 v81, 31, v80
	v_lshlrev_b64 v[112:113], 13, v[80:81]
	v_lshl_add_u64 v[80:81], s[8:9], 0, v[112:113]
	v_lshl_add_u64 v[82:83], s[10:11], 0, v[112:113]
	v_lshl_add_u64 v[80:81], v[80:81], 0, v[160:161]
	v_lshl_add_u64 v[84:85], v[82:83], 0, v[160:161]
	v_cvt_f32_i32_e32 v71, v71
	v_cvt_f32_i32_e32 v70, v70
	v_rcp_f32_e32 v68, v68
	v_add_f32_e32 v69, 1.0, v69
	global_load_dwordx4 v[88:91], v[80:81], off
	s_nop 0
	global_load_dwordx4 v[80:83], v[80:81], off offset:256
	s_nop 0
	global_load_dwordx4 v[92:95], v[84:85], off
	s_nop 0
	global_load_dwordx4 v[84:87], v[84:85], off offset:256
	v_rcp_f32_e32 v69, v69
	v_cvt_f32_i32_e32 v65, v65
	v_cvt_f32_i32_e32 v64, v64
	v_pk_mul_f32 v[116:117], v[170:171], v[78:79] op_sel_hi:[0,1]
	s_waitcnt vmcnt(9)
	v_lshlrev_b32_e32 v114, 16, v104
	s_waitcnt vmcnt(7)
	v_lshlrev_b32_e32 v115, 16, v108
	v_pk_mul_f32 v[70:71], v[116:117], v[70:71]
	v_fmac_f32_e32 v114, v68, v115
	v_and_b32_e32 v68, 0xffff0000, v104
	v_and_b32_e32 v104, 0xffff0000, v108
	v_pk_mul_f32 v[118:119], v[170:171], v[72:73] op_sel_hi:[0,1]
	v_fmac_f32_e32 v68, v69, v104
	v_mul_f32_e32 v69, 0xbfb8aa3b, v70
	v_pk_mul_f32 v[64:65], v[118:119], v[64:65]
	v_exp_f32_e32 v69, v69
	v_mul_f32_e32 v71, 0xbfb8aa3b, v71
	v_exp_f32_e32 v71, v71
	v_mul_f32_e32 v64, 0xbfb8aa3b, v64
	v_exp_f32_e32 v64, v64
	v_mul_f32_e32 v65, 0xbfb8aa3b, v65
	v_exp_f32_e32 v65, v65
	v_add_f32_e32 v69, 1.0, v69
	v_rcp_f32_e32 v69, v69
	v_add_f32_e32 v71, 1.0, v71
	v_rcp_f32_e32 v71, v71
	v_add_f32_e32 v64, 1.0, v64
	v_cvt_f32_i32_e32 v67, v67
	v_cvt_f32_i32_e32 v66, v66
	v_rcp_f32_e32 v64, v64
	v_add_f32_e32 v65, 1.0, v65
	v_lshlrev_b32_e32 v70, 16, v105
	v_lshlrev_b32_e32 v104, 16, v109
	v_rcp_f32_e32 v65, v65
	v_fmac_f32_e32 v70, v69, v104
	v_and_b32_e32 v69, 0xffff0000, v105
	v_and_b32_e32 v104, 0xffff0000, v109
	v_pk_mul_f32 v[120:121], v[170:171], v[74:75] op_sel_hi:[0,1]
	v_fmac_f32_e32 v69, v71, v104
	v_lshlrev_b32_e32 v71, 16, v106
	v_lshlrev_b32_e32 v104, 16, v110
	v_pk_mul_f32 v[66:67], v[120:121], v[66:67]
	v_fmac_f32_e32 v71, v64, v104
	v_and_b32_e32 v104, 0xffff0000, v106
	v_and_b32_e32 v64, 0xffff0000, v110
	v_fmac_f32_e32 v104, v65, v64
	v_mul_f32_e32 v64, 0xbfb8aa3b, v66
	v_exp_f32_e32 v64, v64
	v_mul_f32_e32 v65, 0xbfb8aa3b, v67
	v_exp_f32_e32 v65, v65
	v_lshlrev_b32_e32 v105, 16, v107
	v_add_f32_e32 v64, 1.0, v64
	v_rcp_f32_e32 v64, v64
	v_add_f32_e32 v65, 1.0, v65
	v_rcp_f32_e32 v65, v65
	v_lshlrev_b32_e32 v66, 16, v111
	v_fmac_f32_e32 v105, v64, v66
	v_and_b32_e32 v67, 0xffff0000, v107
	v_and_b32_e32 v64, 0xffff0000, v111
	v_cvt_f32_i32_e32 v53, v53
	v_cvt_f32_i32_e32 v52, v52
	v_fmac_f32_e32 v67, v65, v64
	v_cvt_pk_bf16_f32 v64, v114, v68
	v_cvt_pk_bf16_f32 v65, v70, v69
	v_lshl_add_u64 v[68:69], s[30:31], 0, v[172:173]
	v_lshl_add_u64 v[68:69], v[68:69], 0, v[160:161]
	v_cvt_pk_bf16_f32 v66, v71, v104
	v_cvt_pk_bf16_f32 v67, v105, v67
	global_store_dwordx4 v[68:69], v[64:67], off sc1
	v_cvt_f32_i32_e32 v55, v55
	v_cvt_f32_i32_e32 v54, v54
	v_pk_mul_f32 v[64:65], v[170:171], v[60:61] op_sel_hi:[0,1]
	v_pk_mul_f32 v[52:53], v[64:65], v[52:53]
	v_cvt_f32_i32_e32 v49, v49
	v_mul_f32_e32 v52, 0xbfb8aa3b, v52
	v_exp_f32_e32 v52, v52
	v_mul_f32_e32 v53, 0xbfb8aa3b, v53
	v_exp_f32_e32 v53, v53
	v_cvt_f32_i32_e32 v48, v48
	v_add_f32_e32 v52, 1.0, v52
	v_rcp_f32_e32 v52, v52
	v_add_f32_e32 v53, 1.0, v53
	v_rcp_f32_e32 v53, v53
	v_pk_mul_f32 v[66:67], v[170:171], v[62:63] op_sel_hi:[0,1]
	v_lshlrev_b32_e32 v64, 16, v96
	s_waitcnt vmcnt(7)
;     __device__ __forceinline__ void operator()(const f32x4 (&acc)[2][2][4][2], const Unit& u, int wr, int wc, int fr, int fq) const {
;     ...
;         EPB_LOAD(0);
; #pragma unroll
;         for (int kb = 0; kb < 8; ++kb) { const int ai = kb >> 2, m = kb & 3;
;             if (kb < 7) EPB_LOAD(kb + 1);
;             { const int row = row0 + ai * HALF + m * 16; float rmx = 0.f;
; #pragma unroll
;                 for (int bj = 0; bj < 2; ++bj) { const int col = col0 + bj * HALF; f32x4 v0 = acc[ai][bj][m][0], v1 = acc[ai][bj][m][1];
;                     if (QI8) { const f32x4 c0 = cb[bj][0] * ra[ai][m], c1 = cb[bj][1] * ra[ai][m]; const i32x4 i0 = __builtin_bit_cast(i32x4, v0), i1 = __builtin_bit_cast(i32x4, v1);
;                         v0 = (f32x4){(float)i0[0], (float)i0[1], (float)i0[2], (float)i0[3]} * c0; v1 = (f32x4){(float)i1[0], (float)i1[1], (float)i1[2], (float)i1[3]} * c1; }
;                     else if (MODE == 0) { v0 = v0 * tsc; v1 = v1 * tsc; }
;                     if (!QI8 && MODE == 1) { v0 = v0 * cb[bj][0]; v1 = v1 * cb[bj][1]; }
;                     if (MODE == 2 || MODE == 3) { const u32x4 g = gq[kb & 1][bj];
;                         f32x4 g0 = {sigmoidf_(bflo(g.x)), sigmoidf_(bfhi(g.x)), sigmoidf_(bflo(g.y)), sigmoidf_(bfhi(g.y))};
;                         f32x4 g1 = {sigmoidf_(bflo(g.z)), sigmoidf_(bfhi(g.z)), sigmoidf_(bflo(g.w)), sigmoidf_(bfhi(g.w))};
;                         v0 = v0 * g0; v1 = v1 * g1;
;                         if (MODE == 3) { const u32x4 q = aq[kb & 1][bj];
;                             v0 = v0 + (f32x4){bflo(q.x), bfhi(q.x), bflo(q.y), bfhi(q.y)}; v1 = v1 + (f32x4){bflo(q.z), bfhi(q.z), bflo(q.w), bfhi(q.w)}; } }
;                     if (MODE == 4) { v0 = v0 + rs[kb & 1][bj][0]; v1 = v1 + rs[kb & 1][bj][1]; }
;                     if (MODE == 5) { const u32x4 c = gq[kb & 1][bj], q = aq[kb & 1][bj];
;                         v0 = (f32x4){bflo(c.x) + sigmoidf_(v0[0]) * bflo(q.x), bfhi(c.x) + sigmoidf_(v0[1]) * bfhi(q.x), bflo(c.y) + sigmoidf_(v0[2]) * bflo(q.y), bfhi(c.y) + sigmoidf_(v0[3]) * bfhi(q.y)};
;                         v1 = (f32x4){bflo(c.z) + sigmoidf_(v1[0]) * bflo(q.z), bfhi(c.z) + sigmoidf_(v1[1]) * bfhi(q.z), bflo(c.w) + sigmoidf_(v1[2]) * bflo(q.w), bfhi(c.w) + sigmoidf_(v1[3]) * bfhi(q.w)}; }
	v_lshlrev_b32_e32 v65, 16, v100
	v_pk_mul_f32 v[54:55], v[66:67], v[54:55]
	v_fmac_f32_e32 v64, v52, v65
	v_and_b32_e32 v52, 0xffff0000, v96
	v_and_b32_e32 v65, 0xffff0000, v100
	v_pk_mul_f32 v[70:71], v[170:171], v[56:57] op_sel_hi:[0,1]
	v_fmac_f32_e32 v52, v53, v65
	v_mul_f32_e32 v53, 0xbfb8aa3b, v54
	v_pk_mul_f32 v[48:49], v[70:71], v[48:49]
	v_exp_f32_e32 v53, v53
	v_mul_f32_e32 v55, 0xbfb8aa3b, v55
	v_exp_f32_e32 v55, v55
	v_mul_f32_e32 v48, 0xbfb8aa3b, v48
	v_exp_f32_e32 v48, v48
	v_mul_f32_e32 v49, 0xbfb8aa3b, v49
	v_exp_f32_e32 v49, v49
	v_add_f32_e32 v53, 1.0, v53
	v_rcp_f32_e32 v53, v53
	v_add_f32_e32 v55, 1.0, v55
	v_rcp_f32_e32 v55, v55
	v_add_f32_e32 v48, 1.0, v48
	v_cvt_f32_i32_e32 v51, v51
	v_cvt_f32_i32_e32 v50, v50
	v_rcp_f32_e32 v48, v48
	v_add_f32_e32 v49, 1.0, v49
	v_lshlrev_b32_e32 v54, 16, v97
	v_lshlrev_b32_e32 v65, 16, v101
	v_rcp_f32_e32 v49, v49
	v_fmac_f32_e32 v54, v53, v65
	v_and_b32_e32 v53, 0xffff0000, v97
	v_and_b32_e32 v65, 0xffff0000, v101
	v_pk_mul_f32 v[104:105], v[170:171], v[58:59] op_sel_hi:[0,1]
	v_fmac_f32_e32 v53, v55, v65
	v_lshlrev_b32_e32 v55, 16, v98
	v_lshlrev_b32_e32 v65, 16, v102
	v_pk_mul_f32 v[50:51], v[104:105], v[50:51]
	v_fmac_f32_e32 v55, v48, v65
	v_and_b32_e32 v65, 0xffff0000, v98
	v_and_b32_e32 v48, 0xffff0000, v102
	v_fmac_f32_e32 v65, v49, v48
	v_mul_f32_e32 v48, 0xbfb8aa3b, v50
	v_exp_f32_e32 v48, v48
	v_mul_f32_e32 v49, 0xbfb8aa3b, v51
	v_exp_f32_e32 v49, v49
	v_lshlrev_b32_e32 v66, 16, v99
	v_add_f32_e32 v48, 1.0, v48
	v_rcp_f32_e32 v48, v48
	v_add_f32_e32 v49, 1.0, v49
	v_rcp_f32_e32 v49, v49
	v_lshlrev_b32_e32 v50, 16, v103
	v_cvt_f32_i32_e32 v45, v45
	v_cvt_f32_i32_e32 v44, v44
	v_fmac_f32_e32 v66, v48, v50
	v_and_b32_e32 v51, 0xffff0000, v99
	v_and_b32_e32 v48, 0xffff0000, v103
	v_fmac_f32_e32 v51, v49, v48
	v_cvt_pk_bf16_f32 v48, v64, v52
	v_cvt_pk_bf16_f32 v49, v54, v53
	v_cvt_pk_bf16_f32 v50, v55, v65
	v_cvt_pk_bf16_f32 v51, v66, v51
	global_store_dwordx4 v[68:69], v[48:51], off offset:256 sc1
	v_pk_mul_f32 v[98:99], v[168:169], v[76:77] op_sel_hi:[0,1]
	v_pk_mul_f32 v[44:45], v[98:99], v[44:45]
	v_add_u32_e32 v48, 0xa0, v166
	v_ashrrev_i32_e32 v49, 31, v48
	v_lshlrev_b64 v[96:97], 13, v[48:49]
	v_mul_f32_e32 v44, 0xbfb8aa3b, v44
	v_lshl_add_u64 v[48:49], s[8:9], 0, v[96:97]
	v_lshl_add_u64 v[50:51], s[10:11], 0, v[96:97]
	v_exp_f32_e32 v44, v44
	v_mul_f32_e32 v45, 0xbfb8aa3b, v45
	v_lshl_add_u64 v[48:49], v[48:49], 0, v[160:161]
	v_lshl_add_u64 v[52:53], v[50:51], 0, v[160:161]
	v_exp_f32_e32 v45, v45
	global_load_dwordx4 v[64:67], v[48:49], off
	s_nop 0
	global_load_dwordx4 v[48:51], v[48:49], off offset:256
	s_nop 0
	global_load_dwordx4 v[68:71], v[52:53], off
	s_nop 0
	global_load_dwordx4 v[52:55], v[52:53], off offset:256
	v_add_f32_e32 v44, 1.0, v44
	v_cvt_f32_i32_e32 v47, v47
	v_cvt_f32_i32_e32 v46, v46
	v_rcp_f32_e32 v44, v44
	v_add_f32_e32 v45, 1.0, v45
	v_rcp_f32_e32 v45, v45
	v_cvt_f32_i32_e32 v41, v41
	v_cvt_f32_i32_e32 v40, v40
	v_pk_mul_f32 v[100:101], v[168:169], v[78:79] op_sel_hi:[0,1]
	s_waitcnt vmcnt(9)
	v_lshlrev_b32_e32 v98, 16, v88
	s_waitcnt vmcnt(7)
	v_lshlrev_b32_e32 v99, 16, v92
	v_pk_mul_f32 v[46:47], v[100:101], v[46:47]
	v_fmac_f32_e32 v98, v44, v99
	v_and_b32_e32 v44, 0xffff0000, v88
	v_and_b32_e32 v88, 0xffff0000, v92
	v_pk_mul_f32 v[102:103], v[168:169], v[72:73] op_sel_hi:[0,1]
	v_fmac_f32_e32 v44, v45, v88
	v_mul_f32_e32 v45, 0xbfb8aa3b, v46
	v_pk_mul_f32 v[40:41], v[102:103], v[40:41]
	v_exp_f32_e32 v45, v45
	v_mul_f32_e32 v47, 0xbfb8aa3b, v47
	v_exp_f32_e32 v47, v47
	v_mul_f32_e32 v40, 0xbfb8aa3b, v40
	v_exp_f32_e32 v40, v40
	v_mul_f32_e32 v41, 0xbfb8aa3b, v41
	v_exp_f32_e32 v41, v41
	v_add_f32_e32 v45, 1.0, v45
	v_rcp_f32_e32 v45, v45
	v_add_f32_e32 v47, 1.0, v47
	v_rcp_f32_e32 v47, v47
	v_add_f32_e32 v40, 1.0, v40
	v_cvt_f32_i32_e32 v43, v43
	v_cvt_f32_i32_e32 v42, v42
	v_rcp_f32_e32 v40, v40
	v_add_f32_e32 v41, 1.0, v41
	v_lshlrev_b32_e32 v46, 16, v89
	v_lshlrev_b32_e32 v88, 16, v93
	v_rcp_f32_e32 v41, v41
	v_fmac_f32_e32 v46, v45, v88
	v_and_b32_e32 v45, 0xffff0000, v89
	v_and_b32_e32 v88, 0xffff0000, v93
	v_pk_mul_f32 v[104:105], v[168:169], v[74:75] op_sel_hi:[0,1]
	v_fmac_f32_e32 v45, v47, v88
	v_lshlrev_b32_e32 v47, 16, v90
	v_lshlrev_b32_e32 v88, 16, v94
	v_pk_mul_f32 v[42:43], v[104:105], v[42:43]
	v_fmac_f32_e32 v47, v40, v88
	v_and_b32_e32 v88, 0xffff0000, v90
	v_and_b32_e32 v40, 0xffff0000, v94
	v_fmac_f32_e32 v88, v41, v40
	v_mul_f32_e32 v40, 0xbfb8aa3b, v42
	v_exp_f32_e32 v40, v40
	v_mul_f32_e32 v41, 0xbfb8aa3b, v43
	v_exp_f32_e32 v41, v41
	v_lshlrev_b32_e32 v89, 16, v91
	v_add_f32_e32 v40, 1.0, v40
	v_rcp_f32_e32 v40, v40
	v_add_f32_e32 v41, 1.0, v41
	v_rcp_f32_e32 v41, v41
	v_lshlrev_b32_e32 v42, 16, v95
	v_fmac_f32_e32 v89, v40, v42
	v_and_b32_e32 v43, 0xffff0000, v91
	v_and_b32_e32 v40, 0xffff0000, v95
	v_cvt_f32_i32_e32 v37, v37
	v_cvt_f32_i32_e32 v36, v36
	v_fmac_f32_e32 v43, v41, v40
	v_cvt_pk_bf16_f32 v40, v98, v44
	v_cvt_pk_bf16_f32 v41, v46, v45
	v_lshl_add_u64 v[44:45], s[30:31], 0, v[112:113]
	v_lshl_add_u64 v[44:45], v[44:45], 0, v[160:161]
	v_cvt_pk_bf16_f32 v42, v47, v88
	v_cvt_pk_bf16_f32 v43, v89, v43
	global_store_dwordx4 v[44:45], v[40:43], off sc1
	v_cvt_f32_i32_e32 v39, v39
	v_cvt_f32_i32_e32 v38, v38
	v_pk_mul_f32 v[40:41], v[168:169], v[60:61] op_sel_hi:[0,1]
	v_pk_mul_f32 v[36:37], v[40:41], v[36:37]
	v_cvt_f32_i32_e32 v33, v33
	v_mul_f32_e32 v36, 0xbfb8aa3b, v36
	v_exp_f32_e32 v36, v36
	v_mul_f32_e32 v37, 0xbfb8aa3b, v37
	v_exp_f32_e32 v37, v37
	v_cvt_f32_i32_e32 v32, v32
	v_add_f32_e32 v36, 1.0, v36
	v_rcp_f32_e32 v36, v36
	v_add_f32_e32 v37, 1.0, v37
	v_rcp_f32_e32 v37, v37
	v_pk_mul_f32 v[42:43], v[168:169], v[62:63] op_sel_hi:[0,1]
	v_lshlrev_b32_e32 v40, 16, v80
	s_waitcnt vmcnt(7)
;     __device__ __forceinline__ void operator()(const f32x4 (&acc)[2][2][4][2], const Unit& u, int wr, int wc, int fr, int fq) const {
;     ...
;         EPB_LOAD(0);
; #pragma unroll
;         for (int kb = 0; kb < 8; ++kb) { const int ai = kb >> 2, m = kb & 3;
;             if (kb < 7) EPB_LOAD(kb + 1);
;             { const int row = row0 + ai * HALF + m * 16; float rmx = 0.f;
; #pragma unroll
;                 for (int bj = 0; bj < 2; ++bj) { const int col = col0 + bj * HALF; f32x4 v0 = acc[ai][bj][m][0], v1 = acc[ai][bj][m][1];
;                     if (QI8) { const f32x4 c0 = cb[bj][0] * ra[ai][m], c1 = cb[bj][1] * ra[ai][m]; const i32x4 i0 = __builtin_bit_cast(i32x4, v0), i1 = __builtin_bit_cast(i32x4, v1);
;                         v0 = (f32x4){(float)i0[0], (float)i0[1], (float)i0[2], (float)i0[3]} * c0; v1 = (f32x4){(float)i1[0], (float)i1[1], (float)i1[2], (float)i1[3]} * c1; }
;                     else if (MODE == 0) { v0 = v0 * tsc; v1 = v1 * tsc; }
;                     if (!QI8 && MODE == 1) { v0 = v0 * cb[bj][0]; v1 = v1 * cb[bj][1]; }
;                     if (MODE == 2 || MODE == 3) { const u32x4 g = gq[kb & 1][bj];
;                         f32x4 g0 = {sigmoidf_(bflo(g.x)), sigmoidf_(bfhi(g.x)), sigmoidf_(bflo(g.y)), sigmoidf_(bfhi(g.y))};
;                         f32x4 g1 = {sigmoidf_(bflo(g.z)), sigmoidf_(bfhi(g.z)), sigmoidf_(bflo(g.w)), sigmoidf_(bfhi(g.w))};
;                         v0 = v0 * g0; v1 = v1 * g1;
;                         if (MODE == 3) { const u32x4 q = aq[kb & 1][bj];
;                             v0 = v0 + (f32x4){bflo(q.x), bfhi(q.x), bflo(q.y), bfhi(q.y)}; v1 = v1 + (f32x4){bflo(q.z), bfhi(q.z), bflo(q.w), bfhi(q.w)}; } }
;                     if (MODE == 4) { v0 = v0 + rs[kb & 1][bj][0]; v1 = v1 + rs[kb & 1][bj][1]; }
;                     if (MODE == 5) { const u32x4 c = gq[kb & 1][bj], q = aq[kb & 1][bj];
;                         v0 = (f32x4){bflo(c.x) + sigmoidf_(v0[0]) * bflo(q.x), bfhi(c.x) + sigmoidf_(v0[1]) * bfhi(q.x), bflo(c.y) + sigmoidf_(v0[2]) * bflo(q.y), bfhi(c.y) + sigmoidf_(v0[3]) * bfhi(q.y)};
;                         v1 = (f32x4){bflo(c.z) + sigmoidf_(v1[0]) * bflo(q.z), bfhi(c.z) + sigmoidf_(v1[1]) * bfhi(q.z), bflo(c.w) + sigmoidf_(v1[2]) * bflo(q.w), bfhi(c.w) + sigmoidf_(v1[3]) * bfhi(q.w)}; }
	v_lshlrev_b32_e32 v41, 16, v84
	v_pk_mul_f32 v[38:39], v[42:43], v[38:39]
	v_fmac_f32_e32 v40, v36, v41
	v_and_b32_e32 v36, 0xffff0000, v80
	v_and_b32_e32 v41, 0xffff0000, v84
	v_pk_mul_f32 v[46:47], v[168:169], v[56:57] op_sel_hi:[0,1]
	v_fmac_f32_e32 v36, v37, v41
	v_mul_f32_e32 v37, 0xbfb8aa3b, v38
	v_pk_mul_f32 v[32:33], v[46:47], v[32:33]
	v_exp_f32_e32 v37, v37
	v_mul_f32_e32 v39, 0xbfb8aa3b, v39
	v_exp_f32_e32 v39, v39
	v_mul_f32_e32 v32, 0xbfb8aa3b, v32
	v_exp_f32_e32 v32, v32
	v_mul_f32_e32 v33, 0xbfb8aa3b, v33
	v_exp_f32_e32 v33, v33
	v_add_f32_e32 v37, 1.0, v37
	v_rcp_f32_e32 v37, v37
	v_add_f32_e32 v39, 1.0, v39
	v_rcp_f32_e32 v39, v39
	v_add_f32_e32 v32, 1.0, v32
	v_cvt_f32_i32_e32 v35, v35
	v_cvt_f32_i32_e32 v34, v34
	v_rcp_f32_e32 v32, v32
	v_add_f32_e32 v33, 1.0, v33
	v_lshlrev_b32_e32 v38, 16, v81
	v_lshlrev_b32_e32 v41, 16, v85
	v_rcp_f32_e32 v33, v33
	v_fmac_f32_e32 v38, v37, v41
	v_and_b32_e32 v37, 0xffff0000, v81
	v_and_b32_e32 v41, 0xffff0000, v85
	v_pk_mul_f32 v[88:89], v[168:169], v[58:59] op_sel_hi:[0,1]
	v_fmac_f32_e32 v37, v39, v41
	v_lshlrev_b32_e32 v39, 16, v82
	v_lshlrev_b32_e32 v41, 16, v86
	v_pk_mul_f32 v[34:35], v[88:89], v[34:35]
	v_fmac_f32_e32 v39, v32, v41
	v_and_b32_e32 v41, 0xffff0000, v82
	v_and_b32_e32 v32, 0xffff0000, v86
	v_fmac_f32_e32 v41, v33, v32
	v_mul_f32_e32 v32, 0xbfb8aa3b, v34
	v_exp_f32_e32 v32, v32
	v_mul_f32_e32 v33, 0xbfb8aa3b, v35
	v_exp_f32_e32 v33, v33
	v_cvt_f32_i32_e32 v29, v29
	v_add_f32_e32 v32, 1.0, v32
	v_cvt_f32_i32_e32 v28, v28
	v_rcp_f32_e32 v32, v32
	v_add_f32_e32 v33, 1.0, v33
	v_rcp_f32_e32 v33, v33
	v_lshlrev_b32_e32 v42, 16, v83
	v_and_b32_e32 v35, 0xffff0000, v83
	v_pk_mul_f32 v[82:83], v[164:165], v[76:77] op_sel_hi:[0,1]
	v_lshlrev_b32_e32 v34, 16, v87
	v_pk_mul_f32 v[28:29], v[82:83], v[28:29]
	v_fmac_f32_e32 v42, v32, v34
	v_and_b32_e32 v32, 0xffff0000, v87
	v_mul_f32_e32 v28, 0xbfb8aa3b, v28
	v_fmac_f32_e32 v35, v33, v32
	v_cvt_pk_bf16_f32 v32, v40, v36
	v_exp_f32_e32 v28, v28
	v_mul_f32_e32 v29, 0xbfb8aa3b, v29
	v_cvt_pk_bf16_f32 v33, v38, v37
	v_cvt_pk_bf16_f32 v34, v39, v41
	v_cvt_pk_bf16_f32 v35, v42, v35
	global_store_dwordx4 v[44:45], v[32:35], off offset:256 sc1
	v_exp_f32_e32 v29, v29
	v_add_f32_e32 v28, 1.0, v28
	v_add_u32_e32 v32, 0xb0, v166
	v_ashrrev_i32_e32 v33, 31, v32
	v_lshlrev_b64 v[80:81], 13, v[32:33]
	v_lshl_add_u64 v[32:33], s[8:9], 0, v[80:81]
	v_lshl_add_u64 v[34:35], s[10:11], 0, v[80:81]
	v_lshl_add_u64 v[32:33], v[32:33], 0, v[160:161]
	v_lshl_add_u64 v[36:37], v[34:35], 0, v[160:161]
	v_cvt_f32_i32_e32 v31, v31
	v_cvt_f32_i32_e32 v30, v30
	v_rcp_f32_e32 v28, v28
	v_add_f32_e32 v29, 1.0, v29
	global_load_dwordx4 v[40:43], v[32:33], off
	s_nop 0
	global_load_dwordx4 v[32:35], v[32:33], off offset:256
	s_nop 0
	global_load_dwordx4 v[44:47], v[36:37], off
	s_nop 0
	global_load_dwordx4 v[36:39], v[36:37], off offset:256
	v_rcp_f32_e32 v29, v29
	v_cvt_f32_i32_e32 v25, v25
	v_cvt_f32_i32_e32 v24, v24
	v_pk_mul_f32 v[84:85], v[164:165], v[78:79] op_sel_hi:[0,1]
	s_waitcnt vmcnt(9)
	v_lshlrev_b32_e32 v82, 16, v64
	s_waitcnt vmcnt(7)
	v_lshlrev_b32_e32 v83, 16, v68
	v_pk_mul_f32 v[30:31], v[84:85], v[30:31]
	v_fmac_f32_e32 v82, v28, v83
	v_and_b32_e32 v28, 0xffff0000, v64
	v_and_b32_e32 v64, 0xffff0000, v68
	v_pk_mul_f32 v[86:87], v[164:165], v[72:73] op_sel_hi:[0,1]
	v_fmac_f32_e32 v28, v29, v64
	v_mul_f32_e32 v29, 0xbfb8aa3b, v30
	v_pk_mul_f32 v[24:25], v[86:87], v[24:25]
	v_exp_f32_e32 v29, v29
	v_mul_f32_e32 v31, 0xbfb8aa3b, v31
	v_exp_f32_e32 v31, v31
	v_mul_f32_e32 v24, 0xbfb8aa3b, v24
	v_exp_f32_e32 v24, v24
	v_mul_f32_e32 v25, 0xbfb8aa3b, v25
	v_exp_f32_e32 v25, v25
	v_add_f32_e32 v29, 1.0, v29
	v_rcp_f32_e32 v29, v29
	v_add_f32_e32 v31, 1.0, v31
	v_rcp_f32_e32 v31, v31
	v_add_f32_e32 v24, 1.0, v24
	v_cvt_f32_i32_e32 v27, v27
	v_cvt_f32_i32_e32 v26, v26
	v_rcp_f32_e32 v24, v24
	v_add_f32_e32 v25, 1.0, v25
	v_lshlrev_b32_e32 v30, 16, v65
	v_lshlrev_b32_e32 v64, 16, v69
	v_rcp_f32_e32 v25, v25
	v_fmac_f32_e32 v30, v29, v64
	v_and_b32_e32 v29, 0xffff0000, v65
	v_and_b32_e32 v64, 0xffff0000, v69
	v_pk_mul_f32 v[88:89], v[164:165], v[74:75] op_sel_hi:[0,1]
	v_fmac_f32_e32 v29, v31, v64
	v_lshlrev_b32_e32 v31, 16, v66
	v_lshlrev_b32_e32 v64, 16, v70
	v_pk_mul_f32 v[26:27], v[88:89], v[26:27]
	v_fmac_f32_e32 v31, v24, v64
	v_and_b32_e32 v64, 0xffff0000, v66
	v_and_b32_e32 v24, 0xffff0000, v70
	v_fmac_f32_e32 v64, v25, v24
	v_mul_f32_e32 v24, 0xbfb8aa3b, v26
	v_exp_f32_e32 v24, v24
	v_mul_f32_e32 v25, 0xbfb8aa3b, v27
	v_exp_f32_e32 v25, v25
	v_lshlrev_b32_e32 v65, 16, v67
	v_add_f32_e32 v24, 1.0, v24
	v_rcp_f32_e32 v24, v24
	v_add_f32_e32 v25, 1.0, v25
	v_rcp_f32_e32 v25, v25
	v_lshlrev_b32_e32 v26, 16, v71
	v_fmac_f32_e32 v65, v24, v26
	v_and_b32_e32 v27, 0xffff0000, v67
	v_and_b32_e32 v24, 0xffff0000, v71
	v_cvt_f32_i32_e32 v21, v21
	v_cvt_f32_i32_e32 v20, v20
	v_fmac_f32_e32 v27, v25, v24
	v_cvt_pk_bf16_f32 v24, v82, v28
	v_cvt_pk_bf16_f32 v25, v30, v29
	v_lshl_add_u64 v[28:29], s[30:31], 0, v[96:97]
	v_lshl_add_u64 v[28:29], v[28:29], 0, v[160:161]
	v_cvt_pk_bf16_f32 v26, v31, v64
	v_cvt_pk_bf16_f32 v27, v65, v27
	global_store_dwordx4 v[28:29], v[24:27], off sc1
	v_cvt_f32_i32_e32 v23, v23
	v_cvt_f32_i32_e32 v22, v22
	v_pk_mul_f32 v[24:25], v[164:165], v[60:61] op_sel_hi:[0,1]
	v_pk_mul_f32 v[20:21], v[24:25], v[20:21]
	v_cvt_f32_i32_e32 v17, v17
	v_mul_f32_e32 v20, 0xbfb8aa3b, v20
	v_exp_f32_e32 v20, v20
	v_mul_f32_e32 v21, 0xbfb8aa3b, v21
	v_exp_f32_e32 v21, v21
	v_cvt_f32_i32_e32 v16, v16
	v_add_f32_e32 v20, 1.0, v20
	v_rcp_f32_e32 v20, v20
	v_add_f32_e32 v21, 1.0, v21
	v_rcp_f32_e32 v21, v21
	v_pk_mul_f32 v[26:27], v[164:165], v[62:63] op_sel_hi:[0,1]
	v_lshlrev_b32_e32 v24, 16, v48
	s_waitcnt vmcnt(7)
;     __device__ __forceinline__ void operator()(const f32x4 (&acc)[2][2][4][2], const Unit& u, int wr, int wc, int fr, int fq) const {
;     ...
;         EPB_LOAD(0);
; #pragma unroll
;         for (int kb = 0; kb < 8; ++kb) { const int ai = kb >> 2, m = kb & 3;
;             if (kb < 7) EPB_LOAD(kb + 1);
;             { const int row = row0 + ai * HALF + m * 16; float rmx = 0.f;
; #pragma unroll
;                 for (int bj = 0; bj < 2; ++bj) { const int col = col0 + bj * HALF; f32x4 v0 = acc[ai][bj][m][0], v1 = acc[ai][bj][m][1];
;                     if (QI8) { const f32x4 c0 = cb[bj][0] * ra[ai][m], c1 = cb[bj][1] * ra[ai][m]; const i32x4 i0 = __builtin_bit_cast(i32x4, v0), i1 = __builtin_bit_cast(i32x4, v1);
;                         v0 = (f32x4){(float)i0[0], (float)i0[1], (float)i0[2], (float)i0[3]} * c0; v1 = (f32x4){(float)i1[0], (float)i1[1], (float)i1[2], (float)i1[3]} * c1; }
;                     else if (MODE == 0) { v0 = v0 * tsc; v1 = v1 * tsc; }
;                     if (!QI8 && MODE == 1) { v0 = v0 * cb[bj][0]; v1 = v1 * cb[bj][1]; }
;                     if (MODE == 2 || MODE == 3) { const u32x4 g = gq[kb & 1][bj];
;                         f32x4 g0 = {sigmoidf_(bflo(g.x)), sigmoidf_(bfhi(g.x)), sigmoidf_(bflo(g.y)), sigmoidf_(bfhi(g.y))};
;                         f32x4 g1 = {sigmoidf_(bflo(g.z)), sigmoidf_(bfhi(g.z)), sigmoidf_(bflo(g.w)), sigmoidf_(bfhi(g.w))};
;                         v0 = v0 * g0; v1 = v1 * g1;
;                         if (MODE == 3) { const u32x4 q = aq[kb & 1][bj];
;                             v0 = v0 + (f32x4){bflo(q.x), bfhi(q.x), bflo(q.y), bfhi(q.y)}; v1 = v1 + (f32x4){bflo(q.z), bfhi(q.z), bflo(q.w), bfhi(q.w)}; } }
;                     if (MODE == 4) { v0 = v0 + rs[kb & 1][bj][0]; v1 = v1 + rs[kb & 1][bj][1]; }
;                     if (MODE == 5) { const u32x4 c = gq[kb & 1][bj], q = aq[kb & 1][bj];
;                         v0 = (f32x4){bflo(c.x) + sigmoidf_(v0[0]) * bflo(q.x), bfhi(c.x) + sigmoidf_(v0[1]) * bfhi(q.x), bflo(c.y) + sigmoidf_(v0[2]) * bflo(q.y), bfhi(c.y) + sigmoidf_(v0[3]) * bfhi(q.y)};
;                         v1 = (f32x4){bflo(c.z) + sigmoidf_(v1[0]) * bflo(q.z), bfhi(c.z) + sigmoidf_(v1[1]) * bfhi(q.z), bflo(c.w) + sigmoidf_(v1[2]) * bflo(q.w), bfhi(c.w) + sigmoidf_(v1[3]) * bfhi(q.w)}; }
	v_lshlrev_b32_e32 v25, 16, v52
	v_pk_mul_f32 v[22:23], v[26:27], v[22:23]
	v_fmac_f32_e32 v24, v20, v25
	v_and_b32_e32 v20, 0xffff0000, v48
	v_and_b32_e32 v25, 0xffff0000, v52
	v_pk_mul_f32 v[30:31], v[164:165], v[56:57] op_sel_hi:[0,1]
	v_fmac_f32_e32 v20, v21, v25
	v_mul_f32_e32 v21, 0xbfb8aa3b, v22
	v_pk_mul_f32 v[16:17], v[30:31], v[16:17]
	v_exp_f32_e32 v21, v21
	v_mul_f32_e32 v23, 0xbfb8aa3b, v23
	v_exp_f32_e32 v23, v23
	v_mul_f32_e32 v16, 0xbfb8aa3b, v16
	v_exp_f32_e32 v16, v16
	v_mul_f32_e32 v17, 0xbfb8aa3b, v17
	v_exp_f32_e32 v17, v17
	v_add_f32_e32 v21, 1.0, v21
	v_rcp_f32_e32 v21, v21
	v_add_f32_e32 v23, 1.0, v23
	v_rcp_f32_e32 v23, v23
	v_add_f32_e32 v16, 1.0, v16
	v_cvt_f32_i32_e32 v19, v19
	v_cvt_f32_i32_e32 v18, v18
	v_rcp_f32_e32 v16, v16
	v_add_f32_e32 v17, 1.0, v17
	v_lshlrev_b32_e32 v22, 16, v49
	v_lshlrev_b32_e32 v25, 16, v53
	v_rcp_f32_e32 v17, v17
	v_fmac_f32_e32 v22, v21, v25
	v_and_b32_e32 v21, 0xffff0000, v49
	v_and_b32_e32 v25, 0xffff0000, v53
	v_pk_mul_f32 v[64:65], v[164:165], v[58:59] op_sel_hi:[0,1]
	v_fmac_f32_e32 v21, v23, v25
	v_lshlrev_b32_e32 v23, 16, v50
	v_lshlrev_b32_e32 v25, 16, v54
	v_pk_mul_f32 v[18:19], v[64:65], v[18:19]
	v_fmac_f32_e32 v23, v16, v25
	v_and_b32_e32 v25, 0xffff0000, v50
	v_and_b32_e32 v16, 0xffff0000, v54
	v_fmac_f32_e32 v25, v17, v16
	v_mul_f32_e32 v16, 0xbfb8aa3b, v18
	v_exp_f32_e32 v16, v16
	v_mul_f32_e32 v17, 0xbfb8aa3b, v19
	v_exp_f32_e32 v17, v17
	v_lshlrev_b32_e32 v26, 16, v51
	v_add_f32_e32 v16, 1.0, v16
	v_rcp_f32_e32 v16, v16
	v_add_f32_e32 v17, 1.0, v17
	v_rcp_f32_e32 v17, v17
	v_lshlrev_b32_e32 v18, 16, v55
	v_cvt_f32_i32_e32 v13, v13
	v_cvt_f32_i32_e32 v12, v12
	v_fmac_f32_e32 v26, v16, v18
	v_and_b32_e32 v19, 0xffff0000, v51
	v_and_b32_e32 v16, 0xffff0000, v55
	v_fmac_f32_e32 v19, v17, v16
	v_cvt_pk_bf16_f32 v16, v24, v20
	v_cvt_pk_bf16_f32 v17, v22, v21
	v_cvt_pk_bf16_f32 v18, v23, v25
	v_cvt_pk_bf16_f32 v19, v26, v19
	global_store_dwordx4 v[28:29], v[16:19], off offset:256 sc1
	v_cvt_f32_i32_e32 v15, v15
	v_cvt_f32_i32_e32 v14, v14
	v_pk_mul_f32 v[16:17], v[76:77], v[162:163] op_sel_hi:[1,0]
	v_cvt_f32_i32_e32 v9, v9
	v_pk_mul_f32 v[12:13], v[16:17], v[12:13]
	v_cvt_f32_i32_e32 v8, v8
	v_mul_f32_e32 v12, 0xbfb8aa3b, v12
	v_exp_f32_e32 v12, v12
	v_mul_f32_e32 v13, 0xbfb8aa3b, v13
	v_exp_f32_e32 v13, v13
	v_pk_mul_f32 v[18:19], v[78:79], v[162:163] op_sel_hi:[1,0]
	v_add_f32_e32 v12, 1.0, v12
	v_rcp_f32_e32 v12, v12
	v_add_f32_e32 v13, 1.0, v13
	v_rcp_f32_e32 v13, v13
	s_waitcnt vmcnt(5)
	v_lshlrev_b32_e32 v16, 16, v40
	s_waitcnt vmcnt(3)
	v_lshlrev_b32_e32 v17, 16, v44
	v_pk_mul_f32 v[14:15], v[18:19], v[14:15]
	v_fmac_f32_e32 v16, v12, v17
	v_and_b32_e32 v12, 0xffff0000, v40
	v_and_b32_e32 v17, 0xffff0000, v44
	v_pk_mul_f32 v[20:21], v[162:163], v[72:73] op_sel_hi:[0,1]
	v_fmac_f32_e32 v12, v13, v17
	v_mul_f32_e32 v13, 0xbfb8aa3b, v14
	v_pk_mul_f32 v[8:9], v[20:21], v[8:9]
	v_exp_f32_e32 v13, v13
	v_mul_f32_e32 v15, 0xbfb8aa3b, v15
	v_exp_f32_e32 v15, v15
	v_mul_f32_e32 v8, 0xbfb8aa3b, v8
	v_exp_f32_e32 v8, v8
	v_mul_f32_e32 v9, 0xbfb8aa3b, v9
	v_exp_f32_e32 v9, v9
	v_add_f32_e32 v13, 1.0, v13
	v_rcp_f32_e32 v13, v13
	v_add_f32_e32 v15, 1.0, v15
	v_rcp_f32_e32 v15, v15
	v_add_f32_e32 v8, 1.0, v8
	v_cvt_f32_i32_e32 v11, v11
	v_cvt_f32_i32_e32 v10, v10
	v_rcp_f32_e32 v8, v8
	v_add_f32_e32 v9, 1.0, v9
	v_lshlrev_b32_e32 v14, 16, v41
	v_lshlrev_b32_e32 v17, 16, v45
	v_rcp_f32_e32 v9, v9
	v_fmac_f32_e32 v14, v13, v17
	v_and_b32_e32 v13, 0xffff0000, v41
	v_and_b32_e32 v17, 0xffff0000, v45
	v_pk_mul_f32 v[22:23], v[162:163], v[74:75] op_sel_hi:[0,1]
	v_fmac_f32_e32 v13, v15, v17
	v_lshlrev_b32_e32 v15, 16, v42
	v_lshlrev_b32_e32 v17, 16, v46
	v_pk_mul_f32 v[10:11], v[22:23], v[10:11]
	v_fmac_f32_e32 v15, v8, v17
	v_and_b32_e32 v17, 0xffff0000, v42
	v_and_b32_e32 v8, 0xffff0000, v46
	v_fmac_f32_e32 v17, v9, v8
	v_mul_f32_e32 v8, 0xbfb8aa3b, v10
	v_exp_f32_e32 v8, v8
	v_mul_f32_e32 v9, 0xbfb8aa3b, v11
	v_exp_f32_e32 v9, v9
	v_lshlrev_b32_e32 v18, 16, v43
	v_add_f32_e32 v8, 1.0, v8
	v_rcp_f32_e32 v8, v8
	v_add_f32_e32 v9, 1.0, v9
	v_rcp_f32_e32 v9, v9
	v_lshlrev_b32_e32 v10, 16, v47
	v_fmac_f32_e32 v18, v8, v10
	v_and_b32_e32 v11, 0xffff0000, v43
	v_and_b32_e32 v8, 0xffff0000, v47
	v_cvt_f32_i32_e32 v5, v5
	v_cvt_f32_i32_e32 v4, v4
	v_fmac_f32_e32 v11, v9, v8
	v_cvt_pk_bf16_f32 v8, v16, v12
	v_cvt_pk_bf16_f32 v9, v14, v13
	v_lshl_add_u64 v[12:13], s[30:31], 0, v[80:81]
	v_lshl_add_u64 v[12:13], v[12:13], 0, v[160:161]
	v_cvt_pk_bf16_f32 v10, v15, v17
	v_cvt_pk_bf16_f32 v11, v18, v11
	global_store_dwordx4 v[12:13], v[8:11], off sc1
	v_cvt_f32_i32_e32 v7, v7
	v_cvt_f32_i32_e32 v6, v6
	v_pk_mul_f32 v[8:9], v[162:163], v[60:61] op_sel_hi:[0,1]
	v_pk_mul_f32 v[4:5], v[8:9], v[4:5]
	v_cvt_f32_i32_e32 v1, v1
	v_mul_f32_e32 v4, 0xbfb8aa3b, v4
	v_exp_f32_e32 v4, v4
	v_mul_f32_e32 v5, 0xbfb8aa3b, v5
	v_exp_f32_e32 v5, v5
	v_cvt_f32_i32_e32 v0, v0
	v_add_f32_e32 v4, 1.0, v4
	v_rcp_f32_e32 v4, v4
	v_add_f32_e32 v5, 1.0, v5
	v_rcp_f32_e32 v5, v5
	v_pk_mul_f32 v[10:11], v[162:163], v[62:63] op_sel_hi:[0,1]
	v_lshlrev_b32_e32 v8, 16, v32
	s_waitcnt vmcnt(3)
	v_lshlrev_b32_e32 v9, 16, v36
	v_pk_mul_f32 v[6:7], v[10:11], v[6:7]
	v_fmac_f32_e32 v8, v4, v9
	v_and_b32_e32 v4, 0xffff0000, v32
	v_and_b32_e32 v9, 0xffff0000, v36
	v_pk_mul_f32 v[14:15], v[162:163], v[56:57] op_sel_hi:[0,1]
	v_fmac_f32_e32 v4, v5, v9
	v_mul_f32_e32 v5, 0xbfb8aa3b, v6
	v_pk_mul_f32 v[0:1], v[14:15], v[0:1]
	v_exp_f32_e32 v5, v5
	v_mul_f32_e32 v7, 0xbfb8aa3b, v7
	v_exp_f32_e32 v7, v7
	v_mul_f32_e32 v0, 0xbfb8aa3b, v0
	v_exp_f32_e32 v0, v0
	v_mul_f32_e32 v1, 0xbfb8aa3b, v1
	v_exp_f32_e32 v1, v1
	v_add_f32_e32 v5, 1.0, v5
	v_rcp_f32_e32 v5, v5
	v_add_f32_e32 v7, 1.0, v7
	v_rcp_f32_e32 v7, v7
	v_add_f32_e32 v0, 1.0, v0
	v_cvt_f32_i32_e32 v3, v3
	v_cvt_f32_i32_e32 v2, v2
	v_rcp_f32_e32 v0, v0
	v_add_f32_e32 v1, 1.0, v1
	v_lshlrev_b32_e32 v6, 16, v33
	v_lshlrev_b32_e32 v9, 16, v37
	v_rcp_f32_e32 v1, v1
	v_fmac_f32_e32 v6, v5, v9
	v_and_b32_e32 v5, 0xffff0000, v33
	v_and_b32_e32 v9, 0xffff0000, v37
	v_pk_mul_f32 v[16:17], v[162:163], v[58:59] op_sel_hi:[0,1]
	v_fmac_f32_e32 v5, v7, v9
	v_lshlrev_b32_e32 v7, 16, v34
	v_lshlrev_b32_e32 v9, 16, v38
	v_pk_mul_f32 v[2:3], v[16:17], v[2:3]
	v_fmac_f32_e32 v7, v0, v9
	v_and_b32_e32 v9, 0xffff0000, v34
	v_and_b32_e32 v0, 0xffff0000, v38
	v_fmac_f32_e32 v9, v1, v0
	v_mul_f32_e32 v0, 0xbfb8aa3b, v2
	v_exp_f32_e32 v0, v0
	v_mul_f32_e32 v1, 0xbfb8aa3b, v3
	v_exp_f32_e32 v1, v1
	v_lshlrev_b32_e32 v10, 16, v35
	v_add_f32_e32 v0, 1.0, v0
	v_rcp_f32_e32 v0, v0
	v_add_f32_e32 v1, 1.0, v1
	v_rcp_f32_e32 v1, v1
	v_lshlrev_b32_e32 v2, 16, v39
	v_fmac_f32_e32 v10, v0, v2
	v_and_b32_e32 v3, 0xffff0000, v35
	v_and_b32_e32 v0, 0xffff0000, v39
	v_fmac_f32_e32 v3, v1, v0
	s_andn2_b64 vcc, exec, s[6:7]
	s_mov_b64 s[6:7], -1
	v_cvt_pk_bf16_f32 v0, v8, v4
	v_cvt_pk_bf16_f32 v1, v6, v5
	v_cvt_pk_bf16_f32 v2, v7, v9
	v_cvt_pk_bf16_f32 v3, v10, v3
	global_store_dwordx4 v[12:13], v[0:3], off offset:256 sc1
	s_cbranch_vccnz .LBB0_1722
; #define PG8_BAR __builtin_amdgcn_s_barrier()
; template <class Epi, class Sched, bool ALIGN_EPI = true, bool SP2 = true, class Side = NoSide>
; __device__ __forceinline__ void gemm_phase(LAS unsigned char* lds, const Gemm g, const Sched& S, const Epi& E, const Side side = Side()) {
;     ...
;         if (!has_next) break;
; #pragma unroll
;         for (int a = 0; a < 2; ++a)
; #pragma unroll
;             for (int b = 0; b < 2; ++b)
; #pragma unroll
;                 for (int m = 0; m < 4; ++m)
; #pragma unroll
;                     for (int n = 0; n < 2; ++n) acc[a][b][m][n] = (f32x4){0.f, 0.f, 0.f, 0.f};
;         cur = nxt; cA = nA; cB = nB; ++ui;
;         if constexpr (ALIGN_EPI) { if (wr == 1) PG8_BAR; }
	s_andn2_b64 vcc, exec, s[0:1]
	s_cbranch_vccnz .LBB0_1721
	s_barrier
	s_branch .LBB0_1721
